# PEER gather u pass: row offsets premultiplied and bpermutes in two bursts (waits unchanged) on top of v47
# speedup vs baseline: 1.0057x; 1.0057x over previous
.LBB0_1138:
	v_and_b32_e32 v4, 15, v148
	v_cmp_eq_u32_e32 vcc, 0, v4
	v_lshlrev_b32_e32 v5, 5, v40
	v_add_u32_e32 v10, 0x80, v148
	v_cndmask_b32_e32 v10, v10, v5, vcc
	v_cmp_gt_u32_e64 s[6:7], 8, v4
	v_lshl_add_u32 v32, v10, 2, v111
	v_and_b32_e32 v36, 12, v148
	v_cndmask_b32_e64 v10, 0, v252, s[6:7]
	v_cmp_lt_u32_e64 s[6:7], 3, v4
	v_lshl_or_b32 v4, v41, 3, v5
	v_add_u32_e32 v34, 0x400, v4
	v_lshlrev_b32_e32 v4, 4, v41
	v_lshl_or_b32 v35, v40, 6, v4
	v_mul_u32_u24_e32 v250, 0x600, v130
	ds_bpermute_b32 v4, v36, v250
	v_cmp_eq_u32_e32 vcc, 3, v41
	v_cmp_eq_u32_e64 s[2:3], 2, v41
	v_cmp_eq_u32_e64 s[4:5], 1, v41
	v_lshlrev_b32_e32 v129, 4, v148
	s_waitcnt lgkmcnt(0)
	v_add_u32_e32 v5, v4, v35
	v_add_u32_e32 v4, v4, v34
	buffer_load_dwordx4 v[38:41], v5, s[44:47], 0 offen
	buffer_load_dwordx2 v[42:43], v4, s[44:47], 0 offen
	buffer_load_dwordx4 v[44:47], v5, s[44:47], s21 offen
	buffer_load_dwordx2 v[48:49], v4, s[44:47], s33 offen
	buffer_load_dwordx4 v[50:53], v5, s[44:47], s20 offen
	buffer_load_dwordx2 v[54:55], v4, s[44:47], s21 offen
	buffer_load_dwordx4 v[56:59], v5, s[44:47], s23 offen
	buffer_load_dwordx2 v[60:61], v4, s[44:47], s94 offen
	s_mov_b32 s0, 0
	v_cndmask_b32_e64 v33, 1.0, v10, s[6:7]
	ds_bpermute_b32 v222, v36, v250 offset:32
	ds_bpermute_b32 v223, v36, v250 offset:48
	ds_bpermute_b32 v224, v36, v250 offset:64
	ds_bpermute_b32 v225, v36, v250 offset:80
	ds_bpermute_b32 v226, v36, v250 offset:96
	ds_bpermute_b32 v227, v36, v250 offset:112
	ds_bpermute_b32 v228, v36, v250 offset:128
	ds_bpermute_b32 v229, v36, v250 offset:144
	ds_bpermute_b32 v230, v36, v250 offset:160
	ds_bpermute_b32 v231, v36, v250 offset:176
	ds_bpermute_b32 v232, v36, v250 offset:192
	ds_bpermute_b32 v233, v36, v250 offset:208
	ds_bpermute_b32 v234, v36, v250 offset:224
	ds_bpermute_b32 v235, v36, v250 offset:240
	ds_bpermute_b32 v4, v36, v250 offset:16
	s_waitcnt lgkmcnt(0)
	v_add_u32_e32 v5, v4, v35
	v_add_u32_e32 v4, v4, v34
	buffer_load_dwordx4 v[62:65], v5, s[44:47], 0 offen
	buffer_load_dwordx4 v[68:71], v5, s[44:47], s20 offen
	buffer_load_dwordx4 v[74:77], v5, s[44:47], s21 offen
	buffer_load_dwordx4 v[86:89], v5, s[44:47], s23 offen
	buffer_load_dwordx2 v[66:67], v4, s[44:47], 0 offen
	buffer_load_dwordx2 v[78:79], v4, s[44:47], s33 offen
	buffer_load_dwordx2 v[72:73], v4, s[44:47], s21 offen
	buffer_load_dwordx2 v[90:91], v4, s[44:47], s94 offen
	v_add_u32_e32 v5, v222, v35
	v_add_u32_e32 v4, v222, v34
	buffer_load_dwordx4 v[92:95], v5, s[44:47], 0 offen
	buffer_load_dwordx4 v[98:101], v5, s[44:47], s20 offen
	buffer_load_dwordx4 v[150:153], v5, s[44:47], s21 offen
	buffer_load_dwordx4 v[156:159], v5, s[44:47], s23 offen
	buffer_load_dwordx2 v[96:97], v4, s[44:47], 0 offen
	buffer_load_dwordx2 v[154:155], v4, s[44:47], s33 offen
	buffer_load_dwordx2 v[102:103], v4, s[44:47], s21 offen
	buffer_load_dwordx2 v[160:161], v4, s[44:47], s94 offen
	v_add_u32_e32 v5, v223, v35
	v_add_u32_e32 v4, v223, v34
	buffer_load_dwordx4 v[162:165], v5, s[44:47], 0 offen
	buffer_load_dwordx4 v[168:171], v5, s[44:47], s20 offen
	buffer_load_dwordx4 v[174:177], v5, s[44:47], s21 offen
	buffer_load_dwordx4 v[216:219], v5, s[44:47], s23 offen
	buffer_load_dwordx2 v[166:167], v4, s[44:47], 0 offen
	buffer_load_dwordx2 v[178:179], v4, s[44:47], s33 offen
	buffer_load_dwordx2 v[172:173], v4, s[44:47], s21 offen
	buffer_load_dwordx2 v[220:221], v4, s[44:47], s94 offen
	v_mov_b32_e32 v22, v28
	v_mov_b32_e32 v23, v29
	v_mov_b32_e32 v16, v30
	v_mov_b32_e32 v17, v31
	s_waitcnt vmcnt(30)
	v_mfma_f32_16x16x128_f8f6f4 v[38:41], v[38:43], v[18:23], 0 cbsz:2 blgp:2
	v_mov_b32_e32 v10, v24
	v_mov_b32_e32 v11, v25
	v_mov_b32_e32 v4, v26
	s_waitcnt vmcnt(28)
	v_mfma_f32_16x16x128_f8f6f4 v[28:31], v[44:49], v[12:17], v[38:41] cbsz:2 blgp:2
	v_mov_b32_e32 v5, v27
	s_waitcnt vmcnt(26)
	v_mfma_f32_16x16x128_f8f6f4 v[28:31], v[50:55], v[6:11], v[28:31] cbsz:2 blgp:2
	s_waitcnt vmcnt(24)
	v_mfma_f32_16x16x128_f8f6f4 v[24:27], v[56:61], v[0:5], v[28:31] cbsz:2 blgp:2
	s_nop 7
	v_cndmask_b32_e64 v24, v24, v25, s[4:5]
	v_cndmask_b32_e64 v24, v24, v26, s[2:3]
	v_cndmask_b32_e32 v24, v24, v27, vcc
	v_mul_f32_e32 v25, v33, v24
	s_nop 1
	v_mov_b32_dpp v25, v25 quad_perm:[1,0,3,2] row_mask:0xf bank_mask:0xf bound_ctrl:1
	v_fmac_f32_e32 v25, v33, v24
	s_nop 1
	v_add_f32_dpp v24, v25, v25 quad_perm:[2,3,0,1] row_mask:0xf bank_mask:0xf bound_ctrl:1
	s_nop 1
	v_add_f32_dpp v24, v24, v24 row_half_mirror row_mask:0xf bank_mask:0xf bound_ctrl:1
	ds_write_b32 v32, v24 offset:49152
	v_add_u32_e32 v28, v224, v35
	v_add_u32_e32 v30, v224, v34
	buffer_load_dwordx4 v[24:27], v28, s[44:47], 0 offen
	buffer_load_dwordx4 v[38:41], v28, s[44:47], s20 offen
	buffer_load_dwordx4 v[44:47], v28, s[44:47], s21 offen
	buffer_load_dwordx4 v[50:53], v28, s[44:47], s23 offen
	s_nop 0
	buffer_load_dwordx2 v[28:29], v30, s[44:47], 0 offen
	buffer_load_dwordx2 v[48:49], v30, s[44:47], s33 offen
	buffer_load_dwordx2 v[42:43], v30, s[44:47], s21 offen
	buffer_load_dwordx2 v[54:55], v30, s[44:47], s94 offen
	s_waitcnt vmcnt(27)
	v_mfma_f32_16x16x128_f8f6f4 v[56:59], v[62:67], v[18:23], 0 cbsz:2 blgp:2
	s_waitcnt vmcnt(26)
	v_mfma_f32_16x16x128_f8f6f4 v[56:59], v[74:79], v[12:17], v[56:59] cbsz:2 blgp:2
	s_waitcnt vmcnt(25)
	v_mfma_f32_16x16x128_f8f6f4 v[56:59], v[68:73], v[6:11], v[56:59] cbsz:2 blgp:2
	s_waitcnt vmcnt(24)
	v_mfma_f32_16x16x128_f8f6f4 v[56:59], v[86:91], v[0:5], v[56:59] cbsz:2 blgp:2
	s_nop 7
	v_cndmask_b32_e64 v30, v56, v57, s[4:5]
	v_cndmask_b32_e64 v30, v30, v58, s[2:3]
	v_cndmask_b32_e32 v30, v30, v59, vcc
	v_mul_f32_e32 v31, v33, v30
	s_nop 1
	v_mov_b32_dpp v31, v31 quad_perm:[1,0,3,2] row_mask:0xf bank_mask:0xf bound_ctrl:1
	v_fmac_f32_e32 v31, v33, v30
	s_nop 1
	v_add_f32_dpp v30, v31, v31 quad_perm:[2,3,0,1] row_mask:0xf bank_mask:0xf bound_ctrl:1
	s_nop 1
	v_add_f32_dpp v30, v30, v30 row_half_mirror row_mask:0xf bank_mask:0xf bound_ctrl:1
	ds_write_b32 v32, v30 offset:49156
	v_add_u32_e32 v31, v225, v35
	v_add_u32_e32 v30, v225, v34
	buffer_load_dwordx4 v[56:59], v31, s[44:47], 0 offen
	buffer_load_dwordx4 v[62:65], v31, s[44:47], s20 offen
	buffer_load_dwordx4 v[68:71], v31, s[44:47], s21 offen
	buffer_load_dwordx4 v[74:77], v31, s[44:47], s23 offen
	buffer_load_dwordx2 v[60:61], v30, s[44:47], 0 offen
	buffer_load_dwordx2 v[72:73], v30, s[44:47], s33 offen
	buffer_load_dwordx2 v[66:67], v30, s[44:47], s21 offen
	buffer_load_dwordx2 v[78:79], v30, s[44:47], s94 offen
	s_waitcnt vmcnt(27)
	v_mfma_f32_16x16x128_f8f6f4 v[86:89], v[92:97], v[18:23], 0 cbsz:2 blgp:2
	s_waitcnt vmcnt(26)
	v_mfma_f32_16x16x128_f8f6f4 v[86:89], v[150:155], v[12:17], v[86:89] cbsz:2 blgp:2
	s_waitcnt vmcnt(25)
	v_mfma_f32_16x16x128_f8f6f4 v[86:89], v[98:103], v[6:11], v[86:89] cbsz:2 blgp:2
	s_waitcnt vmcnt(24)
	v_mfma_f32_16x16x128_f8f6f4 v[86:89], v[156:161], v[0:5], v[86:89] cbsz:2 blgp:2
	s_nop 7
	v_cndmask_b32_e64 v30, v86, v87, s[4:5]
	v_cndmask_b32_e64 v30, v30, v88, s[2:3]
	v_cndmask_b32_e32 v30, v30, v89, vcc
	v_mul_f32_e32 v31, v33, v30
	s_nop 1
	v_mov_b32_dpp v31, v31 quad_perm:[1,0,3,2] row_mask:0xf bank_mask:0xf bound_ctrl:1
	v_fmac_f32_e32 v31, v33, v30
	s_nop 1
	v_add_f32_dpp v30, v31, v31 quad_perm:[2,3,0,1] row_mask:0xf bank_mask:0xf bound_ctrl:1
	s_nop 1
	v_add_f32_dpp v30, v30, v30 row_half_mirror row_mask:0xf bank_mask:0xf bound_ctrl:1
	ds_write_b32 v32, v30 offset:49160
	v_add_u32_e32 v31, v226, v35
	v_add_u32_e32 v30, v226, v34
	buffer_load_dwordx4 v[86:89], v31, s[44:47], 0 offen
	buffer_load_dwordx4 v[92:95], v31, s[44:47], s20 offen
	buffer_load_dwordx4 v[98:101], v31, s[44:47], s21 offen
	buffer_load_dwordx4 v[150:153], v31, s[44:47], s23 offen
	buffer_load_dwordx2 v[90:91], v30, s[44:47], 0 offen
	buffer_load_dwordx2 v[102:103], v30, s[44:47], s33 offen
	buffer_load_dwordx2 v[96:97], v30, s[44:47], s21 offen
	buffer_load_dwordx2 v[154:155], v30, s[44:47], s94 offen
	s_waitcnt vmcnt(27)
	v_mfma_f32_16x16x128_f8f6f4 v[156:159], v[162:167], v[18:23], 0 cbsz:2 blgp:2
	s_waitcnt vmcnt(26)
	v_mfma_f32_16x16x128_f8f6f4 v[156:159], v[174:179], v[12:17], v[156:159] cbsz:2 blgp:2
	s_waitcnt vmcnt(25)
	v_mfma_f32_16x16x128_f8f6f4 v[156:159], v[168:173], v[6:11], v[156:159] cbsz:2 blgp:2
	s_waitcnt vmcnt(24)
	v_mfma_f32_16x16x128_f8f6f4 v[156:159], v[216:221], v[0:5], v[156:159] cbsz:2 blgp:2
	s_nop 7
	v_cndmask_b32_e64 v30, v156, v157, s[4:5]
	v_cndmask_b32_e64 v30, v30, v158, s[2:3]
	v_cndmask_b32_e32 v30, v30, v159, vcc
	v_mul_f32_e32 v31, v33, v30
	s_nop 1
	v_mov_b32_dpp v31, v31 quad_perm:[1,0,3,2] row_mask:0xf bank_mask:0xf bound_ctrl:1
	v_fmac_f32_e32 v31, v33, v30
	s_nop 1
	v_add_f32_dpp v30, v31, v31 quad_perm:[2,3,0,1] row_mask:0xf bank_mask:0xf bound_ctrl:1
	s_nop 1
	v_add_f32_dpp v30, v30, v30 row_half_mirror row_mask:0xf bank_mask:0xf bound_ctrl:1
	ds_write_b32 v32, v30 offset:49164
	v_add_u32_e32 v31, v227, v35
	v_add_u32_e32 v30, v227, v34
	buffer_load_dwordx4 v[156:159], v31, s[44:47], 0 offen
	buffer_load_dwordx4 v[162:165], v31, s[44:47], s20 offen
	buffer_load_dwordx4 v[168:171], v31, s[44:47], s21 offen
	buffer_load_dwordx4 v[174:177], v31, s[44:47], s23 offen
	buffer_load_dwordx2 v[160:161], v30, s[44:47], 0 offen
	buffer_load_dwordx2 v[172:173], v30, s[44:47], s33 offen
	buffer_load_dwordx2 v[166:167], v30, s[44:47], s21 offen
	buffer_load_dwordx2 v[178:179], v30, s[44:47], s94 offen
	s_waitcnt vmcnt(27)
	v_mfma_f32_16x16x128_f8f6f4 v[24:27], v[24:29], v[18:23], 0 cbsz:2 blgp:2
	s_waitcnt vmcnt(26)
	v_mfma_f32_16x16x128_f8f6f4 v[24:27], v[44:49], v[12:17], v[24:27] cbsz:2 blgp:2
	s_waitcnt vmcnt(25)
	v_mfma_f32_16x16x128_f8f6f4 v[24:27], v[38:43], v[6:11], v[24:27] cbsz:2 blgp:2
	s_waitcnt vmcnt(24)
	v_mfma_f32_16x16x128_f8f6f4 v[24:27], v[50:55], v[0:5], v[24:27] cbsz:2 blgp:2
	s_nop 7
	v_cndmask_b32_e64 v24, v24, v25, s[4:5]
	v_cndmask_b32_e64 v24, v24, v26, s[2:3]
	v_cndmask_b32_e32 v24, v24, v27, vcc
	v_mul_f32_e32 v25, v33, v24
	s_nop 1
	v_mov_b32_dpp v25, v25 quad_perm:[1,0,3,2] row_mask:0xf bank_mask:0xf bound_ctrl:1
	v_fmac_f32_e32 v25, v33, v24
	s_nop 1
	v_add_f32_dpp v24, v25, v25 quad_perm:[2,3,0,1] row_mask:0xf bank_mask:0xf bound_ctrl:1
	s_nop 1
	v_add_f32_dpp v24, v24, v24 row_half_mirror row_mask:0xf bank_mask:0xf bound_ctrl:1
	ds_write_b32 v32, v24 offset:49168
	v_add_u32_e32 v28, v228, v35
	v_add_u32_e32 v30, v228, v34
	buffer_load_dwordx4 v[24:27], v28, s[44:47], 0 offen
	buffer_load_dwordx4 v[38:41], v28, s[44:47], s20 offen
	buffer_load_dwordx4 v[44:47], v28, s[44:47], s21 offen
	buffer_load_dwordx4 v[50:53], v28, s[44:47], s23 offen
	s_nop 0
	buffer_load_dwordx2 v[28:29], v30, s[44:47], 0 offen
	buffer_load_dwordx2 v[48:49], v30, s[44:47], s33 offen
	buffer_load_dwordx2 v[42:43], v30, s[44:47], s21 offen
	buffer_load_dwordx2 v[54:55], v30, s[44:47], s94 offen
	s_waitcnt vmcnt(27)
	v_mfma_f32_16x16x128_f8f6f4 v[56:59], v[56:61], v[18:23], 0 cbsz:2 blgp:2
	s_waitcnt vmcnt(26)
	v_mfma_f32_16x16x128_f8f6f4 v[56:59], v[68:73], v[12:17], v[56:59] cbsz:2 blgp:2
	s_waitcnt vmcnt(25)
	v_mfma_f32_16x16x128_f8f6f4 v[56:59], v[62:67], v[6:11], v[56:59] cbsz:2 blgp:2
	s_waitcnt vmcnt(24)
	v_mfma_f32_16x16x128_f8f6f4 v[56:59], v[74:79], v[0:5], v[56:59] cbsz:2 blgp:2
	s_nop 7
	v_cndmask_b32_e64 v30, v56, v57, s[4:5]
	v_cndmask_b32_e64 v30, v30, v58, s[2:3]
	v_cndmask_b32_e32 v30, v30, v59, vcc
	v_mul_f32_e32 v31, v33, v30
	s_nop 1
	v_mov_b32_dpp v31, v31 quad_perm:[1,0,3,2] row_mask:0xf bank_mask:0xf bound_ctrl:1
	v_fmac_f32_e32 v31, v33, v30
	s_nop 1
	v_add_f32_dpp v30, v31, v31 quad_perm:[2,3,0,1] row_mask:0xf bank_mask:0xf bound_ctrl:1
	s_nop 1
	v_add_f32_dpp v30, v30, v30 row_half_mirror row_mask:0xf bank_mask:0xf bound_ctrl:1
	ds_write_b32 v32, v30 offset:49172
	v_add_u32_e32 v31, v229, v35
	v_add_u32_e32 v30, v229, v34
	buffer_load_dwordx4 v[56:59], v31, s[44:47], 0 offen
	buffer_load_dwordx4 v[62:65], v31, s[44:47], s20 offen
	buffer_load_dwordx4 v[68:71], v31, s[44:47], s21 offen
	buffer_load_dwordx4 v[74:77], v31, s[44:47], s23 offen
	buffer_load_dwordx2 v[60:61], v30, s[44:47], 0 offen
	buffer_load_dwordx2 v[72:73], v30, s[44:47], s33 offen
	buffer_load_dwordx2 v[66:67], v30, s[44:47], s21 offen
	buffer_load_dwordx2 v[78:79], v30, s[44:47], s94 offen
	s_waitcnt vmcnt(27)
	v_mfma_f32_16x16x128_f8f6f4 v[86:89], v[86:91], v[18:23], 0 cbsz:2 blgp:2
	s_waitcnt vmcnt(26)
	v_mfma_f32_16x16x128_f8f6f4 v[86:89], v[98:103], v[12:17], v[86:89] cbsz:2 blgp:2
	s_waitcnt vmcnt(25)
	v_mfma_f32_16x16x128_f8f6f4 v[86:89], v[92:97], v[6:11], v[86:89] cbsz:2 blgp:2
	s_waitcnt vmcnt(24)
	v_mfma_f32_16x16x128_f8f6f4 v[86:89], v[150:155], v[0:5], v[86:89] cbsz:2 blgp:2
	s_nop 7
	v_cndmask_b32_e64 v30, v86, v87, s[4:5]
	v_cndmask_b32_e64 v30, v30, v88, s[2:3]
	v_cndmask_b32_e32 v30, v30, v89, vcc
	v_mul_f32_e32 v31, v33, v30
	s_nop 1
	v_mov_b32_dpp v31, v31 quad_perm:[1,0,3,2] row_mask:0xf bank_mask:0xf bound_ctrl:1
	v_fmac_f32_e32 v31, v33, v30
	s_nop 1
	v_add_f32_dpp v30, v31, v31 quad_perm:[2,3,0,1] row_mask:0xf bank_mask:0xf bound_ctrl:1
	s_nop 1
	v_add_f32_dpp v30, v30, v30 row_half_mirror row_mask:0xf bank_mask:0xf bound_ctrl:1
	ds_write_b32 v32, v30 offset:49176
	v_add_u32_e32 v31, v230, v35
	v_add_u32_e32 v30, v230, v34
	buffer_load_dwordx4 v[86:89], v31, s[44:47], 0 offen
	buffer_load_dwordx4 v[92:95], v31, s[44:47], s20 offen
	buffer_load_dwordx4 v[98:101], v31, s[44:47], s21 offen
	buffer_load_dwordx4 v[150:153], v31, s[44:47], s23 offen
	buffer_load_dwordx2 v[90:91], v30, s[44:47], 0 offen
	buffer_load_dwordx2 v[102:103], v30, s[44:47], s33 offen
	buffer_load_dwordx2 v[96:97], v30, s[44:47], s21 offen
	buffer_load_dwordx2 v[154:155], v30, s[44:47], s94 offen
	s_waitcnt vmcnt(27)
	v_mfma_f32_16x16x128_f8f6f4 v[156:159], v[156:161], v[18:23], 0 cbsz:2 blgp:2
	s_waitcnt vmcnt(26)
	v_mfma_f32_16x16x128_f8f6f4 v[156:159], v[168:173], v[12:17], v[156:159] cbsz:2 blgp:2
	s_waitcnt vmcnt(25)
	v_mfma_f32_16x16x128_f8f6f4 v[156:159], v[162:167], v[6:11], v[156:159] cbsz:2 blgp:2
	s_waitcnt vmcnt(24)
	v_mfma_f32_16x16x128_f8f6f4 v[156:159], v[174:179], v[0:5], v[156:159] cbsz:2 blgp:2
	s_nop 7
	v_cndmask_b32_e64 v30, v156, v157, s[4:5]
	v_cndmask_b32_e64 v30, v30, v158, s[2:3]
	v_cndmask_b32_e32 v30, v30, v159, vcc
	v_mul_f32_e32 v31, v33, v30
	s_nop 1
	v_mov_b32_dpp v31, v31 quad_perm:[1,0,3,2] row_mask:0xf bank_mask:0xf bound_ctrl:1
	v_fmac_f32_e32 v31, v33, v30
	s_nop 1
	v_add_f32_dpp v30, v31, v31 quad_perm:[2,3,0,1] row_mask:0xf bank_mask:0xf bound_ctrl:1
	s_nop 1
	v_add_f32_dpp v30, v30, v30 row_half_mirror row_mask:0xf bank_mask:0xf bound_ctrl:1
	ds_write_b32 v32, v30 offset:49180
	v_add_u32_e32 v31, v231, v35
	v_add_u32_e32 v30, v231, v34
	buffer_load_dwordx4 v[156:159], v31, s[44:47], 0 offen
	buffer_load_dwordx4 v[162:165], v31, s[44:47], s20 offen
	buffer_load_dwordx4 v[168:171], v31, s[44:47], s21 offen
	buffer_load_dwordx4 v[174:177], v31, s[44:47], s23 offen
	buffer_load_dwordx2 v[160:161], v30, s[44:47], 0 offen
	buffer_load_dwordx2 v[172:173], v30, s[44:47], s33 offen
	buffer_load_dwordx2 v[166:167], v30, s[44:47], s21 offen
	buffer_load_dwordx2 v[178:179], v30, s[44:47], s94 offen
	s_waitcnt vmcnt(27)
	v_mfma_f32_16x16x128_f8f6f4 v[24:27], v[24:29], v[18:23], 0 cbsz:2 blgp:2
	s_waitcnt vmcnt(26)
	v_mfma_f32_16x16x128_f8f6f4 v[24:27], v[44:49], v[12:17], v[24:27] cbsz:2 blgp:2
	s_waitcnt vmcnt(25)
	v_mfma_f32_16x16x128_f8f6f4 v[24:27], v[38:43], v[6:11], v[24:27] cbsz:2 blgp:2
	s_waitcnt vmcnt(24)
	v_mfma_f32_16x16x128_f8f6f4 v[24:27], v[50:55], v[0:5], v[24:27] cbsz:2 blgp:2
	s_nop 7
	v_cndmask_b32_e64 v24, v24, v25, s[4:5]
	v_cndmask_b32_e64 v24, v24, v26, s[2:3]
	v_cndmask_b32_e32 v24, v24, v27, vcc
	v_mul_f32_e32 v25, v33, v24
	s_nop 1
	v_mov_b32_dpp v25, v25 quad_perm:[1,0,3,2] row_mask:0xf bank_mask:0xf bound_ctrl:1
	v_fmac_f32_e32 v25, v33, v24
	s_nop 1
	v_add_f32_dpp v24, v25, v25 quad_perm:[2,3,0,1] row_mask:0xf bank_mask:0xf bound_ctrl:1
	s_nop 1
	v_add_f32_dpp v24, v24, v24 row_half_mirror row_mask:0xf bank_mask:0xf bound_ctrl:1
	ds_write_b32 v32, v24 offset:49184
	v_add_u32_e32 v28, v232, v35
	v_add_u32_e32 v30, v232, v34
	buffer_load_dwordx4 v[24:27], v28, s[44:47], 0 offen
	buffer_load_dwordx4 v[38:41], v28, s[44:47], s20 offen
	buffer_load_dwordx4 v[44:47], v28, s[44:47], s21 offen
	buffer_load_dwordx4 v[50:53], v28, s[44:47], s23 offen
	s_nop 0
	buffer_load_dwordx2 v[28:29], v30, s[44:47], 0 offen
	buffer_load_dwordx2 v[48:49], v30, s[44:47], s33 offen
	buffer_load_dwordx2 v[42:43], v30, s[44:47], s21 offen
	buffer_load_dwordx2 v[54:55], v30, s[44:47], s94 offen
	s_waitcnt vmcnt(27)
	v_mfma_f32_16x16x128_f8f6f4 v[56:59], v[56:61], v[18:23], 0 cbsz:2 blgp:2
	s_waitcnt vmcnt(26)
	v_mfma_f32_16x16x128_f8f6f4 v[56:59], v[68:73], v[12:17], v[56:59] cbsz:2 blgp:2
	s_waitcnt vmcnt(25)
	v_mfma_f32_16x16x128_f8f6f4 v[56:59], v[62:67], v[6:11], v[56:59] cbsz:2 blgp:2
	s_waitcnt vmcnt(24)
	v_mfma_f32_16x16x128_f8f6f4 v[56:59], v[74:79], v[0:5], v[56:59] cbsz:2 blgp:2
	s_nop 7
	v_cndmask_b32_e64 v30, v56, v57, s[4:5]
	v_cndmask_b32_e64 v30, v30, v58, s[2:3]
	v_cndmask_b32_e32 v30, v30, v59, vcc
	v_mul_f32_e32 v31, v33, v30
	s_nop 1
	v_mov_b32_dpp v31, v31 quad_perm:[1,0,3,2] row_mask:0xf bank_mask:0xf bound_ctrl:1
	v_fmac_f32_e32 v31, v33, v30
	s_nop 1
	v_add_f32_dpp v30, v31, v31 quad_perm:[2,3,0,1] row_mask:0xf bank_mask:0xf bound_ctrl:1
	s_nop 1
	v_add_f32_dpp v30, v30, v30 row_half_mirror row_mask:0xf bank_mask:0xf bound_ctrl:1
	ds_write_b32 v32, v30 offset:49188
	v_add_u32_e32 v31, v233, v35
	v_add_u32_e32 v30, v233, v34
	buffer_load_dwordx4 v[56:59], v31, s[44:47], 0 offen
	buffer_load_dwordx4 v[62:65], v31, s[44:47], s20 offen
	buffer_load_dwordx4 v[68:71], v31, s[44:47], s21 offen
	buffer_load_dwordx4 v[74:77], v31, s[44:47], s23 offen
	buffer_load_dwordx2 v[60:61], v30, s[44:47], 0 offen
	buffer_load_dwordx2 v[72:73], v30, s[44:47], s33 offen
	buffer_load_dwordx2 v[66:67], v30, s[44:47], s21 offen
	buffer_load_dwordx2 v[78:79], v30, s[44:47], s94 offen
	s_waitcnt vmcnt(27)
	v_mfma_f32_16x16x128_f8f6f4 v[86:89], v[86:91], v[18:23], 0 cbsz:2 blgp:2
	s_waitcnt vmcnt(26)
	v_mfma_f32_16x16x128_f8f6f4 v[86:89], v[98:103], v[12:17], v[86:89] cbsz:2 blgp:2
	s_waitcnt vmcnt(25)
	v_mfma_f32_16x16x128_f8f6f4 v[86:89], v[92:97], v[6:11], v[86:89] cbsz:2 blgp:2
	s_waitcnt vmcnt(24)
	v_mfma_f32_16x16x128_f8f6f4 v[86:89], v[150:155], v[0:5], v[86:89] cbsz:2 blgp:2
	s_nop 7
	v_cndmask_b32_e64 v30, v86, v87, s[4:5]
	v_cndmask_b32_e64 v30, v30, v88, s[2:3]
	v_cndmask_b32_e32 v30, v30, v89, vcc
	v_mul_f32_e32 v31, v33, v30
	s_nop 1
	v_mov_b32_dpp v31, v31 quad_perm:[1,0,3,2] row_mask:0xf bank_mask:0xf bound_ctrl:1
	v_fmac_f32_e32 v31, v33, v30
	s_nop 1
	v_add_f32_dpp v30, v31, v31 quad_perm:[2,3,0,1] row_mask:0xf bank_mask:0xf bound_ctrl:1
	s_nop 1
	v_add_f32_dpp v30, v30, v30 row_half_mirror row_mask:0xf bank_mask:0xf bound_ctrl:1
	ds_write_b32 v32, v30 offset:49192
	v_add_u32_e32 v31, v234, v35
	v_add_u32_e32 v30, v234, v34
	buffer_load_dwordx4 v[86:89], v31, s[44:47], 0 offen
	buffer_load_dwordx4 v[92:95], v31, s[44:47], s20 offen
	buffer_load_dwordx4 v[98:101], v31, s[44:47], s21 offen
	buffer_load_dwordx4 v[150:153], v31, s[44:47], s23 offen
	buffer_load_dwordx2 v[90:91], v30, s[44:47], 0 offen
	buffer_load_dwordx2 v[102:103], v30, s[44:47], s33 offen
	buffer_load_dwordx2 v[96:97], v30, s[44:47], s21 offen
	buffer_load_dwordx2 v[154:155], v30, s[44:47], s94 offen
	s_waitcnt vmcnt(27)
	v_mfma_f32_16x16x128_f8f6f4 v[156:159], v[156:161], v[18:23], 0 cbsz:2 blgp:2
	s_waitcnt vmcnt(26)
	v_mfma_f32_16x16x128_f8f6f4 v[156:159], v[168:173], v[12:17], v[156:159] cbsz:2 blgp:2
	s_waitcnt vmcnt(25)
	v_mfma_f32_16x16x128_f8f6f4 v[156:159], v[162:167], v[6:11], v[156:159] cbsz:2 blgp:2
	s_waitcnt vmcnt(24)
	v_mfma_f32_16x16x128_f8f6f4 v[156:159], v[174:179], v[0:5], v[156:159] cbsz:2 blgp:2
	s_nop 7
	v_cndmask_b32_e64 v30, v156, v157, s[4:5]
	v_cndmask_b32_e64 v30, v30, v158, s[2:3]
	v_cndmask_b32_e32 v30, v30, v159, vcc
	v_mul_f32_e32 v31, v33, v30
	s_nop 1
	v_mov_b32_dpp v31, v31 quad_perm:[1,0,3,2] row_mask:0xf bank_mask:0xf bound_ctrl:1
	v_fmac_f32_e32 v31, v33, v30
	s_nop 1
	v_add_f32_dpp v30, v31, v31 quad_perm:[2,3,0,1] row_mask:0xf bank_mask:0xf bound_ctrl:1
	s_nop 1
	v_add_f32_dpp v30, v30, v30 row_half_mirror row_mask:0xf bank_mask:0xf bound_ctrl:1
	ds_write_b32 v32, v30 offset:49196
	v_add_u32_e32 v31, v235, v35
	v_add_u32_e32 v30, v235, v34
	buffer_load_dwordx4 v[156:159], v31, s[44:47], 0 offen
	buffer_load_dwordx4 v[162:165], v31, s[44:47], s20 offen
	buffer_load_dwordx4 v[168:171], v31, s[44:47], s21 offen
	buffer_load_dwordx4 v[174:177], v31, s[44:47], s23 offen
	buffer_load_dwordx2 v[160:161], v30, s[44:47], 0 offen
	buffer_load_dwordx2 v[172:173], v30, s[44:47], s33 offen
	buffer_load_dwordx2 v[166:167], v30, s[44:47], s21 offen
	buffer_load_dwordx2 v[178:179], v30, s[44:47], s94 offen
	s_waitcnt vmcnt(27)
	v_mfma_f32_16x16x128_f8f6f4 v[24:27], v[24:29], v[18:23], 0 cbsz:2 blgp:2
	s_waitcnt vmcnt(26)
	v_mfma_f32_16x16x128_f8f6f4 v[24:27], v[44:49], v[12:17], v[24:27] cbsz:2 blgp:2
	s_waitcnt vmcnt(25)
	v_mfma_f32_16x16x128_f8f6f4 v[24:27], v[38:43], v[6:11], v[24:27] cbsz:2 blgp:2
	s_waitcnt vmcnt(24)
	v_mfma_f32_16x16x128_f8f6f4 v[24:27], v[50:55], v[0:5], v[24:27] cbsz:2 blgp:2
	s_nop 7
	v_cndmask_b32_e64 v24, v24, v25, s[4:5]
	v_cndmask_b32_e64 v24, v24, v26, s[2:3]
	v_cndmask_b32_e32 v24, v24, v27, vcc
	v_mul_f32_e32 v25, v33, v24
	s_nop 1
	v_mov_b32_dpp v25, v25 quad_perm:[1,0,3,2] row_mask:0xf bank_mask:0xf bound_ctrl:1
	v_fmac_f32_e32 v25, v33, v24
	s_nop 1
	v_add_f32_dpp v24, v25, v25 quad_perm:[2,3,0,1] row_mask:0xf bank_mask:0xf bound_ctrl:1
	s_nop 1
	v_add_f32_dpp v24, v24, v24 row_half_mirror row_mask:0xf bank_mask:0xf bound_ctrl:1
	ds_write_b32 v32, v24 offset:49200
	v_mul_u32_u24_e32 v251, 0x600, v128
	ds_bpermute_b32 v236, v36, v251 offset:16
	ds_bpermute_b32 v237, v36, v251 offset:32
	ds_bpermute_b32 v238, v36, v251 offset:48
	ds_bpermute_b32 v239, v36, v251 offset:64
	ds_bpermute_b32 v240, v36, v251 offset:80
	ds_bpermute_b32 v241, v36, v251 offset:96
	ds_bpermute_b32 v242, v36, v251 offset:112
	ds_bpermute_b32 v243, v36, v251 offset:128
	ds_bpermute_b32 v244, v36, v251 offset:144
	ds_bpermute_b32 v245, v36, v251 offset:160
	ds_bpermute_b32 v246, v36, v251 offset:176
	ds_bpermute_b32 v247, v36, v251 offset:192
	ds_bpermute_b32 v248, v36, v251 offset:208
	ds_bpermute_b32 v249, v36, v251 offset:224
	ds_bpermute_b32 v24, v36, v251
	s_waitcnt lgkmcnt(0)
	v_add_u32_e32 v28, v24, v35
	v_add_u32_e32 v30, v24, v34
	buffer_load_dwordx4 v[24:27], v28, s[44:47], 0 offen
	buffer_load_dwordx4 v[38:41], v28, s[44:47], s20 offen
	buffer_load_dwordx4 v[44:47], v28, s[44:47], s21 offen
	buffer_load_dwordx4 v[50:53], v28, s[44:47], s23 offen
	s_nop 0
	buffer_load_dwordx2 v[28:29], v30, s[44:47], 0 offen
	buffer_load_dwordx2 v[48:49], v30, s[44:47], s33 offen
	buffer_load_dwordx2 v[42:43], v30, s[44:47], s21 offen
	buffer_load_dwordx2 v[54:55], v30, s[44:47], s94 offen
	s_waitcnt vmcnt(27)
	v_mfma_f32_16x16x128_f8f6f4 v[56:59], v[56:61], v[18:23], 0 cbsz:2 blgp:2
	s_waitcnt vmcnt(26)
	v_mfma_f32_16x16x128_f8f6f4 v[56:59], v[68:73], v[12:17], v[56:59] cbsz:2 blgp:2
	s_waitcnt vmcnt(25)
	v_mfma_f32_16x16x128_f8f6f4 v[56:59], v[62:67], v[6:11], v[56:59] cbsz:2 blgp:2
	s_waitcnt vmcnt(24)
	v_mfma_f32_16x16x128_f8f6f4 v[56:59], v[74:79], v[0:5], v[56:59] cbsz:2 blgp:2
	s_nop 7
	v_cndmask_b32_e64 v30, v56, v57, s[4:5]
	v_cndmask_b32_e64 v30, v30, v58, s[2:3]
	v_cndmask_b32_e32 v30, v30, v59, vcc
	v_mul_f32_e32 v31, v33, v30
	s_nop 1
	v_mov_b32_dpp v31, v31 quad_perm:[1,0,3,2] row_mask:0xf bank_mask:0xf bound_ctrl:1
	v_fmac_f32_e32 v31, v33, v30
	s_nop 1
	v_add_f32_dpp v30, v31, v31 quad_perm:[2,3,0,1] row_mask:0xf bank_mask:0xf bound_ctrl:1
	s_nop 1
	v_add_f32_dpp v30, v30, v30 row_half_mirror row_mask:0xf bank_mask:0xf bound_ctrl:1
	ds_write_b32 v32, v30 offset:49204
	v_add_u32_e32 v31, v236, v35
	v_add_u32_e32 v30, v236, v34
	buffer_load_dwordx4 v[56:59], v31, s[44:47], 0 offen
	buffer_load_dwordx4 v[62:65], v31, s[44:47], s20 offen
	buffer_load_dwordx4 v[68:71], v31, s[44:47], s21 offen
	buffer_load_dwordx4 v[74:77], v31, s[44:47], s23 offen
	buffer_load_dwordx2 v[60:61], v30, s[44:47], 0 offen
	buffer_load_dwordx2 v[72:73], v30, s[44:47], s33 offen
	buffer_load_dwordx2 v[66:67], v30, s[44:47], s21 offen
	buffer_load_dwordx2 v[78:79], v30, s[44:47], s94 offen
	s_waitcnt vmcnt(27)
	v_mfma_f32_16x16x128_f8f6f4 v[86:89], v[86:91], v[18:23], 0 cbsz:2 blgp:2
	s_waitcnt vmcnt(26)
	v_mfma_f32_16x16x128_f8f6f4 v[86:89], v[98:103], v[12:17], v[86:89] cbsz:2 blgp:2
	s_waitcnt vmcnt(25)
	v_mfma_f32_16x16x128_f8f6f4 v[86:89], v[92:97], v[6:11], v[86:89] cbsz:2 blgp:2
	s_waitcnt vmcnt(24)
	v_mfma_f32_16x16x128_f8f6f4 v[86:89], v[150:155], v[0:5], v[86:89] cbsz:2 blgp:2
	s_nop 7
	v_cndmask_b32_e64 v30, v86, v87, s[4:5]
	v_cndmask_b32_e64 v30, v30, v88, s[2:3]
	v_cndmask_b32_e32 v30, v30, v89, vcc
	v_mul_f32_e32 v31, v33, v30
	s_nop 1
	v_mov_b32_dpp v31, v31 quad_perm:[1,0,3,2] row_mask:0xf bank_mask:0xf bound_ctrl:1
	v_fmac_f32_e32 v31, v33, v30
	s_nop 1
	v_add_f32_dpp v30, v31, v31 quad_perm:[2,3,0,1] row_mask:0xf bank_mask:0xf bound_ctrl:1
	s_nop 1
	v_add_f32_dpp v30, v30, v30 row_half_mirror row_mask:0xf bank_mask:0xf bound_ctrl:1
	ds_write_b32 v32, v30 offset:49208
	v_add_u32_e32 v31, v237, v35
	v_add_u32_e32 v30, v237, v34
	buffer_load_dwordx4 v[86:89], v31, s[44:47], 0 offen
	buffer_load_dwordx4 v[92:95], v31, s[44:47], s20 offen
	buffer_load_dwordx4 v[98:101], v31, s[44:47], s21 offen
	buffer_load_dwordx4 v[150:153], v31, s[44:47], s23 offen
	buffer_load_dwordx2 v[90:91], v30, s[44:47], 0 offen
	buffer_load_dwordx2 v[102:103], v30, s[44:47], s33 offen
	buffer_load_dwordx2 v[96:97], v30, s[44:47], s21 offen
	buffer_load_dwordx2 v[154:155], v30, s[44:47], s94 offen
	s_waitcnt vmcnt(27)
	v_mfma_f32_16x16x128_f8f6f4 v[156:159], v[156:161], v[18:23], 0 cbsz:2 blgp:2
	s_waitcnt vmcnt(26)
	v_mfma_f32_16x16x128_f8f6f4 v[156:159], v[168:173], v[12:17], v[156:159] cbsz:2 blgp:2
	s_waitcnt vmcnt(25)
	v_mfma_f32_16x16x128_f8f6f4 v[156:159], v[162:167], v[6:11], v[156:159] cbsz:2 blgp:2
	s_waitcnt vmcnt(24)
	v_mfma_f32_16x16x128_f8f6f4 v[156:159], v[174:179], v[0:5], v[156:159] cbsz:2 blgp:2
	s_nop 7
	v_cndmask_b32_e64 v30, v156, v157, s[4:5]
	v_cndmask_b32_e64 v30, v30, v158, s[2:3]
	v_cndmask_b32_e32 v30, v30, v159, vcc
	v_mul_f32_e32 v31, v33, v30
	s_nop 1
	v_mov_b32_dpp v31, v31 quad_perm:[1,0,3,2] row_mask:0xf bank_mask:0xf bound_ctrl:1
	v_fmac_f32_e32 v31, v33, v30
	s_nop 1
	v_add_f32_dpp v30, v31, v31 quad_perm:[2,3,0,1] row_mask:0xf bank_mask:0xf bound_ctrl:1
	s_nop 1
	v_add_f32_dpp v30, v30, v30 row_half_mirror row_mask:0xf bank_mask:0xf bound_ctrl:1
	ds_write_b32 v32, v30 offset:49212
	v_add_u32_e32 v31, v238, v35
	v_add_u32_e32 v30, v238, v34
	buffer_load_dwordx4 v[156:159], v31, s[44:47], 0 offen
	buffer_load_dwordx4 v[162:165], v31, s[44:47], s20 offen
	buffer_load_dwordx4 v[168:171], v31, s[44:47], s21 offen
	buffer_load_dwordx4 v[174:177], v31, s[44:47], s23 offen
	buffer_load_dwordx2 v[160:161], v30, s[44:47], 0 offen
	buffer_load_dwordx2 v[172:173], v30, s[44:47], s33 offen
	buffer_load_dwordx2 v[166:167], v30, s[44:47], s21 offen
	buffer_load_dwordx2 v[178:179], v30, s[44:47], s94 offen
	s_waitcnt vmcnt(27)
	v_mfma_f32_16x16x128_f8f6f4 v[24:27], v[24:29], v[18:23], 0 cbsz:2 blgp:2
	s_waitcnt vmcnt(26)
	v_mfma_f32_16x16x128_f8f6f4 v[24:27], v[44:49], v[12:17], v[24:27] cbsz:2 blgp:2
	s_waitcnt vmcnt(25)
	v_mfma_f32_16x16x128_f8f6f4 v[24:27], v[38:43], v[6:11], v[24:27] cbsz:2 blgp:2
	s_waitcnt vmcnt(24)
	v_mfma_f32_16x16x128_f8f6f4 v[24:27], v[50:55], v[0:5], v[24:27] cbsz:2 blgp:2
	s_nop 7
	v_cndmask_b32_e64 v24, v24, v25, s[4:5]
	v_cndmask_b32_e64 v24, v24, v26, s[2:3]
	v_cndmask_b32_e32 v24, v24, v27, vcc
	v_mul_f32_e32 v25, v33, v24
	s_nop 1
	v_mov_b32_dpp v25, v25 quad_perm:[1,0,3,2] row_mask:0xf bank_mask:0xf bound_ctrl:1
	v_fmac_f32_e32 v25, v33, v24
	s_nop 1
	v_add_f32_dpp v24, v25, v25 quad_perm:[2,3,0,1] row_mask:0xf bank_mask:0xf bound_ctrl:1
	s_nop 1
	v_add_f32_dpp v24, v24, v24 row_half_mirror row_mask:0xf bank_mask:0xf bound_ctrl:1
	ds_write_b32 v32, v24 offset:49216
	v_add_u32_e32 v28, v239, v35
	v_add_u32_e32 v30, v239, v34
	buffer_load_dwordx4 v[24:27], v28, s[44:47], 0 offen
	buffer_load_dwordx4 v[38:41], v28, s[44:47], s20 offen
	buffer_load_dwordx4 v[44:47], v28, s[44:47], s21 offen
	buffer_load_dwordx4 v[50:53], v28, s[44:47], s23 offen
	s_nop 0
	buffer_load_dwordx2 v[28:29], v30, s[44:47], 0 offen
	buffer_load_dwordx2 v[48:49], v30, s[44:47], s33 offen
	buffer_load_dwordx2 v[42:43], v30, s[44:47], s21 offen
	buffer_load_dwordx2 v[54:55], v30, s[44:47], s94 offen
	s_waitcnt vmcnt(27)
	v_mfma_f32_16x16x128_f8f6f4 v[56:59], v[56:61], v[18:23], 0 cbsz:2 blgp:2
	s_waitcnt vmcnt(26)
	v_mfma_f32_16x16x128_f8f6f4 v[56:59], v[68:73], v[12:17], v[56:59] cbsz:2 blgp:2
	s_waitcnt vmcnt(25)
	v_mfma_f32_16x16x128_f8f6f4 v[56:59], v[62:67], v[6:11], v[56:59] cbsz:2 blgp:2
	s_waitcnt vmcnt(24)
	v_mfma_f32_16x16x128_f8f6f4 v[56:59], v[74:79], v[0:5], v[56:59] cbsz:2 blgp:2
	s_nop 7
	v_cndmask_b32_e64 v30, v56, v57, s[4:5]
	v_cndmask_b32_e64 v30, v30, v58, s[2:3]
	v_cndmask_b32_e32 v30, v30, v59, vcc
	v_mul_f32_e32 v31, v33, v30
	s_nop 1
	v_mov_b32_dpp v31, v31 quad_perm:[1,0,3,2] row_mask:0xf bank_mask:0xf bound_ctrl:1
	v_fmac_f32_e32 v31, v33, v30
	s_nop 1
	v_add_f32_dpp v30, v31, v31 quad_perm:[2,3,0,1] row_mask:0xf bank_mask:0xf bound_ctrl:1
	s_nop 1
	v_add_f32_dpp v30, v30, v30 row_half_mirror row_mask:0xf bank_mask:0xf bound_ctrl:1
	ds_write_b32 v32, v30 offset:49220
	v_add_u32_e32 v31, v240, v35
	v_add_u32_e32 v30, v240, v34
	buffer_load_dwordx4 v[56:59], v31, s[44:47], 0 offen
	buffer_load_dwordx4 v[62:65], v31, s[44:47], s20 offen
	buffer_load_dwordx4 v[68:71], v31, s[44:47], s21 offen
	buffer_load_dwordx4 v[74:77], v31, s[44:47], s23 offen
	buffer_load_dwordx2 v[60:61], v30, s[44:47], 0 offen
	buffer_load_dwordx2 v[72:73], v30, s[44:47], s33 offen
	buffer_load_dwordx2 v[66:67], v30, s[44:47], s21 offen
	buffer_load_dwordx2 v[78:79], v30, s[44:47], s94 offen
	s_waitcnt vmcnt(27)
	v_mfma_f32_16x16x128_f8f6f4 v[86:89], v[86:91], v[18:23], 0 cbsz:2 blgp:2
	s_waitcnt vmcnt(26)
	v_mfma_f32_16x16x128_f8f6f4 v[86:89], v[98:103], v[12:17], v[86:89] cbsz:2 blgp:2
	s_waitcnt vmcnt(25)
	v_mfma_f32_16x16x128_f8f6f4 v[86:89], v[92:97], v[6:11], v[86:89] cbsz:2 blgp:2
	s_waitcnt vmcnt(24)
	v_mfma_f32_16x16x128_f8f6f4 v[86:89], v[150:155], v[0:5], v[86:89] cbsz:2 blgp:2
	s_nop 7
	v_cndmask_b32_e64 v30, v86, v87, s[4:5]
	v_cndmask_b32_e64 v30, v30, v88, s[2:3]
	v_cndmask_b32_e32 v30, v30, v89, vcc
	v_mul_f32_e32 v31, v33, v30
	s_nop 1
	v_mov_b32_dpp v31, v31 quad_perm:[1,0,3,2] row_mask:0xf bank_mask:0xf bound_ctrl:1
	v_fmac_f32_e32 v31, v33, v30
	s_nop 1
	v_add_f32_dpp v30, v31, v31 quad_perm:[2,3,0,1] row_mask:0xf bank_mask:0xf bound_ctrl:1
	s_nop 1
	v_add_f32_dpp v30, v30, v30 row_half_mirror row_mask:0xf bank_mask:0xf bound_ctrl:1
	ds_write_b32 v32, v30 offset:49224
	v_add_u32_e32 v31, v241, v35
	v_add_u32_e32 v30, v241, v34
	buffer_load_dwordx4 v[86:89], v31, s[44:47], 0 offen
	buffer_load_dwordx4 v[92:95], v31, s[44:47], s20 offen
	buffer_load_dwordx4 v[98:101], v31, s[44:47], s21 offen
	buffer_load_dwordx4 v[150:153], v31, s[44:47], s23 offen
	buffer_load_dwordx2 v[90:91], v30, s[44:47], 0 offen
	buffer_load_dwordx2 v[102:103], v30, s[44:47], s33 offen
	buffer_load_dwordx2 v[96:97], v30, s[44:47], s21 offen
	buffer_load_dwordx2 v[154:155], v30, s[44:47], s94 offen
	s_waitcnt vmcnt(27)
	v_mfma_f32_16x16x128_f8f6f4 v[156:159], v[156:161], v[18:23], 0 cbsz:2 blgp:2
	s_waitcnt vmcnt(26)
	v_mfma_f32_16x16x128_f8f6f4 v[156:159], v[168:173], v[12:17], v[156:159] cbsz:2 blgp:2
	s_waitcnt vmcnt(25)
	v_mfma_f32_16x16x128_f8f6f4 v[156:159], v[162:167], v[6:11], v[156:159] cbsz:2 blgp:2
	s_waitcnt vmcnt(24)
	v_mfma_f32_16x16x128_f8f6f4 v[156:159], v[174:179], v[0:5], v[156:159] cbsz:2 blgp:2
	s_nop 7
	v_cndmask_b32_e64 v30, v156, v157, s[4:5]
	v_cndmask_b32_e64 v30, v30, v158, s[2:3]
	v_cndmask_b32_e32 v30, v30, v159, vcc
	v_mul_f32_e32 v31, v33, v30
	s_nop 1
	v_mov_b32_dpp v31, v31 quad_perm:[1,0,3,2] row_mask:0xf bank_mask:0xf bound_ctrl:1
	v_fmac_f32_e32 v31, v33, v30
	s_nop 1
	v_add_f32_dpp v30, v31, v31 quad_perm:[2,3,0,1] row_mask:0xf bank_mask:0xf bound_ctrl:1
	s_nop 1
	v_add_f32_dpp v30, v30, v30 row_half_mirror row_mask:0xf bank_mask:0xf bound_ctrl:1
	ds_write_b32 v32, v30 offset:49228
	v_add_u32_e32 v31, v242, v35
	v_add_u32_e32 v30, v242, v34
	buffer_load_dwordx4 v[156:159], v31, s[44:47], 0 offen
	buffer_load_dwordx4 v[162:165], v31, s[44:47], s20 offen
	buffer_load_dwordx4 v[168:171], v31, s[44:47], s21 offen
	buffer_load_dwordx4 v[174:177], v31, s[44:47], s23 offen
	buffer_load_dwordx2 v[160:161], v30, s[44:47], 0 offen
	buffer_load_dwordx2 v[172:173], v30, s[44:47], s33 offen
	buffer_load_dwordx2 v[166:167], v30, s[44:47], s21 offen
	buffer_load_dwordx2 v[178:179], v30, s[44:47], s94 offen
	s_waitcnt vmcnt(27)
	v_mfma_f32_16x16x128_f8f6f4 v[24:27], v[24:29], v[18:23], 0 cbsz:2 blgp:2
	s_waitcnt vmcnt(26)
	v_mfma_f32_16x16x128_f8f6f4 v[24:27], v[44:49], v[12:17], v[24:27] cbsz:2 blgp:2
	s_waitcnt vmcnt(25)
	v_mfma_f32_16x16x128_f8f6f4 v[24:27], v[38:43], v[6:11], v[24:27] cbsz:2 blgp:2
	s_waitcnt vmcnt(24)
	v_mfma_f32_16x16x128_f8f6f4 v[24:27], v[50:55], v[0:5], v[24:27] cbsz:2 blgp:2
	s_nop 7
	v_cndmask_b32_e64 v24, v24, v25, s[4:5]
	v_cndmask_b32_e64 v24, v24, v26, s[2:3]
	v_cndmask_b32_e32 v24, v24, v27, vcc
	v_mul_f32_e32 v25, v33, v24
	s_nop 1
	v_mov_b32_dpp v25, v25 quad_perm:[1,0,3,2] row_mask:0xf bank_mask:0xf bound_ctrl:1
	v_fmac_f32_e32 v25, v33, v24
	s_nop 1
	v_add_f32_dpp v24, v25, v25 quad_perm:[2,3,0,1] row_mask:0xf bank_mask:0xf bound_ctrl:1
	s_nop 1
	v_add_f32_dpp v24, v24, v24 row_half_mirror row_mask:0xf bank_mask:0xf bound_ctrl:1
	ds_write_b32 v32, v24 offset:49232
	v_add_u32_e32 v28, v243, v35
	v_add_u32_e32 v30, v243, v34
	buffer_load_dwordx4 v[24:27], v28, s[44:47], 0 offen
	buffer_load_dwordx4 v[38:41], v28, s[44:47], s20 offen
	buffer_load_dwordx4 v[44:47], v28, s[44:47], s21 offen
	buffer_load_dwordx4 v[50:53], v28, s[44:47], s23 offen
	s_nop 0
	buffer_load_dwordx2 v[28:29], v30, s[44:47], 0 offen
	buffer_load_dwordx2 v[48:49], v30, s[44:47], s33 offen
	buffer_load_dwordx2 v[42:43], v30, s[44:47], s21 offen
	buffer_load_dwordx2 v[54:55], v30, s[44:47], s94 offen
	s_waitcnt vmcnt(27)
	v_mfma_f32_16x16x128_f8f6f4 v[56:59], v[56:61], v[18:23], 0 cbsz:2 blgp:2
	s_waitcnt vmcnt(26)
	v_mfma_f32_16x16x128_f8f6f4 v[56:59], v[68:73], v[12:17], v[56:59] cbsz:2 blgp:2
	s_waitcnt vmcnt(25)
	v_mfma_f32_16x16x128_f8f6f4 v[56:59], v[62:67], v[6:11], v[56:59] cbsz:2 blgp:2
	s_waitcnt vmcnt(24)
	v_mfma_f32_16x16x128_f8f6f4 v[56:59], v[74:79], v[0:5], v[56:59] cbsz:2 blgp:2
	s_nop 7
	v_cndmask_b32_e64 v30, v56, v57, s[4:5]
	v_cndmask_b32_e64 v30, v30, v58, s[2:3]
	v_cndmask_b32_e32 v30, v30, v59, vcc
	v_mul_f32_e32 v31, v33, v30
	s_nop 1
	v_mov_b32_dpp v31, v31 quad_perm:[1,0,3,2] row_mask:0xf bank_mask:0xf bound_ctrl:1
	v_fmac_f32_e32 v31, v33, v30
	s_nop 1
	v_add_f32_dpp v30, v31, v31 quad_perm:[2,3,0,1] row_mask:0xf bank_mask:0xf bound_ctrl:1
	s_nop 1
	v_add_f32_dpp v30, v30, v30 row_half_mirror row_mask:0xf bank_mask:0xf bound_ctrl:1
	ds_write_b32 v32, v30 offset:49236
	v_add_u32_e32 v31, v244, v35
	v_add_u32_e32 v30, v244, v34
	buffer_load_dwordx4 v[56:59], v31, s[44:47], 0 offen
	buffer_load_dwordx4 v[62:65], v31, s[44:47], s20 offen
	buffer_load_dwordx4 v[68:71], v31, s[44:47], s21 offen
	buffer_load_dwordx4 v[74:77], v31, s[44:47], s23 offen
	buffer_load_dwordx2 v[60:61], v30, s[44:47], 0 offen
	buffer_load_dwordx2 v[72:73], v30, s[44:47], s33 offen
	buffer_load_dwordx2 v[66:67], v30, s[44:47], s21 offen
	buffer_load_dwordx2 v[78:79], v30, s[44:47], s94 offen
	s_waitcnt vmcnt(27)
	v_mfma_f32_16x16x128_f8f6f4 v[86:89], v[86:91], v[18:23], 0 cbsz:2 blgp:2
	s_waitcnt vmcnt(26)
	v_mfma_f32_16x16x128_f8f6f4 v[86:89], v[98:103], v[12:17], v[86:89] cbsz:2 blgp:2
	s_waitcnt vmcnt(25)
	v_mfma_f32_16x16x128_f8f6f4 v[86:89], v[92:97], v[6:11], v[86:89] cbsz:2 blgp:2
	s_waitcnt vmcnt(24)
	v_mfma_f32_16x16x128_f8f6f4 v[86:89], v[150:155], v[0:5], v[86:89] cbsz:2 blgp:2
	s_nop 7
	v_cndmask_b32_e64 v30, v86, v87, s[4:5]
	v_cndmask_b32_e64 v30, v30, v88, s[2:3]
	v_cndmask_b32_e32 v30, v30, v89, vcc
	v_mul_f32_e32 v31, v33, v30
	s_nop 1
	v_mov_b32_dpp v31, v31 quad_perm:[1,0,3,2] row_mask:0xf bank_mask:0xf bound_ctrl:1
	v_fmac_f32_e32 v31, v33, v30
	s_nop 1
	v_add_f32_dpp v30, v31, v31 quad_perm:[2,3,0,1] row_mask:0xf bank_mask:0xf bound_ctrl:1
	s_nop 1
	v_add_f32_dpp v30, v30, v30 row_half_mirror row_mask:0xf bank_mask:0xf bound_ctrl:1
	ds_write_b32 v32, v30 offset:49240
	v_add_u32_e32 v31, v245, v35
	v_add_u32_e32 v30, v245, v34
	buffer_load_dwordx4 v[86:89], v31, s[44:47], 0 offen
	buffer_load_dwordx4 v[92:95], v31, s[44:47], s20 offen
	buffer_load_dwordx4 v[98:101], v31, s[44:47], s21 offen
	buffer_load_dwordx4 v[150:153], v31, s[44:47], s23 offen
	buffer_load_dwordx2 v[90:91], v30, s[44:47], 0 offen
	buffer_load_dwordx2 v[102:103], v30, s[44:47], s33 offen
	buffer_load_dwordx2 v[96:97], v30, s[44:47], s21 offen
	buffer_load_dwordx2 v[154:155], v30, s[44:47], s94 offen
	s_waitcnt vmcnt(27)
	v_mfma_f32_16x16x128_f8f6f4 v[156:159], v[156:161], v[18:23], 0 cbsz:2 blgp:2
	s_waitcnt vmcnt(26)
	v_mfma_f32_16x16x128_f8f6f4 v[156:159], v[168:173], v[12:17], v[156:159] cbsz:2 blgp:2
	s_waitcnt vmcnt(25)
	v_mfma_f32_16x16x128_f8f6f4 v[156:159], v[162:167], v[6:11], v[156:159] cbsz:2 blgp:2
	s_waitcnt vmcnt(24)
	v_mfma_f32_16x16x128_f8f6f4 v[156:159], v[174:179], v[0:5], v[156:159] cbsz:2 blgp:2
	s_nop 7
	v_cndmask_b32_e64 v30, v156, v157, s[4:5]
	v_cndmask_b32_e64 v30, v30, v158, s[2:3]
	v_cndmask_b32_e32 v30, v30, v159, vcc
	v_mul_f32_e32 v31, v33, v30
	s_nop 1
	v_mov_b32_dpp v31, v31 quad_perm:[1,0,3,2] row_mask:0xf bank_mask:0xf bound_ctrl:1
	v_fmac_f32_e32 v31, v33, v30
	s_nop 1
	v_add_f32_dpp v30, v31, v31 quad_perm:[2,3,0,1] row_mask:0xf bank_mask:0xf bound_ctrl:1
	s_nop 1
	v_add_f32_dpp v30, v30, v30 row_half_mirror row_mask:0xf bank_mask:0xf bound_ctrl:1
	ds_write_b32 v32, v30 offset:49244
	v_add_u32_e32 v31, v246, v35
	v_add_u32_e32 v30, v246, v34
	buffer_load_dwordx4 v[156:159], v31, s[44:47], 0 offen
	buffer_load_dwordx4 v[162:165], v31, s[44:47], s20 offen
	buffer_load_dwordx4 v[168:171], v31, s[44:47], s21 offen
	buffer_load_dwordx4 v[174:177], v31, s[44:47], s23 offen
	buffer_load_dwordx2 v[160:161], v30, s[44:47], 0 offen
	buffer_load_dwordx2 v[172:173], v30, s[44:47], s33 offen
	buffer_load_dwordx2 v[166:167], v30, s[44:47], s21 offen
	buffer_load_dwordx2 v[178:179], v30, s[44:47], s94 offen
	s_waitcnt vmcnt(27)
	v_mfma_f32_16x16x128_f8f6f4 v[24:27], v[24:29], v[18:23], 0 cbsz:2 blgp:2
	s_waitcnt vmcnt(26)
	v_mfma_f32_16x16x128_f8f6f4 v[24:27], v[44:49], v[12:17], v[24:27] cbsz:2 blgp:2
	s_waitcnt vmcnt(25)
	v_mfma_f32_16x16x128_f8f6f4 v[24:27], v[38:43], v[6:11], v[24:27] cbsz:2 blgp:2
	s_waitcnt vmcnt(24)
	v_mfma_f32_16x16x128_f8f6f4 v[24:27], v[50:55], v[0:5], v[24:27] cbsz:2 blgp:2
	s_nop 7
	v_cndmask_b32_e64 v24, v24, v25, s[4:5]
	v_cndmask_b32_e64 v24, v24, v26, s[2:3]
	v_cndmask_b32_e32 v24, v24, v27, vcc
	v_mul_f32_e32 v25, v33, v24
	s_nop 1
	v_mov_b32_dpp v25, v25 quad_perm:[1,0,3,2] row_mask:0xf bank_mask:0xf bound_ctrl:1
	v_fmac_f32_e32 v25, v33, v24
	s_nop 1
	v_add_f32_dpp v24, v25, v25 quad_perm:[2,3,0,1] row_mask:0xf bank_mask:0xf bound_ctrl:1
	s_nop 1
	v_add_f32_dpp v24, v24, v24 row_half_mirror row_mask:0xf bank_mask:0xf bound_ctrl:1
	ds_write_b32 v32, v24 offset:49248
	v_add_u32_e32 v28, v247, v35
	v_add_u32_e32 v30, v247, v34
	buffer_load_dwordx4 v[24:27], v28, s[44:47], 0 offen
	buffer_load_dwordx4 v[38:41], v28, s[44:47], s20 offen
	buffer_load_dwordx4 v[44:47], v28, s[44:47], s21 offen
	buffer_load_dwordx4 v[50:53], v28, s[44:47], s23 offen
	s_nop 0
	buffer_load_dwordx2 v[28:29], v30, s[44:47], 0 offen
	buffer_load_dwordx2 v[48:49], v30, s[44:47], s33 offen
	buffer_load_dwordx2 v[42:43], v30, s[44:47], s21 offen
	buffer_load_dwordx2 v[54:55], v30, s[44:47], s94 offen
	s_waitcnt vmcnt(27)
	v_mfma_f32_16x16x128_f8f6f4 v[56:59], v[56:61], v[18:23], 0 cbsz:2 blgp:2
	s_waitcnt vmcnt(26)
	v_mfma_f32_16x16x128_f8f6f4 v[56:59], v[68:73], v[12:17], v[56:59] cbsz:2 blgp:2
	s_waitcnt vmcnt(25)
	v_mfma_f32_16x16x128_f8f6f4 v[56:59], v[62:67], v[6:11], v[56:59] cbsz:2 blgp:2
	s_waitcnt vmcnt(24)
	v_mfma_f32_16x16x128_f8f6f4 v[56:59], v[74:79], v[0:5], v[56:59] cbsz:2 blgp:2
	s_nop 7
	v_cndmask_b32_e64 v30, v56, v57, s[4:5]
	v_cndmask_b32_e64 v30, v30, v58, s[2:3]
	v_cndmask_b32_e32 v30, v30, v59, vcc
	v_mul_f32_e32 v31, v33, v30
	s_nop 1
	v_mov_b32_dpp v31, v31 quad_perm:[1,0,3,2] row_mask:0xf bank_mask:0xf bound_ctrl:1
	v_fmac_f32_e32 v31, v33, v30
	s_nop 1
	v_add_f32_dpp v30, v31, v31 quad_perm:[2,3,0,1] row_mask:0xf bank_mask:0xf bound_ctrl:1
	s_nop 1
	v_add_f32_dpp v30, v30, v30 row_half_mirror row_mask:0xf bank_mask:0xf bound_ctrl:1
	ds_write_b32 v32, v30 offset:49252
	v_add_u32_e32 v31, v248, v35
	v_add_u32_e32 v30, v248, v34
	buffer_load_dwordx4 v[56:59], v31, s[44:47], 0 offen
	buffer_load_dwordx4 v[62:65], v31, s[44:47], s20 offen
	buffer_load_dwordx4 v[68:71], v31, s[44:47], s21 offen
	buffer_load_dwordx4 v[74:77], v31, s[44:47], s23 offen
	buffer_load_dwordx2 v[60:61], v30, s[44:47], 0 offen
	buffer_load_dwordx2 v[72:73], v30, s[44:47], s33 offen
	buffer_load_dwordx2 v[66:67], v30, s[44:47], s21 offen
	buffer_load_dwordx2 v[78:79], v30, s[44:47], s94 offen
	s_waitcnt vmcnt(27)
	v_mfma_f32_16x16x128_f8f6f4 v[86:89], v[86:91], v[18:23], 0 cbsz:2 blgp:2
	s_waitcnt vmcnt(26)
	v_mfma_f32_16x16x128_f8f6f4 v[86:89], v[98:103], v[12:17], v[86:89] cbsz:2 blgp:2
	s_waitcnt vmcnt(25)
	v_mfma_f32_16x16x128_f8f6f4 v[86:89], v[92:97], v[6:11], v[86:89] cbsz:2 blgp:2
	s_waitcnt vmcnt(24)
	v_mfma_f32_16x16x128_f8f6f4 v[86:89], v[150:155], v[0:5], v[86:89] cbsz:2 blgp:2
	s_nop 7
	v_cndmask_b32_e64 v30, v86, v87, s[4:5]
	v_cndmask_b32_e64 v30, v30, v88, s[2:3]
	v_cndmask_b32_e32 v30, v30, v89, vcc
	v_mul_f32_e32 v31, v33, v30
	s_nop 1
	v_mov_b32_dpp v31, v31 quad_perm:[1,0,3,2] row_mask:0xf bank_mask:0xf bound_ctrl:1
	v_fmac_f32_e32 v31, v33, v30
	s_nop 1
	v_add_f32_dpp v30, v31, v31 quad_perm:[2,3,0,1] row_mask:0xf bank_mask:0xf bound_ctrl:1
	s_nop 1
	v_add_f32_dpp v30, v30, v30 row_half_mirror row_mask:0xf bank_mask:0xf bound_ctrl:1
	ds_write_b32 v32, v30 offset:49256
	v_add_u32_e32 v31, v249, v35
	v_add_u32_e32 v30, v249, v34
	buffer_load_dwordx4 v[86:89], v31, s[44:47], 0 offen
	buffer_load_dwordx4 v[92:95], v31, s[44:47], s20 offen
	buffer_load_dwordx4 v[98:101], v31, s[44:47], s21 offen
	buffer_load_dwordx4 v[150:153], v31, s[44:47], s23 offen
	buffer_load_dwordx2 v[90:91], v30, s[44:47], 0 offen
	buffer_load_dwordx2 v[102:103], v30, s[44:47], s33 offen
	buffer_load_dwordx2 v[96:97], v30, s[44:47], s21 offen
	buffer_load_dwordx2 v[154:155], v30, s[44:47], s94 offen
	s_waitcnt vmcnt(27)
	v_mfma_f32_16x16x128_f8f6f4 v[156:159], v[156:161], v[18:23], 0 cbsz:2 blgp:2
	s_waitcnt vmcnt(26)
	v_mfma_f32_16x16x128_f8f6f4 v[156:159], v[168:173], v[12:17], v[156:159] cbsz:2 blgp:2
	s_waitcnt vmcnt(25)
	v_mfma_f32_16x16x128_f8f6f4 v[156:159], v[162:167], v[6:11], v[156:159] cbsz:2 blgp:2
	s_waitcnt vmcnt(24)
	v_mfma_f32_16x16x128_f8f6f4 v[156:159], v[174:179], v[0:5], v[156:159] cbsz:2 blgp:2
	s_nop 7
	v_cndmask_b32_e64 v30, v156, v157, s[4:5]
	v_cndmask_b32_e64 v30, v30, v158, s[2:3]
	v_cndmask_b32_e32 v30, v30, v159, vcc
	v_mul_f32_e32 v31, v33, v30
	s_nop 1
	v_mov_b32_dpp v31, v31 quad_perm:[1,0,3,2] row_mask:0xf bank_mask:0xf bound_ctrl:1
	v_fmac_f32_e32 v31, v33, v30
	s_nop 1
	v_add_f32_dpp v30, v31, v31 quad_perm:[2,3,0,1] row_mask:0xf bank_mask:0xf bound_ctrl:1
	s_nop 1
	v_add_f32_dpp v30, v30, v30 row_half_mirror row_mask:0xf bank_mask:0xf bound_ctrl:1
	ds_write_b32 v32, v30 offset:49260
	ds_bpermute_b32 v30, v36, v251 offset:240
	s_waitcnt lgkmcnt(0)
	v_add_u32_e32 v31, v30, v35
	v_add_u32_e32 v30, v30, v34
	buffer_load_dwordx4 v[156:159], v31, s[44:47], 0 offen
	buffer_load_dwordx4 v[162:165], v31, s[44:47], s20 offen
	buffer_load_dwordx4 v[168:171], v31, s[44:47], s21 offen
	buffer_load_dwordx4 v[174:177], v31, s[44:47], s23 offen
	buffer_load_dwordx2 v[160:161], v30, s[44:47], 0 offen
	buffer_load_dwordx2 v[172:173], v30, s[44:47], s33 offen
	buffer_load_dwordx2 v[166:167], v30, s[44:47], s21 offen
	buffer_load_dwordx2 v[178:179], v30, s[44:47], s94 offen
	s_waitcnt vmcnt(27)
	v_mfma_f32_16x16x128_f8f6f4 v[24:27], v[24:29], v[18:23], 0 cbsz:2 blgp:2
	s_waitcnt vmcnt(26)
	v_mfma_f32_16x16x128_f8f6f4 v[24:27], v[44:49], v[12:17], v[24:27] cbsz:2 blgp:2
	s_waitcnt vmcnt(25)
	v_mfma_f32_16x16x128_f8f6f4 v[24:27], v[38:43], v[6:11], v[24:27] cbsz:2 blgp:2
	s_waitcnt vmcnt(24)
	v_mfma_f32_16x16x128_f8f6f4 v[24:27], v[50:55], v[0:5], v[24:27] cbsz:2 blgp:2
	s_nop 7
	v_cndmask_b32_e64 v24, v24, v25, s[4:5]
	v_cndmask_b32_e64 v24, v24, v26, s[2:3]
	v_cndmask_b32_e32 v24, v24, v27, vcc
	v_mul_f32_e32 v25, v33, v24
	s_nop 1
	v_mov_b32_dpp v25, v25 quad_perm:[1,0,3,2] row_mask:0xf bank_mask:0xf bound_ctrl:1
	v_fmac_f32_e32 v25, v33, v24
	s_nop 1
	v_add_f32_dpp v24, v25, v25 quad_perm:[2,3,0,1] row_mask:0xf bank_mask:0xf bound_ctrl:1
	s_nop 1
	v_add_f32_dpp v24, v24, v24 row_half_mirror row_mask:0xf bank_mask:0xf bound_ctrl:1
	ds_write_b32 v32, v24 offset:49264
	s_waitcnt vmcnt(19)
	v_mfma_f32_16x16x128_f8f6f4 v[24:27], v[56:61], v[18:23], 0 cbsz:2 blgp:2
	s_waitcnt vmcnt(18)
	v_mfma_f32_16x16x128_f8f6f4 v[24:27], v[68:73], v[12:17], v[24:27] cbsz:2 blgp:2
	s_waitcnt vmcnt(17)
	v_mfma_f32_16x16x128_f8f6f4 v[24:27], v[62:67], v[6:11], v[24:27] cbsz:2 blgp:2
	s_waitcnt vmcnt(16)
	v_mfma_f32_16x16x128_f8f6f4 v[24:27], v[74:79], v[0:5], v[24:27] cbsz:2 blgp:2
	s_nop 7
	v_cndmask_b32_e64 v24, v24, v25, s[4:5]
	v_cndmask_b32_e64 v24, v24, v26, s[2:3]
	v_cndmask_b32_e32 v24, v24, v27, vcc
	v_mul_f32_e32 v25, v33, v24
	s_nop 1
	v_mov_b32_dpp v25, v25 quad_perm:[1,0,3,2] row_mask:0xf bank_mask:0xf bound_ctrl:1
	v_fmac_f32_e32 v25, v33, v24
	s_nop 1
	v_add_f32_dpp v24, v25, v25 quad_perm:[2,3,0,1] row_mask:0xf bank_mask:0xf bound_ctrl:1
	s_nop 1
	v_add_f32_dpp v24, v24, v24 row_half_mirror row_mask:0xf bank_mask:0xf bound_ctrl:1
	ds_write_b32 v32, v24 offset:49268
	s_waitcnt vmcnt(11)
	v_mfma_f32_16x16x128_f8f6f4 v[24:27], v[86:91], v[18:23], 0 cbsz:2 blgp:2
	s_waitcnt vmcnt(10)
	v_mfma_f32_16x16x128_f8f6f4 v[24:27], v[98:103], v[12:17], v[24:27] cbsz:2 blgp:2
	s_waitcnt vmcnt(9)
	v_mfma_f32_16x16x128_f8f6f4 v[24:27], v[92:97], v[6:11], v[24:27] cbsz:2 blgp:2
	s_waitcnt vmcnt(8)
	v_mfma_f32_16x16x128_f8f6f4 v[24:27], v[150:155], v[0:5], v[24:27] cbsz:2 blgp:2
	s_nop 7
	v_cndmask_b32_e64 v24, v24, v25, s[4:5]
	v_cndmask_b32_e64 v24, v24, v26, s[2:3]
	v_cndmask_b32_e32 v24, v24, v27, vcc
	v_mul_f32_e32 v25, v33, v24
	s_nop 1
	v_mov_b32_dpp v25, v25 quad_perm:[1,0,3,2] row_mask:0xf bank_mask:0xf bound_ctrl:1
	v_fmac_f32_e32 v25, v33, v24
	s_nop 1
	v_add_f32_dpp v24, v25, v25 quad_perm:[2,3,0,1] row_mask:0xf bank_mask:0xf bound_ctrl:1
	s_nop 1
	v_add_f32_dpp v24, v24, v24 row_half_mirror row_mask:0xf bank_mask:0xf bound_ctrl:1
	ds_write_b32 v32, v24 offset:49272
	s_waitcnt vmcnt(3)
	v_mfma_f32_16x16x128_f8f6f4 v[18:21], v[156:161], v[18:23], 0 cbsz:2 blgp:2
	s_waitcnt vmcnt(2)
	v_mfma_f32_16x16x128_f8f6f4 v[12:15], v[168:173], v[12:17], v[18:21] cbsz:2 blgp:2
	s_waitcnt vmcnt(1)
	v_mfma_f32_16x16x128_f8f6f4 v[6:9], v[162:167], v[6:11], v[12:15] cbsz:2 blgp:2
	s_waitcnt vmcnt(0)
	v_mfma_f32_16x16x128_f8f6f4 v[0:3], v[174:179], v[0:5], v[6:9] cbsz:2 blgp:2
	s_nop 7
	v_cndmask_b32_e64 v0, v0, v1, s[4:5]
	v_cndmask_b32_e64 v0, v0, v2, s[2:3]
	v_cndmask_b32_e32 v0, v0, v3, vcc
	v_mul_f32_e32 v1, v33, v0
	s_nop 1
	v_mov_b32_dpp v1, v1 quad_perm:[1,0,3,2] row_mask:0xf bank_mask:0xf bound_ctrl:1
	v_fmac_f32_e32 v1, v33, v0
	s_nop 1
	v_add_f32_dpp v0, v1, v1 quad_perm:[2,3,0,1] row_mask:0xf bank_mask:0xf bound_ctrl:1
	s_nop 1
	v_add_f32_dpp v0, v0, v0 row_half_mirror row_mask:0xf bank_mask:0xf bound_ctrl:1
	ds_write_b32 v32, v0 offset:49276
	v_mul_u32_u24_e32 v240, 0x600, v130
	v_mul_u32_u24_e32 v241, 0x600, v128
	v_add_u32_e32 v240, 0x8000000, v240
	v_add_u32_e32 v241, 0x8000000, v241
	v_lshrrev_b32_e32 v0, 1, v129
	v_readlane_b32 s100, v240, 0
	v_readlane_b32 s101, v240, 1
	v_readlane_b32 s2, v240, 2
	v_readlane_b32 s3, v240, 3
	s_nop 1
	buffer_load_dwordx4 v[74:77], v129, s[44:47], s100 offen
	buffer_load_dwordx2 v[78:79], v0, s[44:47], s100 offen offset:1024
	buffer_load_dwordx4 v[68:71], v129, s[44:47], s101 offen
	buffer_load_dwordx2 v[72:73], v0, s[44:47], s101 offen offset:1024
	buffer_load_dwordx4 v[56:59], v129, s[44:47], s2 offen
	buffer_load_dwordx2 v[60:61], v0, s[44:47], s2 offen offset:1024
	buffer_load_dwordx4 v[44:47], v129, s[44:47], s3 offen
	buffer_load_dwordx2 v[48:49], v0, s[44:47], s3 offen offset:1024
	v_add_u32_e32 v210, 0x400, v0
	v_readlane_b32 s100, v240, 4
	v_readlane_b32 s101, v240, 5
	v_readlane_b32 s2, v240, 6
	v_readlane_b32 s3, v240, 7
	s_nop 1
	buffer_load_dwordx4 v[62:65], v129, s[44:47], s100 offen
	buffer_load_dwordx2 v[66:67], v0, s[44:47], s100 offen offset:1024
	buffer_load_dwordx4 v[50:53], v129, s[44:47], s101 offen
	buffer_load_dwordx2 v[54:55], v0, s[44:47], s101 offen offset:1024
	buffer_load_dwordx4 v[38:41], v129, s[44:47], s2 offen
	buffer_load_dwordx2 v[42:43], v0, s[44:47], s2 offen offset:1024
	buffer_load_dwordx4 v[32:35], v129, s[44:47], s3 offen
	buffer_load_dwordx2 v[36:37], v0, s[44:47], s3 offen offset:1024
	v_div_scale_f32 v2, s[2:3], v80, v80, 1.0
	v_rcp_f32_e32 v3, v2
	v_div_scale_f32 v4, vcc, 1.0, v80, 1.0
	v_and_b32_e32 v1, -4, v148
	v_fma_f32 v0, -v2, v3, 1.0
	v_fmac_f32_e32 v3, v0, v3
	v_mul_f32_e32 v5, v4, v3
	v_fma_f32 v0, -v2, v5, v4
	v_fmac_f32_e32 v5, v0, v3
	v_lshlrev_b32_e32 v0, 7, v148
	v_and_b32_e32 v0, 0x180, v0
	v_add3_u32 v0, v111, v0, v1
	v_add_u32_e32 v0, 0xc000, v0
	ds_read2_b32 v[0:1], v0 offset1:16
	v_fma_f32 v2, -v2, v5, v4
	v_div_fmas_f32 v2, v2, v3, v5
	v_div_fixup_f32 v2, v2, v80, 1.0
	s_mov_b32 s1, 0x3e6d3388
	s_waitcnt lgkmcnt(0)
	v_mul_f32_e32 v0, v2, v0
	v_mul_f32_e32 v0, v83, v0
	v_fma_f32 v3, |v0|, s1, 1.0
	v_rcp_f32_e32 v3, v3
	v_mul_f32_e32 v5, v0, v0
	v_mul_f32_e32 v5, 0xbf38aa3b, v5
	v_exp_f32_e32 v5, v5
	v_fmamk_f32 v4, v3, 0x3f07dc22, v184
	v_fmaak_f32 v4, v3, v4, 0x3f35f0e3
	v_fmaak_f32 v4, v3, v4, 0xbe11a98e
	v_mul_f32_e32 v1, v2, v1
	v_fmaak_f32 v4, v3, v4, 0x3e027906
	v_mul_f32_e32 v3, v3, v4
	v_mul_f32_e32 v1, v82, v1
	v_mul_f32_e32 v3, v5, v3
	v_fma_f32 v5, |v1|, s1, 1.0
	v_rcp_f32_e32 v5, v5
	v_mul_f32_e32 v4, v0, v3
	v_fma_f32 v3, -v0, v3, v0
	v_cmp_gt_f32_e32 vcc, 0, v0
	v_mul_f32_e32 v2, v206, v84
	v_mov_b32_e32 v180, 0
	v_cndmask_b32_e32 v0, v3, v4, vcc
	v_mul_f32_e32 v211, v2, v0
	v_mul_f32_e32 v2, v1, v1
	v_fmamk_f32 v0, v5, 0x3f07dc22, v184
	v_mul_f32_e32 v2, 0xbf38aa3b, v2
	v_fmaak_f32 v0, v5, v0, 0x3f35f0e3
	v_exp_f32_e32 v2, v2
	v_fmaak_f32 v0, v5, v0, 0xbe11a98e
	v_fmaak_f32 v0, v5, v0, 0x3e027906
	v_mul_f32_e32 v0, v5, v0
	v_mul_f32_e32 v0, v2, v0
	v_mul_f32_e32 v2, v1, v0
	v_fma_f32 v0, -v1, v0, v1
	v_cmp_gt_f32_e32 vcc, 0, v1
	v_mul_f32_e32 v1, v205, v81
	v_mov_b32_e32 v181, v180
	v_cndmask_b32_e32 v0, v0, v2, vcc
	v_mul_f32_e32 v131, v1, v0
	v_mov_b32_e32 v178, v180
	v_mov_b32_e32 v179, v180
	v_mov_b32_e32 v176, v180
	v_mov_b32_e32 v177, v180
	v_mov_b32_e32 v174, v180
	v_mov_b32_e32 v175, v180
	v_mov_b32_e32 v172, v180
	v_mov_b32_e32 v173, v180
	v_mov_b32_e32 v170, v180
	v_mov_b32_e32 v171, v180
	v_mov_b32_e32 v168, v180
	v_mov_b32_e32 v169, v180
	v_mov_b32_e32 v166, v180
	v_mov_b32_e32 v167, v180
	v_mov_b32_e32 v164, v180
	v_mov_b32_e32 v165, v180
	v_mov_b32_e32 v162, v180
	v_mov_b32_e32 v163, v180
	v_mov_b32_e32 v160, v180
	v_mov_b32_e32 v161, v180
	v_mov_b32_e32 v158, v180
	v_mov_b32_e32 v159, v180
	v_mov_b32_e32 v156, v180
	v_mov_b32_e32 v157, v180
	v_mov_b32_e32 v154, v180
	v_mov_b32_e32 v155, v180
	v_mov_b32_e32 v152, v180
	v_mov_b32_e32 v153, v180
	v_mov_b32_e32 v150, v180
	v_mov_b32_e32 v151, v180
	v_readlane_b32 s2, v240, 8
	v_readlane_b32 s3, v240, 9
	v_readlane_b32 s100, v240, 10
	v_readlane_b32 s101, v240, 11
	s_nop 1
	buffer_load_dwordx4 v[98:101], v129, s[44:47], s2 offen
	buffer_load_dwordx2 v[102:103], v210, s[44:47], s2 offen
	buffer_load_dwordx4 v[92:95], v129, s[44:47], s3 offen
	buffer_load_dwordx2 v[96:97], v210, s[44:47], s3 offen
	buffer_load_dwordx4 v[86:89], v129, s[44:47], s100 offen
	buffer_load_dwordx2 v[90:91], v210, s[44:47], s100 offen
	buffer_load_dwordx4 v[80:83], v129, s[44:47], s101 offen
	buffer_load_dwordx2 v[84:85], v210, s[44:47], s101 offen
	v_readlane_b32 s2, v211, 0
	s_waitcnt vmcnt(22)
	v_cvt_scalef32_pk32_f32_fp6 v[0:31], v[74:79], 1.0
	v_pk_fma_f32 v[74:75], v[0:1], s[2:3], v[180:181] op_sel_hi:[1,0,1]
	v_pk_fma_f32 v[76:77], v[2:3], s[2:3], v[178:179] op_sel_hi:[1,0,1]
	v_pk_fma_f32 v[78:79], v[4:5], s[2:3], v[176:177] op_sel_hi:[1,0,1]
	v_pk_fma_f32 v[174:175], v[6:7], s[2:3], v[174:175] op_sel_hi:[1,0,1]
	v_pk_fma_f32 v[172:173], v[8:9], s[2:3], v[172:173] op_sel_hi:[1,0,1]
	v_pk_fma_f32 v[170:171], v[10:11], s[2:3], v[170:171] op_sel_hi:[1,0,1]
	v_pk_fma_f32 v[168:169], v[12:13], s[2:3], v[168:169] op_sel_hi:[1,0,1]
	v_pk_fma_f32 v[166:167], v[14:15], s[2:3], v[166:167] op_sel_hi:[1,0,1]
	v_pk_fma_f32 v[164:165], v[16:17], s[2:3], v[164:165] op_sel_hi:[1,0,1]
	v_pk_fma_f32 v[162:163], v[18:19], s[2:3], v[162:163] op_sel_hi:[1,0,1]
	v_pk_fma_f32 v[160:161], v[20:21], s[2:3], v[160:161] op_sel_hi:[1,0,1]
	v_pk_fma_f32 v[158:159], v[22:23], s[2:3], v[158:159] op_sel_hi:[1,0,1]
	v_pk_fma_f32 v[156:157], v[24:25], s[2:3], v[156:157] op_sel_hi:[1,0,1]
	v_pk_fma_f32 v[154:155], v[26:27], s[2:3], v[154:155] op_sel_hi:[1,0,1]
	v_pk_fma_f32 v[152:153], v[28:29], s[2:3], v[152:153] op_sel_hi:[1,0,1]
	v_pk_fma_f32 v[150:151], v[30:31], s[2:3], v[150:151] op_sel_hi:[1,0,1]
	v_readlane_b32 s2, v211, 1
	s_waitcnt vmcnt(20)
	v_cvt_scalef32_pk32_f32_fp6 v[0:31], v[68:73], 1.0
	v_pk_fma_f32 v[68:69], v[0:1], s[2:3], v[74:75] op_sel_hi:[1,0,1]
	v_pk_fma_f32 v[70:71], v[2:3], s[2:3], v[76:77] op_sel_hi:[1,0,1]
	v_pk_fma_f32 v[72:73], v[4:5], s[2:3], v[78:79] op_sel_hi:[1,0,1]
	v_pk_fma_f32 v[74:75], v[6:7], s[2:3], v[174:175] op_sel_hi:[1,0,1]
	v_pk_fma_f32 v[76:77], v[8:9], s[2:3], v[172:173] op_sel_hi:[1,0,1]
	v_pk_fma_f32 v[78:79], v[10:11], s[2:3], v[170:171] op_sel_hi:[1,0,1]
	v_pk_fma_f32 v[168:169], v[12:13], s[2:3], v[168:169] op_sel_hi:[1,0,1]
	v_pk_fma_f32 v[166:167], v[14:15], s[2:3], v[166:167] op_sel_hi:[1,0,1]
	v_pk_fma_f32 v[164:165], v[16:17], s[2:3], v[164:165] op_sel_hi:[1,0,1]
	v_pk_fma_f32 v[162:163], v[18:19], s[2:3], v[162:163] op_sel_hi:[1,0,1]
	v_pk_fma_f32 v[160:161], v[20:21], s[2:3], v[160:161] op_sel_hi:[1,0,1]
	v_pk_fma_f32 v[158:159], v[22:23], s[2:3], v[158:159] op_sel_hi:[1,0,1]
	v_pk_fma_f32 v[156:157], v[24:25], s[2:3], v[156:157] op_sel_hi:[1,0,1]
	v_pk_fma_f32 v[154:155], v[26:27], s[2:3], v[154:155] op_sel_hi:[1,0,1]
	v_pk_fma_f32 v[152:153], v[28:29], s[2:3], v[152:153] op_sel_hi:[1,0,1]
	v_pk_fma_f32 v[150:151], v[30:31], s[2:3], v[150:151] op_sel_hi:[1,0,1]
	v_readlane_b32 s2, v211, 2
	s_waitcnt vmcnt(18)
	v_cvt_scalef32_pk32_f32_fp6 v[0:31], v[56:61], 1.0
	v_pk_fma_f32 v[56:57], v[0:1], s[2:3], v[68:69] op_sel_hi:[1,0,1]
	v_pk_fma_f32 v[58:59], v[2:3], s[2:3], v[70:71] op_sel_hi:[1,0,1]
	v_pk_fma_f32 v[60:61], v[4:5], s[2:3], v[72:73] op_sel_hi:[1,0,1]
	v_pk_fma_f32 v[68:69], v[6:7], s[2:3], v[74:75] op_sel_hi:[1,0,1]
	v_pk_fma_f32 v[70:71], v[8:9], s[2:3], v[76:77] op_sel_hi:[1,0,1]
	v_pk_fma_f32 v[72:73], v[10:11], s[2:3], v[78:79] op_sel_hi:[1,0,1]
	v_pk_fma_f32 v[74:75], v[12:13], s[2:3], v[168:169] op_sel_hi:[1,0,1]
	v_pk_fma_f32 v[76:77], v[14:15], s[2:3], v[166:167] op_sel_hi:[1,0,1]
	v_pk_fma_f32 v[78:79], v[16:17], s[2:3], v[164:165] op_sel_hi:[1,0,1]
	v_pk_fma_f32 v[162:163], v[18:19], s[2:3], v[162:163] op_sel_hi:[1,0,1]
	v_pk_fma_f32 v[160:161], v[20:21], s[2:3], v[160:161] op_sel_hi:[1,0,1]
	v_pk_fma_f32 v[158:159], v[22:23], s[2:3], v[158:159] op_sel_hi:[1,0,1]
	v_pk_fma_f32 v[156:157], v[24:25], s[2:3], v[156:157] op_sel_hi:[1,0,1]
	v_pk_fma_f32 v[154:155], v[26:27], s[2:3], v[154:155] op_sel_hi:[1,0,1]
	v_pk_fma_f32 v[152:153], v[28:29], s[2:3], v[152:153] op_sel_hi:[1,0,1]
	v_pk_fma_f32 v[150:151], v[30:31], s[2:3], v[150:151] op_sel_hi:[1,0,1]
	v_readlane_b32 s2, v211, 3
	s_waitcnt vmcnt(16)
	v_cvt_scalef32_pk32_f32_fp6 v[0:31], v[44:49], 1.0
	v_pk_fma_f32 v[164:165], v[0:1], s[2:3], v[56:57] op_sel_hi:[1,0,1]
	v_pk_fma_f32 v[166:167], v[2:3], s[2:3], v[58:59] op_sel_hi:[1,0,1]
	v_pk_fma_f32 v[168:169], v[4:5], s[2:3], v[60:61] op_sel_hi:[1,0,1]
	v_pk_fma_f32 v[170:171], v[6:7], s[2:3], v[68:69] op_sel_hi:[1,0,1]
	v_pk_fma_f32 v[172:173], v[8:9], s[2:3], v[70:71] op_sel_hi:[1,0,1]
	v_pk_fma_f32 v[174:175], v[10:11], s[2:3], v[72:73] op_sel_hi:[1,0,1]
	v_pk_fma_f32 v[176:177], v[12:13], s[2:3], v[74:75] op_sel_hi:[1,0,1]
	v_pk_fma_f32 v[178:179], v[14:15], s[2:3], v[76:77] op_sel_hi:[1,0,1]
	v_pk_fma_f32 v[180:181], v[16:17], s[2:3], v[78:79] op_sel_hi:[1,0,1]
	v_pk_fma_f32 v[162:163], v[18:19], s[2:3], v[162:163] op_sel_hi:[1,0,1]
	v_pk_fma_f32 v[160:161], v[20:21], s[2:3], v[160:161] op_sel_hi:[1,0,1]
	v_pk_fma_f32 v[158:159], v[22:23], s[2:3], v[158:159] op_sel_hi:[1,0,1]
	v_pk_fma_f32 v[156:157], v[24:25], s[2:3], v[156:157] op_sel_hi:[1,0,1]
	v_pk_fma_f32 v[154:155], v[26:27], s[2:3], v[154:155] op_sel_hi:[1,0,1]
	v_pk_fma_f32 v[152:153], v[28:29], s[2:3], v[152:153] op_sel_hi:[1,0,1]
	v_pk_fma_f32 v[150:151], v[30:31], s[2:3], v[150:151] op_sel_hi:[1,0,1]
	v_readlane_b32 s2, v240, 12
	v_readlane_b32 s3, v240, 13
	v_readlane_b32 s100, v240, 14
	v_readlane_b32 s101, v240, 15
	s_nop 1
	buffer_load_dwordx4 v[74:77], v129, s[44:47], s2 offen
	buffer_load_dwordx2 v[78:79], v210, s[44:47], s2 offen
	buffer_load_dwordx4 v[68:71], v129, s[44:47], s3 offen
	buffer_load_dwordx2 v[72:73], v210, s[44:47], s3 offen
	buffer_load_dwordx4 v[56:59], v129, s[44:47], s100 offen
	buffer_load_dwordx2 v[60:61], v210, s[44:47], s100 offen
	buffer_load_dwordx4 v[44:47], v129, s[44:47], s101 offen
	buffer_load_dwordx2 v[48:49], v210, s[44:47], s101 offen
	v_readlane_b32 s2, v211, 4
	s_waitcnt vmcnt(22)
	v_cvt_scalef32_pk32_f32_fp6 v[0:31], v[62:67], 1.0
	v_pk_fma_f32 v[62:63], v[0:1], s[2:3], v[164:165] op_sel_hi:[1,0,1]
	v_pk_fma_f32 v[64:65], v[2:3], s[2:3], v[166:167] op_sel_hi:[1,0,1]
	v_pk_fma_f32 v[66:67], v[4:5], s[2:3], v[168:169] op_sel_hi:[1,0,1]
	v_pk_fma_f32 v[164:165], v[6:7], s[2:3], v[170:171] op_sel_hi:[1,0,1]
	v_pk_fma_f32 v[166:167], v[8:9], s[2:3], v[172:173] op_sel_hi:[1,0,1]
	v_pk_fma_f32 v[168:169], v[10:11], s[2:3], v[174:175] op_sel_hi:[1,0,1]
	v_pk_fma_f32 v[170:171], v[12:13], s[2:3], v[176:177] op_sel_hi:[1,0,1]
	v_pk_fma_f32 v[172:173], v[14:15], s[2:3], v[178:179] op_sel_hi:[1,0,1]
	v_pk_fma_f32 v[174:175], v[16:17], s[2:3], v[180:181] op_sel_hi:[1,0,1]
	v_pk_fma_f32 v[162:163], v[18:19], s[2:3], v[162:163] op_sel_hi:[1,0,1]
	v_pk_fma_f32 v[160:161], v[20:21], s[2:3], v[160:161] op_sel_hi:[1,0,1]
	v_pk_fma_f32 v[158:159], v[22:23], s[2:3], v[158:159] op_sel_hi:[1,0,1]
	v_pk_fma_f32 v[156:157], v[24:25], s[2:3], v[156:157] op_sel_hi:[1,0,1]
	v_pk_fma_f32 v[154:155], v[26:27], s[2:3], v[154:155] op_sel_hi:[1,0,1]
	v_pk_fma_f32 v[152:153], v[28:29], s[2:3], v[152:153] op_sel_hi:[1,0,1]
	v_pk_fma_f32 v[150:151], v[30:31], s[2:3], v[150:151] op_sel_hi:[1,0,1]
	v_readlane_b32 s2, v211, 5
	s_waitcnt vmcnt(20)
	v_cvt_scalef32_pk32_f32_fp6 v[0:31], v[50:55], 1.0
	v_pk_fma_f32 v[50:51], v[0:1], s[2:3], v[62:63] op_sel_hi:[1,0,1]
	v_pk_fma_f32 v[52:53], v[2:3], s[2:3], v[64:65] op_sel_hi:[1,0,1]
	v_pk_fma_f32 v[54:55], v[4:5], s[2:3], v[66:67] op_sel_hi:[1,0,1]
	v_pk_fma_f32 v[62:63], v[6:7], s[2:3], v[164:165] op_sel_hi:[1,0,1]
	v_pk_fma_f32 v[64:65], v[8:9], s[2:3], v[166:167] op_sel_hi:[1,0,1]
	v_pk_fma_f32 v[66:67], v[10:11], s[2:3], v[168:169] op_sel_hi:[1,0,1]
	v_pk_fma_f32 v[164:165], v[12:13], s[2:3], v[170:171] op_sel_hi:[1,0,1]
	v_pk_fma_f32 v[166:167], v[14:15], s[2:3], v[172:173] op_sel_hi:[1,0,1]
	v_pk_fma_f32 v[168:169], v[16:17], s[2:3], v[174:175] op_sel_hi:[1,0,1]
	v_pk_fma_f32 v[162:163], v[18:19], s[2:3], v[162:163] op_sel_hi:[1,0,1]
	v_pk_fma_f32 v[160:161], v[20:21], s[2:3], v[160:161] op_sel_hi:[1,0,1]
	v_pk_fma_f32 v[158:159], v[22:23], s[2:3], v[158:159] op_sel_hi:[1,0,1]
	v_pk_fma_f32 v[156:157], v[24:25], s[2:3], v[156:157] op_sel_hi:[1,0,1]
	v_pk_fma_f32 v[154:155], v[26:27], s[2:3], v[154:155] op_sel_hi:[1,0,1]
	v_pk_fma_f32 v[152:153], v[28:29], s[2:3], v[152:153] op_sel_hi:[1,0,1]
	v_pk_fma_f32 v[150:151], v[30:31], s[2:3], v[150:151] op_sel_hi:[1,0,1]
	v_readlane_b32 s2, v211, 6
	s_waitcnt vmcnt(18)
	v_cvt_scalef32_pk32_f32_fp6 v[0:31], v[38:43], 1.0
	v_pk_fma_f32 v[38:39], v[0:1], s[2:3], v[50:51] op_sel_hi:[1,0,1]
	v_pk_fma_f32 v[40:41], v[2:3], s[2:3], v[52:53] op_sel_hi:[1,0,1]
	v_pk_fma_f32 v[42:43], v[4:5], s[2:3], v[54:55] op_sel_hi:[1,0,1]
	v_pk_fma_f32 v[50:51], v[6:7], s[2:3], v[62:63] op_sel_hi:[1,0,1]
	v_pk_fma_f32 v[52:53], v[8:9], s[2:3], v[64:65] op_sel_hi:[1,0,1]
	v_pk_fma_f32 v[54:55], v[10:11], s[2:3], v[66:67] op_sel_hi:[1,0,1]
	v_pk_fma_f32 v[62:63], v[12:13], s[2:3], v[164:165] op_sel_hi:[1,0,1]
	v_pk_fma_f32 v[64:65], v[14:15], s[2:3], v[166:167] op_sel_hi:[1,0,1]
	v_pk_fma_f32 v[66:67], v[16:17], s[2:3], v[168:169] op_sel_hi:[1,0,1]
	v_pk_fma_f32 v[162:163], v[18:19], s[2:3], v[162:163] op_sel_hi:[1,0,1]
	v_pk_fma_f32 v[160:161], v[20:21], s[2:3], v[160:161] op_sel_hi:[1,0,1]
	v_pk_fma_f32 v[158:159], v[22:23], s[2:3], v[158:159] op_sel_hi:[1,0,1]
	v_pk_fma_f32 v[156:157], v[24:25], s[2:3], v[156:157] op_sel_hi:[1,0,1]
	v_pk_fma_f32 v[154:155], v[26:27], s[2:3], v[154:155] op_sel_hi:[1,0,1]
	v_pk_fma_f32 v[152:153], v[28:29], s[2:3], v[152:153] op_sel_hi:[1,0,1]
	v_pk_fma_f32 v[150:151], v[30:31], s[2:3], v[150:151] op_sel_hi:[1,0,1]
	v_readlane_b32 s2, v211, 7
	s_waitcnt vmcnt(16)
	v_cvt_scalef32_pk32_f32_fp6 v[0:31], v[32:37], 1.0
	v_pk_fma_f32 v[164:165], v[0:1], s[2:3], v[38:39] op_sel_hi:[1,0,1]
	v_pk_fma_f32 v[166:167], v[2:3], s[2:3], v[40:41] op_sel_hi:[1,0,1]
	v_pk_fma_f32 v[168:169], v[4:5], s[2:3], v[42:43] op_sel_hi:[1,0,1]
	v_pk_fma_f32 v[170:171], v[6:7], s[2:3], v[50:51] op_sel_hi:[1,0,1]
	v_pk_fma_f32 v[172:173], v[8:9], s[2:3], v[52:53] op_sel_hi:[1,0,1]
	v_pk_fma_f32 v[174:175], v[10:11], s[2:3], v[54:55] op_sel_hi:[1,0,1]
	v_pk_fma_f32 v[176:177], v[12:13], s[2:3], v[62:63] op_sel_hi:[1,0,1]
	v_pk_fma_f32 v[178:179], v[14:15], s[2:3], v[64:65] op_sel_hi:[1,0,1]
	v_pk_fma_f32 v[180:181], v[16:17], s[2:3], v[66:67] op_sel_hi:[1,0,1]
	v_pk_fma_f32 v[162:163], v[18:19], s[2:3], v[162:163] op_sel_hi:[1,0,1]
	v_pk_fma_f32 v[160:161], v[20:21], s[2:3], v[160:161] op_sel_hi:[1,0,1]
	v_pk_fma_f32 v[158:159], v[22:23], s[2:3], v[158:159] op_sel_hi:[1,0,1]
	v_pk_fma_f32 v[156:157], v[24:25], s[2:3], v[156:157] op_sel_hi:[1,0,1]
	v_pk_fma_f32 v[154:155], v[26:27], s[2:3], v[154:155] op_sel_hi:[1,0,1]
	v_pk_fma_f32 v[152:153], v[28:29], s[2:3], v[152:153] op_sel_hi:[1,0,1]
	v_pk_fma_f32 v[150:151], v[30:31], s[2:3], v[150:151] op_sel_hi:[1,0,1]
	v_readlane_b32 s2, v240, 16
	v_readlane_b32 s3, v240, 17
	v_readlane_b32 s100, v240, 18
	v_readlane_b32 s101, v240, 19
	s_nop 1
	buffer_load_dwordx4 v[62:65], v129, s[44:47], s2 offen
	buffer_load_dwordx2 v[66:67], v210, s[44:47], s2 offen
	buffer_load_dwordx4 v[50:53], v129, s[44:47], s3 offen
	buffer_load_dwordx2 v[54:55], v210, s[44:47], s3 offen
	buffer_load_dwordx4 v[38:41], v129, s[44:47], s100 offen
	buffer_load_dwordx2 v[42:43], v210, s[44:47], s100 offen
	buffer_load_dwordx4 v[32:35], v129, s[44:47], s101 offen
	buffer_load_dwordx2 v[36:37], v210, s[44:47], s101 offen
	v_readlane_b32 s2, v211, 8
	s_waitcnt vmcnt(22)
	v_cvt_scalef32_pk32_f32_fp6 v[0:31], v[98:103], 1.0
	v_pk_fma_f32 v[98:99], v[0:1], s[2:3], v[164:165] op_sel_hi:[1,0,1]
	v_pk_fma_f32 v[100:101], v[2:3], s[2:3], v[166:167] op_sel_hi:[1,0,1]
	v_pk_fma_f32 v[102:103], v[4:5], s[2:3], v[168:169] op_sel_hi:[1,0,1]
	v_pk_fma_f32 v[164:165], v[6:7], s[2:3], v[170:171] op_sel_hi:[1,0,1]
	v_pk_fma_f32 v[166:167], v[8:9], s[2:3], v[172:173] op_sel_hi:[1,0,1]
	v_pk_fma_f32 v[168:169], v[10:11], s[2:3], v[174:175] op_sel_hi:[1,0,1]
	v_pk_fma_f32 v[170:171], v[12:13], s[2:3], v[176:177] op_sel_hi:[1,0,1]
	v_pk_fma_f32 v[172:173], v[14:15], s[2:3], v[178:179] op_sel_hi:[1,0,1]
	v_pk_fma_f32 v[174:175], v[16:17], s[2:3], v[180:181] op_sel_hi:[1,0,1]
	v_pk_fma_f32 v[162:163], v[18:19], s[2:3], v[162:163] op_sel_hi:[1,0,1]
	v_pk_fma_f32 v[160:161], v[20:21], s[2:3], v[160:161] op_sel_hi:[1,0,1]
	v_pk_fma_f32 v[158:159], v[22:23], s[2:3], v[158:159] op_sel_hi:[1,0,1]
	v_pk_fma_f32 v[156:157], v[24:25], s[2:3], v[156:157] op_sel_hi:[1,0,1]
	v_pk_fma_f32 v[154:155], v[26:27], s[2:3], v[154:155] op_sel_hi:[1,0,1]
	v_pk_fma_f32 v[152:153], v[28:29], s[2:3], v[152:153] op_sel_hi:[1,0,1]
	v_pk_fma_f32 v[150:151], v[30:31], s[2:3], v[150:151] op_sel_hi:[1,0,1]
	v_readlane_b32 s2, v211, 9
	s_waitcnt vmcnt(20)
	v_cvt_scalef32_pk32_f32_fp6 v[0:31], v[92:97], 1.0
	v_pk_fma_f32 v[92:93], v[0:1], s[2:3], v[98:99] op_sel_hi:[1,0,1]
	v_pk_fma_f32 v[94:95], v[2:3], s[2:3], v[100:101] op_sel_hi:[1,0,1]
	v_pk_fma_f32 v[96:97], v[4:5], s[2:3], v[102:103] op_sel_hi:[1,0,1]
	v_pk_fma_f32 v[98:99], v[6:7], s[2:3], v[164:165] op_sel_hi:[1,0,1]
	v_pk_fma_f32 v[100:101], v[8:9], s[2:3], v[166:167] op_sel_hi:[1,0,1]
	v_pk_fma_f32 v[102:103], v[10:11], s[2:3], v[168:169] op_sel_hi:[1,0,1]
	v_pk_fma_f32 v[164:165], v[12:13], s[2:3], v[170:171] op_sel_hi:[1,0,1]
	v_pk_fma_f32 v[166:167], v[14:15], s[2:3], v[172:173] op_sel_hi:[1,0,1]
	v_pk_fma_f32 v[168:169], v[16:17], s[2:3], v[174:175] op_sel_hi:[1,0,1]
	v_pk_fma_f32 v[162:163], v[18:19], s[2:3], v[162:163] op_sel_hi:[1,0,1]
	v_pk_fma_f32 v[160:161], v[20:21], s[2:3], v[160:161] op_sel_hi:[1,0,1]
	v_pk_fma_f32 v[158:159], v[22:23], s[2:3], v[158:159] op_sel_hi:[1,0,1]
	v_pk_fma_f32 v[156:157], v[24:25], s[2:3], v[156:157] op_sel_hi:[1,0,1]
	v_pk_fma_f32 v[154:155], v[26:27], s[2:3], v[154:155] op_sel_hi:[1,0,1]
	v_pk_fma_f32 v[152:153], v[28:29], s[2:3], v[152:153] op_sel_hi:[1,0,1]
	v_pk_fma_f32 v[150:151], v[30:31], s[2:3], v[150:151] op_sel_hi:[1,0,1]
	v_readlane_b32 s2, v211, 10
	s_waitcnt vmcnt(18)
	v_cvt_scalef32_pk32_f32_fp6 v[0:31], v[86:91], 1.0
	v_pk_fma_f32 v[86:87], v[0:1], s[2:3], v[92:93] op_sel_hi:[1,0,1]
	v_pk_fma_f32 v[88:89], v[2:3], s[2:3], v[94:95] op_sel_hi:[1,0,1]
	v_pk_fma_f32 v[90:91], v[4:5], s[2:3], v[96:97] op_sel_hi:[1,0,1]
	v_pk_fma_f32 v[92:93], v[6:7], s[2:3], v[98:99] op_sel_hi:[1,0,1]
	v_pk_fma_f32 v[94:95], v[8:9], s[2:3], v[100:101] op_sel_hi:[1,0,1]
	v_pk_fma_f32 v[96:97], v[10:11], s[2:3], v[102:103] op_sel_hi:[1,0,1]
	v_pk_fma_f32 v[98:99], v[12:13], s[2:3], v[164:165] op_sel_hi:[1,0,1]
	v_pk_fma_f32 v[100:101], v[14:15], s[2:3], v[166:167] op_sel_hi:[1,0,1]
	v_pk_fma_f32 v[102:103], v[16:17], s[2:3], v[168:169] op_sel_hi:[1,0,1]
	v_pk_fma_f32 v[162:163], v[18:19], s[2:3], v[162:163] op_sel_hi:[1,0,1]
	v_pk_fma_f32 v[160:161], v[20:21], s[2:3], v[160:161] op_sel_hi:[1,0,1]
	v_pk_fma_f32 v[158:159], v[22:23], s[2:3], v[158:159] op_sel_hi:[1,0,1]
	v_pk_fma_f32 v[156:157], v[24:25], s[2:3], v[156:157] op_sel_hi:[1,0,1]
	v_pk_fma_f32 v[154:155], v[26:27], s[2:3], v[154:155] op_sel_hi:[1,0,1]
	v_pk_fma_f32 v[152:153], v[28:29], s[2:3], v[152:153] op_sel_hi:[1,0,1]
	v_pk_fma_f32 v[150:151], v[30:31], s[2:3], v[150:151] op_sel_hi:[1,0,1]
	v_readlane_b32 s2, v211, 11
	s_waitcnt vmcnt(16)
	v_cvt_scalef32_pk32_f32_fp6 v[0:31], v[80:85], 1.0
	v_pk_fma_f32 v[180:181], v[0:1], s[2:3], v[86:87] op_sel_hi:[1,0,1]
	v_pk_fma_f32 v[178:179], v[2:3], s[2:3], v[88:89] op_sel_hi:[1,0,1]
	v_pk_fma_f32 v[176:177], v[4:5], s[2:3], v[90:91] op_sel_hi:[1,0,1]
	v_pk_fma_f32 v[174:175], v[6:7], s[2:3], v[92:93] op_sel_hi:[1,0,1]
	v_pk_fma_f32 v[172:173], v[8:9], s[2:3], v[94:95] op_sel_hi:[1,0,1]
	v_pk_fma_f32 v[170:171], v[10:11], s[2:3], v[96:97] op_sel_hi:[1,0,1]
	v_pk_fma_f32 v[168:169], v[12:13], s[2:3], v[98:99] op_sel_hi:[1,0,1]
	v_pk_fma_f32 v[166:167], v[14:15], s[2:3], v[100:101] op_sel_hi:[1,0,1]
	v_pk_fma_f32 v[164:165], v[16:17], s[2:3], v[102:103] op_sel_hi:[1,0,1]
	v_pk_fma_f32 v[162:163], v[18:19], s[2:3], v[162:163] op_sel_hi:[1,0,1]
	v_pk_fma_f32 v[160:161], v[20:21], s[2:3], v[160:161] op_sel_hi:[1,0,1]
	v_pk_fma_f32 v[158:159], v[22:23], s[2:3], v[158:159] op_sel_hi:[1,0,1]
	v_pk_fma_f32 v[156:157], v[24:25], s[2:3], v[156:157] op_sel_hi:[1,0,1]
	v_pk_fma_f32 v[154:155], v[26:27], s[2:3], v[154:155] op_sel_hi:[1,0,1]
	v_pk_fma_f32 v[152:153], v[28:29], s[2:3], v[152:153] op_sel_hi:[1,0,1]
	v_pk_fma_f32 v[150:151], v[30:31], s[2:3], v[150:151] op_sel_hi:[1,0,1]
	v_readlane_b32 s2, v240, 20
	v_readlane_b32 s3, v240, 21
	v_readlane_b32 s100, v240, 22
	v_readlane_b32 s101, v240, 23
	s_nop 1
	buffer_load_dwordx4 v[98:101], v129, s[44:47], s2 offen
	buffer_load_dwordx2 v[102:103], v210, s[44:47], s2 offen
	buffer_load_dwordx4 v[92:95], v129, s[44:47], s3 offen
	buffer_load_dwordx2 v[96:97], v210, s[44:47], s3 offen
	buffer_load_dwordx4 v[86:89], v129, s[44:47], s100 offen
	buffer_load_dwordx2 v[90:91], v210, s[44:47], s100 offen
	buffer_load_dwordx4 v[80:83], v129, s[44:47], s101 offen
	buffer_load_dwordx2 v[84:85], v210, s[44:47], s101 offen
	v_readlane_b32 s2, v211, 12
	s_waitcnt vmcnt(22)
	v_cvt_scalef32_pk32_f32_fp6 v[0:31], v[74:79], 1.0
	v_pk_fma_f32 v[74:75], v[0:1], s[2:3], v[180:181] op_sel_hi:[1,0,1]
	v_pk_fma_f32 v[76:77], v[2:3], s[2:3], v[178:179] op_sel_hi:[1,0,1]
	v_pk_fma_f32 v[78:79], v[4:5], s[2:3], v[176:177] op_sel_hi:[1,0,1]
	v_pk_fma_f32 v[174:175], v[6:7], s[2:3], v[174:175] op_sel_hi:[1,0,1]
	v_pk_fma_f32 v[172:173], v[8:9], s[2:3], v[172:173] op_sel_hi:[1,0,1]
	v_pk_fma_f32 v[170:171], v[10:11], s[2:3], v[170:171] op_sel_hi:[1,0,1]
	v_pk_fma_f32 v[168:169], v[12:13], s[2:3], v[168:169] op_sel_hi:[1,0,1]
	v_pk_fma_f32 v[166:167], v[14:15], s[2:3], v[166:167] op_sel_hi:[1,0,1]
	v_pk_fma_f32 v[164:165], v[16:17], s[2:3], v[164:165] op_sel_hi:[1,0,1]
	v_pk_fma_f32 v[162:163], v[18:19], s[2:3], v[162:163] op_sel_hi:[1,0,1]
	v_pk_fma_f32 v[160:161], v[20:21], s[2:3], v[160:161] op_sel_hi:[1,0,1]
	v_pk_fma_f32 v[158:159], v[22:23], s[2:3], v[158:159] op_sel_hi:[1,0,1]
	v_pk_fma_f32 v[156:157], v[24:25], s[2:3], v[156:157] op_sel_hi:[1,0,1]
	v_pk_fma_f32 v[154:155], v[26:27], s[2:3], v[154:155] op_sel_hi:[1,0,1]
	v_pk_fma_f32 v[152:153], v[28:29], s[2:3], v[152:153] op_sel_hi:[1,0,1]
	v_pk_fma_f32 v[150:151], v[30:31], s[2:3], v[150:151] op_sel_hi:[1,0,1]
	v_readlane_b32 s2, v211, 13
	s_waitcnt vmcnt(20)
	v_cvt_scalef32_pk32_f32_fp6 v[0:31], v[68:73], 1.0
	v_pk_fma_f32 v[68:69], v[0:1], s[2:3], v[74:75] op_sel_hi:[1,0,1]
	v_pk_fma_f32 v[70:71], v[2:3], s[2:3], v[76:77] op_sel_hi:[1,0,1]
	v_pk_fma_f32 v[72:73], v[4:5], s[2:3], v[78:79] op_sel_hi:[1,0,1]
	v_pk_fma_f32 v[74:75], v[6:7], s[2:3], v[174:175] op_sel_hi:[1,0,1]
	v_pk_fma_f32 v[76:77], v[8:9], s[2:3], v[172:173] op_sel_hi:[1,0,1]
	v_pk_fma_f32 v[78:79], v[10:11], s[2:3], v[170:171] op_sel_hi:[1,0,1]
	v_pk_fma_f32 v[168:169], v[12:13], s[2:3], v[168:169] op_sel_hi:[1,0,1]
	v_pk_fma_f32 v[166:167], v[14:15], s[2:3], v[166:167] op_sel_hi:[1,0,1]
	v_pk_fma_f32 v[164:165], v[16:17], s[2:3], v[164:165] op_sel_hi:[1,0,1]
	v_pk_fma_f32 v[162:163], v[18:19], s[2:3], v[162:163] op_sel_hi:[1,0,1]
	v_pk_fma_f32 v[160:161], v[20:21], s[2:3], v[160:161] op_sel_hi:[1,0,1]
	v_pk_fma_f32 v[158:159], v[22:23], s[2:3], v[158:159] op_sel_hi:[1,0,1]
	v_pk_fma_f32 v[156:157], v[24:25], s[2:3], v[156:157] op_sel_hi:[1,0,1]
	v_pk_fma_f32 v[154:155], v[26:27], s[2:3], v[154:155] op_sel_hi:[1,0,1]
	v_pk_fma_f32 v[152:153], v[28:29], s[2:3], v[152:153] op_sel_hi:[1,0,1]
	v_pk_fma_f32 v[150:151], v[30:31], s[2:3], v[150:151] op_sel_hi:[1,0,1]
	v_readlane_b32 s2, v211, 14
	s_waitcnt vmcnt(18)
	v_cvt_scalef32_pk32_f32_fp6 v[0:31], v[56:61], 1.0
	v_pk_fma_f32 v[56:57], v[0:1], s[2:3], v[68:69] op_sel_hi:[1,0,1]
	v_pk_fma_f32 v[58:59], v[2:3], s[2:3], v[70:71] op_sel_hi:[1,0,1]
	v_pk_fma_f32 v[60:61], v[4:5], s[2:3], v[72:73] op_sel_hi:[1,0,1]
	v_pk_fma_f32 v[68:69], v[6:7], s[2:3], v[74:75] op_sel_hi:[1,0,1]
	v_pk_fma_f32 v[70:71], v[8:9], s[2:3], v[76:77] op_sel_hi:[1,0,1]
	v_pk_fma_f32 v[72:73], v[10:11], s[2:3], v[78:79] op_sel_hi:[1,0,1]
	v_pk_fma_f32 v[74:75], v[12:13], s[2:3], v[168:169] op_sel_hi:[1,0,1]
	v_pk_fma_f32 v[76:77], v[14:15], s[2:3], v[166:167] op_sel_hi:[1,0,1]
	v_pk_fma_f32 v[78:79], v[16:17], s[2:3], v[164:165] op_sel_hi:[1,0,1]
	v_pk_fma_f32 v[162:163], v[18:19], s[2:3], v[162:163] op_sel_hi:[1,0,1]
	v_pk_fma_f32 v[160:161], v[20:21], s[2:3], v[160:161] op_sel_hi:[1,0,1]
	v_pk_fma_f32 v[158:159], v[22:23], s[2:3], v[158:159] op_sel_hi:[1,0,1]
	v_pk_fma_f32 v[156:157], v[24:25], s[2:3], v[156:157] op_sel_hi:[1,0,1]
	v_pk_fma_f32 v[154:155], v[26:27], s[2:3], v[154:155] op_sel_hi:[1,0,1]
	v_pk_fma_f32 v[152:153], v[28:29], s[2:3], v[152:153] op_sel_hi:[1,0,1]
	v_pk_fma_f32 v[150:151], v[30:31], s[2:3], v[150:151] op_sel_hi:[1,0,1]
	v_readlane_b32 s2, v211, 15
	s_waitcnt vmcnt(16)
	v_cvt_scalef32_pk32_f32_fp6 v[0:31], v[44:49], 1.0
	v_pk_fma_f32 v[164:165], v[0:1], s[2:3], v[56:57] op_sel_hi:[1,0,1]
	v_pk_fma_f32 v[166:167], v[2:3], s[2:3], v[58:59] op_sel_hi:[1,0,1]
	v_pk_fma_f32 v[168:169], v[4:5], s[2:3], v[60:61] op_sel_hi:[1,0,1]
	v_pk_fma_f32 v[170:171], v[6:7], s[2:3], v[68:69] op_sel_hi:[1,0,1]
	v_pk_fma_f32 v[172:173], v[8:9], s[2:3], v[70:71] op_sel_hi:[1,0,1]
	v_pk_fma_f32 v[174:175], v[10:11], s[2:3], v[72:73] op_sel_hi:[1,0,1]
	v_pk_fma_f32 v[176:177], v[12:13], s[2:3], v[74:75] op_sel_hi:[1,0,1]
	v_pk_fma_f32 v[178:179], v[14:15], s[2:3], v[76:77] op_sel_hi:[1,0,1]
	v_pk_fma_f32 v[180:181], v[16:17], s[2:3], v[78:79] op_sel_hi:[1,0,1]
	v_pk_fma_f32 v[162:163], v[18:19], s[2:3], v[162:163] op_sel_hi:[1,0,1]
	v_pk_fma_f32 v[160:161], v[20:21], s[2:3], v[160:161] op_sel_hi:[1,0,1]
	v_pk_fma_f32 v[158:159], v[22:23], s[2:3], v[158:159] op_sel_hi:[1,0,1]
	v_pk_fma_f32 v[156:157], v[24:25], s[2:3], v[156:157] op_sel_hi:[1,0,1]
	v_pk_fma_f32 v[154:155], v[26:27], s[2:3], v[154:155] op_sel_hi:[1,0,1]
	v_pk_fma_f32 v[152:153], v[28:29], s[2:3], v[152:153] op_sel_hi:[1,0,1]
	v_pk_fma_f32 v[150:151], v[30:31], s[2:3], v[150:151] op_sel_hi:[1,0,1]
	v_readlane_b32 s2, v240, 24
	v_readlane_b32 s3, v240, 25
	v_readlane_b32 s100, v240, 26
	v_readlane_b32 s101, v240, 27
	s_nop 1
	buffer_load_dwordx4 v[74:77], v129, s[44:47], s2 offen
	buffer_load_dwordx2 v[78:79], v210, s[44:47], s2 offen
	buffer_load_dwordx4 v[68:71], v129, s[44:47], s3 offen
	buffer_load_dwordx2 v[72:73], v210, s[44:47], s3 offen
	buffer_load_dwordx4 v[56:59], v129, s[44:47], s100 offen
	buffer_load_dwordx2 v[60:61], v210, s[44:47], s100 offen
	buffer_load_dwordx4 v[44:47], v129, s[44:47], s101 offen
	buffer_load_dwordx2 v[48:49], v210, s[44:47], s101 offen
	v_readlane_b32 s2, v211, 16
	s_waitcnt vmcnt(22)
	v_cvt_scalef32_pk32_f32_fp6 v[0:31], v[62:67], 1.0
	v_pk_fma_f32 v[62:63], v[0:1], s[2:3], v[164:165] op_sel_hi:[1,0,1]
	v_pk_fma_f32 v[64:65], v[2:3], s[2:3], v[166:167] op_sel_hi:[1,0,1]
	v_pk_fma_f32 v[66:67], v[4:5], s[2:3], v[168:169] op_sel_hi:[1,0,1]
	v_pk_fma_f32 v[164:165], v[6:7], s[2:3], v[170:171] op_sel_hi:[1,0,1]
	v_pk_fma_f32 v[166:167], v[8:9], s[2:3], v[172:173] op_sel_hi:[1,0,1]
	v_pk_fma_f32 v[168:169], v[10:11], s[2:3], v[174:175] op_sel_hi:[1,0,1]
	v_pk_fma_f32 v[170:171], v[12:13], s[2:3], v[176:177] op_sel_hi:[1,0,1]
	v_pk_fma_f32 v[172:173], v[14:15], s[2:3], v[178:179] op_sel_hi:[1,0,1]
	v_pk_fma_f32 v[174:175], v[16:17], s[2:3], v[180:181] op_sel_hi:[1,0,1]
	v_pk_fma_f32 v[162:163], v[18:19], s[2:3], v[162:163] op_sel_hi:[1,0,1]
	v_pk_fma_f32 v[160:161], v[20:21], s[2:3], v[160:161] op_sel_hi:[1,0,1]
	v_pk_fma_f32 v[158:159], v[22:23], s[2:3], v[158:159] op_sel_hi:[1,0,1]
	v_pk_fma_f32 v[156:157], v[24:25], s[2:3], v[156:157] op_sel_hi:[1,0,1]
	v_pk_fma_f32 v[154:155], v[26:27], s[2:3], v[154:155] op_sel_hi:[1,0,1]
	v_pk_fma_f32 v[152:153], v[28:29], s[2:3], v[152:153] op_sel_hi:[1,0,1]
	v_pk_fma_f32 v[150:151], v[30:31], s[2:3], v[150:151] op_sel_hi:[1,0,1]
	v_readlane_b32 s2, v211, 17
	s_waitcnt vmcnt(20)
	v_cvt_scalef32_pk32_f32_fp6 v[0:31], v[50:55], 1.0
	v_pk_fma_f32 v[50:51], v[0:1], s[2:3], v[62:63] op_sel_hi:[1,0,1]
	v_pk_fma_f32 v[52:53], v[2:3], s[2:3], v[64:65] op_sel_hi:[1,0,1]
	v_pk_fma_f32 v[54:55], v[4:5], s[2:3], v[66:67] op_sel_hi:[1,0,1]
	v_pk_fma_f32 v[62:63], v[6:7], s[2:3], v[164:165] op_sel_hi:[1,0,1]
	v_pk_fma_f32 v[64:65], v[8:9], s[2:3], v[166:167] op_sel_hi:[1,0,1]
	v_pk_fma_f32 v[66:67], v[10:11], s[2:3], v[168:169] op_sel_hi:[1,0,1]
	v_pk_fma_f32 v[164:165], v[12:13], s[2:3], v[170:171] op_sel_hi:[1,0,1]
	v_pk_fma_f32 v[166:167], v[14:15], s[2:3], v[172:173] op_sel_hi:[1,0,1]
	v_pk_fma_f32 v[168:169], v[16:17], s[2:3], v[174:175] op_sel_hi:[1,0,1]
	v_pk_fma_f32 v[162:163], v[18:19], s[2:3], v[162:163] op_sel_hi:[1,0,1]
	v_pk_fma_f32 v[160:161], v[20:21], s[2:3], v[160:161] op_sel_hi:[1,0,1]
	v_pk_fma_f32 v[158:159], v[22:23], s[2:3], v[158:159] op_sel_hi:[1,0,1]
	v_pk_fma_f32 v[156:157], v[24:25], s[2:3], v[156:157] op_sel_hi:[1,0,1]
	v_pk_fma_f32 v[154:155], v[26:27], s[2:3], v[154:155] op_sel_hi:[1,0,1]
	v_pk_fma_f32 v[152:153], v[28:29], s[2:3], v[152:153] op_sel_hi:[1,0,1]
	v_pk_fma_f32 v[150:151], v[30:31], s[2:3], v[150:151] op_sel_hi:[1,0,1]
	v_readlane_b32 s2, v211, 18
	s_waitcnt vmcnt(18)
	v_cvt_scalef32_pk32_f32_fp6 v[0:31], v[38:43], 1.0
	v_pk_fma_f32 v[38:39], v[0:1], s[2:3], v[50:51] op_sel_hi:[1,0,1]
	v_pk_fma_f32 v[40:41], v[2:3], s[2:3], v[52:53] op_sel_hi:[1,0,1]
	v_pk_fma_f32 v[42:43], v[4:5], s[2:3], v[54:55] op_sel_hi:[1,0,1]
	v_pk_fma_f32 v[50:51], v[6:7], s[2:3], v[62:63] op_sel_hi:[1,0,1]
	v_pk_fma_f32 v[52:53], v[8:9], s[2:3], v[64:65] op_sel_hi:[1,0,1]
	v_pk_fma_f32 v[54:55], v[10:11], s[2:3], v[66:67] op_sel_hi:[1,0,1]
	v_pk_fma_f32 v[62:63], v[12:13], s[2:3], v[164:165] op_sel_hi:[1,0,1]
	v_pk_fma_f32 v[64:65], v[14:15], s[2:3], v[166:167] op_sel_hi:[1,0,1]
	v_pk_fma_f32 v[66:67], v[16:17], s[2:3], v[168:169] op_sel_hi:[1,0,1]
	v_pk_fma_f32 v[162:163], v[18:19], s[2:3], v[162:163] op_sel_hi:[1,0,1]
	v_pk_fma_f32 v[160:161], v[20:21], s[2:3], v[160:161] op_sel_hi:[1,0,1]
	v_pk_fma_f32 v[158:159], v[22:23], s[2:3], v[158:159] op_sel_hi:[1,0,1]
	v_pk_fma_f32 v[156:157], v[24:25], s[2:3], v[156:157] op_sel_hi:[1,0,1]
	v_pk_fma_f32 v[154:155], v[26:27], s[2:3], v[154:155] op_sel_hi:[1,0,1]
	v_pk_fma_f32 v[152:153], v[28:29], s[2:3], v[152:153] op_sel_hi:[1,0,1]
	v_pk_fma_f32 v[150:151], v[30:31], s[2:3], v[150:151] op_sel_hi:[1,0,1]
	v_readlane_b32 s2, v211, 19
	s_waitcnt vmcnt(16)
	v_cvt_scalef32_pk32_f32_fp6 v[0:31], v[32:37], 1.0
	v_pk_fma_f32 v[164:165], v[0:1], s[2:3], v[38:39] op_sel_hi:[1,0,1]
	v_pk_fma_f32 v[166:167], v[2:3], s[2:3], v[40:41] op_sel_hi:[1,0,1]
	v_pk_fma_f32 v[168:169], v[4:5], s[2:3], v[42:43] op_sel_hi:[1,0,1]
	v_pk_fma_f32 v[170:171], v[6:7], s[2:3], v[50:51] op_sel_hi:[1,0,1]
	v_pk_fma_f32 v[172:173], v[8:9], s[2:3], v[52:53] op_sel_hi:[1,0,1]
	v_pk_fma_f32 v[174:175], v[10:11], s[2:3], v[54:55] op_sel_hi:[1,0,1]
	v_pk_fma_f32 v[176:177], v[12:13], s[2:3], v[62:63] op_sel_hi:[1,0,1]
	v_pk_fma_f32 v[178:179], v[14:15], s[2:3], v[64:65] op_sel_hi:[1,0,1]
	v_pk_fma_f32 v[180:181], v[16:17], s[2:3], v[66:67] op_sel_hi:[1,0,1]
	v_pk_fma_f32 v[162:163], v[18:19], s[2:3], v[162:163] op_sel_hi:[1,0,1]
	v_pk_fma_f32 v[160:161], v[20:21], s[2:3], v[160:161] op_sel_hi:[1,0,1]
	v_pk_fma_f32 v[158:159], v[22:23], s[2:3], v[158:159] op_sel_hi:[1,0,1]
	v_pk_fma_f32 v[156:157], v[24:25], s[2:3], v[156:157] op_sel_hi:[1,0,1]
	v_pk_fma_f32 v[154:155], v[26:27], s[2:3], v[154:155] op_sel_hi:[1,0,1]
	v_pk_fma_f32 v[152:153], v[28:29], s[2:3], v[152:153] op_sel_hi:[1,0,1]
	v_pk_fma_f32 v[150:151], v[30:31], s[2:3], v[150:151] op_sel_hi:[1,0,1]
	v_readlane_b32 s2, v240, 28
	v_readlane_b32 s3, v240, 29
	v_readlane_b32 s100, v240, 30
	v_readlane_b32 s101, v240, 31
	s_nop 1
	buffer_load_dwordx4 v[62:65], v129, s[44:47], s2 offen
	buffer_load_dwordx2 v[66:67], v210, s[44:47], s2 offen
	buffer_load_dwordx4 v[50:53], v129, s[44:47], s3 offen
	buffer_load_dwordx2 v[54:55], v210, s[44:47], s3 offen
	buffer_load_dwordx4 v[38:41], v129, s[44:47], s100 offen
	buffer_load_dwordx2 v[42:43], v210, s[44:47], s100 offen
	buffer_load_dwordx4 v[32:35], v129, s[44:47], s101 offen
	buffer_load_dwordx2 v[36:37], v210, s[44:47], s101 offen
	v_readlane_b32 s2, v211, 20
	s_waitcnt vmcnt(22)
	v_cvt_scalef32_pk32_f32_fp6 v[0:31], v[98:103], 1.0
	v_pk_fma_f32 v[98:99], v[0:1], s[2:3], v[164:165] op_sel_hi:[1,0,1]
	v_pk_fma_f32 v[100:101], v[2:3], s[2:3], v[166:167] op_sel_hi:[1,0,1]
	v_pk_fma_f32 v[102:103], v[4:5], s[2:3], v[168:169] op_sel_hi:[1,0,1]
	v_pk_fma_f32 v[164:165], v[6:7], s[2:3], v[170:171] op_sel_hi:[1,0,1]
	v_pk_fma_f32 v[166:167], v[8:9], s[2:3], v[172:173] op_sel_hi:[1,0,1]
	v_pk_fma_f32 v[168:169], v[10:11], s[2:3], v[174:175] op_sel_hi:[1,0,1]
	v_pk_fma_f32 v[170:171], v[12:13], s[2:3], v[176:177] op_sel_hi:[1,0,1]
	v_pk_fma_f32 v[172:173], v[14:15], s[2:3], v[178:179] op_sel_hi:[1,0,1]
	v_pk_fma_f32 v[174:175], v[16:17], s[2:3], v[180:181] op_sel_hi:[1,0,1]
	v_pk_fma_f32 v[162:163], v[18:19], s[2:3], v[162:163] op_sel_hi:[1,0,1]
	v_pk_fma_f32 v[160:161], v[20:21], s[2:3], v[160:161] op_sel_hi:[1,0,1]
	v_pk_fma_f32 v[158:159], v[22:23], s[2:3], v[158:159] op_sel_hi:[1,0,1]
	v_pk_fma_f32 v[156:157], v[24:25], s[2:3], v[156:157] op_sel_hi:[1,0,1]
	v_pk_fma_f32 v[154:155], v[26:27], s[2:3], v[154:155] op_sel_hi:[1,0,1]
	v_pk_fma_f32 v[152:153], v[28:29], s[2:3], v[152:153] op_sel_hi:[1,0,1]
	v_pk_fma_f32 v[150:151], v[30:31], s[2:3], v[150:151] op_sel_hi:[1,0,1]
	v_readlane_b32 s2, v211, 21
	s_waitcnt vmcnt(20)
	v_cvt_scalef32_pk32_f32_fp6 v[0:31], v[92:97], 1.0
	v_pk_fma_f32 v[92:93], v[0:1], s[2:3], v[98:99] op_sel_hi:[1,0,1]
	v_pk_fma_f32 v[94:95], v[2:3], s[2:3], v[100:101] op_sel_hi:[1,0,1]
	v_pk_fma_f32 v[96:97], v[4:5], s[2:3], v[102:103] op_sel_hi:[1,0,1]
	v_pk_fma_f32 v[98:99], v[6:7], s[2:3], v[164:165] op_sel_hi:[1,0,1]
	v_pk_fma_f32 v[100:101], v[8:9], s[2:3], v[166:167] op_sel_hi:[1,0,1]
	v_pk_fma_f32 v[102:103], v[10:11], s[2:3], v[168:169] op_sel_hi:[1,0,1]
	v_pk_fma_f32 v[164:165], v[12:13], s[2:3], v[170:171] op_sel_hi:[1,0,1]
	v_pk_fma_f32 v[166:167], v[14:15], s[2:3], v[172:173] op_sel_hi:[1,0,1]
	v_pk_fma_f32 v[168:169], v[16:17], s[2:3], v[174:175] op_sel_hi:[1,0,1]
	v_pk_fma_f32 v[162:163], v[18:19], s[2:3], v[162:163] op_sel_hi:[1,0,1]
	v_pk_fma_f32 v[160:161], v[20:21], s[2:3], v[160:161] op_sel_hi:[1,0,1]
	v_pk_fma_f32 v[158:159], v[22:23], s[2:3], v[158:159] op_sel_hi:[1,0,1]
	v_pk_fma_f32 v[156:157], v[24:25], s[2:3], v[156:157] op_sel_hi:[1,0,1]
	v_pk_fma_f32 v[154:155], v[26:27], s[2:3], v[154:155] op_sel_hi:[1,0,1]
	v_pk_fma_f32 v[152:153], v[28:29], s[2:3], v[152:153] op_sel_hi:[1,0,1]
	v_pk_fma_f32 v[150:151], v[30:31], s[2:3], v[150:151] op_sel_hi:[1,0,1]
	v_readlane_b32 s2, v211, 22
	s_waitcnt vmcnt(18)
	v_cvt_scalef32_pk32_f32_fp6 v[0:31], v[86:91], 1.0
	v_pk_fma_f32 v[86:87], v[0:1], s[2:3], v[92:93] op_sel_hi:[1,0,1]
	v_pk_fma_f32 v[88:89], v[2:3], s[2:3], v[94:95] op_sel_hi:[1,0,1]
	v_pk_fma_f32 v[90:91], v[4:5], s[2:3], v[96:97] op_sel_hi:[1,0,1]
	v_pk_fma_f32 v[92:93], v[6:7], s[2:3], v[98:99] op_sel_hi:[1,0,1]
	v_pk_fma_f32 v[94:95], v[8:9], s[2:3], v[100:101] op_sel_hi:[1,0,1]
	v_pk_fma_f32 v[96:97], v[10:11], s[2:3], v[102:103] op_sel_hi:[1,0,1]
	v_pk_fma_f32 v[98:99], v[12:13], s[2:3], v[164:165] op_sel_hi:[1,0,1]
	v_pk_fma_f32 v[100:101], v[14:15], s[2:3], v[166:167] op_sel_hi:[1,0,1]
	v_pk_fma_f32 v[102:103], v[16:17], s[2:3], v[168:169] op_sel_hi:[1,0,1]
	v_pk_fma_f32 v[162:163], v[18:19], s[2:3], v[162:163] op_sel_hi:[1,0,1]
	v_pk_fma_f32 v[160:161], v[20:21], s[2:3], v[160:161] op_sel_hi:[1,0,1]
	v_pk_fma_f32 v[158:159], v[22:23], s[2:3], v[158:159] op_sel_hi:[1,0,1]
	v_pk_fma_f32 v[156:157], v[24:25], s[2:3], v[156:157] op_sel_hi:[1,0,1]
	v_pk_fma_f32 v[154:155], v[26:27], s[2:3], v[154:155] op_sel_hi:[1,0,1]
	v_pk_fma_f32 v[152:153], v[28:29], s[2:3], v[152:153] op_sel_hi:[1,0,1]
	v_pk_fma_f32 v[150:151], v[30:31], s[2:3], v[150:151] op_sel_hi:[1,0,1]
	v_readlane_b32 s2, v211, 23
	s_waitcnt vmcnt(16)
	v_cvt_scalef32_pk32_f32_fp6 v[0:31], v[80:85], 1.0
	v_pk_fma_f32 v[180:181], v[0:1], s[2:3], v[86:87] op_sel_hi:[1,0,1]
	v_pk_fma_f32 v[178:179], v[2:3], s[2:3], v[88:89] op_sel_hi:[1,0,1]
	v_pk_fma_f32 v[176:177], v[4:5], s[2:3], v[90:91] op_sel_hi:[1,0,1]
	v_pk_fma_f32 v[174:175], v[6:7], s[2:3], v[92:93] op_sel_hi:[1,0,1]
	v_pk_fma_f32 v[172:173], v[8:9], s[2:3], v[94:95] op_sel_hi:[1,0,1]
	v_pk_fma_f32 v[170:171], v[10:11], s[2:3], v[96:97] op_sel_hi:[1,0,1]
	v_pk_fma_f32 v[168:169], v[12:13], s[2:3], v[98:99] op_sel_hi:[1,0,1]
	v_pk_fma_f32 v[166:167], v[14:15], s[2:3], v[100:101] op_sel_hi:[1,0,1]
	v_pk_fma_f32 v[164:165], v[16:17], s[2:3], v[102:103] op_sel_hi:[1,0,1]
	v_pk_fma_f32 v[162:163], v[18:19], s[2:3], v[162:163] op_sel_hi:[1,0,1]
	v_pk_fma_f32 v[160:161], v[20:21], s[2:3], v[160:161] op_sel_hi:[1,0,1]
	v_pk_fma_f32 v[158:159], v[22:23], s[2:3], v[158:159] op_sel_hi:[1,0,1]
	v_pk_fma_f32 v[156:157], v[24:25], s[2:3], v[156:157] op_sel_hi:[1,0,1]
	v_pk_fma_f32 v[154:155], v[26:27], s[2:3], v[154:155] op_sel_hi:[1,0,1]
	v_pk_fma_f32 v[152:153], v[28:29], s[2:3], v[152:153] op_sel_hi:[1,0,1]
	v_pk_fma_f32 v[150:151], v[30:31], s[2:3], v[150:151] op_sel_hi:[1,0,1]
	v_readlane_b32 s2, v240, 32
	v_readlane_b32 s3, v240, 33
	v_readlane_b32 s100, v240, 34
	v_readlane_b32 s101, v240, 35
	s_nop 1
	buffer_load_dwordx4 v[98:101], v129, s[44:47], s2 offen
	buffer_load_dwordx2 v[102:103], v210, s[44:47], s2 offen
	buffer_load_dwordx4 v[92:95], v129, s[44:47], s3 offen
	buffer_load_dwordx2 v[96:97], v210, s[44:47], s3 offen
	buffer_load_dwordx4 v[86:89], v129, s[44:47], s100 offen
	buffer_load_dwordx2 v[90:91], v210, s[44:47], s100 offen
	buffer_load_dwordx4 v[80:83], v129, s[44:47], s101 offen
	buffer_load_dwordx2 v[84:85], v210, s[44:47], s101 offen
	v_readlane_b32 s2, v211, 24
	s_waitcnt vmcnt(22)
	v_cvt_scalef32_pk32_f32_fp6 v[0:31], v[74:79], 1.0
	v_pk_fma_f32 v[74:75], v[0:1], s[2:3], v[180:181] op_sel_hi:[1,0,1]
	v_pk_fma_f32 v[76:77], v[2:3], s[2:3], v[178:179] op_sel_hi:[1,0,1]
	v_pk_fma_f32 v[78:79], v[4:5], s[2:3], v[176:177] op_sel_hi:[1,0,1]
	v_pk_fma_f32 v[174:175], v[6:7], s[2:3], v[174:175] op_sel_hi:[1,0,1]
	v_pk_fma_f32 v[172:173], v[8:9], s[2:3], v[172:173] op_sel_hi:[1,0,1]
	v_pk_fma_f32 v[170:171], v[10:11], s[2:3], v[170:171] op_sel_hi:[1,0,1]
	v_pk_fma_f32 v[168:169], v[12:13], s[2:3], v[168:169] op_sel_hi:[1,0,1]
	v_pk_fma_f32 v[166:167], v[14:15], s[2:3], v[166:167] op_sel_hi:[1,0,1]
	v_pk_fma_f32 v[164:165], v[16:17], s[2:3], v[164:165] op_sel_hi:[1,0,1]
	v_pk_fma_f32 v[162:163], v[18:19], s[2:3], v[162:163] op_sel_hi:[1,0,1]
	v_pk_fma_f32 v[160:161], v[20:21], s[2:3], v[160:161] op_sel_hi:[1,0,1]
	v_pk_fma_f32 v[158:159], v[22:23], s[2:3], v[158:159] op_sel_hi:[1,0,1]
	v_pk_fma_f32 v[156:157], v[24:25], s[2:3], v[156:157] op_sel_hi:[1,0,1]
	v_pk_fma_f32 v[154:155], v[26:27], s[2:3], v[154:155] op_sel_hi:[1,0,1]
	v_pk_fma_f32 v[152:153], v[28:29], s[2:3], v[152:153] op_sel_hi:[1,0,1]
	v_pk_fma_f32 v[150:151], v[30:31], s[2:3], v[150:151] op_sel_hi:[1,0,1]
	v_readlane_b32 s2, v211, 25
	s_waitcnt vmcnt(20)
	v_cvt_scalef32_pk32_f32_fp6 v[0:31], v[68:73], 1.0
	v_pk_fma_f32 v[68:69], v[0:1], s[2:3], v[74:75] op_sel_hi:[1,0,1]
	v_pk_fma_f32 v[70:71], v[2:3], s[2:3], v[76:77] op_sel_hi:[1,0,1]
	v_pk_fma_f32 v[72:73], v[4:5], s[2:3], v[78:79] op_sel_hi:[1,0,1]
	v_pk_fma_f32 v[74:75], v[6:7], s[2:3], v[174:175] op_sel_hi:[1,0,1]
	v_pk_fma_f32 v[76:77], v[8:9], s[2:3], v[172:173] op_sel_hi:[1,0,1]
	v_pk_fma_f32 v[78:79], v[10:11], s[2:3], v[170:171] op_sel_hi:[1,0,1]
	v_pk_fma_f32 v[168:169], v[12:13], s[2:3], v[168:169] op_sel_hi:[1,0,1]
	v_pk_fma_f32 v[166:167], v[14:15], s[2:3], v[166:167] op_sel_hi:[1,0,1]
	v_pk_fma_f32 v[164:165], v[16:17], s[2:3], v[164:165] op_sel_hi:[1,0,1]
	v_pk_fma_f32 v[162:163], v[18:19], s[2:3], v[162:163] op_sel_hi:[1,0,1]
	v_pk_fma_f32 v[160:161], v[20:21], s[2:3], v[160:161] op_sel_hi:[1,0,1]
	v_pk_fma_f32 v[158:159], v[22:23], s[2:3], v[158:159] op_sel_hi:[1,0,1]
	v_pk_fma_f32 v[156:157], v[24:25], s[2:3], v[156:157] op_sel_hi:[1,0,1]
	v_pk_fma_f32 v[154:155], v[26:27], s[2:3], v[154:155] op_sel_hi:[1,0,1]
	v_pk_fma_f32 v[152:153], v[28:29], s[2:3], v[152:153] op_sel_hi:[1,0,1]
	v_pk_fma_f32 v[150:151], v[30:31], s[2:3], v[150:151] op_sel_hi:[1,0,1]
	v_readlane_b32 s2, v211, 26
	s_waitcnt vmcnt(18)
	v_cvt_scalef32_pk32_f32_fp6 v[0:31], v[56:61], 1.0
	v_pk_fma_f32 v[56:57], v[0:1], s[2:3], v[68:69] op_sel_hi:[1,0,1]
	v_pk_fma_f32 v[58:59], v[2:3], s[2:3], v[70:71] op_sel_hi:[1,0,1]
	v_pk_fma_f32 v[60:61], v[4:5], s[2:3], v[72:73] op_sel_hi:[1,0,1]
	v_pk_fma_f32 v[68:69], v[6:7], s[2:3], v[74:75] op_sel_hi:[1,0,1]
	v_pk_fma_f32 v[70:71], v[8:9], s[2:3], v[76:77] op_sel_hi:[1,0,1]
	v_pk_fma_f32 v[72:73], v[10:11], s[2:3], v[78:79] op_sel_hi:[1,0,1]
	v_pk_fma_f32 v[74:75], v[12:13], s[2:3], v[168:169] op_sel_hi:[1,0,1]
	v_pk_fma_f32 v[76:77], v[14:15], s[2:3], v[166:167] op_sel_hi:[1,0,1]
	v_pk_fma_f32 v[78:79], v[16:17], s[2:3], v[164:165] op_sel_hi:[1,0,1]
	v_pk_fma_f32 v[162:163], v[18:19], s[2:3], v[162:163] op_sel_hi:[1,0,1]
	v_pk_fma_f32 v[160:161], v[20:21], s[2:3], v[160:161] op_sel_hi:[1,0,1]
	v_pk_fma_f32 v[158:159], v[22:23], s[2:3], v[158:159] op_sel_hi:[1,0,1]
	v_pk_fma_f32 v[156:157], v[24:25], s[2:3], v[156:157] op_sel_hi:[1,0,1]
	v_pk_fma_f32 v[154:155], v[26:27], s[2:3], v[154:155] op_sel_hi:[1,0,1]
	v_pk_fma_f32 v[152:153], v[28:29], s[2:3], v[152:153] op_sel_hi:[1,0,1]
	v_pk_fma_f32 v[150:151], v[30:31], s[2:3], v[150:151] op_sel_hi:[1,0,1]
	v_readlane_b32 s2, v211, 27
	s_waitcnt vmcnt(16)
	v_cvt_scalef32_pk32_f32_fp6 v[0:31], v[44:49], 1.0
	v_pk_fma_f32 v[164:165], v[0:1], s[2:3], v[56:57] op_sel_hi:[1,0,1]
	v_pk_fma_f32 v[166:167], v[2:3], s[2:3], v[58:59] op_sel_hi:[1,0,1]
	v_pk_fma_f32 v[168:169], v[4:5], s[2:3], v[60:61] op_sel_hi:[1,0,1]
	v_pk_fma_f32 v[170:171], v[6:7], s[2:3], v[68:69] op_sel_hi:[1,0,1]
	v_pk_fma_f32 v[172:173], v[8:9], s[2:3], v[70:71] op_sel_hi:[1,0,1]
	v_pk_fma_f32 v[174:175], v[10:11], s[2:3], v[72:73] op_sel_hi:[1,0,1]
	v_pk_fma_f32 v[176:177], v[12:13], s[2:3], v[74:75] op_sel_hi:[1,0,1]
	v_pk_fma_f32 v[178:179], v[14:15], s[2:3], v[76:77] op_sel_hi:[1,0,1]
	v_pk_fma_f32 v[180:181], v[16:17], s[2:3], v[78:79] op_sel_hi:[1,0,1]
	v_pk_fma_f32 v[162:163], v[18:19], s[2:3], v[162:163] op_sel_hi:[1,0,1]
	v_pk_fma_f32 v[160:161], v[20:21], s[2:3], v[160:161] op_sel_hi:[1,0,1]
	v_pk_fma_f32 v[158:159], v[22:23], s[2:3], v[158:159] op_sel_hi:[1,0,1]
	v_pk_fma_f32 v[156:157], v[24:25], s[2:3], v[156:157] op_sel_hi:[1,0,1]
	v_pk_fma_f32 v[154:155], v[26:27], s[2:3], v[154:155] op_sel_hi:[1,0,1]
	v_pk_fma_f32 v[152:153], v[28:29], s[2:3], v[152:153] op_sel_hi:[1,0,1]
	v_pk_fma_f32 v[150:151], v[30:31], s[2:3], v[150:151] op_sel_hi:[1,0,1]
	v_readlane_b32 s2, v240, 36
	v_readlane_b32 s3, v240, 37
	v_readlane_b32 s100, v240, 38
	v_readlane_b32 s101, v240, 39
	s_nop 1
	buffer_load_dwordx4 v[74:77], v129, s[44:47], s2 offen
	buffer_load_dwordx2 v[78:79], v210, s[44:47], s2 offen
	buffer_load_dwordx4 v[68:71], v129, s[44:47], s3 offen
	buffer_load_dwordx2 v[72:73], v210, s[44:47], s3 offen
	buffer_load_dwordx4 v[56:59], v129, s[44:47], s100 offen
	buffer_load_dwordx2 v[60:61], v210, s[44:47], s100 offen
	buffer_load_dwordx4 v[44:47], v129, s[44:47], s101 offen
	buffer_load_dwordx2 v[48:49], v210, s[44:47], s101 offen
	v_readlane_b32 s2, v211, 28
	s_waitcnt vmcnt(22)
	v_cvt_scalef32_pk32_f32_fp6 v[0:31], v[62:67], 1.0
	v_pk_fma_f32 v[62:63], v[0:1], s[2:3], v[164:165] op_sel_hi:[1,0,1]
	v_pk_fma_f32 v[64:65], v[2:3], s[2:3], v[166:167] op_sel_hi:[1,0,1]
	v_pk_fma_f32 v[66:67], v[4:5], s[2:3], v[168:169] op_sel_hi:[1,0,1]
	v_pk_fma_f32 v[164:165], v[6:7], s[2:3], v[170:171] op_sel_hi:[1,0,1]
	v_pk_fma_f32 v[166:167], v[8:9], s[2:3], v[172:173] op_sel_hi:[1,0,1]
	v_pk_fma_f32 v[168:169], v[10:11], s[2:3], v[174:175] op_sel_hi:[1,0,1]
	v_pk_fma_f32 v[170:171], v[12:13], s[2:3], v[176:177] op_sel_hi:[1,0,1]
	v_pk_fma_f32 v[172:173], v[14:15], s[2:3], v[178:179] op_sel_hi:[1,0,1]
	v_pk_fma_f32 v[174:175], v[16:17], s[2:3], v[180:181] op_sel_hi:[1,0,1]
	v_pk_fma_f32 v[162:163], v[18:19], s[2:3], v[162:163] op_sel_hi:[1,0,1]
	v_pk_fma_f32 v[160:161], v[20:21], s[2:3], v[160:161] op_sel_hi:[1,0,1]
	v_pk_fma_f32 v[158:159], v[22:23], s[2:3], v[158:159] op_sel_hi:[1,0,1]
	v_pk_fma_f32 v[156:157], v[24:25], s[2:3], v[156:157] op_sel_hi:[1,0,1]
	v_pk_fma_f32 v[154:155], v[26:27], s[2:3], v[154:155] op_sel_hi:[1,0,1]
	v_pk_fma_f32 v[152:153], v[28:29], s[2:3], v[152:153] op_sel_hi:[1,0,1]
	v_pk_fma_f32 v[150:151], v[30:31], s[2:3], v[150:151] op_sel_hi:[1,0,1]
	v_readlane_b32 s2, v211, 29
	s_waitcnt vmcnt(20)
	v_cvt_scalef32_pk32_f32_fp6 v[0:31], v[50:55], 1.0
	v_pk_fma_f32 v[50:51], v[0:1], s[2:3], v[62:63] op_sel_hi:[1,0,1]
	v_pk_fma_f32 v[52:53], v[2:3], s[2:3], v[64:65] op_sel_hi:[1,0,1]
	v_pk_fma_f32 v[54:55], v[4:5], s[2:3], v[66:67] op_sel_hi:[1,0,1]
	v_pk_fma_f32 v[62:63], v[6:7], s[2:3], v[164:165] op_sel_hi:[1,0,1]
	v_pk_fma_f32 v[64:65], v[8:9], s[2:3], v[166:167] op_sel_hi:[1,0,1]
	v_pk_fma_f32 v[66:67], v[10:11], s[2:3], v[168:169] op_sel_hi:[1,0,1]
	v_pk_fma_f32 v[164:165], v[12:13], s[2:3], v[170:171] op_sel_hi:[1,0,1]
	v_pk_fma_f32 v[166:167], v[14:15], s[2:3], v[172:173] op_sel_hi:[1,0,1]
	v_pk_fma_f32 v[168:169], v[16:17], s[2:3], v[174:175] op_sel_hi:[1,0,1]
	v_pk_fma_f32 v[162:163], v[18:19], s[2:3], v[162:163] op_sel_hi:[1,0,1]
	v_pk_fma_f32 v[160:161], v[20:21], s[2:3], v[160:161] op_sel_hi:[1,0,1]
	v_pk_fma_f32 v[158:159], v[22:23], s[2:3], v[158:159] op_sel_hi:[1,0,1]
	v_pk_fma_f32 v[156:157], v[24:25], s[2:3], v[156:157] op_sel_hi:[1,0,1]
	v_pk_fma_f32 v[154:155], v[26:27], s[2:3], v[154:155] op_sel_hi:[1,0,1]
	v_pk_fma_f32 v[152:153], v[28:29], s[2:3], v[152:153] op_sel_hi:[1,0,1]
	v_pk_fma_f32 v[150:151], v[30:31], s[2:3], v[150:151] op_sel_hi:[1,0,1]
	v_readlane_b32 s2, v211, 30
	s_waitcnt vmcnt(18)
	v_cvt_scalef32_pk32_f32_fp6 v[0:31], v[38:43], 1.0
	v_pk_fma_f32 v[38:39], v[0:1], s[2:3], v[50:51] op_sel_hi:[1,0,1]
	v_pk_fma_f32 v[40:41], v[2:3], s[2:3], v[52:53] op_sel_hi:[1,0,1]
	v_pk_fma_f32 v[42:43], v[4:5], s[2:3], v[54:55] op_sel_hi:[1,0,1]
	v_pk_fma_f32 v[50:51], v[6:7], s[2:3], v[62:63] op_sel_hi:[1,0,1]
	v_pk_fma_f32 v[52:53], v[8:9], s[2:3], v[64:65] op_sel_hi:[1,0,1]
	v_pk_fma_f32 v[54:55], v[10:11], s[2:3], v[66:67] op_sel_hi:[1,0,1]
	v_pk_fma_f32 v[62:63], v[12:13], s[2:3], v[164:165] op_sel_hi:[1,0,1]
	v_pk_fma_f32 v[64:65], v[14:15], s[2:3], v[166:167] op_sel_hi:[1,0,1]
	v_pk_fma_f32 v[66:67], v[16:17], s[2:3], v[168:169] op_sel_hi:[1,0,1]
	v_pk_fma_f32 v[162:163], v[18:19], s[2:3], v[162:163] op_sel_hi:[1,0,1]
	v_pk_fma_f32 v[160:161], v[20:21], s[2:3], v[160:161] op_sel_hi:[1,0,1]
	v_pk_fma_f32 v[158:159], v[22:23], s[2:3], v[158:159] op_sel_hi:[1,0,1]
	v_pk_fma_f32 v[156:157], v[24:25], s[2:3], v[156:157] op_sel_hi:[1,0,1]
	v_pk_fma_f32 v[154:155], v[26:27], s[2:3], v[154:155] op_sel_hi:[1,0,1]
	v_pk_fma_f32 v[152:153], v[28:29], s[2:3], v[152:153] op_sel_hi:[1,0,1]
	v_pk_fma_f32 v[150:151], v[30:31], s[2:3], v[150:151] op_sel_hi:[1,0,1]
	v_readlane_b32 s2, v211, 31
	s_waitcnt vmcnt(16)
	v_cvt_scalef32_pk32_f32_fp6 v[0:31], v[32:37], 1.0
	v_pk_fma_f32 v[164:165], v[0:1], s[2:3], v[38:39] op_sel_hi:[1,0,1]
	v_pk_fma_f32 v[166:167], v[2:3], s[2:3], v[40:41] op_sel_hi:[1,0,1]
	v_pk_fma_f32 v[168:169], v[4:5], s[2:3], v[42:43] op_sel_hi:[1,0,1]
	v_pk_fma_f32 v[170:171], v[6:7], s[2:3], v[50:51] op_sel_hi:[1,0,1]
	v_pk_fma_f32 v[172:173], v[8:9], s[2:3], v[52:53] op_sel_hi:[1,0,1]
	v_pk_fma_f32 v[174:175], v[10:11], s[2:3], v[54:55] op_sel_hi:[1,0,1]
	v_pk_fma_f32 v[176:177], v[12:13], s[2:3], v[62:63] op_sel_hi:[1,0,1]
	v_pk_fma_f32 v[178:179], v[14:15], s[2:3], v[64:65] op_sel_hi:[1,0,1]
	v_pk_fma_f32 v[180:181], v[16:17], s[2:3], v[66:67] op_sel_hi:[1,0,1]
	v_pk_fma_f32 v[162:163], v[18:19], s[2:3], v[162:163] op_sel_hi:[1,0,1]
	v_pk_fma_f32 v[160:161], v[20:21], s[2:3], v[160:161] op_sel_hi:[1,0,1]
	v_pk_fma_f32 v[158:159], v[22:23], s[2:3], v[158:159] op_sel_hi:[1,0,1]
	v_pk_fma_f32 v[156:157], v[24:25], s[2:3], v[156:157] op_sel_hi:[1,0,1]
	v_pk_fma_f32 v[154:155], v[26:27], s[2:3], v[154:155] op_sel_hi:[1,0,1]
	v_pk_fma_f32 v[152:153], v[28:29], s[2:3], v[152:153] op_sel_hi:[1,0,1]
	v_pk_fma_f32 v[150:151], v[30:31], s[2:3], v[150:151] op_sel_hi:[1,0,1]
	v_readlane_b32 s2, v240, 40
	v_readlane_b32 s3, v240, 41
	v_readlane_b32 s100, v240, 42
	v_readlane_b32 s101, v240, 43
	s_nop 1
	buffer_load_dwordx4 v[62:65], v129, s[44:47], s2 offen
	buffer_load_dwordx2 v[66:67], v210, s[44:47], s2 offen
	buffer_load_dwordx4 v[50:53], v129, s[44:47], s3 offen
	buffer_load_dwordx2 v[54:55], v210, s[44:47], s3 offen
	buffer_load_dwordx4 v[38:41], v129, s[44:47], s100 offen
	buffer_load_dwordx2 v[42:43], v210, s[44:47], s100 offen
	buffer_load_dwordx4 v[32:35], v129, s[44:47], s101 offen
	buffer_load_dwordx2 v[36:37], v210, s[44:47], s101 offen
	v_readlane_b32 s2, v211, 32
	s_waitcnt vmcnt(22)
	v_cvt_scalef32_pk32_f32_fp6 v[0:31], v[98:103], 1.0
	v_pk_fma_f32 v[98:99], v[0:1], s[2:3], v[164:165] op_sel_hi:[1,0,1]
	v_pk_fma_f32 v[100:101], v[2:3], s[2:3], v[166:167] op_sel_hi:[1,0,1]
	v_pk_fma_f32 v[102:103], v[4:5], s[2:3], v[168:169] op_sel_hi:[1,0,1]
	v_pk_fma_f32 v[164:165], v[6:7], s[2:3], v[170:171] op_sel_hi:[1,0,1]
	v_pk_fma_f32 v[166:167], v[8:9], s[2:3], v[172:173] op_sel_hi:[1,0,1]
	v_pk_fma_f32 v[168:169], v[10:11], s[2:3], v[174:175] op_sel_hi:[1,0,1]
	v_pk_fma_f32 v[170:171], v[12:13], s[2:3], v[176:177] op_sel_hi:[1,0,1]
	v_pk_fma_f32 v[172:173], v[14:15], s[2:3], v[178:179] op_sel_hi:[1,0,1]
	v_pk_fma_f32 v[174:175], v[16:17], s[2:3], v[180:181] op_sel_hi:[1,0,1]
	v_pk_fma_f32 v[162:163], v[18:19], s[2:3], v[162:163] op_sel_hi:[1,0,1]
	v_pk_fma_f32 v[160:161], v[20:21], s[2:3], v[160:161] op_sel_hi:[1,0,1]
	v_pk_fma_f32 v[158:159], v[22:23], s[2:3], v[158:159] op_sel_hi:[1,0,1]
	v_pk_fma_f32 v[156:157], v[24:25], s[2:3], v[156:157] op_sel_hi:[1,0,1]
	v_pk_fma_f32 v[154:155], v[26:27], s[2:3], v[154:155] op_sel_hi:[1,0,1]
	v_pk_fma_f32 v[152:153], v[28:29], s[2:3], v[152:153] op_sel_hi:[1,0,1]
	v_pk_fma_f32 v[150:151], v[30:31], s[2:3], v[150:151] op_sel_hi:[1,0,1]
	v_readlane_b32 s2, v211, 33
	s_waitcnt vmcnt(20)
	v_cvt_scalef32_pk32_f32_fp6 v[0:31], v[92:97], 1.0
	v_pk_fma_f32 v[92:93], v[0:1], s[2:3], v[98:99] op_sel_hi:[1,0,1]
	v_pk_fma_f32 v[94:95], v[2:3], s[2:3], v[100:101] op_sel_hi:[1,0,1]
	v_pk_fma_f32 v[96:97], v[4:5], s[2:3], v[102:103] op_sel_hi:[1,0,1]
	v_pk_fma_f32 v[98:99], v[6:7], s[2:3], v[164:165] op_sel_hi:[1,0,1]
	v_pk_fma_f32 v[100:101], v[8:9], s[2:3], v[166:167] op_sel_hi:[1,0,1]
	v_pk_fma_f32 v[102:103], v[10:11], s[2:3], v[168:169] op_sel_hi:[1,0,1]
	v_pk_fma_f32 v[164:165], v[12:13], s[2:3], v[170:171] op_sel_hi:[1,0,1]
	v_pk_fma_f32 v[166:167], v[14:15], s[2:3], v[172:173] op_sel_hi:[1,0,1]
	v_pk_fma_f32 v[168:169], v[16:17], s[2:3], v[174:175] op_sel_hi:[1,0,1]
	v_pk_fma_f32 v[162:163], v[18:19], s[2:3], v[162:163] op_sel_hi:[1,0,1]
	v_pk_fma_f32 v[160:161], v[20:21], s[2:3], v[160:161] op_sel_hi:[1,0,1]
	v_pk_fma_f32 v[158:159], v[22:23], s[2:3], v[158:159] op_sel_hi:[1,0,1]
	v_pk_fma_f32 v[156:157], v[24:25], s[2:3], v[156:157] op_sel_hi:[1,0,1]
	v_pk_fma_f32 v[154:155], v[26:27], s[2:3], v[154:155] op_sel_hi:[1,0,1]
	v_pk_fma_f32 v[152:153], v[28:29], s[2:3], v[152:153] op_sel_hi:[1,0,1]
	v_pk_fma_f32 v[150:151], v[30:31], s[2:3], v[150:151] op_sel_hi:[1,0,1]
	v_readlane_b32 s2, v211, 34
	s_waitcnt vmcnt(18)
	v_cvt_scalef32_pk32_f32_fp6 v[0:31], v[86:91], 1.0
	v_pk_fma_f32 v[86:87], v[0:1], s[2:3], v[92:93] op_sel_hi:[1,0,1]
	v_pk_fma_f32 v[88:89], v[2:3], s[2:3], v[94:95] op_sel_hi:[1,0,1]
	v_pk_fma_f32 v[90:91], v[4:5], s[2:3], v[96:97] op_sel_hi:[1,0,1]
	v_pk_fma_f32 v[92:93], v[6:7], s[2:3], v[98:99] op_sel_hi:[1,0,1]
	v_pk_fma_f32 v[94:95], v[8:9], s[2:3], v[100:101] op_sel_hi:[1,0,1]
	v_pk_fma_f32 v[96:97], v[10:11], s[2:3], v[102:103] op_sel_hi:[1,0,1]
	v_pk_fma_f32 v[98:99], v[12:13], s[2:3], v[164:165] op_sel_hi:[1,0,1]
	v_pk_fma_f32 v[100:101], v[14:15], s[2:3], v[166:167] op_sel_hi:[1,0,1]
	v_pk_fma_f32 v[102:103], v[16:17], s[2:3], v[168:169] op_sel_hi:[1,0,1]
	v_pk_fma_f32 v[162:163], v[18:19], s[2:3], v[162:163] op_sel_hi:[1,0,1]
	v_pk_fma_f32 v[160:161], v[20:21], s[2:3], v[160:161] op_sel_hi:[1,0,1]
	v_pk_fma_f32 v[158:159], v[22:23], s[2:3], v[158:159] op_sel_hi:[1,0,1]
	v_pk_fma_f32 v[156:157], v[24:25], s[2:3], v[156:157] op_sel_hi:[1,0,1]
	v_pk_fma_f32 v[154:155], v[26:27], s[2:3], v[154:155] op_sel_hi:[1,0,1]
	v_pk_fma_f32 v[152:153], v[28:29], s[2:3], v[152:153] op_sel_hi:[1,0,1]
	v_pk_fma_f32 v[150:151], v[30:31], s[2:3], v[150:151] op_sel_hi:[1,0,1]
	v_readlane_b32 s2, v211, 35
	s_waitcnt vmcnt(16)
	v_cvt_scalef32_pk32_f32_fp6 v[0:31], v[80:85], 1.0
	v_pk_fma_f32 v[180:181], v[0:1], s[2:3], v[86:87] op_sel_hi:[1,0,1]
	v_pk_fma_f32 v[178:179], v[2:3], s[2:3], v[88:89] op_sel_hi:[1,0,1]
	v_pk_fma_f32 v[176:177], v[4:5], s[2:3], v[90:91] op_sel_hi:[1,0,1]
	v_pk_fma_f32 v[174:175], v[6:7], s[2:3], v[92:93] op_sel_hi:[1,0,1]
	v_pk_fma_f32 v[172:173], v[8:9], s[2:3], v[94:95] op_sel_hi:[1,0,1]
	v_pk_fma_f32 v[170:171], v[10:11], s[2:3], v[96:97] op_sel_hi:[1,0,1]
	v_pk_fma_f32 v[168:169], v[12:13], s[2:3], v[98:99] op_sel_hi:[1,0,1]
	v_pk_fma_f32 v[166:167], v[14:15], s[2:3], v[100:101] op_sel_hi:[1,0,1]
	v_pk_fma_f32 v[164:165], v[16:17], s[2:3], v[102:103] op_sel_hi:[1,0,1]
	v_pk_fma_f32 v[162:163], v[18:19], s[2:3], v[162:163] op_sel_hi:[1,0,1]
	v_pk_fma_f32 v[160:161], v[20:21], s[2:3], v[160:161] op_sel_hi:[1,0,1]
	v_pk_fma_f32 v[158:159], v[22:23], s[2:3], v[158:159] op_sel_hi:[1,0,1]
	v_pk_fma_f32 v[156:157], v[24:25], s[2:3], v[156:157] op_sel_hi:[1,0,1]
	v_pk_fma_f32 v[154:155], v[26:27], s[2:3], v[154:155] op_sel_hi:[1,0,1]
	v_pk_fma_f32 v[152:153], v[28:29], s[2:3], v[152:153] op_sel_hi:[1,0,1]
	v_pk_fma_f32 v[150:151], v[30:31], s[2:3], v[150:151] op_sel_hi:[1,0,1]
	v_readlane_b32 s2, v240, 44
	v_readlane_b32 s3, v240, 45
	v_readlane_b32 s100, v240, 46
	v_readlane_b32 s101, v240, 47
	s_nop 1
	buffer_load_dwordx4 v[98:101], v129, s[44:47], s2 offen
	buffer_load_dwordx2 v[102:103], v210, s[44:47], s2 offen
	buffer_load_dwordx4 v[92:95], v129, s[44:47], s3 offen
	buffer_load_dwordx2 v[96:97], v210, s[44:47], s3 offen
	buffer_load_dwordx4 v[86:89], v129, s[44:47], s100 offen
	buffer_load_dwordx2 v[90:91], v210, s[44:47], s100 offen
	buffer_load_dwordx4 v[80:83], v129, s[44:47], s101 offen
	buffer_load_dwordx2 v[84:85], v210, s[44:47], s101 offen
	v_readlane_b32 s2, v211, 36
	s_waitcnt vmcnt(22)
	v_cvt_scalef32_pk32_f32_fp6 v[0:31], v[74:79], 1.0
	v_pk_fma_f32 v[74:75], v[0:1], s[2:3], v[180:181] op_sel_hi:[1,0,1]
	v_pk_fma_f32 v[76:77], v[2:3], s[2:3], v[178:179] op_sel_hi:[1,0,1]
	v_pk_fma_f32 v[78:79], v[4:5], s[2:3], v[176:177] op_sel_hi:[1,0,1]
	v_pk_fma_f32 v[174:175], v[6:7], s[2:3], v[174:175] op_sel_hi:[1,0,1]
	v_pk_fma_f32 v[172:173], v[8:9], s[2:3], v[172:173] op_sel_hi:[1,0,1]
	v_pk_fma_f32 v[170:171], v[10:11], s[2:3], v[170:171] op_sel_hi:[1,0,1]
	v_pk_fma_f32 v[168:169], v[12:13], s[2:3], v[168:169] op_sel_hi:[1,0,1]
	v_pk_fma_f32 v[166:167], v[14:15], s[2:3], v[166:167] op_sel_hi:[1,0,1]
	v_pk_fma_f32 v[164:165], v[16:17], s[2:3], v[164:165] op_sel_hi:[1,0,1]
	v_pk_fma_f32 v[162:163], v[18:19], s[2:3], v[162:163] op_sel_hi:[1,0,1]
	v_pk_fma_f32 v[160:161], v[20:21], s[2:3], v[160:161] op_sel_hi:[1,0,1]
	v_pk_fma_f32 v[158:159], v[22:23], s[2:3], v[158:159] op_sel_hi:[1,0,1]
	v_pk_fma_f32 v[156:157], v[24:25], s[2:3], v[156:157] op_sel_hi:[1,0,1]
	v_pk_fma_f32 v[154:155], v[26:27], s[2:3], v[154:155] op_sel_hi:[1,0,1]
	v_pk_fma_f32 v[152:153], v[28:29], s[2:3], v[152:153] op_sel_hi:[1,0,1]
	v_pk_fma_f32 v[150:151], v[30:31], s[2:3], v[150:151] op_sel_hi:[1,0,1]
	v_readlane_b32 s2, v211, 37
	s_waitcnt vmcnt(20)
	v_cvt_scalef32_pk32_f32_fp6 v[0:31], v[68:73], 1.0
	v_pk_fma_f32 v[68:69], v[0:1], s[2:3], v[74:75] op_sel_hi:[1,0,1]
	v_pk_fma_f32 v[70:71], v[2:3], s[2:3], v[76:77] op_sel_hi:[1,0,1]
	v_pk_fma_f32 v[72:73], v[4:5], s[2:3], v[78:79] op_sel_hi:[1,0,1]
	v_pk_fma_f32 v[74:75], v[6:7], s[2:3], v[174:175] op_sel_hi:[1,0,1]
	v_pk_fma_f32 v[76:77], v[8:9], s[2:3], v[172:173] op_sel_hi:[1,0,1]
	v_pk_fma_f32 v[78:79], v[10:11], s[2:3], v[170:171] op_sel_hi:[1,0,1]
	v_pk_fma_f32 v[168:169], v[12:13], s[2:3], v[168:169] op_sel_hi:[1,0,1]
	v_pk_fma_f32 v[166:167], v[14:15], s[2:3], v[166:167] op_sel_hi:[1,0,1]
	v_pk_fma_f32 v[164:165], v[16:17], s[2:3], v[164:165] op_sel_hi:[1,0,1]
	v_pk_fma_f32 v[162:163], v[18:19], s[2:3], v[162:163] op_sel_hi:[1,0,1]
	v_pk_fma_f32 v[160:161], v[20:21], s[2:3], v[160:161] op_sel_hi:[1,0,1]
	v_pk_fma_f32 v[158:159], v[22:23], s[2:3], v[158:159] op_sel_hi:[1,0,1]
	v_pk_fma_f32 v[156:157], v[24:25], s[2:3], v[156:157] op_sel_hi:[1,0,1]
	v_pk_fma_f32 v[154:155], v[26:27], s[2:3], v[154:155] op_sel_hi:[1,0,1]
	v_pk_fma_f32 v[152:153], v[28:29], s[2:3], v[152:153] op_sel_hi:[1,0,1]
	v_pk_fma_f32 v[150:151], v[30:31], s[2:3], v[150:151] op_sel_hi:[1,0,1]
	v_readlane_b32 s2, v211, 38
	s_waitcnt vmcnt(18)
	v_cvt_scalef32_pk32_f32_fp6 v[0:31], v[56:61], 1.0
	v_pk_fma_f32 v[56:57], v[0:1], s[2:3], v[68:69] op_sel_hi:[1,0,1]
	v_pk_fma_f32 v[58:59], v[2:3], s[2:3], v[70:71] op_sel_hi:[1,0,1]
	v_pk_fma_f32 v[60:61], v[4:5], s[2:3], v[72:73] op_sel_hi:[1,0,1]
	v_pk_fma_f32 v[68:69], v[6:7], s[2:3], v[74:75] op_sel_hi:[1,0,1]
	v_pk_fma_f32 v[70:71], v[8:9], s[2:3], v[76:77] op_sel_hi:[1,0,1]
	v_pk_fma_f32 v[72:73], v[10:11], s[2:3], v[78:79] op_sel_hi:[1,0,1]
	v_pk_fma_f32 v[74:75], v[12:13], s[2:3], v[168:169] op_sel_hi:[1,0,1]
	v_pk_fma_f32 v[76:77], v[14:15], s[2:3], v[166:167] op_sel_hi:[1,0,1]
	v_pk_fma_f32 v[78:79], v[16:17], s[2:3], v[164:165] op_sel_hi:[1,0,1]
	v_pk_fma_f32 v[162:163], v[18:19], s[2:3], v[162:163] op_sel_hi:[1,0,1]
	v_pk_fma_f32 v[160:161], v[20:21], s[2:3], v[160:161] op_sel_hi:[1,0,1]
	v_pk_fma_f32 v[158:159], v[22:23], s[2:3], v[158:159] op_sel_hi:[1,0,1]
	v_pk_fma_f32 v[156:157], v[24:25], s[2:3], v[156:157] op_sel_hi:[1,0,1]
	v_pk_fma_f32 v[154:155], v[26:27], s[2:3], v[154:155] op_sel_hi:[1,0,1]
	v_pk_fma_f32 v[152:153], v[28:29], s[2:3], v[152:153] op_sel_hi:[1,0,1]
	v_pk_fma_f32 v[150:151], v[30:31], s[2:3], v[150:151] op_sel_hi:[1,0,1]
	v_readlane_b32 s2, v211, 39
	s_waitcnt vmcnt(16)
	v_cvt_scalef32_pk32_f32_fp6 v[0:31], v[44:49], 1.0
	v_pk_fma_f32 v[164:165], v[0:1], s[2:3], v[56:57] op_sel_hi:[1,0,1]
	v_pk_fma_f32 v[166:167], v[2:3], s[2:3], v[58:59] op_sel_hi:[1,0,1]
	v_pk_fma_f32 v[168:169], v[4:5], s[2:3], v[60:61] op_sel_hi:[1,0,1]
	v_pk_fma_f32 v[170:171], v[6:7], s[2:3], v[68:69] op_sel_hi:[1,0,1]
	v_pk_fma_f32 v[172:173], v[8:9], s[2:3], v[70:71] op_sel_hi:[1,0,1]
	v_pk_fma_f32 v[174:175], v[10:11], s[2:3], v[72:73] op_sel_hi:[1,0,1]
	v_pk_fma_f32 v[176:177], v[12:13], s[2:3], v[74:75] op_sel_hi:[1,0,1]
	v_pk_fma_f32 v[178:179], v[14:15], s[2:3], v[76:77] op_sel_hi:[1,0,1]
	v_pk_fma_f32 v[180:181], v[16:17], s[2:3], v[78:79] op_sel_hi:[1,0,1]
	v_pk_fma_f32 v[162:163], v[18:19], s[2:3], v[162:163] op_sel_hi:[1,0,1]
	v_pk_fma_f32 v[160:161], v[20:21], s[2:3], v[160:161] op_sel_hi:[1,0,1]
	v_pk_fma_f32 v[158:159], v[22:23], s[2:3], v[158:159] op_sel_hi:[1,0,1]
	v_pk_fma_f32 v[156:157], v[24:25], s[2:3], v[156:157] op_sel_hi:[1,0,1]
	v_pk_fma_f32 v[154:155], v[26:27], s[2:3], v[154:155] op_sel_hi:[1,0,1]
	v_pk_fma_f32 v[152:153], v[28:29], s[2:3], v[152:153] op_sel_hi:[1,0,1]
	v_pk_fma_f32 v[150:151], v[30:31], s[2:3], v[150:151] op_sel_hi:[1,0,1]
	v_readlane_b32 s2, v240, 48
	v_readlane_b32 s3, v240, 49
	v_readlane_b32 s100, v240, 50
	v_readlane_b32 s101, v240, 51
	s_nop 1
	buffer_load_dwordx4 v[74:77], v129, s[44:47], s2 offen
	buffer_load_dwordx2 v[78:79], v210, s[44:47], s2 offen
	buffer_load_dwordx4 v[68:71], v129, s[44:47], s3 offen
	buffer_load_dwordx2 v[72:73], v210, s[44:47], s3 offen
	buffer_load_dwordx4 v[56:59], v129, s[44:47], s100 offen
	buffer_load_dwordx2 v[60:61], v210, s[44:47], s100 offen
	buffer_load_dwordx4 v[44:47], v129, s[44:47], s101 offen
	buffer_load_dwordx2 v[48:49], v210, s[44:47], s101 offen
	v_readlane_b32 s2, v211, 40
	s_waitcnt vmcnt(22)
	v_cvt_scalef32_pk32_f32_fp6 v[0:31], v[62:67], 1.0
	v_pk_fma_f32 v[62:63], v[0:1], s[2:3], v[164:165] op_sel_hi:[1,0,1]
	v_pk_fma_f32 v[64:65], v[2:3], s[2:3], v[166:167] op_sel_hi:[1,0,1]
	v_pk_fma_f32 v[66:67], v[4:5], s[2:3], v[168:169] op_sel_hi:[1,0,1]
	v_pk_fma_f32 v[164:165], v[6:7], s[2:3], v[170:171] op_sel_hi:[1,0,1]
	v_pk_fma_f32 v[166:167], v[8:9], s[2:3], v[172:173] op_sel_hi:[1,0,1]
	v_pk_fma_f32 v[168:169], v[10:11], s[2:3], v[174:175] op_sel_hi:[1,0,1]
	v_pk_fma_f32 v[170:171], v[12:13], s[2:3], v[176:177] op_sel_hi:[1,0,1]
	v_pk_fma_f32 v[172:173], v[14:15], s[2:3], v[178:179] op_sel_hi:[1,0,1]
	v_pk_fma_f32 v[174:175], v[16:17], s[2:3], v[180:181] op_sel_hi:[1,0,1]
	v_pk_fma_f32 v[162:163], v[18:19], s[2:3], v[162:163] op_sel_hi:[1,0,1]
	v_pk_fma_f32 v[160:161], v[20:21], s[2:3], v[160:161] op_sel_hi:[1,0,1]
	v_pk_fma_f32 v[158:159], v[22:23], s[2:3], v[158:159] op_sel_hi:[1,0,1]
	v_pk_fma_f32 v[156:157], v[24:25], s[2:3], v[156:157] op_sel_hi:[1,0,1]
	v_pk_fma_f32 v[154:155], v[26:27], s[2:3], v[154:155] op_sel_hi:[1,0,1]
	v_pk_fma_f32 v[152:153], v[28:29], s[2:3], v[152:153] op_sel_hi:[1,0,1]
	v_pk_fma_f32 v[150:151], v[30:31], s[2:3], v[150:151] op_sel_hi:[1,0,1]
	v_readlane_b32 s2, v211, 41
	s_waitcnt vmcnt(20)
	v_cvt_scalef32_pk32_f32_fp6 v[0:31], v[50:55], 1.0
	v_pk_fma_f32 v[50:51], v[0:1], s[2:3], v[62:63] op_sel_hi:[1,0,1]
	v_pk_fma_f32 v[52:53], v[2:3], s[2:3], v[64:65] op_sel_hi:[1,0,1]
	v_pk_fma_f32 v[54:55], v[4:5], s[2:3], v[66:67] op_sel_hi:[1,0,1]
	v_pk_fma_f32 v[62:63], v[6:7], s[2:3], v[164:165] op_sel_hi:[1,0,1]
	v_pk_fma_f32 v[64:65], v[8:9], s[2:3], v[166:167] op_sel_hi:[1,0,1]
	v_pk_fma_f32 v[66:67], v[10:11], s[2:3], v[168:169] op_sel_hi:[1,0,1]
	v_pk_fma_f32 v[164:165], v[12:13], s[2:3], v[170:171] op_sel_hi:[1,0,1]
	v_pk_fma_f32 v[166:167], v[14:15], s[2:3], v[172:173] op_sel_hi:[1,0,1]
	v_pk_fma_f32 v[168:169], v[16:17], s[2:3], v[174:175] op_sel_hi:[1,0,1]
	v_pk_fma_f32 v[162:163], v[18:19], s[2:3], v[162:163] op_sel_hi:[1,0,1]
	v_pk_fma_f32 v[160:161], v[20:21], s[2:3], v[160:161] op_sel_hi:[1,0,1]
	v_pk_fma_f32 v[158:159], v[22:23], s[2:3], v[158:159] op_sel_hi:[1,0,1]
	v_pk_fma_f32 v[156:157], v[24:25], s[2:3], v[156:157] op_sel_hi:[1,0,1]
	v_pk_fma_f32 v[154:155], v[26:27], s[2:3], v[154:155] op_sel_hi:[1,0,1]
	v_pk_fma_f32 v[152:153], v[28:29], s[2:3], v[152:153] op_sel_hi:[1,0,1]
	v_pk_fma_f32 v[150:151], v[30:31], s[2:3], v[150:151] op_sel_hi:[1,0,1]
	v_readlane_b32 s2, v211, 42
	s_waitcnt vmcnt(18)
	v_cvt_scalef32_pk32_f32_fp6 v[0:31], v[38:43], 1.0
	v_pk_fma_f32 v[38:39], v[0:1], s[2:3], v[50:51] op_sel_hi:[1,0,1]
	v_pk_fma_f32 v[40:41], v[2:3], s[2:3], v[52:53] op_sel_hi:[1,0,1]
	v_pk_fma_f32 v[42:43], v[4:5], s[2:3], v[54:55] op_sel_hi:[1,0,1]
	v_pk_fma_f32 v[50:51], v[6:7], s[2:3], v[62:63] op_sel_hi:[1,0,1]
	v_pk_fma_f32 v[52:53], v[8:9], s[2:3], v[64:65] op_sel_hi:[1,0,1]
	v_pk_fma_f32 v[54:55], v[10:11], s[2:3], v[66:67] op_sel_hi:[1,0,1]
	v_pk_fma_f32 v[62:63], v[12:13], s[2:3], v[164:165] op_sel_hi:[1,0,1]
	v_pk_fma_f32 v[64:65], v[14:15], s[2:3], v[166:167] op_sel_hi:[1,0,1]
	v_pk_fma_f32 v[66:67], v[16:17], s[2:3], v[168:169] op_sel_hi:[1,0,1]
	v_pk_fma_f32 v[162:163], v[18:19], s[2:3], v[162:163] op_sel_hi:[1,0,1]
	v_pk_fma_f32 v[160:161], v[20:21], s[2:3], v[160:161] op_sel_hi:[1,0,1]
	v_pk_fma_f32 v[158:159], v[22:23], s[2:3], v[158:159] op_sel_hi:[1,0,1]
	v_pk_fma_f32 v[156:157], v[24:25], s[2:3], v[156:157] op_sel_hi:[1,0,1]
	v_pk_fma_f32 v[154:155], v[26:27], s[2:3], v[154:155] op_sel_hi:[1,0,1]
	v_pk_fma_f32 v[152:153], v[28:29], s[2:3], v[152:153] op_sel_hi:[1,0,1]
	v_pk_fma_f32 v[150:151], v[30:31], s[2:3], v[150:151] op_sel_hi:[1,0,1]
	v_readlane_b32 s2, v211, 43
	s_waitcnt vmcnt(16)
	v_cvt_scalef32_pk32_f32_fp6 v[0:31], v[32:37], 1.0
	v_pk_fma_f32 v[164:165], v[0:1], s[2:3], v[38:39] op_sel_hi:[1,0,1]
	v_pk_fma_f32 v[166:167], v[2:3], s[2:3], v[40:41] op_sel_hi:[1,0,1]
	v_pk_fma_f32 v[168:169], v[4:5], s[2:3], v[42:43] op_sel_hi:[1,0,1]
	v_pk_fma_f32 v[170:171], v[6:7], s[2:3], v[50:51] op_sel_hi:[1,0,1]
	v_pk_fma_f32 v[172:173], v[8:9], s[2:3], v[52:53] op_sel_hi:[1,0,1]
	v_pk_fma_f32 v[174:175], v[10:11], s[2:3], v[54:55] op_sel_hi:[1,0,1]
	v_pk_fma_f32 v[176:177], v[12:13], s[2:3], v[62:63] op_sel_hi:[1,0,1]
	v_pk_fma_f32 v[178:179], v[14:15], s[2:3], v[64:65] op_sel_hi:[1,0,1]
	v_pk_fma_f32 v[180:181], v[16:17], s[2:3], v[66:67] op_sel_hi:[1,0,1]
	v_pk_fma_f32 v[162:163], v[18:19], s[2:3], v[162:163] op_sel_hi:[1,0,1]
	v_pk_fma_f32 v[160:161], v[20:21], s[2:3], v[160:161] op_sel_hi:[1,0,1]
	v_pk_fma_f32 v[158:159], v[22:23], s[2:3], v[158:159] op_sel_hi:[1,0,1]
	v_pk_fma_f32 v[156:157], v[24:25], s[2:3], v[156:157] op_sel_hi:[1,0,1]
	v_pk_fma_f32 v[154:155], v[26:27], s[2:3], v[154:155] op_sel_hi:[1,0,1]
	v_pk_fma_f32 v[152:153], v[28:29], s[2:3], v[152:153] op_sel_hi:[1,0,1]
	v_pk_fma_f32 v[150:151], v[30:31], s[2:3], v[150:151] op_sel_hi:[1,0,1]
	v_readlane_b32 s2, v240, 52
	v_readlane_b32 s3, v240, 53
	v_readlane_b32 s100, v240, 54
	v_readlane_b32 s101, v240, 55
	s_nop 1
	buffer_load_dwordx4 v[62:65], v129, s[44:47], s2 offen
	buffer_load_dwordx2 v[66:67], v210, s[44:47], s2 offen
	buffer_load_dwordx4 v[50:53], v129, s[44:47], s3 offen
	buffer_load_dwordx2 v[54:55], v210, s[44:47], s3 offen
	buffer_load_dwordx4 v[38:41], v129, s[44:47], s100 offen
	buffer_load_dwordx2 v[42:43], v210, s[44:47], s100 offen
	buffer_load_dwordx4 v[32:35], v129, s[44:47], s101 offen
	buffer_load_dwordx2 v[36:37], v210, s[44:47], s101 offen
	v_readlane_b32 s2, v211, 44
	s_waitcnt vmcnt(22)
	v_cvt_scalef32_pk32_f32_fp6 v[0:31], v[98:103], 1.0
	v_pk_fma_f32 v[98:99], v[0:1], s[2:3], v[164:165] op_sel_hi:[1,0,1]
	v_pk_fma_f32 v[100:101], v[2:3], s[2:3], v[166:167] op_sel_hi:[1,0,1]
	v_pk_fma_f32 v[102:103], v[4:5], s[2:3], v[168:169] op_sel_hi:[1,0,1]
	v_pk_fma_f32 v[164:165], v[6:7], s[2:3], v[170:171] op_sel_hi:[1,0,1]
	v_pk_fma_f32 v[166:167], v[8:9], s[2:3], v[172:173] op_sel_hi:[1,0,1]
	v_pk_fma_f32 v[168:169], v[10:11], s[2:3], v[174:175] op_sel_hi:[1,0,1]
	v_pk_fma_f32 v[170:171], v[12:13], s[2:3], v[176:177] op_sel_hi:[1,0,1]
	v_pk_fma_f32 v[172:173], v[14:15], s[2:3], v[178:179] op_sel_hi:[1,0,1]
	v_pk_fma_f32 v[174:175], v[16:17], s[2:3], v[180:181] op_sel_hi:[1,0,1]
	v_pk_fma_f32 v[162:163], v[18:19], s[2:3], v[162:163] op_sel_hi:[1,0,1]
	v_pk_fma_f32 v[160:161], v[20:21], s[2:3], v[160:161] op_sel_hi:[1,0,1]
	v_pk_fma_f32 v[158:159], v[22:23], s[2:3], v[158:159] op_sel_hi:[1,0,1]
	v_pk_fma_f32 v[156:157], v[24:25], s[2:3], v[156:157] op_sel_hi:[1,0,1]
	v_pk_fma_f32 v[154:155], v[26:27], s[2:3], v[154:155] op_sel_hi:[1,0,1]
	v_pk_fma_f32 v[152:153], v[28:29], s[2:3], v[152:153] op_sel_hi:[1,0,1]
	v_pk_fma_f32 v[150:151], v[30:31], s[2:3], v[150:151] op_sel_hi:[1,0,1]
	v_readlane_b32 s2, v211, 45
	s_waitcnt vmcnt(20)
	v_cvt_scalef32_pk32_f32_fp6 v[0:31], v[92:97], 1.0
	v_pk_fma_f32 v[92:93], v[0:1], s[2:3], v[98:99] op_sel_hi:[1,0,1]
	v_pk_fma_f32 v[94:95], v[2:3], s[2:3], v[100:101] op_sel_hi:[1,0,1]
	v_pk_fma_f32 v[96:97], v[4:5], s[2:3], v[102:103] op_sel_hi:[1,0,1]
	v_pk_fma_f32 v[98:99], v[6:7], s[2:3], v[164:165] op_sel_hi:[1,0,1]
	v_pk_fma_f32 v[100:101], v[8:9], s[2:3], v[166:167] op_sel_hi:[1,0,1]
	v_pk_fma_f32 v[102:103], v[10:11], s[2:3], v[168:169] op_sel_hi:[1,0,1]
	v_pk_fma_f32 v[164:165], v[12:13], s[2:3], v[170:171] op_sel_hi:[1,0,1]
	v_pk_fma_f32 v[166:167], v[14:15], s[2:3], v[172:173] op_sel_hi:[1,0,1]
	v_pk_fma_f32 v[168:169], v[16:17], s[2:3], v[174:175] op_sel_hi:[1,0,1]
	v_pk_fma_f32 v[162:163], v[18:19], s[2:3], v[162:163] op_sel_hi:[1,0,1]
	v_pk_fma_f32 v[160:161], v[20:21], s[2:3], v[160:161] op_sel_hi:[1,0,1]
	v_pk_fma_f32 v[158:159], v[22:23], s[2:3], v[158:159] op_sel_hi:[1,0,1]
	v_pk_fma_f32 v[156:157], v[24:25], s[2:3], v[156:157] op_sel_hi:[1,0,1]
	v_pk_fma_f32 v[154:155], v[26:27], s[2:3], v[154:155] op_sel_hi:[1,0,1]
	v_pk_fma_f32 v[152:153], v[28:29], s[2:3], v[152:153] op_sel_hi:[1,0,1]
	v_pk_fma_f32 v[150:151], v[30:31], s[2:3], v[150:151] op_sel_hi:[1,0,1]
	v_readlane_b32 s2, v211, 46
	s_waitcnt vmcnt(18)
	v_cvt_scalef32_pk32_f32_fp6 v[0:31], v[86:91], 1.0
	v_pk_fma_f32 v[86:87], v[0:1], s[2:3], v[92:93] op_sel_hi:[1,0,1]
	v_pk_fma_f32 v[88:89], v[2:3], s[2:3], v[94:95] op_sel_hi:[1,0,1]
	v_pk_fma_f32 v[90:91], v[4:5], s[2:3], v[96:97] op_sel_hi:[1,0,1]
	v_pk_fma_f32 v[92:93], v[6:7], s[2:3], v[98:99] op_sel_hi:[1,0,1]
	v_pk_fma_f32 v[94:95], v[8:9], s[2:3], v[100:101] op_sel_hi:[1,0,1]
	v_pk_fma_f32 v[96:97], v[10:11], s[2:3], v[102:103] op_sel_hi:[1,0,1]
	v_pk_fma_f32 v[98:99], v[12:13], s[2:3], v[164:165] op_sel_hi:[1,0,1]
	v_pk_fma_f32 v[100:101], v[14:15], s[2:3], v[166:167] op_sel_hi:[1,0,1]
	v_pk_fma_f32 v[102:103], v[16:17], s[2:3], v[168:169] op_sel_hi:[1,0,1]
	v_pk_fma_f32 v[162:163], v[18:19], s[2:3], v[162:163] op_sel_hi:[1,0,1]
	v_pk_fma_f32 v[160:161], v[20:21], s[2:3], v[160:161] op_sel_hi:[1,0,1]
	v_pk_fma_f32 v[158:159], v[22:23], s[2:3], v[158:159] op_sel_hi:[1,0,1]
	v_pk_fma_f32 v[156:157], v[24:25], s[2:3], v[156:157] op_sel_hi:[1,0,1]
	v_pk_fma_f32 v[154:155], v[26:27], s[2:3], v[154:155] op_sel_hi:[1,0,1]
	v_pk_fma_f32 v[152:153], v[28:29], s[2:3], v[152:153] op_sel_hi:[1,0,1]
	v_pk_fma_f32 v[150:151], v[30:31], s[2:3], v[150:151] op_sel_hi:[1,0,1]
	v_readlane_b32 s2, v211, 47
	s_waitcnt vmcnt(16)
	v_cvt_scalef32_pk32_f32_fp6 v[0:31], v[80:85], 1.0
	v_pk_fma_f32 v[180:181], v[0:1], s[2:3], v[86:87] op_sel_hi:[1,0,1]
	v_pk_fma_f32 v[178:179], v[2:3], s[2:3], v[88:89] op_sel_hi:[1,0,1]
	v_pk_fma_f32 v[176:177], v[4:5], s[2:3], v[90:91] op_sel_hi:[1,0,1]
	v_pk_fma_f32 v[174:175], v[6:7], s[2:3], v[92:93] op_sel_hi:[1,0,1]
	v_pk_fma_f32 v[172:173], v[8:9], s[2:3], v[94:95] op_sel_hi:[1,0,1]
	v_pk_fma_f32 v[170:171], v[10:11], s[2:3], v[96:97] op_sel_hi:[1,0,1]
	v_pk_fma_f32 v[168:169], v[12:13], s[2:3], v[98:99] op_sel_hi:[1,0,1]
	v_pk_fma_f32 v[166:167], v[14:15], s[2:3], v[100:101] op_sel_hi:[1,0,1]
	v_pk_fma_f32 v[164:165], v[16:17], s[2:3], v[102:103] op_sel_hi:[1,0,1]
	v_pk_fma_f32 v[162:163], v[18:19], s[2:3], v[162:163] op_sel_hi:[1,0,1]
	v_pk_fma_f32 v[160:161], v[20:21], s[2:3], v[160:161] op_sel_hi:[1,0,1]
	v_pk_fma_f32 v[158:159], v[22:23], s[2:3], v[158:159] op_sel_hi:[1,0,1]
	v_pk_fma_f32 v[156:157], v[24:25], s[2:3], v[156:157] op_sel_hi:[1,0,1]
	v_pk_fma_f32 v[154:155], v[26:27], s[2:3], v[154:155] op_sel_hi:[1,0,1]
	v_pk_fma_f32 v[152:153], v[28:29], s[2:3], v[152:153] op_sel_hi:[1,0,1]
	v_pk_fma_f32 v[150:151], v[30:31], s[2:3], v[150:151] op_sel_hi:[1,0,1]
	v_readlane_b32 s2, v240, 56
	v_readlane_b32 s3, v240, 57
	v_readlane_b32 s100, v240, 58
	v_readlane_b32 s101, v240, 59
	s_nop 1
	buffer_load_dwordx4 v[98:101], v129, s[44:47], s2 offen
	buffer_load_dwordx2 v[102:103], v210, s[44:47], s2 offen
	buffer_load_dwordx4 v[92:95], v129, s[44:47], s3 offen
	buffer_load_dwordx2 v[96:97], v210, s[44:47], s3 offen
	buffer_load_dwordx4 v[86:89], v129, s[44:47], s100 offen
	buffer_load_dwordx2 v[90:91], v210, s[44:47], s100 offen
	buffer_load_dwordx4 v[80:83], v129, s[44:47], s101 offen
	buffer_load_dwordx2 v[84:85], v210, s[44:47], s101 offen
	v_readlane_b32 s2, v211, 48
	s_waitcnt vmcnt(22)
	v_cvt_scalef32_pk32_f32_fp6 v[0:31], v[74:79], 1.0
	v_pk_fma_f32 v[74:75], v[0:1], s[2:3], v[180:181] op_sel_hi:[1,0,1]
	v_pk_fma_f32 v[76:77], v[2:3], s[2:3], v[178:179] op_sel_hi:[1,0,1]
	v_pk_fma_f32 v[78:79], v[4:5], s[2:3], v[176:177] op_sel_hi:[1,0,1]
	v_pk_fma_f32 v[174:175], v[6:7], s[2:3], v[174:175] op_sel_hi:[1,0,1]
	v_pk_fma_f32 v[172:173], v[8:9], s[2:3], v[172:173] op_sel_hi:[1,0,1]
	v_pk_fma_f32 v[170:171], v[10:11], s[2:3], v[170:171] op_sel_hi:[1,0,1]
	v_pk_fma_f32 v[168:169], v[12:13], s[2:3], v[168:169] op_sel_hi:[1,0,1]
	v_pk_fma_f32 v[166:167], v[14:15], s[2:3], v[166:167] op_sel_hi:[1,0,1]
	v_pk_fma_f32 v[164:165], v[16:17], s[2:3], v[164:165] op_sel_hi:[1,0,1]
	v_pk_fma_f32 v[162:163], v[18:19], s[2:3], v[162:163] op_sel_hi:[1,0,1]
	v_pk_fma_f32 v[160:161], v[20:21], s[2:3], v[160:161] op_sel_hi:[1,0,1]
	v_pk_fma_f32 v[158:159], v[22:23], s[2:3], v[158:159] op_sel_hi:[1,0,1]
	v_pk_fma_f32 v[156:157], v[24:25], s[2:3], v[156:157] op_sel_hi:[1,0,1]
	v_pk_fma_f32 v[154:155], v[26:27], s[2:3], v[154:155] op_sel_hi:[1,0,1]
	v_pk_fma_f32 v[152:153], v[28:29], s[2:3], v[152:153] op_sel_hi:[1,0,1]
	v_pk_fma_f32 v[150:151], v[30:31], s[2:3], v[150:151] op_sel_hi:[1,0,1]
	v_readlane_b32 s2, v211, 49
	s_waitcnt vmcnt(20)
	v_cvt_scalef32_pk32_f32_fp6 v[0:31], v[68:73], 1.0
	v_pk_fma_f32 v[68:69], v[0:1], s[2:3], v[74:75] op_sel_hi:[1,0,1]
	v_pk_fma_f32 v[70:71], v[2:3], s[2:3], v[76:77] op_sel_hi:[1,0,1]
	v_pk_fma_f32 v[72:73], v[4:5], s[2:3], v[78:79] op_sel_hi:[1,0,1]
	v_pk_fma_f32 v[74:75], v[6:7], s[2:3], v[174:175] op_sel_hi:[1,0,1]
	v_pk_fma_f32 v[76:77], v[8:9], s[2:3], v[172:173] op_sel_hi:[1,0,1]
	v_pk_fma_f32 v[78:79], v[10:11], s[2:3], v[170:171] op_sel_hi:[1,0,1]
	v_pk_fma_f32 v[168:169], v[12:13], s[2:3], v[168:169] op_sel_hi:[1,0,1]
	v_pk_fma_f32 v[166:167], v[14:15], s[2:3], v[166:167] op_sel_hi:[1,0,1]
	v_pk_fma_f32 v[164:165], v[16:17], s[2:3], v[164:165] op_sel_hi:[1,0,1]
	v_pk_fma_f32 v[162:163], v[18:19], s[2:3], v[162:163] op_sel_hi:[1,0,1]
	v_pk_fma_f32 v[160:161], v[20:21], s[2:3], v[160:161] op_sel_hi:[1,0,1]
	v_pk_fma_f32 v[158:159], v[22:23], s[2:3], v[158:159] op_sel_hi:[1,0,1]
	v_pk_fma_f32 v[156:157], v[24:25], s[2:3], v[156:157] op_sel_hi:[1,0,1]
	v_pk_fma_f32 v[154:155], v[26:27], s[2:3], v[154:155] op_sel_hi:[1,0,1]
	v_pk_fma_f32 v[152:153], v[28:29], s[2:3], v[152:153] op_sel_hi:[1,0,1]
	v_pk_fma_f32 v[150:151], v[30:31], s[2:3], v[150:151] op_sel_hi:[1,0,1]
	v_readlane_b32 s2, v211, 50
	s_waitcnt vmcnt(18)
	v_cvt_scalef32_pk32_f32_fp6 v[0:31], v[56:61], 1.0
	v_pk_fma_f32 v[56:57], v[0:1], s[2:3], v[68:69] op_sel_hi:[1,0,1]
	v_pk_fma_f32 v[58:59], v[2:3], s[2:3], v[70:71] op_sel_hi:[1,0,1]
	v_pk_fma_f32 v[60:61], v[4:5], s[2:3], v[72:73] op_sel_hi:[1,0,1]
	v_pk_fma_f32 v[68:69], v[6:7], s[2:3], v[74:75] op_sel_hi:[1,0,1]
	v_pk_fma_f32 v[70:71], v[8:9], s[2:3], v[76:77] op_sel_hi:[1,0,1]
	v_pk_fma_f32 v[72:73], v[10:11], s[2:3], v[78:79] op_sel_hi:[1,0,1]
	v_pk_fma_f32 v[74:75], v[12:13], s[2:3], v[168:169] op_sel_hi:[1,0,1]
	v_pk_fma_f32 v[76:77], v[14:15], s[2:3], v[166:167] op_sel_hi:[1,0,1]
	v_pk_fma_f32 v[78:79], v[16:17], s[2:3], v[164:165] op_sel_hi:[1,0,1]
	v_pk_fma_f32 v[162:163], v[18:19], s[2:3], v[162:163] op_sel_hi:[1,0,1]
	v_pk_fma_f32 v[160:161], v[20:21], s[2:3], v[160:161] op_sel_hi:[1,0,1]
	v_pk_fma_f32 v[158:159], v[22:23], s[2:3], v[158:159] op_sel_hi:[1,0,1]
	v_pk_fma_f32 v[156:157], v[24:25], s[2:3], v[156:157] op_sel_hi:[1,0,1]
	v_pk_fma_f32 v[154:155], v[26:27], s[2:3], v[154:155] op_sel_hi:[1,0,1]
	v_pk_fma_f32 v[152:153], v[28:29], s[2:3], v[152:153] op_sel_hi:[1,0,1]
	v_pk_fma_f32 v[150:151], v[30:31], s[2:3], v[150:151] op_sel_hi:[1,0,1]
	v_readlane_b32 s2, v211, 51
	s_waitcnt vmcnt(16)
	v_cvt_scalef32_pk32_f32_fp6 v[0:31], v[44:49], 1.0
	v_pk_fma_f32 v[164:165], v[0:1], s[2:3], v[56:57] op_sel_hi:[1,0,1]
	v_pk_fma_f32 v[166:167], v[2:3], s[2:3], v[58:59] op_sel_hi:[1,0,1]
	v_pk_fma_f32 v[168:169], v[4:5], s[2:3], v[60:61] op_sel_hi:[1,0,1]
	v_pk_fma_f32 v[170:171], v[6:7], s[2:3], v[68:69] op_sel_hi:[1,0,1]
	v_pk_fma_f32 v[172:173], v[8:9], s[2:3], v[70:71] op_sel_hi:[1,0,1]
	v_pk_fma_f32 v[174:175], v[10:11], s[2:3], v[72:73] op_sel_hi:[1,0,1]
	v_pk_fma_f32 v[176:177], v[12:13], s[2:3], v[74:75] op_sel_hi:[1,0,1]
	v_pk_fma_f32 v[178:179], v[14:15], s[2:3], v[76:77] op_sel_hi:[1,0,1]
	v_pk_fma_f32 v[180:181], v[16:17], s[2:3], v[78:79] op_sel_hi:[1,0,1]
	v_pk_fma_f32 v[162:163], v[18:19], s[2:3], v[162:163] op_sel_hi:[1,0,1]
	v_pk_fma_f32 v[160:161], v[20:21], s[2:3], v[160:161] op_sel_hi:[1,0,1]
	v_pk_fma_f32 v[158:159], v[22:23], s[2:3], v[158:159] op_sel_hi:[1,0,1]
	v_pk_fma_f32 v[156:157], v[24:25], s[2:3], v[156:157] op_sel_hi:[1,0,1]
	v_pk_fma_f32 v[154:155], v[26:27], s[2:3], v[154:155] op_sel_hi:[1,0,1]
	v_pk_fma_f32 v[152:153], v[28:29], s[2:3], v[152:153] op_sel_hi:[1,0,1]
	v_pk_fma_f32 v[150:151], v[30:31], s[2:3], v[150:151] op_sel_hi:[1,0,1]
	v_readlane_b32 s2, v240, 60
	v_readlane_b32 s3, v240, 61
	v_readlane_b32 s100, v240, 62
	v_readlane_b32 s101, v240, 63
	s_nop 1
	buffer_load_dwordx4 v[74:77], v129, s[44:47], s2 offen
	buffer_load_dwordx2 v[78:79], v210, s[44:47], s2 offen
	buffer_load_dwordx4 v[68:71], v129, s[44:47], s3 offen
	buffer_load_dwordx2 v[72:73], v210, s[44:47], s3 offen
	buffer_load_dwordx4 v[56:59], v129, s[44:47], s100 offen
	buffer_load_dwordx2 v[60:61], v210, s[44:47], s100 offen
	buffer_load_dwordx4 v[44:47], v129, s[44:47], s101 offen
	buffer_load_dwordx2 v[48:49], v210, s[44:47], s101 offen
	v_readlane_b32 s2, v211, 52
	s_waitcnt vmcnt(22)
	v_cvt_scalef32_pk32_f32_fp6 v[0:31], v[62:67], 1.0
	v_pk_fma_f32 v[62:63], v[0:1], s[2:3], v[164:165] op_sel_hi:[1,0,1]
	v_pk_fma_f32 v[64:65], v[2:3], s[2:3], v[166:167] op_sel_hi:[1,0,1]
	v_pk_fma_f32 v[66:67], v[4:5], s[2:3], v[168:169] op_sel_hi:[1,0,1]
	v_pk_fma_f32 v[164:165], v[6:7], s[2:3], v[170:171] op_sel_hi:[1,0,1]
	v_pk_fma_f32 v[166:167], v[8:9], s[2:3], v[172:173] op_sel_hi:[1,0,1]
	v_pk_fma_f32 v[168:169], v[10:11], s[2:3], v[174:175] op_sel_hi:[1,0,1]
	v_pk_fma_f32 v[170:171], v[12:13], s[2:3], v[176:177] op_sel_hi:[1,0,1]
	v_pk_fma_f32 v[172:173], v[14:15], s[2:3], v[178:179] op_sel_hi:[1,0,1]
	v_pk_fma_f32 v[174:175], v[16:17], s[2:3], v[180:181] op_sel_hi:[1,0,1]
	v_pk_fma_f32 v[162:163], v[18:19], s[2:3], v[162:163] op_sel_hi:[1,0,1]
	v_pk_fma_f32 v[160:161], v[20:21], s[2:3], v[160:161] op_sel_hi:[1,0,1]
	v_pk_fma_f32 v[158:159], v[22:23], s[2:3], v[158:159] op_sel_hi:[1,0,1]
	v_pk_fma_f32 v[156:157], v[24:25], s[2:3], v[156:157] op_sel_hi:[1,0,1]
	v_pk_fma_f32 v[154:155], v[26:27], s[2:3], v[154:155] op_sel_hi:[1,0,1]
	v_pk_fma_f32 v[152:153], v[28:29], s[2:3], v[152:153] op_sel_hi:[1,0,1]
	v_pk_fma_f32 v[150:151], v[30:31], s[2:3], v[150:151] op_sel_hi:[1,0,1]
	v_readlane_b32 s2, v211, 53
	s_waitcnt vmcnt(20)
	v_cvt_scalef32_pk32_f32_fp6 v[0:31], v[50:55], 1.0
	v_pk_fma_f32 v[50:51], v[0:1], s[2:3], v[62:63] op_sel_hi:[1,0,1]
	v_pk_fma_f32 v[52:53], v[2:3], s[2:3], v[64:65] op_sel_hi:[1,0,1]
	v_pk_fma_f32 v[54:55], v[4:5], s[2:3], v[66:67] op_sel_hi:[1,0,1]
	v_pk_fma_f32 v[62:63], v[6:7], s[2:3], v[164:165] op_sel_hi:[1,0,1]
	v_pk_fma_f32 v[64:65], v[8:9], s[2:3], v[166:167] op_sel_hi:[1,0,1]
	v_pk_fma_f32 v[66:67], v[10:11], s[2:3], v[168:169] op_sel_hi:[1,0,1]
	v_pk_fma_f32 v[164:165], v[12:13], s[2:3], v[170:171] op_sel_hi:[1,0,1]
	v_pk_fma_f32 v[166:167], v[14:15], s[2:3], v[172:173] op_sel_hi:[1,0,1]
	v_pk_fma_f32 v[168:169], v[16:17], s[2:3], v[174:175] op_sel_hi:[1,0,1]
	v_pk_fma_f32 v[162:163], v[18:19], s[2:3], v[162:163] op_sel_hi:[1,0,1]
	v_pk_fma_f32 v[160:161], v[20:21], s[2:3], v[160:161] op_sel_hi:[1,0,1]
	v_pk_fma_f32 v[158:159], v[22:23], s[2:3], v[158:159] op_sel_hi:[1,0,1]
	v_pk_fma_f32 v[156:157], v[24:25], s[2:3], v[156:157] op_sel_hi:[1,0,1]
	v_pk_fma_f32 v[154:155], v[26:27], s[2:3], v[154:155] op_sel_hi:[1,0,1]
	v_pk_fma_f32 v[152:153], v[28:29], s[2:3], v[152:153] op_sel_hi:[1,0,1]
	v_pk_fma_f32 v[150:151], v[30:31], s[2:3], v[150:151] op_sel_hi:[1,0,1]
	v_readlane_b32 s2, v211, 54
	s_waitcnt vmcnt(18)
	v_cvt_scalef32_pk32_f32_fp6 v[0:31], v[38:43], 1.0
	v_pk_fma_f32 v[38:39], v[0:1], s[2:3], v[50:51] op_sel_hi:[1,0,1]
	v_pk_fma_f32 v[40:41], v[2:3], s[2:3], v[52:53] op_sel_hi:[1,0,1]
	v_pk_fma_f32 v[42:43], v[4:5], s[2:3], v[54:55] op_sel_hi:[1,0,1]
	v_pk_fma_f32 v[50:51], v[6:7], s[2:3], v[62:63] op_sel_hi:[1,0,1]
	v_pk_fma_f32 v[52:53], v[8:9], s[2:3], v[64:65] op_sel_hi:[1,0,1]
	v_pk_fma_f32 v[54:55], v[10:11], s[2:3], v[66:67] op_sel_hi:[1,0,1]
	v_pk_fma_f32 v[62:63], v[12:13], s[2:3], v[164:165] op_sel_hi:[1,0,1]
	v_pk_fma_f32 v[64:65], v[14:15], s[2:3], v[166:167] op_sel_hi:[1,0,1]
	v_pk_fma_f32 v[66:67], v[16:17], s[2:3], v[168:169] op_sel_hi:[1,0,1]
	v_pk_fma_f32 v[162:163], v[18:19], s[2:3], v[162:163] op_sel_hi:[1,0,1]
	v_pk_fma_f32 v[160:161], v[20:21], s[2:3], v[160:161] op_sel_hi:[1,0,1]
	v_pk_fma_f32 v[158:159], v[22:23], s[2:3], v[158:159] op_sel_hi:[1,0,1]
	v_pk_fma_f32 v[156:157], v[24:25], s[2:3], v[156:157] op_sel_hi:[1,0,1]
	v_pk_fma_f32 v[154:155], v[26:27], s[2:3], v[154:155] op_sel_hi:[1,0,1]
	v_pk_fma_f32 v[152:153], v[28:29], s[2:3], v[152:153] op_sel_hi:[1,0,1]
	v_pk_fma_f32 v[150:151], v[30:31], s[2:3], v[150:151] op_sel_hi:[1,0,1]
	v_readlane_b32 s2, v211, 55
	s_waitcnt vmcnt(16)
	v_cvt_scalef32_pk32_f32_fp6 v[0:31], v[32:37], 1.0
	v_pk_fma_f32 v[164:165], v[0:1], s[2:3], v[38:39] op_sel_hi:[1,0,1]
	v_pk_fma_f32 v[166:167], v[2:3], s[2:3], v[40:41] op_sel_hi:[1,0,1]
	v_pk_fma_f32 v[168:169], v[4:5], s[2:3], v[42:43] op_sel_hi:[1,0,1]
	v_pk_fma_f32 v[170:171], v[6:7], s[2:3], v[50:51] op_sel_hi:[1,0,1]
	v_pk_fma_f32 v[172:173], v[8:9], s[2:3], v[52:53] op_sel_hi:[1,0,1]
	v_pk_fma_f32 v[174:175], v[10:11], s[2:3], v[54:55] op_sel_hi:[1,0,1]
	v_pk_fma_f32 v[176:177], v[12:13], s[2:3], v[62:63] op_sel_hi:[1,0,1]
	v_pk_fma_f32 v[178:179], v[14:15], s[2:3], v[64:65] op_sel_hi:[1,0,1]
	v_pk_fma_f32 v[180:181], v[16:17], s[2:3], v[66:67] op_sel_hi:[1,0,1]
	v_pk_fma_f32 v[162:163], v[18:19], s[2:3], v[162:163] op_sel_hi:[1,0,1]
	v_pk_fma_f32 v[160:161], v[20:21], s[2:3], v[160:161] op_sel_hi:[1,0,1]
	v_pk_fma_f32 v[158:159], v[22:23], s[2:3], v[158:159] op_sel_hi:[1,0,1]
	v_pk_fma_f32 v[156:157], v[24:25], s[2:3], v[156:157] op_sel_hi:[1,0,1]
	v_pk_fma_f32 v[154:155], v[26:27], s[2:3], v[154:155] op_sel_hi:[1,0,1]
	v_pk_fma_f32 v[152:153], v[28:29], s[2:3], v[152:153] op_sel_hi:[1,0,1]
	v_pk_fma_f32 v[150:151], v[30:31], s[2:3], v[150:151] op_sel_hi:[1,0,1]
	v_readlane_b32 s2, v241, 0
	v_readlane_b32 s3, v241, 1
	v_readlane_b32 s100, v241, 2
	v_readlane_b32 s101, v241, 3
	s_nop 1
	buffer_load_dwordx4 v[62:65], v129, s[44:47], s2 offen
	buffer_load_dwordx2 v[66:67], v210, s[44:47], s2 offen
	buffer_load_dwordx4 v[50:53], v129, s[44:47], s3 offen
	buffer_load_dwordx2 v[54:55], v210, s[44:47], s3 offen
	buffer_load_dwordx4 v[38:41], v129, s[44:47], s100 offen
	buffer_load_dwordx2 v[42:43], v210, s[44:47], s100 offen
	buffer_load_dwordx4 v[32:35], v129, s[44:47], s101 offen
	buffer_load_dwordx2 v[36:37], v210, s[44:47], s101 offen
	v_readlane_b32 s2, v211, 56
	s_waitcnt vmcnt(22)
	v_cvt_scalef32_pk32_f32_fp6 v[0:31], v[98:103], 1.0
	v_pk_fma_f32 v[98:99], v[0:1], s[2:3], v[164:165] op_sel_hi:[1,0,1]
	v_pk_fma_f32 v[100:101], v[2:3], s[2:3], v[166:167] op_sel_hi:[1,0,1]
	v_pk_fma_f32 v[102:103], v[4:5], s[2:3], v[168:169] op_sel_hi:[1,0,1]
	v_pk_fma_f32 v[164:165], v[6:7], s[2:3], v[170:171] op_sel_hi:[1,0,1]
	v_pk_fma_f32 v[166:167], v[8:9], s[2:3], v[172:173] op_sel_hi:[1,0,1]
	v_pk_fma_f32 v[168:169], v[10:11], s[2:3], v[174:175] op_sel_hi:[1,0,1]
	v_pk_fma_f32 v[170:171], v[12:13], s[2:3], v[176:177] op_sel_hi:[1,0,1]
	v_pk_fma_f32 v[172:173], v[14:15], s[2:3], v[178:179] op_sel_hi:[1,0,1]
	v_pk_fma_f32 v[174:175], v[16:17], s[2:3], v[180:181] op_sel_hi:[1,0,1]
	v_pk_fma_f32 v[162:163], v[18:19], s[2:3], v[162:163] op_sel_hi:[1,0,1]
	v_pk_fma_f32 v[160:161], v[20:21], s[2:3], v[160:161] op_sel_hi:[1,0,1]
	v_pk_fma_f32 v[158:159], v[22:23], s[2:3], v[158:159] op_sel_hi:[1,0,1]
	v_pk_fma_f32 v[156:157], v[24:25], s[2:3], v[156:157] op_sel_hi:[1,0,1]
	v_pk_fma_f32 v[154:155], v[26:27], s[2:3], v[154:155] op_sel_hi:[1,0,1]
	v_pk_fma_f32 v[152:153], v[28:29], s[2:3], v[152:153] op_sel_hi:[1,0,1]
	v_pk_fma_f32 v[150:151], v[30:31], s[2:3], v[150:151] op_sel_hi:[1,0,1]
	v_readlane_b32 s2, v211, 57
	s_waitcnt vmcnt(20)
	v_cvt_scalef32_pk32_f32_fp6 v[0:31], v[92:97], 1.0
	v_pk_fma_f32 v[92:93], v[0:1], s[2:3], v[98:99] op_sel_hi:[1,0,1]
	v_pk_fma_f32 v[94:95], v[2:3], s[2:3], v[100:101] op_sel_hi:[1,0,1]
	v_pk_fma_f32 v[96:97], v[4:5], s[2:3], v[102:103] op_sel_hi:[1,0,1]
	v_pk_fma_f32 v[98:99], v[6:7], s[2:3], v[164:165] op_sel_hi:[1,0,1]
	v_pk_fma_f32 v[100:101], v[8:9], s[2:3], v[166:167] op_sel_hi:[1,0,1]
	v_pk_fma_f32 v[102:103], v[10:11], s[2:3], v[168:169] op_sel_hi:[1,0,1]
	v_pk_fma_f32 v[164:165], v[12:13], s[2:3], v[170:171] op_sel_hi:[1,0,1]
	v_pk_fma_f32 v[166:167], v[14:15], s[2:3], v[172:173] op_sel_hi:[1,0,1]
	v_pk_fma_f32 v[168:169], v[16:17], s[2:3], v[174:175] op_sel_hi:[1,0,1]
	v_pk_fma_f32 v[162:163], v[18:19], s[2:3], v[162:163] op_sel_hi:[1,0,1]
	v_pk_fma_f32 v[160:161], v[20:21], s[2:3], v[160:161] op_sel_hi:[1,0,1]
	v_pk_fma_f32 v[158:159], v[22:23], s[2:3], v[158:159] op_sel_hi:[1,0,1]
	v_pk_fma_f32 v[156:157], v[24:25], s[2:3], v[156:157] op_sel_hi:[1,0,1]
	v_pk_fma_f32 v[154:155], v[26:27], s[2:3], v[154:155] op_sel_hi:[1,0,1]
	v_pk_fma_f32 v[152:153], v[28:29], s[2:3], v[152:153] op_sel_hi:[1,0,1]
	v_pk_fma_f32 v[150:151], v[30:31], s[2:3], v[150:151] op_sel_hi:[1,0,1]
	v_readlane_b32 s2, v211, 58
	s_waitcnt vmcnt(18)
	v_cvt_scalef32_pk32_f32_fp6 v[0:31], v[86:91], 1.0
	v_pk_fma_f32 v[86:87], v[0:1], s[2:3], v[92:93] op_sel_hi:[1,0,1]
	v_pk_fma_f32 v[88:89], v[2:3], s[2:3], v[94:95] op_sel_hi:[1,0,1]
	v_pk_fma_f32 v[90:91], v[4:5], s[2:3], v[96:97] op_sel_hi:[1,0,1]
	v_pk_fma_f32 v[92:93], v[6:7], s[2:3], v[98:99] op_sel_hi:[1,0,1]
	v_pk_fma_f32 v[94:95], v[8:9], s[2:3], v[100:101] op_sel_hi:[1,0,1]
	v_pk_fma_f32 v[96:97], v[10:11], s[2:3], v[102:103] op_sel_hi:[1,0,1]
	v_pk_fma_f32 v[98:99], v[12:13], s[2:3], v[164:165] op_sel_hi:[1,0,1]
	v_pk_fma_f32 v[100:101], v[14:15], s[2:3], v[166:167] op_sel_hi:[1,0,1]
	v_pk_fma_f32 v[102:103], v[16:17], s[2:3], v[168:169] op_sel_hi:[1,0,1]
	v_pk_fma_f32 v[162:163], v[18:19], s[2:3], v[162:163] op_sel_hi:[1,0,1]
	v_pk_fma_f32 v[160:161], v[20:21], s[2:3], v[160:161] op_sel_hi:[1,0,1]
	v_pk_fma_f32 v[158:159], v[22:23], s[2:3], v[158:159] op_sel_hi:[1,0,1]
	v_pk_fma_f32 v[156:157], v[24:25], s[2:3], v[156:157] op_sel_hi:[1,0,1]
	v_pk_fma_f32 v[154:155], v[26:27], s[2:3], v[154:155] op_sel_hi:[1,0,1]
	v_pk_fma_f32 v[152:153], v[28:29], s[2:3], v[152:153] op_sel_hi:[1,0,1]
	v_pk_fma_f32 v[150:151], v[30:31], s[2:3], v[150:151] op_sel_hi:[1,0,1]
	v_readlane_b32 s2, v211, 59
	s_waitcnt vmcnt(16)
	v_cvt_scalef32_pk32_f32_fp6 v[0:31], v[80:85], 1.0
	v_pk_fma_f32 v[180:181], v[0:1], s[2:3], v[86:87] op_sel_hi:[1,0,1]
	v_pk_fma_f32 v[178:179], v[2:3], s[2:3], v[88:89] op_sel_hi:[1,0,1]
	v_pk_fma_f32 v[176:177], v[4:5], s[2:3], v[90:91] op_sel_hi:[1,0,1]
	v_pk_fma_f32 v[174:175], v[6:7], s[2:3], v[92:93] op_sel_hi:[1,0,1]
	v_pk_fma_f32 v[172:173], v[8:9], s[2:3], v[94:95] op_sel_hi:[1,0,1]
	v_pk_fma_f32 v[170:171], v[10:11], s[2:3], v[96:97] op_sel_hi:[1,0,1]
	v_pk_fma_f32 v[168:169], v[12:13], s[2:3], v[98:99] op_sel_hi:[1,0,1]
	v_pk_fma_f32 v[166:167], v[14:15], s[2:3], v[100:101] op_sel_hi:[1,0,1]
	v_pk_fma_f32 v[164:165], v[16:17], s[2:3], v[102:103] op_sel_hi:[1,0,1]
	v_pk_fma_f32 v[162:163], v[18:19], s[2:3], v[162:163] op_sel_hi:[1,0,1]
	v_pk_fma_f32 v[160:161], v[20:21], s[2:3], v[160:161] op_sel_hi:[1,0,1]
	v_pk_fma_f32 v[158:159], v[22:23], s[2:3], v[158:159] op_sel_hi:[1,0,1]
	v_pk_fma_f32 v[156:157], v[24:25], s[2:3], v[156:157] op_sel_hi:[1,0,1]
	v_pk_fma_f32 v[154:155], v[26:27], s[2:3], v[154:155] op_sel_hi:[1,0,1]
	v_pk_fma_f32 v[152:153], v[28:29], s[2:3], v[152:153] op_sel_hi:[1,0,1]
	v_pk_fma_f32 v[150:151], v[30:31], s[2:3], v[150:151] op_sel_hi:[1,0,1]
	v_readlane_b32 s2, v241, 4
	v_readlane_b32 s3, v241, 5
	v_readlane_b32 s100, v241, 6
	v_readlane_b32 s101, v241, 7
	s_nop 1
	buffer_load_dwordx4 v[98:101], v129, s[44:47], s2 offen
	buffer_load_dwordx2 v[102:103], v210, s[44:47], s2 offen
	buffer_load_dwordx4 v[92:95], v129, s[44:47], s3 offen
	buffer_load_dwordx2 v[96:97], v210, s[44:47], s3 offen
	buffer_load_dwordx4 v[86:89], v129, s[44:47], s100 offen
	buffer_load_dwordx2 v[90:91], v210, s[44:47], s100 offen
	buffer_load_dwordx4 v[80:83], v129, s[44:47], s101 offen
	buffer_load_dwordx2 v[84:85], v210, s[44:47], s101 offen
	v_readlane_b32 s2, v211, 60
	s_waitcnt vmcnt(22)
	v_cvt_scalef32_pk32_f32_fp6 v[0:31], v[74:79], 1.0
	v_pk_fma_f32 v[74:75], v[0:1], s[2:3], v[180:181] op_sel_hi:[1,0,1]
	v_pk_fma_f32 v[76:77], v[2:3], s[2:3], v[178:179] op_sel_hi:[1,0,1]
	v_pk_fma_f32 v[78:79], v[4:5], s[2:3], v[176:177] op_sel_hi:[1,0,1]
	v_pk_fma_f32 v[174:175], v[6:7], s[2:3], v[174:175] op_sel_hi:[1,0,1]
	v_pk_fma_f32 v[172:173], v[8:9], s[2:3], v[172:173] op_sel_hi:[1,0,1]
	v_pk_fma_f32 v[170:171], v[10:11], s[2:3], v[170:171] op_sel_hi:[1,0,1]
	v_pk_fma_f32 v[168:169], v[12:13], s[2:3], v[168:169] op_sel_hi:[1,0,1]
	v_pk_fma_f32 v[166:167], v[14:15], s[2:3], v[166:167] op_sel_hi:[1,0,1]
	v_pk_fma_f32 v[164:165], v[16:17], s[2:3], v[164:165] op_sel_hi:[1,0,1]
	v_pk_fma_f32 v[162:163], v[18:19], s[2:3], v[162:163] op_sel_hi:[1,0,1]
	v_pk_fma_f32 v[160:161], v[20:21], s[2:3], v[160:161] op_sel_hi:[1,0,1]
	v_pk_fma_f32 v[158:159], v[22:23], s[2:3], v[158:159] op_sel_hi:[1,0,1]
	v_pk_fma_f32 v[156:157], v[24:25], s[2:3], v[156:157] op_sel_hi:[1,0,1]
	v_pk_fma_f32 v[154:155], v[26:27], s[2:3], v[154:155] op_sel_hi:[1,0,1]
	v_pk_fma_f32 v[152:153], v[28:29], s[2:3], v[152:153] op_sel_hi:[1,0,1]
	v_pk_fma_f32 v[150:151], v[30:31], s[2:3], v[150:151] op_sel_hi:[1,0,1]
	v_readlane_b32 s2, v211, 61
	s_waitcnt vmcnt(20)
	v_cvt_scalef32_pk32_f32_fp6 v[0:31], v[68:73], 1.0
	v_pk_fma_f32 v[68:69], v[0:1], s[2:3], v[74:75] op_sel_hi:[1,0,1]
	v_pk_fma_f32 v[70:71], v[2:3], s[2:3], v[76:77] op_sel_hi:[1,0,1]
	v_pk_fma_f32 v[72:73], v[4:5], s[2:3], v[78:79] op_sel_hi:[1,0,1]
	v_pk_fma_f32 v[74:75], v[6:7], s[2:3], v[174:175] op_sel_hi:[1,0,1]
	v_pk_fma_f32 v[76:77], v[8:9], s[2:3], v[172:173] op_sel_hi:[1,0,1]
	v_pk_fma_f32 v[78:79], v[10:11], s[2:3], v[170:171] op_sel_hi:[1,0,1]
	v_pk_fma_f32 v[168:169], v[12:13], s[2:3], v[168:169] op_sel_hi:[1,0,1]
	v_pk_fma_f32 v[166:167], v[14:15], s[2:3], v[166:167] op_sel_hi:[1,0,1]
	v_pk_fma_f32 v[164:165], v[16:17], s[2:3], v[164:165] op_sel_hi:[1,0,1]
	v_pk_fma_f32 v[162:163], v[18:19], s[2:3], v[162:163] op_sel_hi:[1,0,1]
	v_pk_fma_f32 v[160:161], v[20:21], s[2:3], v[160:161] op_sel_hi:[1,0,1]
	v_pk_fma_f32 v[158:159], v[22:23], s[2:3], v[158:159] op_sel_hi:[1,0,1]
	v_pk_fma_f32 v[156:157], v[24:25], s[2:3], v[156:157] op_sel_hi:[1,0,1]
	v_pk_fma_f32 v[154:155], v[26:27], s[2:3], v[154:155] op_sel_hi:[1,0,1]
	v_pk_fma_f32 v[152:153], v[28:29], s[2:3], v[152:153] op_sel_hi:[1,0,1]
	v_pk_fma_f32 v[150:151], v[30:31], s[2:3], v[150:151] op_sel_hi:[1,0,1]
	v_readlane_b32 s2, v211, 62
	s_waitcnt vmcnt(18)
	v_cvt_scalef32_pk32_f32_fp6 v[0:31], v[56:61], 1.0
	v_pk_fma_f32 v[56:57], v[0:1], s[2:3], v[68:69] op_sel_hi:[1,0,1]
	v_pk_fma_f32 v[58:59], v[2:3], s[2:3], v[70:71] op_sel_hi:[1,0,1]
	v_pk_fma_f32 v[60:61], v[4:5], s[2:3], v[72:73] op_sel_hi:[1,0,1]
	v_pk_fma_f32 v[68:69], v[6:7], s[2:3], v[74:75] op_sel_hi:[1,0,1]
	v_pk_fma_f32 v[70:71], v[8:9], s[2:3], v[76:77] op_sel_hi:[1,0,1]
	v_pk_fma_f32 v[72:73], v[10:11], s[2:3], v[78:79] op_sel_hi:[1,0,1]
	v_pk_fma_f32 v[74:75], v[12:13], s[2:3], v[168:169] op_sel_hi:[1,0,1]
	v_pk_fma_f32 v[76:77], v[14:15], s[2:3], v[166:167] op_sel_hi:[1,0,1]
	v_pk_fma_f32 v[78:79], v[16:17], s[2:3], v[164:165] op_sel_hi:[1,0,1]
	v_pk_fma_f32 v[162:163], v[18:19], s[2:3], v[162:163] op_sel_hi:[1,0,1]
	v_pk_fma_f32 v[160:161], v[20:21], s[2:3], v[160:161] op_sel_hi:[1,0,1]
	v_pk_fma_f32 v[158:159], v[22:23], s[2:3], v[158:159] op_sel_hi:[1,0,1]
	v_pk_fma_f32 v[156:157], v[24:25], s[2:3], v[156:157] op_sel_hi:[1,0,1]
	v_pk_fma_f32 v[154:155], v[26:27], s[2:3], v[154:155] op_sel_hi:[1,0,1]
	v_pk_fma_f32 v[152:153], v[28:29], s[2:3], v[152:153] op_sel_hi:[1,0,1]
	v_pk_fma_f32 v[150:151], v[30:31], s[2:3], v[150:151] op_sel_hi:[1,0,1]
	v_readlane_b32 s2, v211, 63
	s_waitcnt vmcnt(16)
	v_cvt_scalef32_pk32_f32_fp6 v[0:31], v[44:49], 1.0
	v_pk_fma_f32 v[164:165], v[0:1], s[2:3], v[56:57] op_sel_hi:[1,0,1]
	v_pk_fma_f32 v[166:167], v[2:3], s[2:3], v[58:59] op_sel_hi:[1,0,1]
	v_pk_fma_f32 v[168:169], v[4:5], s[2:3], v[60:61] op_sel_hi:[1,0,1]
	v_pk_fma_f32 v[170:171], v[6:7], s[2:3], v[68:69] op_sel_hi:[1,0,1]
	v_pk_fma_f32 v[172:173], v[8:9], s[2:3], v[70:71] op_sel_hi:[1,0,1]
	v_pk_fma_f32 v[174:175], v[10:11], s[2:3], v[72:73] op_sel_hi:[1,0,1]
	v_pk_fma_f32 v[176:177], v[12:13], s[2:3], v[74:75] op_sel_hi:[1,0,1]
	v_pk_fma_f32 v[178:179], v[14:15], s[2:3], v[76:77] op_sel_hi:[1,0,1]
	v_pk_fma_f32 v[180:181], v[16:17], s[2:3], v[78:79] op_sel_hi:[1,0,1]
	v_pk_fma_f32 v[162:163], v[18:19], s[2:3], v[162:163] op_sel_hi:[1,0,1]
	v_pk_fma_f32 v[160:161], v[20:21], s[2:3], v[160:161] op_sel_hi:[1,0,1]
	v_pk_fma_f32 v[158:159], v[22:23], s[2:3], v[158:159] op_sel_hi:[1,0,1]
	v_pk_fma_f32 v[156:157], v[24:25], s[2:3], v[156:157] op_sel_hi:[1,0,1]
	v_pk_fma_f32 v[154:155], v[26:27], s[2:3], v[154:155] op_sel_hi:[1,0,1]
	v_pk_fma_f32 v[152:153], v[28:29], s[2:3], v[152:153] op_sel_hi:[1,0,1]
	v_pk_fma_f32 v[150:151], v[30:31], s[2:3], v[150:151] op_sel_hi:[1,0,1]
	v_readlane_b32 s2, v241, 8
	v_readlane_b32 s3, v241, 9
	v_readlane_b32 s100, v241, 10
	v_readlane_b32 s101, v241, 11
	s_nop 1
	buffer_load_dwordx4 v[74:77], v129, s[44:47], s2 offen
	buffer_load_dwordx2 v[78:79], v210, s[44:47], s2 offen
	buffer_load_dwordx4 v[68:71], v129, s[44:47], s3 offen
	buffer_load_dwordx2 v[72:73], v210, s[44:47], s3 offen
	buffer_load_dwordx4 v[56:59], v129, s[44:47], s100 offen
	buffer_load_dwordx2 v[60:61], v210, s[44:47], s100 offen
	buffer_load_dwordx4 v[44:47], v129, s[44:47], s101 offen
	buffer_load_dwordx2 v[48:49], v210, s[44:47], s101 offen
	v_readlane_b32 s2, v131, 0
	s_waitcnt vmcnt(22)
	v_cvt_scalef32_pk32_f32_fp6 v[0:31], v[62:67], 1.0
	v_pk_fma_f32 v[62:63], v[0:1], s[2:3], v[164:165] op_sel_hi:[1,0,1]
	v_pk_fma_f32 v[64:65], v[2:3], s[2:3], v[166:167] op_sel_hi:[1,0,1]
	v_pk_fma_f32 v[66:67], v[4:5], s[2:3], v[168:169] op_sel_hi:[1,0,1]
	v_pk_fma_f32 v[164:165], v[6:7], s[2:3], v[170:171] op_sel_hi:[1,0,1]
	v_pk_fma_f32 v[166:167], v[8:9], s[2:3], v[172:173] op_sel_hi:[1,0,1]
	v_pk_fma_f32 v[168:169], v[10:11], s[2:3], v[174:175] op_sel_hi:[1,0,1]
	v_pk_fma_f32 v[170:171], v[12:13], s[2:3], v[176:177] op_sel_hi:[1,0,1]
	v_pk_fma_f32 v[172:173], v[14:15], s[2:3], v[178:179] op_sel_hi:[1,0,1]
	v_pk_fma_f32 v[174:175], v[16:17], s[2:3], v[180:181] op_sel_hi:[1,0,1]
	v_pk_fma_f32 v[162:163], v[18:19], s[2:3], v[162:163] op_sel_hi:[1,0,1]
	v_pk_fma_f32 v[160:161], v[20:21], s[2:3], v[160:161] op_sel_hi:[1,0,1]
	v_pk_fma_f32 v[158:159], v[22:23], s[2:3], v[158:159] op_sel_hi:[1,0,1]
	v_pk_fma_f32 v[156:157], v[24:25], s[2:3], v[156:157] op_sel_hi:[1,0,1]
	v_pk_fma_f32 v[154:155], v[26:27], s[2:3], v[154:155] op_sel_hi:[1,0,1]
	v_pk_fma_f32 v[152:153], v[28:29], s[2:3], v[152:153] op_sel_hi:[1,0,1]
	v_pk_fma_f32 v[150:151], v[30:31], s[2:3], v[150:151] op_sel_hi:[1,0,1]
	v_readlane_b32 s2, v131, 1
	s_waitcnt vmcnt(20)
	v_cvt_scalef32_pk32_f32_fp6 v[0:31], v[50:55], 1.0
	v_pk_fma_f32 v[50:51], v[0:1], s[2:3], v[62:63] op_sel_hi:[1,0,1]
	v_pk_fma_f32 v[52:53], v[2:3], s[2:3], v[64:65] op_sel_hi:[1,0,1]
	v_pk_fma_f32 v[54:55], v[4:5], s[2:3], v[66:67] op_sel_hi:[1,0,1]
	v_pk_fma_f32 v[62:63], v[6:7], s[2:3], v[164:165] op_sel_hi:[1,0,1]
	v_pk_fma_f32 v[64:65], v[8:9], s[2:3], v[166:167] op_sel_hi:[1,0,1]
	v_pk_fma_f32 v[66:67], v[10:11], s[2:3], v[168:169] op_sel_hi:[1,0,1]
	v_pk_fma_f32 v[164:165], v[12:13], s[2:3], v[170:171] op_sel_hi:[1,0,1]
	v_pk_fma_f32 v[166:167], v[14:15], s[2:3], v[172:173] op_sel_hi:[1,0,1]
	v_pk_fma_f32 v[168:169], v[16:17], s[2:3], v[174:175] op_sel_hi:[1,0,1]
	v_pk_fma_f32 v[162:163], v[18:19], s[2:3], v[162:163] op_sel_hi:[1,0,1]
	v_pk_fma_f32 v[160:161], v[20:21], s[2:3], v[160:161] op_sel_hi:[1,0,1]
	v_pk_fma_f32 v[158:159], v[22:23], s[2:3], v[158:159] op_sel_hi:[1,0,1]
	v_pk_fma_f32 v[156:157], v[24:25], s[2:3], v[156:157] op_sel_hi:[1,0,1]
	v_pk_fma_f32 v[154:155], v[26:27], s[2:3], v[154:155] op_sel_hi:[1,0,1]
	v_pk_fma_f32 v[152:153], v[28:29], s[2:3], v[152:153] op_sel_hi:[1,0,1]
	v_pk_fma_f32 v[150:151], v[30:31], s[2:3], v[150:151] op_sel_hi:[1,0,1]
	v_readlane_b32 s2, v131, 2
	s_waitcnt vmcnt(18)
	v_cvt_scalef32_pk32_f32_fp6 v[0:31], v[38:43], 1.0
	v_pk_fma_f32 v[38:39], v[0:1], s[2:3], v[50:51] op_sel_hi:[1,0,1]
	v_pk_fma_f32 v[40:41], v[2:3], s[2:3], v[52:53] op_sel_hi:[1,0,1]
	v_pk_fma_f32 v[42:43], v[4:5], s[2:3], v[54:55] op_sel_hi:[1,0,1]
	v_pk_fma_f32 v[50:51], v[6:7], s[2:3], v[62:63] op_sel_hi:[1,0,1]
	v_pk_fma_f32 v[52:53], v[8:9], s[2:3], v[64:65] op_sel_hi:[1,0,1]
	v_pk_fma_f32 v[54:55], v[10:11], s[2:3], v[66:67] op_sel_hi:[1,0,1]
	v_pk_fma_f32 v[62:63], v[12:13], s[2:3], v[164:165] op_sel_hi:[1,0,1]
	v_pk_fma_f32 v[64:65], v[14:15], s[2:3], v[166:167] op_sel_hi:[1,0,1]
	v_pk_fma_f32 v[66:67], v[16:17], s[2:3], v[168:169] op_sel_hi:[1,0,1]
	v_pk_fma_f32 v[162:163], v[18:19], s[2:3], v[162:163] op_sel_hi:[1,0,1]
	v_pk_fma_f32 v[160:161], v[20:21], s[2:3], v[160:161] op_sel_hi:[1,0,1]
	v_pk_fma_f32 v[158:159], v[22:23], s[2:3], v[158:159] op_sel_hi:[1,0,1]
	v_pk_fma_f32 v[156:157], v[24:25], s[2:3], v[156:157] op_sel_hi:[1,0,1]
	v_pk_fma_f32 v[154:155], v[26:27], s[2:3], v[154:155] op_sel_hi:[1,0,1]
	v_pk_fma_f32 v[152:153], v[28:29], s[2:3], v[152:153] op_sel_hi:[1,0,1]
	v_pk_fma_f32 v[150:151], v[30:31], s[2:3], v[150:151] op_sel_hi:[1,0,1]
	v_readlane_b32 s2, v131, 3
	s_waitcnt vmcnt(16)
	v_cvt_scalef32_pk32_f32_fp6 v[0:31], v[32:37], 1.0
	v_pk_fma_f32 v[164:165], v[0:1], s[2:3], v[38:39] op_sel_hi:[1,0,1]
	v_pk_fma_f32 v[166:167], v[2:3], s[2:3], v[40:41] op_sel_hi:[1,0,1]
	v_pk_fma_f32 v[168:169], v[4:5], s[2:3], v[42:43] op_sel_hi:[1,0,1]
	v_pk_fma_f32 v[170:171], v[6:7], s[2:3], v[50:51] op_sel_hi:[1,0,1]
	v_pk_fma_f32 v[172:173], v[8:9], s[2:3], v[52:53] op_sel_hi:[1,0,1]
	v_pk_fma_f32 v[174:175], v[10:11], s[2:3], v[54:55] op_sel_hi:[1,0,1]
	v_pk_fma_f32 v[176:177], v[12:13], s[2:3], v[62:63] op_sel_hi:[1,0,1]
	v_pk_fma_f32 v[178:179], v[14:15], s[2:3], v[64:65] op_sel_hi:[1,0,1]
	v_pk_fma_f32 v[180:181], v[16:17], s[2:3], v[66:67] op_sel_hi:[1,0,1]
	v_pk_fma_f32 v[162:163], v[18:19], s[2:3], v[162:163] op_sel_hi:[1,0,1]
	v_pk_fma_f32 v[160:161], v[20:21], s[2:3], v[160:161] op_sel_hi:[1,0,1]
	v_pk_fma_f32 v[158:159], v[22:23], s[2:3], v[158:159] op_sel_hi:[1,0,1]
	v_pk_fma_f32 v[156:157], v[24:25], s[2:3], v[156:157] op_sel_hi:[1,0,1]
	v_pk_fma_f32 v[154:155], v[26:27], s[2:3], v[154:155] op_sel_hi:[1,0,1]
	v_pk_fma_f32 v[152:153], v[28:29], s[2:3], v[152:153] op_sel_hi:[1,0,1]
	v_pk_fma_f32 v[150:151], v[30:31], s[2:3], v[150:151] op_sel_hi:[1,0,1]
	v_readlane_b32 s2, v241, 12
	v_readlane_b32 s3, v241, 13
	v_readlane_b32 s100, v241, 14
	v_readlane_b32 s101, v241, 15
	s_nop 1
	buffer_load_dwordx4 v[62:65], v129, s[44:47], s2 offen
	buffer_load_dwordx2 v[66:67], v210, s[44:47], s2 offen
	buffer_load_dwordx4 v[50:53], v129, s[44:47], s3 offen
	buffer_load_dwordx2 v[54:55], v210, s[44:47], s3 offen
	buffer_load_dwordx4 v[38:41], v129, s[44:47], s100 offen
	buffer_load_dwordx2 v[42:43], v210, s[44:47], s100 offen
	buffer_load_dwordx4 v[32:35], v129, s[44:47], s101 offen
	buffer_load_dwordx2 v[36:37], v210, s[44:47], s101 offen
	v_readlane_b32 s2, v131, 4
	s_waitcnt vmcnt(22)
	v_cvt_scalef32_pk32_f32_fp6 v[0:31], v[98:103], 1.0
	v_pk_fma_f32 v[98:99], v[0:1], s[2:3], v[164:165] op_sel_hi:[1,0,1]
	v_pk_fma_f32 v[100:101], v[2:3], s[2:3], v[166:167] op_sel_hi:[1,0,1]
	v_pk_fma_f32 v[102:103], v[4:5], s[2:3], v[168:169] op_sel_hi:[1,0,1]
	v_pk_fma_f32 v[164:165], v[6:7], s[2:3], v[170:171] op_sel_hi:[1,0,1]
	v_pk_fma_f32 v[166:167], v[8:9], s[2:3], v[172:173] op_sel_hi:[1,0,1]
	v_pk_fma_f32 v[168:169], v[10:11], s[2:3], v[174:175] op_sel_hi:[1,0,1]
	v_pk_fma_f32 v[170:171], v[12:13], s[2:3], v[176:177] op_sel_hi:[1,0,1]
	v_pk_fma_f32 v[172:173], v[14:15], s[2:3], v[178:179] op_sel_hi:[1,0,1]
	v_pk_fma_f32 v[174:175], v[16:17], s[2:3], v[180:181] op_sel_hi:[1,0,1]
	v_pk_fma_f32 v[162:163], v[18:19], s[2:3], v[162:163] op_sel_hi:[1,0,1]
	v_pk_fma_f32 v[160:161], v[20:21], s[2:3], v[160:161] op_sel_hi:[1,0,1]
	v_pk_fma_f32 v[158:159], v[22:23], s[2:3], v[158:159] op_sel_hi:[1,0,1]
	v_pk_fma_f32 v[156:157], v[24:25], s[2:3], v[156:157] op_sel_hi:[1,0,1]
	v_pk_fma_f32 v[154:155], v[26:27], s[2:3], v[154:155] op_sel_hi:[1,0,1]
	v_pk_fma_f32 v[152:153], v[28:29], s[2:3], v[152:153] op_sel_hi:[1,0,1]
	v_pk_fma_f32 v[150:151], v[30:31], s[2:3], v[150:151] op_sel_hi:[1,0,1]
	v_readlane_b32 s2, v131, 5
	s_waitcnt vmcnt(20)
	v_cvt_scalef32_pk32_f32_fp6 v[0:31], v[92:97], 1.0
	v_pk_fma_f32 v[92:93], v[0:1], s[2:3], v[98:99] op_sel_hi:[1,0,1]
	v_pk_fma_f32 v[94:95], v[2:3], s[2:3], v[100:101] op_sel_hi:[1,0,1]
	v_pk_fma_f32 v[96:97], v[4:5], s[2:3], v[102:103] op_sel_hi:[1,0,1]
	v_pk_fma_f32 v[98:99], v[6:7], s[2:3], v[164:165] op_sel_hi:[1,0,1]
	v_pk_fma_f32 v[100:101], v[8:9], s[2:3], v[166:167] op_sel_hi:[1,0,1]
	v_pk_fma_f32 v[102:103], v[10:11], s[2:3], v[168:169] op_sel_hi:[1,0,1]
	v_pk_fma_f32 v[164:165], v[12:13], s[2:3], v[170:171] op_sel_hi:[1,0,1]
	v_pk_fma_f32 v[166:167], v[14:15], s[2:3], v[172:173] op_sel_hi:[1,0,1]
	v_pk_fma_f32 v[168:169], v[16:17], s[2:3], v[174:175] op_sel_hi:[1,0,1]
	v_pk_fma_f32 v[162:163], v[18:19], s[2:3], v[162:163] op_sel_hi:[1,0,1]
	v_pk_fma_f32 v[160:161], v[20:21], s[2:3], v[160:161] op_sel_hi:[1,0,1]
	v_pk_fma_f32 v[158:159], v[22:23], s[2:3], v[158:159] op_sel_hi:[1,0,1]
	v_pk_fma_f32 v[156:157], v[24:25], s[2:3], v[156:157] op_sel_hi:[1,0,1]
	v_pk_fma_f32 v[154:155], v[26:27], s[2:3], v[154:155] op_sel_hi:[1,0,1]
	v_pk_fma_f32 v[152:153], v[28:29], s[2:3], v[152:153] op_sel_hi:[1,0,1]
	v_pk_fma_f32 v[150:151], v[30:31], s[2:3], v[150:151] op_sel_hi:[1,0,1]
	v_readlane_b32 s2, v131, 6
	s_waitcnt vmcnt(18)
	v_cvt_scalef32_pk32_f32_fp6 v[0:31], v[86:91], 1.0
	v_pk_fma_f32 v[86:87], v[0:1], s[2:3], v[92:93] op_sel_hi:[1,0,1]
	v_pk_fma_f32 v[88:89], v[2:3], s[2:3], v[94:95] op_sel_hi:[1,0,1]
	v_pk_fma_f32 v[90:91], v[4:5], s[2:3], v[96:97] op_sel_hi:[1,0,1]
	v_pk_fma_f32 v[92:93], v[6:7], s[2:3], v[98:99] op_sel_hi:[1,0,1]
	v_pk_fma_f32 v[94:95], v[8:9], s[2:3], v[100:101] op_sel_hi:[1,0,1]
	v_pk_fma_f32 v[96:97], v[10:11], s[2:3], v[102:103] op_sel_hi:[1,0,1]
	v_pk_fma_f32 v[98:99], v[12:13], s[2:3], v[164:165] op_sel_hi:[1,0,1]
	v_pk_fma_f32 v[100:101], v[14:15], s[2:3], v[166:167] op_sel_hi:[1,0,1]
	v_pk_fma_f32 v[102:103], v[16:17], s[2:3], v[168:169] op_sel_hi:[1,0,1]
	v_pk_fma_f32 v[162:163], v[18:19], s[2:3], v[162:163] op_sel_hi:[1,0,1]
	v_pk_fma_f32 v[160:161], v[20:21], s[2:3], v[160:161] op_sel_hi:[1,0,1]
	v_pk_fma_f32 v[158:159], v[22:23], s[2:3], v[158:159] op_sel_hi:[1,0,1]
	v_pk_fma_f32 v[156:157], v[24:25], s[2:3], v[156:157] op_sel_hi:[1,0,1]
	v_pk_fma_f32 v[154:155], v[26:27], s[2:3], v[154:155] op_sel_hi:[1,0,1]
	v_pk_fma_f32 v[152:153], v[28:29], s[2:3], v[152:153] op_sel_hi:[1,0,1]
	v_pk_fma_f32 v[150:151], v[30:31], s[2:3], v[150:151] op_sel_hi:[1,0,1]
	v_readlane_b32 s2, v131, 7
	s_waitcnt vmcnt(16)
	v_cvt_scalef32_pk32_f32_fp6 v[0:31], v[80:85], 1.0
	v_pk_fma_f32 v[180:181], v[0:1], s[2:3], v[86:87] op_sel_hi:[1,0,1]
	v_pk_fma_f32 v[178:179], v[2:3], s[2:3], v[88:89] op_sel_hi:[1,0,1]
	v_pk_fma_f32 v[176:177], v[4:5], s[2:3], v[90:91] op_sel_hi:[1,0,1]
	v_pk_fma_f32 v[174:175], v[6:7], s[2:3], v[92:93] op_sel_hi:[1,0,1]
	v_pk_fma_f32 v[172:173], v[8:9], s[2:3], v[94:95] op_sel_hi:[1,0,1]
	v_pk_fma_f32 v[170:171], v[10:11], s[2:3], v[96:97] op_sel_hi:[1,0,1]
	v_pk_fma_f32 v[168:169], v[12:13], s[2:3], v[98:99] op_sel_hi:[1,0,1]
	v_pk_fma_f32 v[166:167], v[14:15], s[2:3], v[100:101] op_sel_hi:[1,0,1]
	v_pk_fma_f32 v[164:165], v[16:17], s[2:3], v[102:103] op_sel_hi:[1,0,1]
	v_pk_fma_f32 v[162:163], v[18:19], s[2:3], v[162:163] op_sel_hi:[1,0,1]
	v_pk_fma_f32 v[160:161], v[20:21], s[2:3], v[160:161] op_sel_hi:[1,0,1]
	v_pk_fma_f32 v[158:159], v[22:23], s[2:3], v[158:159] op_sel_hi:[1,0,1]
	v_pk_fma_f32 v[156:157], v[24:25], s[2:3], v[156:157] op_sel_hi:[1,0,1]
	v_pk_fma_f32 v[154:155], v[26:27], s[2:3], v[154:155] op_sel_hi:[1,0,1]
	v_pk_fma_f32 v[152:153], v[28:29], s[2:3], v[152:153] op_sel_hi:[1,0,1]
	v_pk_fma_f32 v[150:151], v[30:31], s[2:3], v[150:151] op_sel_hi:[1,0,1]
	v_readlane_b32 s2, v241, 16
	v_readlane_b32 s3, v241, 17
	v_readlane_b32 s100, v241, 18
	v_readlane_b32 s101, v241, 19
	s_nop 1
	buffer_load_dwordx4 v[98:101], v129, s[44:47], s2 offen
	buffer_load_dwordx2 v[102:103], v210, s[44:47], s2 offen
	buffer_load_dwordx4 v[92:95], v129, s[44:47], s3 offen
	buffer_load_dwordx2 v[96:97], v210, s[44:47], s3 offen
	buffer_load_dwordx4 v[86:89], v129, s[44:47], s100 offen
	buffer_load_dwordx2 v[90:91], v210, s[44:47], s100 offen
	buffer_load_dwordx4 v[80:83], v129, s[44:47], s101 offen
	buffer_load_dwordx2 v[84:85], v210, s[44:47], s101 offen
	v_readlane_b32 s2, v131, 8
	s_waitcnt vmcnt(22)
	v_cvt_scalef32_pk32_f32_fp6 v[0:31], v[74:79], 1.0
	v_pk_fma_f32 v[74:75], v[0:1], s[2:3], v[180:181] op_sel_hi:[1,0,1]
	v_pk_fma_f32 v[76:77], v[2:3], s[2:3], v[178:179] op_sel_hi:[1,0,1]
	v_pk_fma_f32 v[78:79], v[4:5], s[2:3], v[176:177] op_sel_hi:[1,0,1]
	v_pk_fma_f32 v[174:175], v[6:7], s[2:3], v[174:175] op_sel_hi:[1,0,1]
	v_pk_fma_f32 v[172:173], v[8:9], s[2:3], v[172:173] op_sel_hi:[1,0,1]
	v_pk_fma_f32 v[170:171], v[10:11], s[2:3], v[170:171] op_sel_hi:[1,0,1]
	v_pk_fma_f32 v[168:169], v[12:13], s[2:3], v[168:169] op_sel_hi:[1,0,1]
	v_pk_fma_f32 v[166:167], v[14:15], s[2:3], v[166:167] op_sel_hi:[1,0,1]
	v_pk_fma_f32 v[164:165], v[16:17], s[2:3], v[164:165] op_sel_hi:[1,0,1]
	v_pk_fma_f32 v[162:163], v[18:19], s[2:3], v[162:163] op_sel_hi:[1,0,1]
	v_pk_fma_f32 v[160:161], v[20:21], s[2:3], v[160:161] op_sel_hi:[1,0,1]
	v_pk_fma_f32 v[158:159], v[22:23], s[2:3], v[158:159] op_sel_hi:[1,0,1]
	v_pk_fma_f32 v[156:157], v[24:25], s[2:3], v[156:157] op_sel_hi:[1,0,1]
	v_pk_fma_f32 v[154:155], v[26:27], s[2:3], v[154:155] op_sel_hi:[1,0,1]
	v_pk_fma_f32 v[152:153], v[28:29], s[2:3], v[152:153] op_sel_hi:[1,0,1]
	v_pk_fma_f32 v[150:151], v[30:31], s[2:3], v[150:151] op_sel_hi:[1,0,1]
	v_readlane_b32 s2, v131, 9
	s_waitcnt vmcnt(20)
	v_cvt_scalef32_pk32_f32_fp6 v[0:31], v[68:73], 1.0
	v_pk_fma_f32 v[68:69], v[0:1], s[2:3], v[74:75] op_sel_hi:[1,0,1]
	v_pk_fma_f32 v[70:71], v[2:3], s[2:3], v[76:77] op_sel_hi:[1,0,1]
	v_pk_fma_f32 v[72:73], v[4:5], s[2:3], v[78:79] op_sel_hi:[1,0,1]
	v_pk_fma_f32 v[74:75], v[6:7], s[2:3], v[174:175] op_sel_hi:[1,0,1]
	v_pk_fma_f32 v[76:77], v[8:9], s[2:3], v[172:173] op_sel_hi:[1,0,1]
	v_pk_fma_f32 v[78:79], v[10:11], s[2:3], v[170:171] op_sel_hi:[1,0,1]
	v_pk_fma_f32 v[168:169], v[12:13], s[2:3], v[168:169] op_sel_hi:[1,0,1]
	v_pk_fma_f32 v[166:167], v[14:15], s[2:3], v[166:167] op_sel_hi:[1,0,1]
	v_pk_fma_f32 v[164:165], v[16:17], s[2:3], v[164:165] op_sel_hi:[1,0,1]
	v_pk_fma_f32 v[162:163], v[18:19], s[2:3], v[162:163] op_sel_hi:[1,0,1]
	v_pk_fma_f32 v[160:161], v[20:21], s[2:3], v[160:161] op_sel_hi:[1,0,1]
	v_pk_fma_f32 v[158:159], v[22:23], s[2:3], v[158:159] op_sel_hi:[1,0,1]
	v_pk_fma_f32 v[156:157], v[24:25], s[2:3], v[156:157] op_sel_hi:[1,0,1]
	v_pk_fma_f32 v[154:155], v[26:27], s[2:3], v[154:155] op_sel_hi:[1,0,1]
	v_pk_fma_f32 v[152:153], v[28:29], s[2:3], v[152:153] op_sel_hi:[1,0,1]
	v_pk_fma_f32 v[150:151], v[30:31], s[2:3], v[150:151] op_sel_hi:[1,0,1]
	v_readlane_b32 s2, v131, 10
	s_waitcnt vmcnt(18)
	v_cvt_scalef32_pk32_f32_fp6 v[0:31], v[56:61], 1.0
	v_pk_fma_f32 v[56:57], v[0:1], s[2:3], v[68:69] op_sel_hi:[1,0,1]
	v_pk_fma_f32 v[58:59], v[2:3], s[2:3], v[70:71] op_sel_hi:[1,0,1]
	v_pk_fma_f32 v[60:61], v[4:5], s[2:3], v[72:73] op_sel_hi:[1,0,1]
	v_pk_fma_f32 v[68:69], v[6:7], s[2:3], v[74:75] op_sel_hi:[1,0,1]
	v_pk_fma_f32 v[70:71], v[8:9], s[2:3], v[76:77] op_sel_hi:[1,0,1]
	v_pk_fma_f32 v[72:73], v[10:11], s[2:3], v[78:79] op_sel_hi:[1,0,1]
	v_pk_fma_f32 v[74:75], v[12:13], s[2:3], v[168:169] op_sel_hi:[1,0,1]
	v_pk_fma_f32 v[76:77], v[14:15], s[2:3], v[166:167] op_sel_hi:[1,0,1]
	v_pk_fma_f32 v[78:79], v[16:17], s[2:3], v[164:165] op_sel_hi:[1,0,1]
	v_pk_fma_f32 v[162:163], v[18:19], s[2:3], v[162:163] op_sel_hi:[1,0,1]
	v_pk_fma_f32 v[160:161], v[20:21], s[2:3], v[160:161] op_sel_hi:[1,0,1]
	v_pk_fma_f32 v[158:159], v[22:23], s[2:3], v[158:159] op_sel_hi:[1,0,1]
	v_pk_fma_f32 v[156:157], v[24:25], s[2:3], v[156:157] op_sel_hi:[1,0,1]
	v_pk_fma_f32 v[154:155], v[26:27], s[2:3], v[154:155] op_sel_hi:[1,0,1]
	v_pk_fma_f32 v[152:153], v[28:29], s[2:3], v[152:153] op_sel_hi:[1,0,1]
	v_pk_fma_f32 v[150:151], v[30:31], s[2:3], v[150:151] op_sel_hi:[1,0,1]
	v_readlane_b32 s2, v131, 11
	s_waitcnt vmcnt(16)
	v_cvt_scalef32_pk32_f32_fp6 v[0:31], v[44:49], 1.0
	v_pk_fma_f32 v[164:165], v[0:1], s[2:3], v[56:57] op_sel_hi:[1,0,1]
	v_pk_fma_f32 v[166:167], v[2:3], s[2:3], v[58:59] op_sel_hi:[1,0,1]
	v_pk_fma_f32 v[168:169], v[4:5], s[2:3], v[60:61] op_sel_hi:[1,0,1]
	v_pk_fma_f32 v[170:171], v[6:7], s[2:3], v[68:69] op_sel_hi:[1,0,1]
	v_pk_fma_f32 v[172:173], v[8:9], s[2:3], v[70:71] op_sel_hi:[1,0,1]
	v_pk_fma_f32 v[174:175], v[10:11], s[2:3], v[72:73] op_sel_hi:[1,0,1]
	v_pk_fma_f32 v[176:177], v[12:13], s[2:3], v[74:75] op_sel_hi:[1,0,1]
	v_pk_fma_f32 v[178:179], v[14:15], s[2:3], v[76:77] op_sel_hi:[1,0,1]
	v_pk_fma_f32 v[180:181], v[16:17], s[2:3], v[78:79] op_sel_hi:[1,0,1]
	v_pk_fma_f32 v[162:163], v[18:19], s[2:3], v[162:163] op_sel_hi:[1,0,1]
	v_pk_fma_f32 v[160:161], v[20:21], s[2:3], v[160:161] op_sel_hi:[1,0,1]
	v_pk_fma_f32 v[158:159], v[22:23], s[2:3], v[158:159] op_sel_hi:[1,0,1]
	v_pk_fma_f32 v[156:157], v[24:25], s[2:3], v[156:157] op_sel_hi:[1,0,1]
	v_pk_fma_f32 v[154:155], v[26:27], s[2:3], v[154:155] op_sel_hi:[1,0,1]
	v_pk_fma_f32 v[152:153], v[28:29], s[2:3], v[152:153] op_sel_hi:[1,0,1]
	v_pk_fma_f32 v[150:151], v[30:31], s[2:3], v[150:151] op_sel_hi:[1,0,1]
	v_readlane_b32 s2, v241, 20
	v_readlane_b32 s3, v241, 21
	v_readlane_b32 s100, v241, 22
	v_readlane_b32 s101, v241, 23
	s_nop 1
	buffer_load_dwordx4 v[74:77], v129, s[44:47], s2 offen
	buffer_load_dwordx2 v[78:79], v210, s[44:47], s2 offen
	buffer_load_dwordx4 v[68:71], v129, s[44:47], s3 offen
	buffer_load_dwordx2 v[72:73], v210, s[44:47], s3 offen
	buffer_load_dwordx4 v[56:59], v129, s[44:47], s100 offen
	buffer_load_dwordx2 v[60:61], v210, s[44:47], s100 offen
	buffer_load_dwordx4 v[44:47], v129, s[44:47], s101 offen
	buffer_load_dwordx2 v[48:49], v210, s[44:47], s101 offen
	v_readlane_b32 s2, v131, 12
	s_waitcnt vmcnt(22)
	v_cvt_scalef32_pk32_f32_fp6 v[0:31], v[62:67], 1.0
	v_pk_fma_f32 v[62:63], v[0:1], s[2:3], v[164:165] op_sel_hi:[1,0,1]
	v_pk_fma_f32 v[64:65], v[2:3], s[2:3], v[166:167] op_sel_hi:[1,0,1]
	v_pk_fma_f32 v[66:67], v[4:5], s[2:3], v[168:169] op_sel_hi:[1,0,1]
	v_pk_fma_f32 v[164:165], v[6:7], s[2:3], v[170:171] op_sel_hi:[1,0,1]
	v_pk_fma_f32 v[166:167], v[8:9], s[2:3], v[172:173] op_sel_hi:[1,0,1]
	v_pk_fma_f32 v[168:169], v[10:11], s[2:3], v[174:175] op_sel_hi:[1,0,1]
	v_pk_fma_f32 v[170:171], v[12:13], s[2:3], v[176:177] op_sel_hi:[1,0,1]
	v_pk_fma_f32 v[172:173], v[14:15], s[2:3], v[178:179] op_sel_hi:[1,0,1]
	v_pk_fma_f32 v[174:175], v[16:17], s[2:3], v[180:181] op_sel_hi:[1,0,1]
	v_pk_fma_f32 v[162:163], v[18:19], s[2:3], v[162:163] op_sel_hi:[1,0,1]
	v_pk_fma_f32 v[160:161], v[20:21], s[2:3], v[160:161] op_sel_hi:[1,0,1]
	v_pk_fma_f32 v[158:159], v[22:23], s[2:3], v[158:159] op_sel_hi:[1,0,1]
	v_pk_fma_f32 v[156:157], v[24:25], s[2:3], v[156:157] op_sel_hi:[1,0,1]
	v_pk_fma_f32 v[154:155], v[26:27], s[2:3], v[154:155] op_sel_hi:[1,0,1]
	v_pk_fma_f32 v[152:153], v[28:29], s[2:3], v[152:153] op_sel_hi:[1,0,1]
	v_pk_fma_f32 v[150:151], v[30:31], s[2:3], v[150:151] op_sel_hi:[1,0,1]
	v_readlane_b32 s2, v131, 13
	s_waitcnt vmcnt(20)
	v_cvt_scalef32_pk32_f32_fp6 v[0:31], v[50:55], 1.0
	v_pk_fma_f32 v[50:51], v[0:1], s[2:3], v[62:63] op_sel_hi:[1,0,1]
	v_pk_fma_f32 v[52:53], v[2:3], s[2:3], v[64:65] op_sel_hi:[1,0,1]
	v_pk_fma_f32 v[54:55], v[4:5], s[2:3], v[66:67] op_sel_hi:[1,0,1]
	v_pk_fma_f32 v[62:63], v[6:7], s[2:3], v[164:165] op_sel_hi:[1,0,1]
	v_pk_fma_f32 v[64:65], v[8:9], s[2:3], v[166:167] op_sel_hi:[1,0,1]
	v_pk_fma_f32 v[66:67], v[10:11], s[2:3], v[168:169] op_sel_hi:[1,0,1]
	v_pk_fma_f32 v[164:165], v[12:13], s[2:3], v[170:171] op_sel_hi:[1,0,1]
	v_pk_fma_f32 v[166:167], v[14:15], s[2:3], v[172:173] op_sel_hi:[1,0,1]
	v_pk_fma_f32 v[168:169], v[16:17], s[2:3], v[174:175] op_sel_hi:[1,0,1]
	v_pk_fma_f32 v[162:163], v[18:19], s[2:3], v[162:163] op_sel_hi:[1,0,1]
	v_pk_fma_f32 v[160:161], v[20:21], s[2:3], v[160:161] op_sel_hi:[1,0,1]
	v_pk_fma_f32 v[158:159], v[22:23], s[2:3], v[158:159] op_sel_hi:[1,0,1]
	v_pk_fma_f32 v[156:157], v[24:25], s[2:3], v[156:157] op_sel_hi:[1,0,1]
	v_pk_fma_f32 v[154:155], v[26:27], s[2:3], v[154:155] op_sel_hi:[1,0,1]
	v_pk_fma_f32 v[152:153], v[28:29], s[2:3], v[152:153] op_sel_hi:[1,0,1]
	v_pk_fma_f32 v[150:151], v[30:31], s[2:3], v[150:151] op_sel_hi:[1,0,1]
	v_readlane_b32 s2, v131, 14
	s_waitcnt vmcnt(18)
	v_cvt_scalef32_pk32_f32_fp6 v[0:31], v[38:43], 1.0
	v_pk_fma_f32 v[38:39], v[0:1], s[2:3], v[50:51] op_sel_hi:[1,0,1]
	v_pk_fma_f32 v[40:41], v[2:3], s[2:3], v[52:53] op_sel_hi:[1,0,1]
	v_pk_fma_f32 v[42:43], v[4:5], s[2:3], v[54:55] op_sel_hi:[1,0,1]
	v_pk_fma_f32 v[50:51], v[6:7], s[2:3], v[62:63] op_sel_hi:[1,0,1]
	v_pk_fma_f32 v[52:53], v[8:9], s[2:3], v[64:65] op_sel_hi:[1,0,1]
	v_pk_fma_f32 v[54:55], v[10:11], s[2:3], v[66:67] op_sel_hi:[1,0,1]
	v_pk_fma_f32 v[62:63], v[12:13], s[2:3], v[164:165] op_sel_hi:[1,0,1]
	v_pk_fma_f32 v[64:65], v[14:15], s[2:3], v[166:167] op_sel_hi:[1,0,1]
	v_pk_fma_f32 v[66:67], v[16:17], s[2:3], v[168:169] op_sel_hi:[1,0,1]
	v_pk_fma_f32 v[162:163], v[18:19], s[2:3], v[162:163] op_sel_hi:[1,0,1]
	v_pk_fma_f32 v[160:161], v[20:21], s[2:3], v[160:161] op_sel_hi:[1,0,1]
	v_pk_fma_f32 v[158:159], v[22:23], s[2:3], v[158:159] op_sel_hi:[1,0,1]
	v_pk_fma_f32 v[156:157], v[24:25], s[2:3], v[156:157] op_sel_hi:[1,0,1]
	v_pk_fma_f32 v[154:155], v[26:27], s[2:3], v[154:155] op_sel_hi:[1,0,1]
	v_pk_fma_f32 v[152:153], v[28:29], s[2:3], v[152:153] op_sel_hi:[1,0,1]
	v_pk_fma_f32 v[150:151], v[30:31], s[2:3], v[150:151] op_sel_hi:[1,0,1]
	v_readlane_b32 s2, v131, 15
	s_waitcnt vmcnt(16)
	v_cvt_scalef32_pk32_f32_fp6 v[0:31], v[32:37], 1.0
	v_pk_fma_f32 v[164:165], v[0:1], s[2:3], v[38:39] op_sel_hi:[1,0,1]
	v_pk_fma_f32 v[166:167], v[2:3], s[2:3], v[40:41] op_sel_hi:[1,0,1]
	v_pk_fma_f32 v[168:169], v[4:5], s[2:3], v[42:43] op_sel_hi:[1,0,1]
	v_pk_fma_f32 v[170:171], v[6:7], s[2:3], v[50:51] op_sel_hi:[1,0,1]
	v_pk_fma_f32 v[172:173], v[8:9], s[2:3], v[52:53] op_sel_hi:[1,0,1]
	v_pk_fma_f32 v[174:175], v[10:11], s[2:3], v[54:55] op_sel_hi:[1,0,1]
	v_pk_fma_f32 v[176:177], v[12:13], s[2:3], v[62:63] op_sel_hi:[1,0,1]
	v_pk_fma_f32 v[178:179], v[14:15], s[2:3], v[64:65] op_sel_hi:[1,0,1]
	v_pk_fma_f32 v[180:181], v[16:17], s[2:3], v[66:67] op_sel_hi:[1,0,1]
	v_pk_fma_f32 v[162:163], v[18:19], s[2:3], v[162:163] op_sel_hi:[1,0,1]
	v_pk_fma_f32 v[160:161], v[20:21], s[2:3], v[160:161] op_sel_hi:[1,0,1]
	v_pk_fma_f32 v[158:159], v[22:23], s[2:3], v[158:159] op_sel_hi:[1,0,1]
	v_pk_fma_f32 v[156:157], v[24:25], s[2:3], v[156:157] op_sel_hi:[1,0,1]
	v_pk_fma_f32 v[154:155], v[26:27], s[2:3], v[154:155] op_sel_hi:[1,0,1]
	v_pk_fma_f32 v[152:153], v[28:29], s[2:3], v[152:153] op_sel_hi:[1,0,1]
	v_pk_fma_f32 v[150:151], v[30:31], s[2:3], v[150:151] op_sel_hi:[1,0,1]
	v_readlane_b32 s2, v241, 24
	v_readlane_b32 s3, v241, 25
	v_readlane_b32 s100, v241, 26
	v_readlane_b32 s101, v241, 27
	s_nop 1
	buffer_load_dwordx4 v[62:65], v129, s[44:47], s2 offen
	buffer_load_dwordx2 v[66:67], v210, s[44:47], s2 offen
	buffer_load_dwordx4 v[50:53], v129, s[44:47], s3 offen
	buffer_load_dwordx2 v[54:55], v210, s[44:47], s3 offen
	buffer_load_dwordx4 v[38:41], v129, s[44:47], s100 offen
	buffer_load_dwordx2 v[42:43], v210, s[44:47], s100 offen
	buffer_load_dwordx4 v[32:35], v129, s[44:47], s101 offen
	buffer_load_dwordx2 v[36:37], v210, s[44:47], s101 offen
	v_readlane_b32 s2, v131, 16
	s_waitcnt vmcnt(22)
	v_cvt_scalef32_pk32_f32_fp6 v[0:31], v[98:103], 1.0
	v_pk_fma_f32 v[98:99], v[0:1], s[2:3], v[164:165] op_sel_hi:[1,0,1]
	v_pk_fma_f32 v[100:101], v[2:3], s[2:3], v[166:167] op_sel_hi:[1,0,1]
	v_pk_fma_f32 v[102:103], v[4:5], s[2:3], v[168:169] op_sel_hi:[1,0,1]
	v_pk_fma_f32 v[164:165], v[6:7], s[2:3], v[170:171] op_sel_hi:[1,0,1]
	v_pk_fma_f32 v[166:167], v[8:9], s[2:3], v[172:173] op_sel_hi:[1,0,1]
	v_pk_fma_f32 v[168:169], v[10:11], s[2:3], v[174:175] op_sel_hi:[1,0,1]
	v_pk_fma_f32 v[170:171], v[12:13], s[2:3], v[176:177] op_sel_hi:[1,0,1]
	v_pk_fma_f32 v[172:173], v[14:15], s[2:3], v[178:179] op_sel_hi:[1,0,1]
	v_pk_fma_f32 v[174:175], v[16:17], s[2:3], v[180:181] op_sel_hi:[1,0,1]
	v_pk_fma_f32 v[162:163], v[18:19], s[2:3], v[162:163] op_sel_hi:[1,0,1]
	v_pk_fma_f32 v[160:161], v[20:21], s[2:3], v[160:161] op_sel_hi:[1,0,1]
	v_pk_fma_f32 v[158:159], v[22:23], s[2:3], v[158:159] op_sel_hi:[1,0,1]
	v_pk_fma_f32 v[156:157], v[24:25], s[2:3], v[156:157] op_sel_hi:[1,0,1]
	v_pk_fma_f32 v[154:155], v[26:27], s[2:3], v[154:155] op_sel_hi:[1,0,1]
	v_pk_fma_f32 v[152:153], v[28:29], s[2:3], v[152:153] op_sel_hi:[1,0,1]
	v_pk_fma_f32 v[150:151], v[30:31], s[2:3], v[150:151] op_sel_hi:[1,0,1]
	v_readlane_b32 s2, v131, 17
	s_waitcnt vmcnt(20)
	v_cvt_scalef32_pk32_f32_fp6 v[0:31], v[92:97], 1.0
	v_pk_fma_f32 v[92:93], v[0:1], s[2:3], v[98:99] op_sel_hi:[1,0,1]
	v_pk_fma_f32 v[94:95], v[2:3], s[2:3], v[100:101] op_sel_hi:[1,0,1]
	v_pk_fma_f32 v[96:97], v[4:5], s[2:3], v[102:103] op_sel_hi:[1,0,1]
	v_pk_fma_f32 v[98:99], v[6:7], s[2:3], v[164:165] op_sel_hi:[1,0,1]
	v_pk_fma_f32 v[100:101], v[8:9], s[2:3], v[166:167] op_sel_hi:[1,0,1]
	v_pk_fma_f32 v[102:103], v[10:11], s[2:3], v[168:169] op_sel_hi:[1,0,1]
	v_pk_fma_f32 v[164:165], v[12:13], s[2:3], v[170:171] op_sel_hi:[1,0,1]
	v_pk_fma_f32 v[166:167], v[14:15], s[2:3], v[172:173] op_sel_hi:[1,0,1]
	v_pk_fma_f32 v[168:169], v[16:17], s[2:3], v[174:175] op_sel_hi:[1,0,1]
	v_pk_fma_f32 v[162:163], v[18:19], s[2:3], v[162:163] op_sel_hi:[1,0,1]
	v_pk_fma_f32 v[160:161], v[20:21], s[2:3], v[160:161] op_sel_hi:[1,0,1]
	v_pk_fma_f32 v[158:159], v[22:23], s[2:3], v[158:159] op_sel_hi:[1,0,1]
	v_pk_fma_f32 v[156:157], v[24:25], s[2:3], v[156:157] op_sel_hi:[1,0,1]
	v_pk_fma_f32 v[154:155], v[26:27], s[2:3], v[154:155] op_sel_hi:[1,0,1]
	v_pk_fma_f32 v[152:153], v[28:29], s[2:3], v[152:153] op_sel_hi:[1,0,1]
	v_pk_fma_f32 v[150:151], v[30:31], s[2:3], v[150:151] op_sel_hi:[1,0,1]
	v_readlane_b32 s2, v131, 18
	s_waitcnt vmcnt(18)
	v_cvt_scalef32_pk32_f32_fp6 v[0:31], v[86:91], 1.0
	v_pk_fma_f32 v[86:87], v[0:1], s[2:3], v[92:93] op_sel_hi:[1,0,1]
	v_pk_fma_f32 v[88:89], v[2:3], s[2:3], v[94:95] op_sel_hi:[1,0,1]
	v_pk_fma_f32 v[90:91], v[4:5], s[2:3], v[96:97] op_sel_hi:[1,0,1]
	v_pk_fma_f32 v[92:93], v[6:7], s[2:3], v[98:99] op_sel_hi:[1,0,1]
	v_pk_fma_f32 v[94:95], v[8:9], s[2:3], v[100:101] op_sel_hi:[1,0,1]
	v_pk_fma_f32 v[96:97], v[10:11], s[2:3], v[102:103] op_sel_hi:[1,0,1]
	v_pk_fma_f32 v[98:99], v[12:13], s[2:3], v[164:165] op_sel_hi:[1,0,1]
	v_pk_fma_f32 v[100:101], v[14:15], s[2:3], v[166:167] op_sel_hi:[1,0,1]
	v_pk_fma_f32 v[102:103], v[16:17], s[2:3], v[168:169] op_sel_hi:[1,0,1]
	v_pk_fma_f32 v[162:163], v[18:19], s[2:3], v[162:163] op_sel_hi:[1,0,1]
	v_pk_fma_f32 v[160:161], v[20:21], s[2:3], v[160:161] op_sel_hi:[1,0,1]
	v_pk_fma_f32 v[158:159], v[22:23], s[2:3], v[158:159] op_sel_hi:[1,0,1]
	v_pk_fma_f32 v[156:157], v[24:25], s[2:3], v[156:157] op_sel_hi:[1,0,1]
	v_pk_fma_f32 v[154:155], v[26:27], s[2:3], v[154:155] op_sel_hi:[1,0,1]
	v_pk_fma_f32 v[152:153], v[28:29], s[2:3], v[152:153] op_sel_hi:[1,0,1]
	v_pk_fma_f32 v[150:151], v[30:31], s[2:3], v[150:151] op_sel_hi:[1,0,1]
	v_readlane_b32 s2, v131, 19
	s_waitcnt vmcnt(16)
	v_cvt_scalef32_pk32_f32_fp6 v[0:31], v[80:85], 1.0
	v_pk_fma_f32 v[180:181], v[0:1], s[2:3], v[86:87] op_sel_hi:[1,0,1]
	v_pk_fma_f32 v[178:179], v[2:3], s[2:3], v[88:89] op_sel_hi:[1,0,1]
	v_pk_fma_f32 v[176:177], v[4:5], s[2:3], v[90:91] op_sel_hi:[1,0,1]
	v_pk_fma_f32 v[174:175], v[6:7], s[2:3], v[92:93] op_sel_hi:[1,0,1]
	v_pk_fma_f32 v[172:173], v[8:9], s[2:3], v[94:95] op_sel_hi:[1,0,1]
	v_pk_fma_f32 v[170:171], v[10:11], s[2:3], v[96:97] op_sel_hi:[1,0,1]
	v_pk_fma_f32 v[168:169], v[12:13], s[2:3], v[98:99] op_sel_hi:[1,0,1]
	v_pk_fma_f32 v[166:167], v[14:15], s[2:3], v[100:101] op_sel_hi:[1,0,1]
	v_pk_fma_f32 v[164:165], v[16:17], s[2:3], v[102:103] op_sel_hi:[1,0,1]
	v_pk_fma_f32 v[162:163], v[18:19], s[2:3], v[162:163] op_sel_hi:[1,0,1]
	v_pk_fma_f32 v[160:161], v[20:21], s[2:3], v[160:161] op_sel_hi:[1,0,1]
	v_pk_fma_f32 v[158:159], v[22:23], s[2:3], v[158:159] op_sel_hi:[1,0,1]
	v_pk_fma_f32 v[156:157], v[24:25], s[2:3], v[156:157] op_sel_hi:[1,0,1]
	v_pk_fma_f32 v[154:155], v[26:27], s[2:3], v[154:155] op_sel_hi:[1,0,1]
	v_pk_fma_f32 v[152:153], v[28:29], s[2:3], v[152:153] op_sel_hi:[1,0,1]
	v_pk_fma_f32 v[150:151], v[30:31], s[2:3], v[150:151] op_sel_hi:[1,0,1]
	v_readlane_b32 s2, v241, 28
	v_readlane_b32 s3, v241, 29
	v_readlane_b32 s100, v241, 30
	v_readlane_b32 s101, v241, 31
	s_nop 1
	buffer_load_dwordx4 v[98:101], v129, s[44:47], s2 offen
	buffer_load_dwordx2 v[102:103], v210, s[44:47], s2 offen
	buffer_load_dwordx4 v[92:95], v129, s[44:47], s3 offen
	buffer_load_dwordx2 v[96:97], v210, s[44:47], s3 offen
	buffer_load_dwordx4 v[86:89], v129, s[44:47], s100 offen
	buffer_load_dwordx2 v[90:91], v210, s[44:47], s100 offen
	buffer_load_dwordx4 v[80:83], v129, s[44:47], s101 offen
	buffer_load_dwordx2 v[84:85], v210, s[44:47], s101 offen
	v_readlane_b32 s2, v131, 20
	s_waitcnt vmcnt(22)
	v_cvt_scalef32_pk32_f32_fp6 v[0:31], v[74:79], 1.0
	v_pk_fma_f32 v[74:75], v[0:1], s[2:3], v[180:181] op_sel_hi:[1,0,1]
	v_pk_fma_f32 v[76:77], v[2:3], s[2:3], v[178:179] op_sel_hi:[1,0,1]
	v_pk_fma_f32 v[78:79], v[4:5], s[2:3], v[176:177] op_sel_hi:[1,0,1]
	v_pk_fma_f32 v[174:175], v[6:7], s[2:3], v[174:175] op_sel_hi:[1,0,1]
	v_pk_fma_f32 v[172:173], v[8:9], s[2:3], v[172:173] op_sel_hi:[1,0,1]
	v_pk_fma_f32 v[170:171], v[10:11], s[2:3], v[170:171] op_sel_hi:[1,0,1]
	v_pk_fma_f32 v[168:169], v[12:13], s[2:3], v[168:169] op_sel_hi:[1,0,1]
	v_pk_fma_f32 v[166:167], v[14:15], s[2:3], v[166:167] op_sel_hi:[1,0,1]
	v_pk_fma_f32 v[164:165], v[16:17], s[2:3], v[164:165] op_sel_hi:[1,0,1]
	v_pk_fma_f32 v[162:163], v[18:19], s[2:3], v[162:163] op_sel_hi:[1,0,1]
	v_pk_fma_f32 v[160:161], v[20:21], s[2:3], v[160:161] op_sel_hi:[1,0,1]
	v_pk_fma_f32 v[158:159], v[22:23], s[2:3], v[158:159] op_sel_hi:[1,0,1]
	v_pk_fma_f32 v[156:157], v[24:25], s[2:3], v[156:157] op_sel_hi:[1,0,1]
	v_pk_fma_f32 v[154:155], v[26:27], s[2:3], v[154:155] op_sel_hi:[1,0,1]
	v_pk_fma_f32 v[152:153], v[28:29], s[2:3], v[152:153] op_sel_hi:[1,0,1]
	v_pk_fma_f32 v[150:151], v[30:31], s[2:3], v[150:151] op_sel_hi:[1,0,1]
	v_readlane_b32 s2, v131, 21
	s_waitcnt vmcnt(20)
	v_cvt_scalef32_pk32_f32_fp6 v[0:31], v[68:73], 1.0
	v_pk_fma_f32 v[68:69], v[0:1], s[2:3], v[74:75] op_sel_hi:[1,0,1]
	v_pk_fma_f32 v[70:71], v[2:3], s[2:3], v[76:77] op_sel_hi:[1,0,1]
	v_pk_fma_f32 v[72:73], v[4:5], s[2:3], v[78:79] op_sel_hi:[1,0,1]
	v_pk_fma_f32 v[74:75], v[6:7], s[2:3], v[174:175] op_sel_hi:[1,0,1]
	v_pk_fma_f32 v[76:77], v[8:9], s[2:3], v[172:173] op_sel_hi:[1,0,1]
	v_pk_fma_f32 v[78:79], v[10:11], s[2:3], v[170:171] op_sel_hi:[1,0,1]
	v_pk_fma_f32 v[168:169], v[12:13], s[2:3], v[168:169] op_sel_hi:[1,0,1]
	v_pk_fma_f32 v[166:167], v[14:15], s[2:3], v[166:167] op_sel_hi:[1,0,1]
	v_pk_fma_f32 v[164:165], v[16:17], s[2:3], v[164:165] op_sel_hi:[1,0,1]
	v_pk_fma_f32 v[162:163], v[18:19], s[2:3], v[162:163] op_sel_hi:[1,0,1]
	v_pk_fma_f32 v[160:161], v[20:21], s[2:3], v[160:161] op_sel_hi:[1,0,1]
	v_pk_fma_f32 v[158:159], v[22:23], s[2:3], v[158:159] op_sel_hi:[1,0,1]
	v_pk_fma_f32 v[156:157], v[24:25], s[2:3], v[156:157] op_sel_hi:[1,0,1]
	v_pk_fma_f32 v[154:155], v[26:27], s[2:3], v[154:155] op_sel_hi:[1,0,1]
	v_pk_fma_f32 v[152:153], v[28:29], s[2:3], v[152:153] op_sel_hi:[1,0,1]
	v_pk_fma_f32 v[150:151], v[30:31], s[2:3], v[150:151] op_sel_hi:[1,0,1]
	v_readlane_b32 s2, v131, 22
	s_waitcnt vmcnt(18)
	v_cvt_scalef32_pk32_f32_fp6 v[0:31], v[56:61], 1.0
	v_pk_fma_f32 v[56:57], v[0:1], s[2:3], v[68:69] op_sel_hi:[1,0,1]
	v_pk_fma_f32 v[58:59], v[2:3], s[2:3], v[70:71] op_sel_hi:[1,0,1]
	v_pk_fma_f32 v[60:61], v[4:5], s[2:3], v[72:73] op_sel_hi:[1,0,1]
	v_pk_fma_f32 v[68:69], v[6:7], s[2:3], v[74:75] op_sel_hi:[1,0,1]
	v_pk_fma_f32 v[70:71], v[8:9], s[2:3], v[76:77] op_sel_hi:[1,0,1]
	v_pk_fma_f32 v[72:73], v[10:11], s[2:3], v[78:79] op_sel_hi:[1,0,1]
	v_pk_fma_f32 v[74:75], v[12:13], s[2:3], v[168:169] op_sel_hi:[1,0,1]
	v_pk_fma_f32 v[76:77], v[14:15], s[2:3], v[166:167] op_sel_hi:[1,0,1]
	v_pk_fma_f32 v[78:79], v[16:17], s[2:3], v[164:165] op_sel_hi:[1,0,1]
	v_pk_fma_f32 v[162:163], v[18:19], s[2:3], v[162:163] op_sel_hi:[1,0,1]
	v_pk_fma_f32 v[160:161], v[20:21], s[2:3], v[160:161] op_sel_hi:[1,0,1]
	v_pk_fma_f32 v[158:159], v[22:23], s[2:3], v[158:159] op_sel_hi:[1,0,1]
	v_pk_fma_f32 v[156:157], v[24:25], s[2:3], v[156:157] op_sel_hi:[1,0,1]
	v_pk_fma_f32 v[154:155], v[26:27], s[2:3], v[154:155] op_sel_hi:[1,0,1]
	v_pk_fma_f32 v[152:153], v[28:29], s[2:3], v[152:153] op_sel_hi:[1,0,1]
	v_pk_fma_f32 v[150:151], v[30:31], s[2:3], v[150:151] op_sel_hi:[1,0,1]
	v_readlane_b32 s2, v131, 23
	s_waitcnt vmcnt(16)
	v_cvt_scalef32_pk32_f32_fp6 v[0:31], v[44:49], 1.0
	v_pk_fma_f32 v[164:165], v[0:1], s[2:3], v[56:57] op_sel_hi:[1,0,1]
	v_pk_fma_f32 v[166:167], v[2:3], s[2:3], v[58:59] op_sel_hi:[1,0,1]
	v_pk_fma_f32 v[168:169], v[4:5], s[2:3], v[60:61] op_sel_hi:[1,0,1]
	v_pk_fma_f32 v[170:171], v[6:7], s[2:3], v[68:69] op_sel_hi:[1,0,1]
	v_pk_fma_f32 v[172:173], v[8:9], s[2:3], v[70:71] op_sel_hi:[1,0,1]
	v_pk_fma_f32 v[174:175], v[10:11], s[2:3], v[72:73] op_sel_hi:[1,0,1]
	v_pk_fma_f32 v[176:177], v[12:13], s[2:3], v[74:75] op_sel_hi:[1,0,1]
	v_pk_fma_f32 v[178:179], v[14:15], s[2:3], v[76:77] op_sel_hi:[1,0,1]
	v_pk_fma_f32 v[180:181], v[16:17], s[2:3], v[78:79] op_sel_hi:[1,0,1]
	v_pk_fma_f32 v[162:163], v[18:19], s[2:3], v[162:163] op_sel_hi:[1,0,1]
	v_pk_fma_f32 v[160:161], v[20:21], s[2:3], v[160:161] op_sel_hi:[1,0,1]
	v_pk_fma_f32 v[158:159], v[22:23], s[2:3], v[158:159] op_sel_hi:[1,0,1]
	v_pk_fma_f32 v[156:157], v[24:25], s[2:3], v[156:157] op_sel_hi:[1,0,1]
	v_pk_fma_f32 v[154:155], v[26:27], s[2:3], v[154:155] op_sel_hi:[1,0,1]
	v_pk_fma_f32 v[152:153], v[28:29], s[2:3], v[152:153] op_sel_hi:[1,0,1]
	v_pk_fma_f32 v[150:151], v[30:31], s[2:3], v[150:151] op_sel_hi:[1,0,1]
	v_readlane_b32 s2, v241, 32
	v_readlane_b32 s3, v241, 33
	v_readlane_b32 s100, v241, 34
	v_readlane_b32 s101, v241, 35
	s_nop 1
	buffer_load_dwordx4 v[74:77], v129, s[44:47], s2 offen
	buffer_load_dwordx2 v[78:79], v210, s[44:47], s2 offen
	buffer_load_dwordx4 v[68:71], v129, s[44:47], s3 offen
	buffer_load_dwordx2 v[72:73], v210, s[44:47], s3 offen
	buffer_load_dwordx4 v[56:59], v129, s[44:47], s100 offen
	buffer_load_dwordx2 v[60:61], v210, s[44:47], s100 offen
	buffer_load_dwordx4 v[44:47], v129, s[44:47], s101 offen
	buffer_load_dwordx2 v[48:49], v210, s[44:47], s101 offen
	v_readlane_b32 s2, v131, 24
	s_waitcnt vmcnt(22)
	v_cvt_scalef32_pk32_f32_fp6 v[0:31], v[62:67], 1.0
	v_pk_fma_f32 v[62:63], v[0:1], s[2:3], v[164:165] op_sel_hi:[1,0,1]
	v_pk_fma_f32 v[64:65], v[2:3], s[2:3], v[166:167] op_sel_hi:[1,0,1]
	v_pk_fma_f32 v[66:67], v[4:5], s[2:3], v[168:169] op_sel_hi:[1,0,1]
	v_pk_fma_f32 v[164:165], v[6:7], s[2:3], v[170:171] op_sel_hi:[1,0,1]
	v_pk_fma_f32 v[166:167], v[8:9], s[2:3], v[172:173] op_sel_hi:[1,0,1]
	v_pk_fma_f32 v[168:169], v[10:11], s[2:3], v[174:175] op_sel_hi:[1,0,1]
	v_pk_fma_f32 v[170:171], v[12:13], s[2:3], v[176:177] op_sel_hi:[1,0,1]
	v_pk_fma_f32 v[172:173], v[14:15], s[2:3], v[178:179] op_sel_hi:[1,0,1]
	v_pk_fma_f32 v[174:175], v[16:17], s[2:3], v[180:181] op_sel_hi:[1,0,1]
	v_pk_fma_f32 v[162:163], v[18:19], s[2:3], v[162:163] op_sel_hi:[1,0,1]
	v_pk_fma_f32 v[160:161], v[20:21], s[2:3], v[160:161] op_sel_hi:[1,0,1]
	v_pk_fma_f32 v[158:159], v[22:23], s[2:3], v[158:159] op_sel_hi:[1,0,1]
	v_pk_fma_f32 v[156:157], v[24:25], s[2:3], v[156:157] op_sel_hi:[1,0,1]
	v_pk_fma_f32 v[154:155], v[26:27], s[2:3], v[154:155] op_sel_hi:[1,0,1]
	v_pk_fma_f32 v[152:153], v[28:29], s[2:3], v[152:153] op_sel_hi:[1,0,1]
	v_pk_fma_f32 v[150:151], v[30:31], s[2:3], v[150:151] op_sel_hi:[1,0,1]
	v_readlane_b32 s2, v131, 25
	s_waitcnt vmcnt(20)
	v_cvt_scalef32_pk32_f32_fp6 v[0:31], v[50:55], 1.0
	v_pk_fma_f32 v[50:51], v[0:1], s[2:3], v[62:63] op_sel_hi:[1,0,1]
	v_pk_fma_f32 v[52:53], v[2:3], s[2:3], v[64:65] op_sel_hi:[1,0,1]
	v_pk_fma_f32 v[54:55], v[4:5], s[2:3], v[66:67] op_sel_hi:[1,0,1]
	v_pk_fma_f32 v[62:63], v[6:7], s[2:3], v[164:165] op_sel_hi:[1,0,1]
	v_pk_fma_f32 v[64:65], v[8:9], s[2:3], v[166:167] op_sel_hi:[1,0,1]
	v_pk_fma_f32 v[66:67], v[10:11], s[2:3], v[168:169] op_sel_hi:[1,0,1]
	v_pk_fma_f32 v[164:165], v[12:13], s[2:3], v[170:171] op_sel_hi:[1,0,1]
	v_pk_fma_f32 v[166:167], v[14:15], s[2:3], v[172:173] op_sel_hi:[1,0,1]
	v_pk_fma_f32 v[168:169], v[16:17], s[2:3], v[174:175] op_sel_hi:[1,0,1]
	v_pk_fma_f32 v[162:163], v[18:19], s[2:3], v[162:163] op_sel_hi:[1,0,1]
	v_pk_fma_f32 v[160:161], v[20:21], s[2:3], v[160:161] op_sel_hi:[1,0,1]
	v_pk_fma_f32 v[158:159], v[22:23], s[2:3], v[158:159] op_sel_hi:[1,0,1]
	v_pk_fma_f32 v[156:157], v[24:25], s[2:3], v[156:157] op_sel_hi:[1,0,1]
	v_pk_fma_f32 v[154:155], v[26:27], s[2:3], v[154:155] op_sel_hi:[1,0,1]
	v_pk_fma_f32 v[152:153], v[28:29], s[2:3], v[152:153] op_sel_hi:[1,0,1]
	v_pk_fma_f32 v[150:151], v[30:31], s[2:3], v[150:151] op_sel_hi:[1,0,1]
	v_readlane_b32 s2, v131, 26
	s_waitcnt vmcnt(18)
	v_cvt_scalef32_pk32_f32_fp6 v[0:31], v[38:43], 1.0
	v_pk_fma_f32 v[38:39], v[0:1], s[2:3], v[50:51] op_sel_hi:[1,0,1]
	v_pk_fma_f32 v[40:41], v[2:3], s[2:3], v[52:53] op_sel_hi:[1,0,1]
	v_pk_fma_f32 v[42:43], v[4:5], s[2:3], v[54:55] op_sel_hi:[1,0,1]
	v_pk_fma_f32 v[50:51], v[6:7], s[2:3], v[62:63] op_sel_hi:[1,0,1]
	v_pk_fma_f32 v[52:53], v[8:9], s[2:3], v[64:65] op_sel_hi:[1,0,1]
	v_pk_fma_f32 v[54:55], v[10:11], s[2:3], v[66:67] op_sel_hi:[1,0,1]
	v_pk_fma_f32 v[62:63], v[12:13], s[2:3], v[164:165] op_sel_hi:[1,0,1]
	v_pk_fma_f32 v[64:65], v[14:15], s[2:3], v[166:167] op_sel_hi:[1,0,1]
	v_pk_fma_f32 v[66:67], v[16:17], s[2:3], v[168:169] op_sel_hi:[1,0,1]
	v_pk_fma_f32 v[162:163], v[18:19], s[2:3], v[162:163] op_sel_hi:[1,0,1]
	v_pk_fma_f32 v[160:161], v[20:21], s[2:3], v[160:161] op_sel_hi:[1,0,1]
	v_pk_fma_f32 v[158:159], v[22:23], s[2:3], v[158:159] op_sel_hi:[1,0,1]
	v_pk_fma_f32 v[156:157], v[24:25], s[2:3], v[156:157] op_sel_hi:[1,0,1]
	v_pk_fma_f32 v[154:155], v[26:27], s[2:3], v[154:155] op_sel_hi:[1,0,1]
	v_pk_fma_f32 v[152:153], v[28:29], s[2:3], v[152:153] op_sel_hi:[1,0,1]
	v_pk_fma_f32 v[150:151], v[30:31], s[2:3], v[150:151] op_sel_hi:[1,0,1]
	v_readlane_b32 s2, v131, 27
	s_waitcnt vmcnt(16)
	v_cvt_scalef32_pk32_f32_fp6 v[0:31], v[32:37], 1.0
	v_pk_fma_f32 v[164:165], v[0:1], s[2:3], v[38:39] op_sel_hi:[1,0,1]
	v_pk_fma_f32 v[166:167], v[2:3], s[2:3], v[40:41] op_sel_hi:[1,0,1]
	v_pk_fma_f32 v[168:169], v[4:5], s[2:3], v[42:43] op_sel_hi:[1,0,1]
	v_pk_fma_f32 v[170:171], v[6:7], s[2:3], v[50:51] op_sel_hi:[1,0,1]
	v_pk_fma_f32 v[172:173], v[8:9], s[2:3], v[52:53] op_sel_hi:[1,0,1]
	v_pk_fma_f32 v[174:175], v[10:11], s[2:3], v[54:55] op_sel_hi:[1,0,1]
	v_pk_fma_f32 v[176:177], v[12:13], s[2:3], v[62:63] op_sel_hi:[1,0,1]
	v_pk_fma_f32 v[178:179], v[14:15], s[2:3], v[64:65] op_sel_hi:[1,0,1]
	v_pk_fma_f32 v[180:181], v[16:17], s[2:3], v[66:67] op_sel_hi:[1,0,1]
	v_pk_fma_f32 v[162:163], v[18:19], s[2:3], v[162:163] op_sel_hi:[1,0,1]
	v_pk_fma_f32 v[160:161], v[20:21], s[2:3], v[160:161] op_sel_hi:[1,0,1]
	v_pk_fma_f32 v[158:159], v[22:23], s[2:3], v[158:159] op_sel_hi:[1,0,1]
	v_pk_fma_f32 v[156:157], v[24:25], s[2:3], v[156:157] op_sel_hi:[1,0,1]
	v_pk_fma_f32 v[154:155], v[26:27], s[2:3], v[154:155] op_sel_hi:[1,0,1]
	v_pk_fma_f32 v[152:153], v[28:29], s[2:3], v[152:153] op_sel_hi:[1,0,1]
	v_pk_fma_f32 v[150:151], v[30:31], s[2:3], v[150:151] op_sel_hi:[1,0,1]
	v_readlane_b32 s2, v241, 36
	v_readlane_b32 s3, v241, 37
	v_readlane_b32 s100, v241, 38
	v_readlane_b32 s101, v241, 39
	s_nop 1
	buffer_load_dwordx4 v[62:65], v129, s[44:47], s2 offen
	buffer_load_dwordx2 v[66:67], v210, s[44:47], s2 offen
	buffer_load_dwordx4 v[50:53], v129, s[44:47], s3 offen
	buffer_load_dwordx2 v[54:55], v210, s[44:47], s3 offen
	buffer_load_dwordx4 v[38:41], v129, s[44:47], s100 offen
	buffer_load_dwordx2 v[42:43], v210, s[44:47], s100 offen
	buffer_load_dwordx4 v[32:35], v129, s[44:47], s101 offen
	buffer_load_dwordx2 v[36:37], v210, s[44:47], s101 offen
	v_readlane_b32 s2, v131, 28
	s_waitcnt vmcnt(22)
	v_cvt_scalef32_pk32_f32_fp6 v[0:31], v[98:103], 1.0
	v_pk_fma_f32 v[98:99], v[0:1], s[2:3], v[164:165] op_sel_hi:[1,0,1]
	v_pk_fma_f32 v[100:101], v[2:3], s[2:3], v[166:167] op_sel_hi:[1,0,1]
	v_pk_fma_f32 v[102:103], v[4:5], s[2:3], v[168:169] op_sel_hi:[1,0,1]
	v_pk_fma_f32 v[164:165], v[6:7], s[2:3], v[170:171] op_sel_hi:[1,0,1]
	v_pk_fma_f32 v[166:167], v[8:9], s[2:3], v[172:173] op_sel_hi:[1,0,1]
	v_pk_fma_f32 v[168:169], v[10:11], s[2:3], v[174:175] op_sel_hi:[1,0,1]
	v_pk_fma_f32 v[170:171], v[12:13], s[2:3], v[176:177] op_sel_hi:[1,0,1]
	v_pk_fma_f32 v[172:173], v[14:15], s[2:3], v[178:179] op_sel_hi:[1,0,1]
	v_pk_fma_f32 v[174:175], v[16:17], s[2:3], v[180:181] op_sel_hi:[1,0,1]
	v_pk_fma_f32 v[162:163], v[18:19], s[2:3], v[162:163] op_sel_hi:[1,0,1]
	v_pk_fma_f32 v[160:161], v[20:21], s[2:3], v[160:161] op_sel_hi:[1,0,1]
	v_pk_fma_f32 v[158:159], v[22:23], s[2:3], v[158:159] op_sel_hi:[1,0,1]
	v_pk_fma_f32 v[156:157], v[24:25], s[2:3], v[156:157] op_sel_hi:[1,0,1]
	v_pk_fma_f32 v[154:155], v[26:27], s[2:3], v[154:155] op_sel_hi:[1,0,1]
	v_pk_fma_f32 v[152:153], v[28:29], s[2:3], v[152:153] op_sel_hi:[1,0,1]
	v_pk_fma_f32 v[150:151], v[30:31], s[2:3], v[150:151] op_sel_hi:[1,0,1]
	v_readlane_b32 s2, v131, 29
	s_waitcnt vmcnt(20)
	v_cvt_scalef32_pk32_f32_fp6 v[0:31], v[92:97], 1.0
	v_pk_fma_f32 v[92:93], v[0:1], s[2:3], v[98:99] op_sel_hi:[1,0,1]
	v_pk_fma_f32 v[94:95], v[2:3], s[2:3], v[100:101] op_sel_hi:[1,0,1]
	v_pk_fma_f32 v[96:97], v[4:5], s[2:3], v[102:103] op_sel_hi:[1,0,1]
	v_pk_fma_f32 v[98:99], v[6:7], s[2:3], v[164:165] op_sel_hi:[1,0,1]
	v_pk_fma_f32 v[100:101], v[8:9], s[2:3], v[166:167] op_sel_hi:[1,0,1]
	v_pk_fma_f32 v[102:103], v[10:11], s[2:3], v[168:169] op_sel_hi:[1,0,1]
	v_pk_fma_f32 v[164:165], v[12:13], s[2:3], v[170:171] op_sel_hi:[1,0,1]
	v_pk_fma_f32 v[166:167], v[14:15], s[2:3], v[172:173] op_sel_hi:[1,0,1]
	v_pk_fma_f32 v[168:169], v[16:17], s[2:3], v[174:175] op_sel_hi:[1,0,1]
	v_pk_fma_f32 v[162:163], v[18:19], s[2:3], v[162:163] op_sel_hi:[1,0,1]
	v_pk_fma_f32 v[160:161], v[20:21], s[2:3], v[160:161] op_sel_hi:[1,0,1]
	v_pk_fma_f32 v[158:159], v[22:23], s[2:3], v[158:159] op_sel_hi:[1,0,1]
	v_pk_fma_f32 v[156:157], v[24:25], s[2:3], v[156:157] op_sel_hi:[1,0,1]
	v_pk_fma_f32 v[154:155], v[26:27], s[2:3], v[154:155] op_sel_hi:[1,0,1]
	v_pk_fma_f32 v[152:153], v[28:29], s[2:3], v[152:153] op_sel_hi:[1,0,1]
	v_pk_fma_f32 v[150:151], v[30:31], s[2:3], v[150:151] op_sel_hi:[1,0,1]
	v_readlane_b32 s2, v131, 30
	s_waitcnt vmcnt(18)
	v_cvt_scalef32_pk32_f32_fp6 v[0:31], v[86:91], 1.0
	v_pk_fma_f32 v[86:87], v[0:1], s[2:3], v[92:93] op_sel_hi:[1,0,1]
	v_pk_fma_f32 v[88:89], v[2:3], s[2:3], v[94:95] op_sel_hi:[1,0,1]
	v_pk_fma_f32 v[90:91], v[4:5], s[2:3], v[96:97] op_sel_hi:[1,0,1]
	v_pk_fma_f32 v[92:93], v[6:7], s[2:3], v[98:99] op_sel_hi:[1,0,1]
	v_pk_fma_f32 v[94:95], v[8:9], s[2:3], v[100:101] op_sel_hi:[1,0,1]
	v_pk_fma_f32 v[96:97], v[10:11], s[2:3], v[102:103] op_sel_hi:[1,0,1]
	v_pk_fma_f32 v[98:99], v[12:13], s[2:3], v[164:165] op_sel_hi:[1,0,1]
	v_pk_fma_f32 v[100:101], v[14:15], s[2:3], v[166:167] op_sel_hi:[1,0,1]
	v_pk_fma_f32 v[102:103], v[16:17], s[2:3], v[168:169] op_sel_hi:[1,0,1]
	v_pk_fma_f32 v[162:163], v[18:19], s[2:3], v[162:163] op_sel_hi:[1,0,1]
	v_pk_fma_f32 v[160:161], v[20:21], s[2:3], v[160:161] op_sel_hi:[1,0,1]
	v_pk_fma_f32 v[158:159], v[22:23], s[2:3], v[158:159] op_sel_hi:[1,0,1]
	v_pk_fma_f32 v[156:157], v[24:25], s[2:3], v[156:157] op_sel_hi:[1,0,1]
	v_pk_fma_f32 v[154:155], v[26:27], s[2:3], v[154:155] op_sel_hi:[1,0,1]
	v_pk_fma_f32 v[152:153], v[28:29], s[2:3], v[152:153] op_sel_hi:[1,0,1]
	v_pk_fma_f32 v[150:151], v[30:31], s[2:3], v[150:151] op_sel_hi:[1,0,1]
	v_readlane_b32 s2, v131, 31
	s_waitcnt vmcnt(16)
	v_cvt_scalef32_pk32_f32_fp6 v[0:31], v[80:85], 1.0
	v_pk_fma_f32 v[180:181], v[0:1], s[2:3], v[86:87] op_sel_hi:[1,0,1]
	v_pk_fma_f32 v[178:179], v[2:3], s[2:3], v[88:89] op_sel_hi:[1,0,1]
	v_pk_fma_f32 v[176:177], v[4:5], s[2:3], v[90:91] op_sel_hi:[1,0,1]
	v_pk_fma_f32 v[174:175], v[6:7], s[2:3], v[92:93] op_sel_hi:[1,0,1]
	v_pk_fma_f32 v[172:173], v[8:9], s[2:3], v[94:95] op_sel_hi:[1,0,1]
	v_pk_fma_f32 v[170:171], v[10:11], s[2:3], v[96:97] op_sel_hi:[1,0,1]
	v_pk_fma_f32 v[168:169], v[12:13], s[2:3], v[98:99] op_sel_hi:[1,0,1]
	v_pk_fma_f32 v[166:167], v[14:15], s[2:3], v[100:101] op_sel_hi:[1,0,1]
	v_pk_fma_f32 v[164:165], v[16:17], s[2:3], v[102:103] op_sel_hi:[1,0,1]
	v_pk_fma_f32 v[162:163], v[18:19], s[2:3], v[162:163] op_sel_hi:[1,0,1]
	v_pk_fma_f32 v[160:161], v[20:21], s[2:3], v[160:161] op_sel_hi:[1,0,1]
	v_pk_fma_f32 v[158:159], v[22:23], s[2:3], v[158:159] op_sel_hi:[1,0,1]
	v_pk_fma_f32 v[156:157], v[24:25], s[2:3], v[156:157] op_sel_hi:[1,0,1]
	v_pk_fma_f32 v[154:155], v[26:27], s[2:3], v[154:155] op_sel_hi:[1,0,1]
	v_pk_fma_f32 v[152:153], v[28:29], s[2:3], v[152:153] op_sel_hi:[1,0,1]
	v_pk_fma_f32 v[150:151], v[30:31], s[2:3], v[150:151] op_sel_hi:[1,0,1]
	v_readlane_b32 s2, v241, 40
	v_readlane_b32 s3, v241, 41
	v_readlane_b32 s100, v241, 42
	v_readlane_b32 s101, v241, 43
	s_nop 1
	buffer_load_dwordx4 v[98:101], v129, s[44:47], s2 offen
	buffer_load_dwordx2 v[102:103], v210, s[44:47], s2 offen
	buffer_load_dwordx4 v[92:95], v129, s[44:47], s3 offen
	buffer_load_dwordx2 v[96:97], v210, s[44:47], s3 offen
	buffer_load_dwordx4 v[86:89], v129, s[44:47], s100 offen
	buffer_load_dwordx2 v[90:91], v210, s[44:47], s100 offen
	buffer_load_dwordx4 v[80:83], v129, s[44:47], s101 offen
	buffer_load_dwordx2 v[84:85], v210, s[44:47], s101 offen
	v_readlane_b32 s2, v131, 32
	s_waitcnt vmcnt(22)
	v_cvt_scalef32_pk32_f32_fp6 v[0:31], v[74:79], 1.0
	v_pk_fma_f32 v[74:75], v[0:1], s[2:3], v[180:181] op_sel_hi:[1,0,1]
	v_pk_fma_f32 v[76:77], v[2:3], s[2:3], v[178:179] op_sel_hi:[1,0,1]
	v_pk_fma_f32 v[78:79], v[4:5], s[2:3], v[176:177] op_sel_hi:[1,0,1]
	v_pk_fma_f32 v[174:175], v[6:7], s[2:3], v[174:175] op_sel_hi:[1,0,1]
	v_pk_fma_f32 v[172:173], v[8:9], s[2:3], v[172:173] op_sel_hi:[1,0,1]
	v_pk_fma_f32 v[170:171], v[10:11], s[2:3], v[170:171] op_sel_hi:[1,0,1]
	v_pk_fma_f32 v[168:169], v[12:13], s[2:3], v[168:169] op_sel_hi:[1,0,1]
	v_pk_fma_f32 v[166:167], v[14:15], s[2:3], v[166:167] op_sel_hi:[1,0,1]
	v_pk_fma_f32 v[164:165], v[16:17], s[2:3], v[164:165] op_sel_hi:[1,0,1]
	v_pk_fma_f32 v[162:163], v[18:19], s[2:3], v[162:163] op_sel_hi:[1,0,1]
	v_pk_fma_f32 v[160:161], v[20:21], s[2:3], v[160:161] op_sel_hi:[1,0,1]
	v_pk_fma_f32 v[158:159], v[22:23], s[2:3], v[158:159] op_sel_hi:[1,0,1]
	v_pk_fma_f32 v[156:157], v[24:25], s[2:3], v[156:157] op_sel_hi:[1,0,1]
	v_pk_fma_f32 v[154:155], v[26:27], s[2:3], v[154:155] op_sel_hi:[1,0,1]
	v_pk_fma_f32 v[152:153], v[28:29], s[2:3], v[152:153] op_sel_hi:[1,0,1]
	v_pk_fma_f32 v[150:151], v[30:31], s[2:3], v[150:151] op_sel_hi:[1,0,1]
	v_readlane_b32 s2, v131, 33
	s_waitcnt vmcnt(20)
	v_cvt_scalef32_pk32_f32_fp6 v[0:31], v[68:73], 1.0
	v_pk_fma_f32 v[68:69], v[0:1], s[2:3], v[74:75] op_sel_hi:[1,0,1]
	v_pk_fma_f32 v[70:71], v[2:3], s[2:3], v[76:77] op_sel_hi:[1,0,1]
	v_pk_fma_f32 v[72:73], v[4:5], s[2:3], v[78:79] op_sel_hi:[1,0,1]
	v_pk_fma_f32 v[74:75], v[6:7], s[2:3], v[174:175] op_sel_hi:[1,0,1]
	v_pk_fma_f32 v[76:77], v[8:9], s[2:3], v[172:173] op_sel_hi:[1,0,1]
	v_pk_fma_f32 v[78:79], v[10:11], s[2:3], v[170:171] op_sel_hi:[1,0,1]
	v_pk_fma_f32 v[168:169], v[12:13], s[2:3], v[168:169] op_sel_hi:[1,0,1]
	v_pk_fma_f32 v[166:167], v[14:15], s[2:3], v[166:167] op_sel_hi:[1,0,1]
	v_pk_fma_f32 v[164:165], v[16:17], s[2:3], v[164:165] op_sel_hi:[1,0,1]
	v_pk_fma_f32 v[162:163], v[18:19], s[2:3], v[162:163] op_sel_hi:[1,0,1]
	v_pk_fma_f32 v[160:161], v[20:21], s[2:3], v[160:161] op_sel_hi:[1,0,1]
	v_pk_fma_f32 v[158:159], v[22:23], s[2:3], v[158:159] op_sel_hi:[1,0,1]
	v_pk_fma_f32 v[156:157], v[24:25], s[2:3], v[156:157] op_sel_hi:[1,0,1]
	v_pk_fma_f32 v[154:155], v[26:27], s[2:3], v[154:155] op_sel_hi:[1,0,1]
	v_pk_fma_f32 v[152:153], v[28:29], s[2:3], v[152:153] op_sel_hi:[1,0,1]
	v_pk_fma_f32 v[150:151], v[30:31], s[2:3], v[150:151] op_sel_hi:[1,0,1]
	v_readlane_b32 s2, v131, 34
	s_waitcnt vmcnt(18)
	v_cvt_scalef32_pk32_f32_fp6 v[0:31], v[56:61], 1.0
	v_pk_fma_f32 v[56:57], v[0:1], s[2:3], v[68:69] op_sel_hi:[1,0,1]
	v_pk_fma_f32 v[58:59], v[2:3], s[2:3], v[70:71] op_sel_hi:[1,0,1]
	v_pk_fma_f32 v[60:61], v[4:5], s[2:3], v[72:73] op_sel_hi:[1,0,1]
	v_pk_fma_f32 v[68:69], v[6:7], s[2:3], v[74:75] op_sel_hi:[1,0,1]
	v_pk_fma_f32 v[70:71], v[8:9], s[2:3], v[76:77] op_sel_hi:[1,0,1]
	v_pk_fma_f32 v[72:73], v[10:11], s[2:3], v[78:79] op_sel_hi:[1,0,1]
	v_pk_fma_f32 v[74:75], v[12:13], s[2:3], v[168:169] op_sel_hi:[1,0,1]
	v_pk_fma_f32 v[76:77], v[14:15], s[2:3], v[166:167] op_sel_hi:[1,0,1]
	v_pk_fma_f32 v[78:79], v[16:17], s[2:3], v[164:165] op_sel_hi:[1,0,1]
	v_pk_fma_f32 v[162:163], v[18:19], s[2:3], v[162:163] op_sel_hi:[1,0,1]
	v_pk_fma_f32 v[160:161], v[20:21], s[2:3], v[160:161] op_sel_hi:[1,0,1]
	v_pk_fma_f32 v[158:159], v[22:23], s[2:3], v[158:159] op_sel_hi:[1,0,1]
	v_pk_fma_f32 v[156:157], v[24:25], s[2:3], v[156:157] op_sel_hi:[1,0,1]
	v_pk_fma_f32 v[154:155], v[26:27], s[2:3], v[154:155] op_sel_hi:[1,0,1]
	v_pk_fma_f32 v[152:153], v[28:29], s[2:3], v[152:153] op_sel_hi:[1,0,1]
	v_pk_fma_f32 v[150:151], v[30:31], s[2:3], v[150:151] op_sel_hi:[1,0,1]
	v_readlane_b32 s2, v131, 35
	s_waitcnt vmcnt(16)
	v_cvt_scalef32_pk32_f32_fp6 v[0:31], v[44:49], 1.0
	v_pk_fma_f32 v[164:165], v[0:1], s[2:3], v[56:57] op_sel_hi:[1,0,1]
	v_pk_fma_f32 v[166:167], v[2:3], s[2:3], v[58:59] op_sel_hi:[1,0,1]
	v_pk_fma_f32 v[168:169], v[4:5], s[2:3], v[60:61] op_sel_hi:[1,0,1]
	v_pk_fma_f32 v[170:171], v[6:7], s[2:3], v[68:69] op_sel_hi:[1,0,1]
	v_pk_fma_f32 v[172:173], v[8:9], s[2:3], v[70:71] op_sel_hi:[1,0,1]
	v_pk_fma_f32 v[174:175], v[10:11], s[2:3], v[72:73] op_sel_hi:[1,0,1]
	v_pk_fma_f32 v[176:177], v[12:13], s[2:3], v[74:75] op_sel_hi:[1,0,1]
	v_pk_fma_f32 v[178:179], v[14:15], s[2:3], v[76:77] op_sel_hi:[1,0,1]
	v_pk_fma_f32 v[180:181], v[16:17], s[2:3], v[78:79] op_sel_hi:[1,0,1]
	v_pk_fma_f32 v[162:163], v[18:19], s[2:3], v[162:163] op_sel_hi:[1,0,1]
	v_pk_fma_f32 v[160:161], v[20:21], s[2:3], v[160:161] op_sel_hi:[1,0,1]
	v_pk_fma_f32 v[158:159], v[22:23], s[2:3], v[158:159] op_sel_hi:[1,0,1]
	v_pk_fma_f32 v[156:157], v[24:25], s[2:3], v[156:157] op_sel_hi:[1,0,1]
	v_pk_fma_f32 v[154:155], v[26:27], s[2:3], v[154:155] op_sel_hi:[1,0,1]
	v_pk_fma_f32 v[152:153], v[28:29], s[2:3], v[152:153] op_sel_hi:[1,0,1]
	v_pk_fma_f32 v[150:151], v[30:31], s[2:3], v[150:151] op_sel_hi:[1,0,1]
	v_readlane_b32 s2, v241, 44
	v_readlane_b32 s3, v241, 45
	v_readlane_b32 s100, v241, 46
	v_readlane_b32 s101, v241, 47
	s_nop 1
	buffer_load_dwordx4 v[74:77], v129, s[44:47], s2 offen
	buffer_load_dwordx2 v[78:79], v210, s[44:47], s2 offen
	buffer_load_dwordx4 v[68:71], v129, s[44:47], s3 offen
	buffer_load_dwordx2 v[72:73], v210, s[44:47], s3 offen
	buffer_load_dwordx4 v[56:59], v129, s[44:47], s100 offen
	buffer_load_dwordx2 v[60:61], v210, s[44:47], s100 offen
	buffer_load_dwordx4 v[44:47], v129, s[44:47], s101 offen
	buffer_load_dwordx2 v[48:49], v210, s[44:47], s101 offen
	v_readlane_b32 s2, v131, 36
	s_waitcnt vmcnt(22)
	v_cvt_scalef32_pk32_f32_fp6 v[0:31], v[62:67], 1.0
	v_pk_fma_f32 v[62:63], v[0:1], s[2:3], v[164:165] op_sel_hi:[1,0,1]
	v_pk_fma_f32 v[64:65], v[2:3], s[2:3], v[166:167] op_sel_hi:[1,0,1]
	v_pk_fma_f32 v[66:67], v[4:5], s[2:3], v[168:169] op_sel_hi:[1,0,1]
	v_pk_fma_f32 v[164:165], v[6:7], s[2:3], v[170:171] op_sel_hi:[1,0,1]
	v_pk_fma_f32 v[166:167], v[8:9], s[2:3], v[172:173] op_sel_hi:[1,0,1]
	v_pk_fma_f32 v[168:169], v[10:11], s[2:3], v[174:175] op_sel_hi:[1,0,1]
	v_pk_fma_f32 v[170:171], v[12:13], s[2:3], v[176:177] op_sel_hi:[1,0,1]
	v_pk_fma_f32 v[172:173], v[14:15], s[2:3], v[178:179] op_sel_hi:[1,0,1]
	v_pk_fma_f32 v[174:175], v[16:17], s[2:3], v[180:181] op_sel_hi:[1,0,1]
	v_pk_fma_f32 v[162:163], v[18:19], s[2:3], v[162:163] op_sel_hi:[1,0,1]
	v_pk_fma_f32 v[160:161], v[20:21], s[2:3], v[160:161] op_sel_hi:[1,0,1]
	v_pk_fma_f32 v[158:159], v[22:23], s[2:3], v[158:159] op_sel_hi:[1,0,1]
	v_pk_fma_f32 v[156:157], v[24:25], s[2:3], v[156:157] op_sel_hi:[1,0,1]
	v_pk_fma_f32 v[154:155], v[26:27], s[2:3], v[154:155] op_sel_hi:[1,0,1]
	v_pk_fma_f32 v[152:153], v[28:29], s[2:3], v[152:153] op_sel_hi:[1,0,1]
	v_pk_fma_f32 v[150:151], v[30:31], s[2:3], v[150:151] op_sel_hi:[1,0,1]
	v_readlane_b32 s2, v131, 37
	s_waitcnt vmcnt(20)
	v_cvt_scalef32_pk32_f32_fp6 v[0:31], v[50:55], 1.0
	v_pk_fma_f32 v[50:51], v[0:1], s[2:3], v[62:63] op_sel_hi:[1,0,1]
	v_pk_fma_f32 v[52:53], v[2:3], s[2:3], v[64:65] op_sel_hi:[1,0,1]
	v_pk_fma_f32 v[54:55], v[4:5], s[2:3], v[66:67] op_sel_hi:[1,0,1]
	v_pk_fma_f32 v[62:63], v[6:7], s[2:3], v[164:165] op_sel_hi:[1,0,1]
	v_pk_fma_f32 v[64:65], v[8:9], s[2:3], v[166:167] op_sel_hi:[1,0,1]
	v_pk_fma_f32 v[66:67], v[10:11], s[2:3], v[168:169] op_sel_hi:[1,0,1]
	v_pk_fma_f32 v[164:165], v[12:13], s[2:3], v[170:171] op_sel_hi:[1,0,1]
	v_pk_fma_f32 v[166:167], v[14:15], s[2:3], v[172:173] op_sel_hi:[1,0,1]
	v_pk_fma_f32 v[168:169], v[16:17], s[2:3], v[174:175] op_sel_hi:[1,0,1]
	v_pk_fma_f32 v[162:163], v[18:19], s[2:3], v[162:163] op_sel_hi:[1,0,1]
	v_pk_fma_f32 v[160:161], v[20:21], s[2:3], v[160:161] op_sel_hi:[1,0,1]
	v_pk_fma_f32 v[158:159], v[22:23], s[2:3], v[158:159] op_sel_hi:[1,0,1]
	v_pk_fma_f32 v[156:157], v[24:25], s[2:3], v[156:157] op_sel_hi:[1,0,1]
	v_pk_fma_f32 v[154:155], v[26:27], s[2:3], v[154:155] op_sel_hi:[1,0,1]
	v_pk_fma_f32 v[152:153], v[28:29], s[2:3], v[152:153] op_sel_hi:[1,0,1]
	v_pk_fma_f32 v[150:151], v[30:31], s[2:3], v[150:151] op_sel_hi:[1,0,1]
	v_readlane_b32 s2, v131, 38
	s_waitcnt vmcnt(18)
	v_cvt_scalef32_pk32_f32_fp6 v[0:31], v[38:43], 1.0
	v_pk_fma_f32 v[38:39], v[0:1], s[2:3], v[50:51] op_sel_hi:[1,0,1]
	v_pk_fma_f32 v[40:41], v[2:3], s[2:3], v[52:53] op_sel_hi:[1,0,1]
	v_pk_fma_f32 v[42:43], v[4:5], s[2:3], v[54:55] op_sel_hi:[1,0,1]
	v_pk_fma_f32 v[50:51], v[6:7], s[2:3], v[62:63] op_sel_hi:[1,0,1]
	v_pk_fma_f32 v[52:53], v[8:9], s[2:3], v[64:65] op_sel_hi:[1,0,1]
	v_pk_fma_f32 v[54:55], v[10:11], s[2:3], v[66:67] op_sel_hi:[1,0,1]
	v_pk_fma_f32 v[62:63], v[12:13], s[2:3], v[164:165] op_sel_hi:[1,0,1]
	v_pk_fma_f32 v[64:65], v[14:15], s[2:3], v[166:167] op_sel_hi:[1,0,1]
	v_pk_fma_f32 v[66:67], v[16:17], s[2:3], v[168:169] op_sel_hi:[1,0,1]
	v_pk_fma_f32 v[162:163], v[18:19], s[2:3], v[162:163] op_sel_hi:[1,0,1]
	v_pk_fma_f32 v[160:161], v[20:21], s[2:3], v[160:161] op_sel_hi:[1,0,1]
	v_pk_fma_f32 v[158:159], v[22:23], s[2:3], v[158:159] op_sel_hi:[1,0,1]
	v_pk_fma_f32 v[156:157], v[24:25], s[2:3], v[156:157] op_sel_hi:[1,0,1]
	v_pk_fma_f32 v[154:155], v[26:27], s[2:3], v[154:155] op_sel_hi:[1,0,1]
	v_pk_fma_f32 v[152:153], v[28:29], s[2:3], v[152:153] op_sel_hi:[1,0,1]
	v_pk_fma_f32 v[150:151], v[30:31], s[2:3], v[150:151] op_sel_hi:[1,0,1]
	v_readlane_b32 s2, v131, 39
	s_waitcnt vmcnt(16)
	v_cvt_scalef32_pk32_f32_fp6 v[0:31], v[32:37], 1.0
	v_pk_fma_f32 v[164:165], v[0:1], s[2:3], v[38:39] op_sel_hi:[1,0,1]
	v_pk_fma_f32 v[166:167], v[2:3], s[2:3], v[40:41] op_sel_hi:[1,0,1]
	v_pk_fma_f32 v[168:169], v[4:5], s[2:3], v[42:43] op_sel_hi:[1,0,1]
	v_pk_fma_f32 v[170:171], v[6:7], s[2:3], v[50:51] op_sel_hi:[1,0,1]
	v_pk_fma_f32 v[172:173], v[8:9], s[2:3], v[52:53] op_sel_hi:[1,0,1]
	v_pk_fma_f32 v[174:175], v[10:11], s[2:3], v[54:55] op_sel_hi:[1,0,1]
	v_pk_fma_f32 v[176:177], v[12:13], s[2:3], v[62:63] op_sel_hi:[1,0,1]
	v_pk_fma_f32 v[178:179], v[14:15], s[2:3], v[64:65] op_sel_hi:[1,0,1]
	v_pk_fma_f32 v[180:181], v[16:17], s[2:3], v[66:67] op_sel_hi:[1,0,1]
	v_pk_fma_f32 v[162:163], v[18:19], s[2:3], v[162:163] op_sel_hi:[1,0,1]
	v_pk_fma_f32 v[160:161], v[20:21], s[2:3], v[160:161] op_sel_hi:[1,0,1]
	v_pk_fma_f32 v[158:159], v[22:23], s[2:3], v[158:159] op_sel_hi:[1,0,1]
	v_pk_fma_f32 v[156:157], v[24:25], s[2:3], v[156:157] op_sel_hi:[1,0,1]
	v_pk_fma_f32 v[154:155], v[26:27], s[2:3], v[154:155] op_sel_hi:[1,0,1]
	v_pk_fma_f32 v[152:153], v[28:29], s[2:3], v[152:153] op_sel_hi:[1,0,1]
	v_pk_fma_f32 v[150:151], v[30:31], s[2:3], v[150:151] op_sel_hi:[1,0,1]
	v_readlane_b32 s2, v241, 48
	v_readlane_b32 s3, v241, 49
	v_readlane_b32 s100, v241, 50
	v_readlane_b32 s101, v241, 51
	s_nop 1
	buffer_load_dwordx4 v[62:65], v129, s[44:47], s2 offen
	buffer_load_dwordx2 v[66:67], v210, s[44:47], s2 offen
	buffer_load_dwordx4 v[50:53], v129, s[44:47], s3 offen
	buffer_load_dwordx2 v[54:55], v210, s[44:47], s3 offen
	buffer_load_dwordx4 v[38:41], v129, s[44:47], s100 offen
	buffer_load_dwordx2 v[42:43], v210, s[44:47], s100 offen
	buffer_load_dwordx4 v[32:35], v129, s[44:47], s101 offen
	buffer_load_dwordx2 v[36:37], v210, s[44:47], s101 offen
	v_readlane_b32 s2, v131, 40
	s_waitcnt vmcnt(22)
	v_cvt_scalef32_pk32_f32_fp6 v[0:31], v[98:103], 1.0
	v_pk_fma_f32 v[98:99], v[0:1], s[2:3], v[164:165] op_sel_hi:[1,0,1]
	v_pk_fma_f32 v[100:101], v[2:3], s[2:3], v[166:167] op_sel_hi:[1,0,1]
	v_pk_fma_f32 v[102:103], v[4:5], s[2:3], v[168:169] op_sel_hi:[1,0,1]
	v_pk_fma_f32 v[164:165], v[6:7], s[2:3], v[170:171] op_sel_hi:[1,0,1]
	v_pk_fma_f32 v[166:167], v[8:9], s[2:3], v[172:173] op_sel_hi:[1,0,1]
	v_pk_fma_f32 v[168:169], v[10:11], s[2:3], v[174:175] op_sel_hi:[1,0,1]
	v_pk_fma_f32 v[170:171], v[12:13], s[2:3], v[176:177] op_sel_hi:[1,0,1]
	v_pk_fma_f32 v[172:173], v[14:15], s[2:3], v[178:179] op_sel_hi:[1,0,1]
	v_pk_fma_f32 v[174:175], v[16:17], s[2:3], v[180:181] op_sel_hi:[1,0,1]
	v_pk_fma_f32 v[162:163], v[18:19], s[2:3], v[162:163] op_sel_hi:[1,0,1]
	v_pk_fma_f32 v[160:161], v[20:21], s[2:3], v[160:161] op_sel_hi:[1,0,1]
	v_pk_fma_f32 v[158:159], v[22:23], s[2:3], v[158:159] op_sel_hi:[1,0,1]
	v_pk_fma_f32 v[156:157], v[24:25], s[2:3], v[156:157] op_sel_hi:[1,0,1]
	v_pk_fma_f32 v[154:155], v[26:27], s[2:3], v[154:155] op_sel_hi:[1,0,1]
	v_pk_fma_f32 v[152:153], v[28:29], s[2:3], v[152:153] op_sel_hi:[1,0,1]
	v_pk_fma_f32 v[150:151], v[30:31], s[2:3], v[150:151] op_sel_hi:[1,0,1]
	v_readlane_b32 s2, v131, 41
	s_waitcnt vmcnt(20)
	v_cvt_scalef32_pk32_f32_fp6 v[0:31], v[92:97], 1.0
	v_pk_fma_f32 v[92:93], v[0:1], s[2:3], v[98:99] op_sel_hi:[1,0,1]
	v_pk_fma_f32 v[94:95], v[2:3], s[2:3], v[100:101] op_sel_hi:[1,0,1]
	v_pk_fma_f32 v[96:97], v[4:5], s[2:3], v[102:103] op_sel_hi:[1,0,1]
	v_pk_fma_f32 v[98:99], v[6:7], s[2:3], v[164:165] op_sel_hi:[1,0,1]
	v_pk_fma_f32 v[100:101], v[8:9], s[2:3], v[166:167] op_sel_hi:[1,0,1]
	v_pk_fma_f32 v[102:103], v[10:11], s[2:3], v[168:169] op_sel_hi:[1,0,1]
	v_pk_fma_f32 v[164:165], v[12:13], s[2:3], v[170:171] op_sel_hi:[1,0,1]
	v_pk_fma_f32 v[166:167], v[14:15], s[2:3], v[172:173] op_sel_hi:[1,0,1]
	v_pk_fma_f32 v[168:169], v[16:17], s[2:3], v[174:175] op_sel_hi:[1,0,1]
	v_pk_fma_f32 v[162:163], v[18:19], s[2:3], v[162:163] op_sel_hi:[1,0,1]
	v_pk_fma_f32 v[160:161], v[20:21], s[2:3], v[160:161] op_sel_hi:[1,0,1]
	v_pk_fma_f32 v[158:159], v[22:23], s[2:3], v[158:159] op_sel_hi:[1,0,1]
	v_pk_fma_f32 v[156:157], v[24:25], s[2:3], v[156:157] op_sel_hi:[1,0,1]
	v_pk_fma_f32 v[154:155], v[26:27], s[2:3], v[154:155] op_sel_hi:[1,0,1]
	v_pk_fma_f32 v[152:153], v[28:29], s[2:3], v[152:153] op_sel_hi:[1,0,1]
	v_pk_fma_f32 v[150:151], v[30:31], s[2:3], v[150:151] op_sel_hi:[1,0,1]
	v_readlane_b32 s2, v131, 42
	s_waitcnt vmcnt(18)
	v_cvt_scalef32_pk32_f32_fp6 v[0:31], v[86:91], 1.0
	v_pk_fma_f32 v[86:87], v[0:1], s[2:3], v[92:93] op_sel_hi:[1,0,1]
	v_pk_fma_f32 v[88:89], v[2:3], s[2:3], v[94:95] op_sel_hi:[1,0,1]
	v_pk_fma_f32 v[90:91], v[4:5], s[2:3], v[96:97] op_sel_hi:[1,0,1]
	v_pk_fma_f32 v[92:93], v[6:7], s[2:3], v[98:99] op_sel_hi:[1,0,1]
	v_pk_fma_f32 v[94:95], v[8:9], s[2:3], v[100:101] op_sel_hi:[1,0,1]
	v_pk_fma_f32 v[96:97], v[10:11], s[2:3], v[102:103] op_sel_hi:[1,0,1]
	v_pk_fma_f32 v[98:99], v[12:13], s[2:3], v[164:165] op_sel_hi:[1,0,1]
	v_pk_fma_f32 v[100:101], v[14:15], s[2:3], v[166:167] op_sel_hi:[1,0,1]
	v_pk_fma_f32 v[102:103], v[16:17], s[2:3], v[168:169] op_sel_hi:[1,0,1]
	v_pk_fma_f32 v[162:163], v[18:19], s[2:3], v[162:163] op_sel_hi:[1,0,1]
	v_pk_fma_f32 v[160:161], v[20:21], s[2:3], v[160:161] op_sel_hi:[1,0,1]
	v_pk_fma_f32 v[158:159], v[22:23], s[2:3], v[158:159] op_sel_hi:[1,0,1]
	v_pk_fma_f32 v[156:157], v[24:25], s[2:3], v[156:157] op_sel_hi:[1,0,1]
	v_pk_fma_f32 v[154:155], v[26:27], s[2:3], v[154:155] op_sel_hi:[1,0,1]
	v_pk_fma_f32 v[152:153], v[28:29], s[2:3], v[152:153] op_sel_hi:[1,0,1]
	v_pk_fma_f32 v[150:151], v[30:31], s[2:3], v[150:151] op_sel_hi:[1,0,1]
	v_readlane_b32 s2, v131, 43
	s_waitcnt vmcnt(16)
	v_cvt_scalef32_pk32_f32_fp6 v[0:31], v[80:85], 1.0
	v_pk_fma_f32 v[180:181], v[0:1], s[2:3], v[86:87] op_sel_hi:[1,0,1]
	v_pk_fma_f32 v[178:179], v[2:3], s[2:3], v[88:89] op_sel_hi:[1,0,1]
	v_pk_fma_f32 v[176:177], v[4:5], s[2:3], v[90:91] op_sel_hi:[1,0,1]
	v_pk_fma_f32 v[174:175], v[6:7], s[2:3], v[92:93] op_sel_hi:[1,0,1]
	v_pk_fma_f32 v[172:173], v[8:9], s[2:3], v[94:95] op_sel_hi:[1,0,1]
	v_pk_fma_f32 v[170:171], v[10:11], s[2:3], v[96:97] op_sel_hi:[1,0,1]
	v_pk_fma_f32 v[168:169], v[12:13], s[2:3], v[98:99] op_sel_hi:[1,0,1]
	v_pk_fma_f32 v[166:167], v[14:15], s[2:3], v[100:101] op_sel_hi:[1,0,1]
	v_pk_fma_f32 v[164:165], v[16:17], s[2:3], v[102:103] op_sel_hi:[1,0,1]
	v_pk_fma_f32 v[162:163], v[18:19], s[2:3], v[162:163] op_sel_hi:[1,0,1]
	v_pk_fma_f32 v[160:161], v[20:21], s[2:3], v[160:161] op_sel_hi:[1,0,1]
	v_pk_fma_f32 v[158:159], v[22:23], s[2:3], v[158:159] op_sel_hi:[1,0,1]
	v_pk_fma_f32 v[156:157], v[24:25], s[2:3], v[156:157] op_sel_hi:[1,0,1]
	v_pk_fma_f32 v[154:155], v[26:27], s[2:3], v[154:155] op_sel_hi:[1,0,1]
	v_pk_fma_f32 v[152:153], v[28:29], s[2:3], v[152:153] op_sel_hi:[1,0,1]
	v_pk_fma_f32 v[150:151], v[30:31], s[2:3], v[150:151] op_sel_hi:[1,0,1]
	v_readlane_b32 s2, v241, 52
	v_readlane_b32 s3, v241, 53
	v_readlane_b32 s100, v241, 54
	v_readlane_b32 s101, v241, 55
	s_nop 1
	buffer_load_dwordx4 v[98:101], v129, s[44:47], s2 offen
	buffer_load_dwordx2 v[102:103], v210, s[44:47], s2 offen
	buffer_load_dwordx4 v[92:95], v129, s[44:47], s3 offen
	buffer_load_dwordx2 v[96:97], v210, s[44:47], s3 offen
	buffer_load_dwordx4 v[86:89], v129, s[44:47], s100 offen
	buffer_load_dwordx2 v[90:91], v210, s[44:47], s100 offen
	buffer_load_dwordx4 v[80:83], v129, s[44:47], s101 offen
	buffer_load_dwordx2 v[84:85], v210, s[44:47], s101 offen
	v_readlane_b32 s2, v131, 44
	s_waitcnt vmcnt(22)
	v_cvt_scalef32_pk32_f32_fp6 v[0:31], v[74:79], 1.0
	v_pk_fma_f32 v[74:75], v[0:1], s[2:3], v[180:181] op_sel_hi:[1,0,1]
	v_pk_fma_f32 v[76:77], v[2:3], s[2:3], v[178:179] op_sel_hi:[1,0,1]
	v_pk_fma_f32 v[78:79], v[4:5], s[2:3], v[176:177] op_sel_hi:[1,0,1]
	v_pk_fma_f32 v[174:175], v[6:7], s[2:3], v[174:175] op_sel_hi:[1,0,1]
	v_pk_fma_f32 v[172:173], v[8:9], s[2:3], v[172:173] op_sel_hi:[1,0,1]
	v_pk_fma_f32 v[170:171], v[10:11], s[2:3], v[170:171] op_sel_hi:[1,0,1]
	v_pk_fma_f32 v[168:169], v[12:13], s[2:3], v[168:169] op_sel_hi:[1,0,1]
	v_pk_fma_f32 v[166:167], v[14:15], s[2:3], v[166:167] op_sel_hi:[1,0,1]
	v_pk_fma_f32 v[164:165], v[16:17], s[2:3], v[164:165] op_sel_hi:[1,0,1]
	v_pk_fma_f32 v[162:163], v[18:19], s[2:3], v[162:163] op_sel_hi:[1,0,1]
	v_pk_fma_f32 v[160:161], v[20:21], s[2:3], v[160:161] op_sel_hi:[1,0,1]
	v_pk_fma_f32 v[158:159], v[22:23], s[2:3], v[158:159] op_sel_hi:[1,0,1]
	v_pk_fma_f32 v[156:157], v[24:25], s[2:3], v[156:157] op_sel_hi:[1,0,1]
	v_pk_fma_f32 v[154:155], v[26:27], s[2:3], v[154:155] op_sel_hi:[1,0,1]
	v_pk_fma_f32 v[152:153], v[28:29], s[2:3], v[152:153] op_sel_hi:[1,0,1]
	v_pk_fma_f32 v[150:151], v[30:31], s[2:3], v[150:151] op_sel_hi:[1,0,1]
	v_readlane_b32 s2, v131, 45
	s_waitcnt vmcnt(20)
	v_cvt_scalef32_pk32_f32_fp6 v[0:31], v[68:73], 1.0
	v_pk_fma_f32 v[68:69], v[0:1], s[2:3], v[74:75] op_sel_hi:[1,0,1]
	v_pk_fma_f32 v[70:71], v[2:3], s[2:3], v[76:77] op_sel_hi:[1,0,1]
	v_pk_fma_f32 v[72:73], v[4:5], s[2:3], v[78:79] op_sel_hi:[1,0,1]
	v_pk_fma_f32 v[74:75], v[6:7], s[2:3], v[174:175] op_sel_hi:[1,0,1]
	v_pk_fma_f32 v[76:77], v[8:9], s[2:3], v[172:173] op_sel_hi:[1,0,1]
	v_pk_fma_f32 v[78:79], v[10:11], s[2:3], v[170:171] op_sel_hi:[1,0,1]
	v_pk_fma_f32 v[168:169], v[12:13], s[2:3], v[168:169] op_sel_hi:[1,0,1]
	v_pk_fma_f32 v[166:167], v[14:15], s[2:3], v[166:167] op_sel_hi:[1,0,1]
	v_pk_fma_f32 v[164:165], v[16:17], s[2:3], v[164:165] op_sel_hi:[1,0,1]
	v_pk_fma_f32 v[162:163], v[18:19], s[2:3], v[162:163] op_sel_hi:[1,0,1]
	v_pk_fma_f32 v[160:161], v[20:21], s[2:3], v[160:161] op_sel_hi:[1,0,1]
	v_pk_fma_f32 v[158:159], v[22:23], s[2:3], v[158:159] op_sel_hi:[1,0,1]
	v_pk_fma_f32 v[156:157], v[24:25], s[2:3], v[156:157] op_sel_hi:[1,0,1]
	v_pk_fma_f32 v[154:155], v[26:27], s[2:3], v[154:155] op_sel_hi:[1,0,1]
	v_pk_fma_f32 v[152:153], v[28:29], s[2:3], v[152:153] op_sel_hi:[1,0,1]
	v_pk_fma_f32 v[150:151], v[30:31], s[2:3], v[150:151] op_sel_hi:[1,0,1]
	v_readlane_b32 s2, v131, 46
	s_waitcnt vmcnt(18)
	v_cvt_scalef32_pk32_f32_fp6 v[0:31], v[56:61], 1.0
	v_pk_fma_f32 v[56:57], v[0:1], s[2:3], v[68:69] op_sel_hi:[1,0,1]
	v_pk_fma_f32 v[58:59], v[2:3], s[2:3], v[70:71] op_sel_hi:[1,0,1]
	v_pk_fma_f32 v[60:61], v[4:5], s[2:3], v[72:73] op_sel_hi:[1,0,1]
	v_pk_fma_f32 v[68:69], v[6:7], s[2:3], v[74:75] op_sel_hi:[1,0,1]
	v_pk_fma_f32 v[70:71], v[8:9], s[2:3], v[76:77] op_sel_hi:[1,0,1]
	v_pk_fma_f32 v[72:73], v[10:11], s[2:3], v[78:79] op_sel_hi:[1,0,1]
	v_pk_fma_f32 v[74:75], v[12:13], s[2:3], v[168:169] op_sel_hi:[1,0,1]
	v_pk_fma_f32 v[76:77], v[14:15], s[2:3], v[166:167] op_sel_hi:[1,0,1]
	v_pk_fma_f32 v[78:79], v[16:17], s[2:3], v[164:165] op_sel_hi:[1,0,1]
	v_pk_fma_f32 v[162:163], v[18:19], s[2:3], v[162:163] op_sel_hi:[1,0,1]
	v_pk_fma_f32 v[160:161], v[20:21], s[2:3], v[160:161] op_sel_hi:[1,0,1]
	v_pk_fma_f32 v[158:159], v[22:23], s[2:3], v[158:159] op_sel_hi:[1,0,1]
	v_pk_fma_f32 v[156:157], v[24:25], s[2:3], v[156:157] op_sel_hi:[1,0,1]
	v_pk_fma_f32 v[154:155], v[26:27], s[2:3], v[154:155] op_sel_hi:[1,0,1]
	v_pk_fma_f32 v[152:153], v[28:29], s[2:3], v[152:153] op_sel_hi:[1,0,1]
	v_pk_fma_f32 v[150:151], v[30:31], s[2:3], v[150:151] op_sel_hi:[1,0,1]
	v_readlane_b32 s2, v131, 47
	s_waitcnt vmcnt(16)
	v_cvt_scalef32_pk32_f32_fp6 v[0:31], v[44:49], 1.0
	v_pk_fma_f32 v[164:165], v[0:1], s[2:3], v[56:57] op_sel_hi:[1,0,1]
	v_pk_fma_f32 v[166:167], v[2:3], s[2:3], v[58:59] op_sel_hi:[1,0,1]
	v_pk_fma_f32 v[168:169], v[4:5], s[2:3], v[60:61] op_sel_hi:[1,0,1]
	v_pk_fma_f32 v[170:171], v[6:7], s[2:3], v[68:69] op_sel_hi:[1,0,1]
	v_pk_fma_f32 v[172:173], v[8:9], s[2:3], v[70:71] op_sel_hi:[1,0,1]
	v_pk_fma_f32 v[174:175], v[10:11], s[2:3], v[72:73] op_sel_hi:[1,0,1]
	v_pk_fma_f32 v[176:177], v[12:13], s[2:3], v[74:75] op_sel_hi:[1,0,1]
	v_pk_fma_f32 v[178:179], v[14:15], s[2:3], v[76:77] op_sel_hi:[1,0,1]
	v_pk_fma_f32 v[180:181], v[16:17], s[2:3], v[78:79] op_sel_hi:[1,0,1]
	v_pk_fma_f32 v[162:163], v[18:19], s[2:3], v[162:163] op_sel_hi:[1,0,1]
	v_pk_fma_f32 v[160:161], v[20:21], s[2:3], v[160:161] op_sel_hi:[1,0,1]
	v_pk_fma_f32 v[158:159], v[22:23], s[2:3], v[158:159] op_sel_hi:[1,0,1]
	v_pk_fma_f32 v[156:157], v[24:25], s[2:3], v[156:157] op_sel_hi:[1,0,1]
	v_pk_fma_f32 v[154:155], v[26:27], s[2:3], v[154:155] op_sel_hi:[1,0,1]
	v_pk_fma_f32 v[152:153], v[28:29], s[2:3], v[152:153] op_sel_hi:[1,0,1]
	v_pk_fma_f32 v[150:151], v[30:31], s[2:3], v[150:151] op_sel_hi:[1,0,1]
	v_readlane_b32 s2, v241, 56
	v_readlane_b32 s3, v241, 57
	v_readlane_b32 s100, v241, 58
	v_readlane_b32 s101, v241, 59
	s_nop 1
	buffer_load_dwordx4 v[74:77], v129, s[44:47], s2 offen
	buffer_load_dwordx2 v[78:79], v210, s[44:47], s2 offen
	buffer_load_dwordx4 v[68:71], v129, s[44:47], s3 offen
	buffer_load_dwordx2 v[72:73], v210, s[44:47], s3 offen
	buffer_load_dwordx4 v[56:59], v129, s[44:47], s100 offen
	buffer_load_dwordx2 v[60:61], v210, s[44:47], s100 offen
	buffer_load_dwordx4 v[44:47], v129, s[44:47], s101 offen
	buffer_load_dwordx2 v[48:49], v210, s[44:47], s101 offen
	v_readlane_b32 s2, v131, 48
	s_waitcnt vmcnt(22)
	v_cvt_scalef32_pk32_f32_fp6 v[0:31], v[62:67], 1.0
	v_pk_fma_f32 v[62:63], v[0:1], s[2:3], v[164:165] op_sel_hi:[1,0,1]
	v_pk_fma_f32 v[64:65], v[2:3], s[2:3], v[166:167] op_sel_hi:[1,0,1]
	v_pk_fma_f32 v[66:67], v[4:5], s[2:3], v[168:169] op_sel_hi:[1,0,1]
	v_pk_fma_f32 v[164:165], v[6:7], s[2:3], v[170:171] op_sel_hi:[1,0,1]
	v_pk_fma_f32 v[166:167], v[8:9], s[2:3], v[172:173] op_sel_hi:[1,0,1]
	v_pk_fma_f32 v[168:169], v[10:11], s[2:3], v[174:175] op_sel_hi:[1,0,1]
	v_pk_fma_f32 v[170:171], v[12:13], s[2:3], v[176:177] op_sel_hi:[1,0,1]
	v_pk_fma_f32 v[172:173], v[14:15], s[2:3], v[178:179] op_sel_hi:[1,0,1]
	v_pk_fma_f32 v[174:175], v[16:17], s[2:3], v[180:181] op_sel_hi:[1,0,1]
	v_pk_fma_f32 v[162:163], v[18:19], s[2:3], v[162:163] op_sel_hi:[1,0,1]
	v_pk_fma_f32 v[160:161], v[20:21], s[2:3], v[160:161] op_sel_hi:[1,0,1]
	v_pk_fma_f32 v[158:159], v[22:23], s[2:3], v[158:159] op_sel_hi:[1,0,1]
	v_pk_fma_f32 v[156:157], v[24:25], s[2:3], v[156:157] op_sel_hi:[1,0,1]
	v_pk_fma_f32 v[154:155], v[26:27], s[2:3], v[154:155] op_sel_hi:[1,0,1]
	v_pk_fma_f32 v[152:153], v[28:29], s[2:3], v[152:153] op_sel_hi:[1,0,1]
	v_pk_fma_f32 v[150:151], v[30:31], s[2:3], v[150:151] op_sel_hi:[1,0,1]
	v_readlane_b32 s2, v131, 49
	s_waitcnt vmcnt(20)
	v_cvt_scalef32_pk32_f32_fp6 v[0:31], v[50:55], 1.0
	v_pk_fma_f32 v[50:51], v[0:1], s[2:3], v[62:63] op_sel_hi:[1,0,1]
	v_pk_fma_f32 v[52:53], v[2:3], s[2:3], v[64:65] op_sel_hi:[1,0,1]
	v_pk_fma_f32 v[54:55], v[4:5], s[2:3], v[66:67] op_sel_hi:[1,0,1]
	v_pk_fma_f32 v[62:63], v[6:7], s[2:3], v[164:165] op_sel_hi:[1,0,1]
	v_pk_fma_f32 v[64:65], v[8:9], s[2:3], v[166:167] op_sel_hi:[1,0,1]
	v_pk_fma_f32 v[66:67], v[10:11], s[2:3], v[168:169] op_sel_hi:[1,0,1]
	v_pk_fma_f32 v[164:165], v[12:13], s[2:3], v[170:171] op_sel_hi:[1,0,1]
	v_pk_fma_f32 v[166:167], v[14:15], s[2:3], v[172:173] op_sel_hi:[1,0,1]
	v_pk_fma_f32 v[168:169], v[16:17], s[2:3], v[174:175] op_sel_hi:[1,0,1]
	v_pk_fma_f32 v[162:163], v[18:19], s[2:3], v[162:163] op_sel_hi:[1,0,1]
	v_pk_fma_f32 v[160:161], v[20:21], s[2:3], v[160:161] op_sel_hi:[1,0,1]
	v_pk_fma_f32 v[158:159], v[22:23], s[2:3], v[158:159] op_sel_hi:[1,0,1]
	v_pk_fma_f32 v[156:157], v[24:25], s[2:3], v[156:157] op_sel_hi:[1,0,1]
	v_pk_fma_f32 v[154:155], v[26:27], s[2:3], v[154:155] op_sel_hi:[1,0,1]
	v_pk_fma_f32 v[152:153], v[28:29], s[2:3], v[152:153] op_sel_hi:[1,0,1]
	v_pk_fma_f32 v[150:151], v[30:31], s[2:3], v[150:151] op_sel_hi:[1,0,1]
	v_readlane_b32 s2, v131, 50
	s_waitcnt vmcnt(18)
	v_cvt_scalef32_pk32_f32_fp6 v[0:31], v[38:43], 1.0
	v_pk_fma_f32 v[38:39], v[0:1], s[2:3], v[50:51] op_sel_hi:[1,0,1]
	v_pk_fma_f32 v[40:41], v[2:3], s[2:3], v[52:53] op_sel_hi:[1,0,1]
	v_pk_fma_f32 v[42:43], v[4:5], s[2:3], v[54:55] op_sel_hi:[1,0,1]
	v_pk_fma_f32 v[50:51], v[6:7], s[2:3], v[62:63] op_sel_hi:[1,0,1]
	v_pk_fma_f32 v[52:53], v[8:9], s[2:3], v[64:65] op_sel_hi:[1,0,1]
	v_pk_fma_f32 v[54:55], v[10:11], s[2:3], v[66:67] op_sel_hi:[1,0,1]
	v_pk_fma_f32 v[62:63], v[12:13], s[2:3], v[164:165] op_sel_hi:[1,0,1]
	v_pk_fma_f32 v[64:65], v[14:15], s[2:3], v[166:167] op_sel_hi:[1,0,1]
	v_pk_fma_f32 v[66:67], v[16:17], s[2:3], v[168:169] op_sel_hi:[1,0,1]
	v_pk_fma_f32 v[162:163], v[18:19], s[2:3], v[162:163] op_sel_hi:[1,0,1]
	v_pk_fma_f32 v[160:161], v[20:21], s[2:3], v[160:161] op_sel_hi:[1,0,1]
	v_pk_fma_f32 v[158:159], v[22:23], s[2:3], v[158:159] op_sel_hi:[1,0,1]
	v_pk_fma_f32 v[156:157], v[24:25], s[2:3], v[156:157] op_sel_hi:[1,0,1]
	v_pk_fma_f32 v[154:155], v[26:27], s[2:3], v[154:155] op_sel_hi:[1,0,1]
	v_pk_fma_f32 v[152:153], v[28:29], s[2:3], v[152:153] op_sel_hi:[1,0,1]
	v_pk_fma_f32 v[150:151], v[30:31], s[2:3], v[150:151] op_sel_hi:[1,0,1]
	v_readlane_b32 s2, v131, 51
	s_waitcnt vmcnt(16)
	v_cvt_scalef32_pk32_f32_fp6 v[0:31], v[32:37], 1.0
	v_pk_fma_f32 v[164:165], v[0:1], s[2:3], v[38:39] op_sel_hi:[1,0,1]
	v_pk_fma_f32 v[166:167], v[2:3], s[2:3], v[40:41] op_sel_hi:[1,0,1]
	v_pk_fma_f32 v[168:169], v[4:5], s[2:3], v[42:43] op_sel_hi:[1,0,1]
	v_pk_fma_f32 v[170:171], v[6:7], s[2:3], v[50:51] op_sel_hi:[1,0,1]
	v_pk_fma_f32 v[172:173], v[8:9], s[2:3], v[52:53] op_sel_hi:[1,0,1]
	v_pk_fma_f32 v[174:175], v[10:11], s[2:3], v[54:55] op_sel_hi:[1,0,1]
	v_pk_fma_f32 v[176:177], v[12:13], s[2:3], v[62:63] op_sel_hi:[1,0,1]
	v_pk_fma_f32 v[178:179], v[14:15], s[2:3], v[64:65] op_sel_hi:[1,0,1]
	v_pk_fma_f32 v[180:181], v[16:17], s[2:3], v[66:67] op_sel_hi:[1,0,1]
	v_pk_fma_f32 v[162:163], v[18:19], s[2:3], v[162:163] op_sel_hi:[1,0,1]
	v_pk_fma_f32 v[160:161], v[20:21], s[2:3], v[160:161] op_sel_hi:[1,0,1]
	v_pk_fma_f32 v[158:159], v[22:23], s[2:3], v[158:159] op_sel_hi:[1,0,1]
	v_pk_fma_f32 v[156:157], v[24:25], s[2:3], v[156:157] op_sel_hi:[1,0,1]
	v_pk_fma_f32 v[154:155], v[26:27], s[2:3], v[154:155] op_sel_hi:[1,0,1]
	v_pk_fma_f32 v[152:153], v[28:29], s[2:3], v[152:153] op_sel_hi:[1,0,1]
	v_pk_fma_f32 v[150:151], v[30:31], s[2:3], v[150:151] op_sel_hi:[1,0,1]
	v_readlane_b32 s2, v241, 60
	v_readlane_b32 s3, v241, 61
	v_readlane_b32 s100, v241, 62
	v_readlane_b32 s101, v241, 63
	s_nop 1
	buffer_load_dwordx4 v[62:65], v129, s[44:47], s2 offen
	buffer_load_dwordx2 v[66:67], v210, s[44:47], s2 offen
	buffer_load_dwordx4 v[50:53], v129, s[44:47], s3 offen
	buffer_load_dwordx2 v[54:55], v210, s[44:47], s3 offen
	buffer_load_dwordx4 v[38:41], v129, s[44:47], s100 offen
	buffer_load_dwordx2 v[42:43], v210, s[44:47], s100 offen
	buffer_load_dwordx4 v[32:35], v129, s[44:47], s101 offen
	buffer_load_dwordx2 v[36:37], v210, s[44:47], s101 offen
	v_readlane_b32 s2, v131, 52
	s_waitcnt vmcnt(22)
	v_cvt_scalef32_pk32_f32_fp6 v[0:31], v[98:103], 1.0
	v_pk_fma_f32 v[98:99], v[0:1], s[2:3], v[164:165] op_sel_hi:[1,0,1]
	v_pk_fma_f32 v[100:101], v[2:3], s[2:3], v[166:167] op_sel_hi:[1,0,1]
	v_pk_fma_f32 v[102:103], v[4:5], s[2:3], v[168:169] op_sel_hi:[1,0,1]
	v_pk_fma_f32 v[164:165], v[6:7], s[2:3], v[170:171] op_sel_hi:[1,0,1]
	v_pk_fma_f32 v[166:167], v[8:9], s[2:3], v[172:173] op_sel_hi:[1,0,1]
	v_pk_fma_f32 v[168:169], v[10:11], s[2:3], v[174:175] op_sel_hi:[1,0,1]
	v_pk_fma_f32 v[170:171], v[12:13], s[2:3], v[176:177] op_sel_hi:[1,0,1]
	v_pk_fma_f32 v[172:173], v[14:15], s[2:3], v[178:179] op_sel_hi:[1,0,1]
	v_pk_fma_f32 v[174:175], v[16:17], s[2:3], v[180:181] op_sel_hi:[1,0,1]
	v_pk_fma_f32 v[162:163], v[18:19], s[2:3], v[162:163] op_sel_hi:[1,0,1]
	v_pk_fma_f32 v[160:161], v[20:21], s[2:3], v[160:161] op_sel_hi:[1,0,1]
	v_pk_fma_f32 v[158:159], v[22:23], s[2:3], v[158:159] op_sel_hi:[1,0,1]
	v_pk_fma_f32 v[156:157], v[24:25], s[2:3], v[156:157] op_sel_hi:[1,0,1]
	v_pk_fma_f32 v[154:155], v[26:27], s[2:3], v[154:155] op_sel_hi:[1,0,1]
	v_pk_fma_f32 v[152:153], v[28:29], s[2:3], v[152:153] op_sel_hi:[1,0,1]
	v_pk_fma_f32 v[150:151], v[30:31], s[2:3], v[150:151] op_sel_hi:[1,0,1]
	v_readlane_b32 s2, v131, 53
	s_waitcnt vmcnt(20)
	v_cvt_scalef32_pk32_f32_fp6 v[0:31], v[92:97], 1.0
	v_pk_fma_f32 v[92:93], v[0:1], s[2:3], v[98:99] op_sel_hi:[1,0,1]
	v_pk_fma_f32 v[94:95], v[2:3], s[2:3], v[100:101] op_sel_hi:[1,0,1]
	v_pk_fma_f32 v[96:97], v[4:5], s[2:3], v[102:103] op_sel_hi:[1,0,1]
	v_pk_fma_f32 v[98:99], v[6:7], s[2:3], v[164:165] op_sel_hi:[1,0,1]
	v_pk_fma_f32 v[100:101], v[8:9], s[2:3], v[166:167] op_sel_hi:[1,0,1]
	v_pk_fma_f32 v[102:103], v[10:11], s[2:3], v[168:169] op_sel_hi:[1,0,1]
	v_pk_fma_f32 v[164:165], v[12:13], s[2:3], v[170:171] op_sel_hi:[1,0,1]
	v_pk_fma_f32 v[166:167], v[14:15], s[2:3], v[172:173] op_sel_hi:[1,0,1]
	v_pk_fma_f32 v[168:169], v[16:17], s[2:3], v[174:175] op_sel_hi:[1,0,1]
	v_pk_fma_f32 v[162:163], v[18:19], s[2:3], v[162:163] op_sel_hi:[1,0,1]
	v_pk_fma_f32 v[160:161], v[20:21], s[2:3], v[160:161] op_sel_hi:[1,0,1]
	v_pk_fma_f32 v[158:159], v[22:23], s[2:3], v[158:159] op_sel_hi:[1,0,1]
	v_pk_fma_f32 v[156:157], v[24:25], s[2:3], v[156:157] op_sel_hi:[1,0,1]
	v_pk_fma_f32 v[154:155], v[26:27], s[2:3], v[154:155] op_sel_hi:[1,0,1]
	v_pk_fma_f32 v[152:153], v[28:29], s[2:3], v[152:153] op_sel_hi:[1,0,1]
	v_pk_fma_f32 v[150:151], v[30:31], s[2:3], v[150:151] op_sel_hi:[1,0,1]
	v_readlane_b32 s2, v131, 54
	s_waitcnt vmcnt(18)
	v_cvt_scalef32_pk32_f32_fp6 v[0:31], v[86:91], 1.0
	v_pk_fma_f32 v[86:87], v[0:1], s[2:3], v[92:93] op_sel_hi:[1,0,1]
	v_pk_fma_f32 v[88:89], v[2:3], s[2:3], v[94:95] op_sel_hi:[1,0,1]
	v_pk_fma_f32 v[90:91], v[4:5], s[2:3], v[96:97] op_sel_hi:[1,0,1]
	v_pk_fma_f32 v[92:93], v[6:7], s[2:3], v[98:99] op_sel_hi:[1,0,1]
	v_pk_fma_f32 v[94:95], v[8:9], s[2:3], v[100:101] op_sel_hi:[1,0,1]
	v_pk_fma_f32 v[96:97], v[10:11], s[2:3], v[102:103] op_sel_hi:[1,0,1]
	v_pk_fma_f32 v[98:99], v[12:13], s[2:3], v[164:165] op_sel_hi:[1,0,1]
	v_pk_fma_f32 v[100:101], v[14:15], s[2:3], v[166:167] op_sel_hi:[1,0,1]
	v_pk_fma_f32 v[102:103], v[16:17], s[2:3], v[168:169] op_sel_hi:[1,0,1]
	v_pk_fma_f32 v[162:163], v[18:19], s[2:3], v[162:163] op_sel_hi:[1,0,1]
	v_pk_fma_f32 v[160:161], v[20:21], s[2:3], v[160:161] op_sel_hi:[1,0,1]
	v_pk_fma_f32 v[158:159], v[22:23], s[2:3], v[158:159] op_sel_hi:[1,0,1]
	v_pk_fma_f32 v[156:157], v[24:25], s[2:3], v[156:157] op_sel_hi:[1,0,1]
	v_pk_fma_f32 v[154:155], v[26:27], s[2:3], v[154:155] op_sel_hi:[1,0,1]
	v_pk_fma_f32 v[152:153], v[28:29], s[2:3], v[152:153] op_sel_hi:[1,0,1]
	v_pk_fma_f32 v[150:151], v[30:31], s[2:3], v[150:151] op_sel_hi:[1,0,1]
	v_readlane_b32 s2, v131, 55
	s_waitcnt vmcnt(16)
	v_cvt_scalef32_pk32_f32_fp6 v[0:31], v[80:85], 1.0
	v_pk_fma_f32 v[180:181], v[0:1], s[2:3], v[86:87] op_sel_hi:[1,0,1]
	v_pk_fma_f32 v[178:179], v[2:3], s[2:3], v[88:89] op_sel_hi:[1,0,1]
	v_pk_fma_f32 v[176:177], v[4:5], s[2:3], v[90:91] op_sel_hi:[1,0,1]
	v_pk_fma_f32 v[174:175], v[6:7], s[2:3], v[92:93] op_sel_hi:[1,0,1]
	v_pk_fma_f32 v[172:173], v[8:9], s[2:3], v[94:95] op_sel_hi:[1,0,1]
	v_pk_fma_f32 v[170:171], v[10:11], s[2:3], v[96:97] op_sel_hi:[1,0,1]
	v_pk_fma_f32 v[168:169], v[12:13], s[2:3], v[98:99] op_sel_hi:[1,0,1]
	v_pk_fma_f32 v[166:167], v[14:15], s[2:3], v[100:101] op_sel_hi:[1,0,1]
	v_pk_fma_f32 v[164:165], v[16:17], s[2:3], v[102:103] op_sel_hi:[1,0,1]
	v_pk_fma_f32 v[162:163], v[18:19], s[2:3], v[162:163] op_sel_hi:[1,0,1]
	v_pk_fma_f32 v[160:161], v[20:21], s[2:3], v[160:161] op_sel_hi:[1,0,1]
	v_pk_fma_f32 v[158:159], v[22:23], s[2:3], v[158:159] op_sel_hi:[1,0,1]
	v_pk_fma_f32 v[156:157], v[24:25], s[2:3], v[156:157] op_sel_hi:[1,0,1]
	v_pk_fma_f32 v[154:155], v[26:27], s[2:3], v[154:155] op_sel_hi:[1,0,1]
	v_pk_fma_f32 v[152:153], v[28:29], s[2:3], v[152:153] op_sel_hi:[1,0,1]
	v_pk_fma_f32 v[150:151], v[30:31], s[2:3], v[150:151] op_sel_hi:[1,0,1]
	v_readlane_b32 s0, v131, 56
	s_waitcnt vmcnt(14)
	v_cvt_scalef32_pk32_f32_fp6 v[0:31], v[74:79], 1.0
	v_pk_fma_f32 v[74:75], v[0:1], s[0:1], v[180:181] op_sel_hi:[1,0,1]
	v_pk_fma_f32 v[76:77], v[2:3], s[0:1], v[178:179] op_sel_hi:[1,0,1]
	v_pk_fma_f32 v[78:79], v[4:5], s[0:1], v[176:177] op_sel_hi:[1,0,1]
	v_pk_fma_f32 v[80:81], v[6:7], s[0:1], v[174:175] op_sel_hi:[1,0,1]
	v_pk_fma_f32 v[82:83], v[8:9], s[0:1], v[172:173] op_sel_hi:[1,0,1]
	v_pk_fma_f32 v[84:85], v[10:11], s[0:1], v[170:171] op_sel_hi:[1,0,1]
	v_pk_fma_f32 v[86:87], v[12:13], s[0:1], v[168:169] op_sel_hi:[1,0,1]
	v_pk_fma_f32 v[88:89], v[14:15], s[0:1], v[166:167] op_sel_hi:[1,0,1]
	v_pk_fma_f32 v[90:91], v[16:17], s[0:1], v[164:165] op_sel_hi:[1,0,1]
	v_pk_fma_f32 v[92:93], v[18:19], s[0:1], v[162:163] op_sel_hi:[1,0,1]
	v_pk_fma_f32 v[94:95], v[20:21], s[0:1], v[160:161] op_sel_hi:[1,0,1]
	v_pk_fma_f32 v[96:97], v[22:23], s[0:1], v[158:159] op_sel_hi:[1,0,1]
	v_pk_fma_f32 v[98:99], v[24:25], s[0:1], v[156:157] op_sel_hi:[1,0,1]
	v_pk_fma_f32 v[100:101], v[26:27], s[0:1], v[154:155] op_sel_hi:[1,0,1]
	v_pk_fma_f32 v[102:103], v[28:29], s[0:1], v[152:153] op_sel_hi:[1,0,1]
	v_pk_fma_f32 v[150:151], v[30:31], s[0:1], v[150:151] op_sel_hi:[1,0,1]
	v_readlane_b32 s0, v131, 57
	s_waitcnt vmcnt(12)
	v_cvt_scalef32_pk32_f32_fp6 v[0:31], v[68:73], 1.0
	v_pk_fma_f32 v[68:69], v[0:1], s[0:1], v[74:75] op_sel_hi:[1,0,1]
	v_pk_fma_f32 v[70:71], v[2:3], s[0:1], v[76:77] op_sel_hi:[1,0,1]
	v_pk_fma_f32 v[72:73], v[4:5], s[0:1], v[78:79] op_sel_hi:[1,0,1]
	v_pk_fma_f32 v[74:75], v[6:7], s[0:1], v[80:81] op_sel_hi:[1,0,1]
	v_pk_fma_f32 v[76:77], v[8:9], s[0:1], v[82:83] op_sel_hi:[1,0,1]
	v_pk_fma_f32 v[78:79], v[10:11], s[0:1], v[84:85] op_sel_hi:[1,0,1]
	v_pk_fma_f32 v[80:81], v[12:13], s[0:1], v[86:87] op_sel_hi:[1,0,1]
	v_pk_fma_f32 v[82:83], v[14:15], s[0:1], v[88:89] op_sel_hi:[1,0,1]
	v_pk_fma_f32 v[84:85], v[16:17], s[0:1], v[90:91] op_sel_hi:[1,0,1]
	v_pk_fma_f32 v[86:87], v[18:19], s[0:1], v[92:93] op_sel_hi:[1,0,1]
	v_pk_fma_f32 v[88:89], v[20:21], s[0:1], v[94:95] op_sel_hi:[1,0,1]
	v_pk_fma_f32 v[90:91], v[22:23], s[0:1], v[96:97] op_sel_hi:[1,0,1]
	v_pk_fma_f32 v[92:93], v[24:25], s[0:1], v[98:99] op_sel_hi:[1,0,1]
	v_pk_fma_f32 v[94:95], v[26:27], s[0:1], v[100:101] op_sel_hi:[1,0,1]
	v_pk_fma_f32 v[96:97], v[28:29], s[0:1], v[102:103] op_sel_hi:[1,0,1]
	v_pk_fma_f32 v[98:99], v[30:31], s[0:1], v[150:151] op_sel_hi:[1,0,1]
	v_readlane_b32 s0, v131, 58
	s_waitcnt vmcnt(10)
	v_cvt_scalef32_pk32_f32_fp6 v[0:31], v[56:61], 1.0
	v_pk_fma_f32 v[56:57], v[0:1], s[0:1], v[68:69] op_sel_hi:[1,0,1]
	v_pk_fma_f32 v[58:59], v[2:3], s[0:1], v[70:71] op_sel_hi:[1,0,1]
	v_pk_fma_f32 v[60:61], v[4:5], s[0:1], v[72:73] op_sel_hi:[1,0,1]
	v_pk_fma_f32 v[68:69], v[6:7], s[0:1], v[74:75] op_sel_hi:[1,0,1]
	v_pk_fma_f32 v[70:71], v[8:9], s[0:1], v[76:77] op_sel_hi:[1,0,1]
	v_pk_fma_f32 v[72:73], v[10:11], s[0:1], v[78:79] op_sel_hi:[1,0,1]
	v_pk_fma_f32 v[74:75], v[12:13], s[0:1], v[80:81] op_sel_hi:[1,0,1]
	v_pk_fma_f32 v[76:77], v[14:15], s[0:1], v[82:83] op_sel_hi:[1,0,1]
	v_pk_fma_f32 v[78:79], v[16:17], s[0:1], v[84:85] op_sel_hi:[1,0,1]
	v_pk_fma_f32 v[80:81], v[18:19], s[0:1], v[86:87] op_sel_hi:[1,0,1]
	v_pk_fma_f32 v[82:83], v[20:21], s[0:1], v[88:89] op_sel_hi:[1,0,1]
	v_pk_fma_f32 v[84:85], v[22:23], s[0:1], v[90:91] op_sel_hi:[1,0,1]
	v_pk_fma_f32 v[86:87], v[24:25], s[0:1], v[92:93] op_sel_hi:[1,0,1]
	v_pk_fma_f32 v[88:89], v[26:27], s[0:1], v[94:95] op_sel_hi:[1,0,1]
	v_pk_fma_f32 v[90:91], v[28:29], s[0:1], v[96:97] op_sel_hi:[1,0,1]
	v_pk_fma_f32 v[92:93], v[30:31], s[0:1], v[98:99] op_sel_hi:[1,0,1]
	v_readlane_b32 s0, v131, 59
	s_waitcnt vmcnt(8)
	v_cvt_scalef32_pk32_f32_fp6 v[0:31], v[44:49], 1.0
	v_pk_fma_f32 v[46:47], v[2:3], s[0:1], v[58:59] op_sel_hi:[1,0,1]
	v_pk_fma_f32 v[44:45], v[0:1], s[0:1], v[56:57] op_sel_hi:[1,0,1]
	v_pk_fma_f32 v[48:49], v[4:5], s[0:1], v[60:61] op_sel_hi:[1,0,1]
	v_pk_fma_f32 v[56:57], v[6:7], s[0:1], v[68:69] op_sel_hi:[1,0,1]
	v_pk_fma_f32 v[58:59], v[8:9], s[0:1], v[70:71] op_sel_hi:[1,0,1]
	v_pk_fma_f32 v[60:61], v[10:11], s[0:1], v[72:73] op_sel_hi:[1,0,1]
	v_pk_fma_f32 v[68:69], v[12:13], s[0:1], v[74:75] op_sel_hi:[1,0,1]
	v_pk_fma_f32 v[70:71], v[14:15], s[0:1], v[76:77] op_sel_hi:[1,0,1]
	v_pk_fma_f32 v[72:73], v[16:17], s[0:1], v[78:79] op_sel_hi:[1,0,1]
	v_pk_fma_f32 v[74:75], v[18:19], s[0:1], v[80:81] op_sel_hi:[1,0,1]
	v_pk_fma_f32 v[76:77], v[20:21], s[0:1], v[82:83] op_sel_hi:[1,0,1]
	v_pk_fma_f32 v[78:79], v[22:23], s[0:1], v[84:85] op_sel_hi:[1,0,1]
	v_pk_fma_f32 v[80:81], v[24:25], s[0:1], v[86:87] op_sel_hi:[1,0,1]
	v_pk_fma_f32 v[82:83], v[26:27], s[0:1], v[88:89] op_sel_hi:[1,0,1]
	v_pk_fma_f32 v[84:85], v[28:29], s[0:1], v[90:91] op_sel_hi:[1,0,1]
	v_pk_fma_f32 v[86:87], v[30:31], s[0:1], v[92:93] op_sel_hi:[1,0,1]
	v_readlane_b32 s0, v131, 60
	s_waitcnt vmcnt(6)
	v_cvt_scalef32_pk32_f32_fp6 v[0:31], v[62:67], 1.0
	v_pk_fma_f32 v[44:45], v[0:1], s[0:1], v[44:45] op_sel_hi:[1,0,1]
	v_pk_fma_f32 v[46:47], v[2:3], s[0:1], v[46:47] op_sel_hi:[1,0,1]
	v_pk_fma_f32 v[48:49], v[4:5], s[0:1], v[48:49] op_sel_hi:[1,0,1]
	v_pk_fma_f32 v[56:57], v[6:7], s[0:1], v[56:57] op_sel_hi:[1,0,1]
	v_pk_fma_f32 v[58:59], v[8:9], s[0:1], v[58:59] op_sel_hi:[1,0,1]
	v_pk_fma_f32 v[60:61], v[10:11], s[0:1], v[60:61] op_sel_hi:[1,0,1]
	v_pk_fma_f32 v[62:63], v[12:13], s[0:1], v[68:69] op_sel_hi:[1,0,1]
	v_pk_fma_f32 v[64:65], v[14:15], s[0:1], v[70:71] op_sel_hi:[1,0,1]
	v_pk_fma_f32 v[66:67], v[16:17], s[0:1], v[72:73] op_sel_hi:[1,0,1]
	v_pk_fma_f32 v[68:69], v[18:19], s[0:1], v[74:75] op_sel_hi:[1,0,1]
	v_pk_fma_f32 v[70:71], v[20:21], s[0:1], v[76:77] op_sel_hi:[1,0,1]
	v_pk_fma_f32 v[72:73], v[22:23], s[0:1], v[78:79] op_sel_hi:[1,0,1]
	v_pk_fma_f32 v[74:75], v[24:25], s[0:1], v[80:81] op_sel_hi:[1,0,1]
	v_pk_fma_f32 v[76:77], v[26:27], s[0:1], v[82:83] op_sel_hi:[1,0,1]
	v_pk_fma_f32 v[78:79], v[28:29], s[0:1], v[84:85] op_sel_hi:[1,0,1]
	v_pk_fma_f32 v[80:81], v[30:31], s[0:1], v[86:87] op_sel_hi:[1,0,1]
	v_readlane_b32 s0, v131, 61
	s_waitcnt vmcnt(4)
	v_cvt_scalef32_pk32_f32_fp6 v[0:31], v[50:55], 1.0
	v_pk_fma_f32 v[44:45], v[0:1], s[0:1], v[44:45] op_sel_hi:[1,0,1]
	v_pk_fma_f32 v[46:47], v[2:3], s[0:1], v[46:47] op_sel_hi:[1,0,1]
	v_pk_fma_f32 v[48:49], v[4:5], s[0:1], v[48:49] op_sel_hi:[1,0,1]
	v_pk_fma_f32 v[50:51], v[6:7], s[0:1], v[56:57] op_sel_hi:[1,0,1]
	v_pk_fma_f32 v[52:53], v[8:9], s[0:1], v[58:59] op_sel_hi:[1,0,1]
	v_pk_fma_f32 v[54:55], v[10:11], s[0:1], v[60:61] op_sel_hi:[1,0,1]
	v_pk_fma_f32 v[56:57], v[12:13], s[0:1], v[62:63] op_sel_hi:[1,0,1]
	v_pk_fma_f32 v[58:59], v[14:15], s[0:1], v[64:65] op_sel_hi:[1,0,1]
	v_pk_fma_f32 v[60:61], v[16:17], s[0:1], v[66:67] op_sel_hi:[1,0,1]
	v_pk_fma_f32 v[62:63], v[18:19], s[0:1], v[68:69] op_sel_hi:[1,0,1]
	v_pk_fma_f32 v[64:65], v[20:21], s[0:1], v[70:71] op_sel_hi:[1,0,1]
	v_pk_fma_f32 v[66:67], v[22:23], s[0:1], v[72:73] op_sel_hi:[1,0,1]
	v_pk_fma_f32 v[68:69], v[24:25], s[0:1], v[74:75] op_sel_hi:[1,0,1]
	v_pk_fma_f32 v[70:71], v[26:27], s[0:1], v[76:77] op_sel_hi:[1,0,1]
	v_pk_fma_f32 v[72:73], v[28:29], s[0:1], v[78:79] op_sel_hi:[1,0,1]
	v_pk_fma_f32 v[74:75], v[30:31], s[0:1], v[80:81] op_sel_hi:[1,0,1]
	v_readlane_b32 s0, v131, 62
	s_waitcnt vmcnt(2)
	v_cvt_scalef32_pk32_f32_fp6 v[0:31], v[38:43], 1.0
	v_pk_fma_f32 v[38:39], v[0:1], s[0:1], v[44:45] op_sel_hi:[1,0,1]
	v_pk_fma_f32 v[40:41], v[2:3], s[0:1], v[46:47] op_sel_hi:[1,0,1]
	v_pk_fma_f32 v[42:43], v[4:5], s[0:1], v[48:49] op_sel_hi:[1,0,1]
	v_pk_fma_f32 v[44:45], v[6:7], s[0:1], v[50:51] op_sel_hi:[1,0,1]
	v_pk_fma_f32 v[46:47], v[8:9], s[0:1], v[52:53] op_sel_hi:[1,0,1]
	v_pk_fma_f32 v[48:49], v[10:11], s[0:1], v[54:55] op_sel_hi:[1,0,1]
	v_pk_fma_f32 v[50:51], v[12:13], s[0:1], v[56:57] op_sel_hi:[1,0,1]
	v_pk_fma_f32 v[52:53], v[14:15], s[0:1], v[58:59] op_sel_hi:[1,0,1]
	v_pk_fma_f32 v[54:55], v[16:17], s[0:1], v[60:61] op_sel_hi:[1,0,1]
	v_pk_fma_f32 v[56:57], v[18:19], s[0:1], v[62:63] op_sel_hi:[1,0,1]
	v_pk_fma_f32 v[58:59], v[20:21], s[0:1], v[64:65] op_sel_hi:[1,0,1]
	v_pk_fma_f32 v[62:63], v[22:23], s[0:1], v[66:67] op_sel_hi:[1,0,1]
	v_pk_fma_f32 v[64:65], v[24:25], s[0:1], v[68:69] op_sel_hi:[1,0,1]
	v_pk_fma_f32 v[66:67], v[26:27], s[0:1], v[70:71] op_sel_hi:[1,0,1]
	v_pk_fma_f32 v[68:69], v[28:29], s[0:1], v[72:73] op_sel_hi:[1,0,1]
	v_pk_fma_f32 v[70:71], v[30:31], s[0:1], v[74:75] op_sel_hi:[1,0,1]
	v_readlane_b32 s0, v131, 63
	s_waitcnt vmcnt(0)
	v_cvt_scalef32_pk32_f32_fp6 v[0:31], v[32:37], 1.0
	v_pk_fma_f32 v[34:35], v[0:1], s[0:1], v[38:39] op_sel_hi:[1,0,1]
	v_pk_fma_f32 v[32:33], v[2:3], s[0:1], v[40:41] op_sel_hi:[1,0,1]
	v_pk_fma_f32 v[38:39], v[4:5], s[0:1], v[42:43] op_sel_hi:[1,0,1]
	v_pk_fma_f32 v[36:37], v[6:7], s[0:1], v[44:45] op_sel_hi:[1,0,1]
	v_pk_fma_f32 v[42:43], v[8:9], s[0:1], v[46:47] op_sel_hi:[1,0,1]
	v_pk_fma_f32 v[40:41], v[10:11], s[0:1], v[48:49] op_sel_hi:[1,0,1]
	v_pk_fma_f32 v[48:49], v[12:13], s[0:1], v[50:51] op_sel_hi:[1,0,1]
	v_pk_fma_f32 v[46:47], v[14:15], s[0:1], v[52:53] op_sel_hi:[1,0,1]
	v_pk_fma_f32 v[50:51], v[18:19], s[0:1], v[56:57] op_sel_hi:[1,0,1]
	v_pk_fma_f32 v[54:55], v[16:17], s[0:1], v[54:55] op_sel_hi:[1,0,1]
	v_pk_fma_f32 v[60:61], v[20:21], s[0:1], v[58:59] op_sel_hi:[1,0,1]
	v_pk_fma_f32 v[56:57], v[22:23], s[0:1], v[62:63] op_sel_hi:[1,0,1]
	v_pk_fma_f32 v[44:45], v[24:25], s[0:1], v[64:65] op_sel_hi:[1,0,1]
	v_pk_fma_f32 v[64:65], v[26:27], s[0:1], v[66:67] op_sel_hi:[1,0,1]
	v_pk_fma_f32 v[18:19], v[28:29], s[0:1], v[68:69] op_sel_hi:[1,0,1]
	v_pk_fma_f32 v[24:25], v[30:31], s[0:1], v[70:71] op_sel_hi:[1,0,1]
	s_lshr_b32 s0, s58, 12
	s_ashr_i32 s59, s58, 31
	s_mul_i32 s4, s0, 0x3000
	s_lshl_b64 s[0:1], s[58:59], 12
	s_add_u32 s2, s71, s0
	v_lshlrev_b32_e32 v12, 2, v148
	s_addc_u32 s3, s74, s1
	v_ashrrev_i32_e32 v13, 31, v12
	v_lshlrev_b32_e32 v63, 3, v148
	v_lshl_add_u64 v[14:15], v[12:13], 1, s[2:3]
	v_add3_u32 v62, v201, s4, v63
	global_load_dwordx2 v[16:17], v[14:15], off
	ds_read2st64_b64 v[0:3], v62 offset1:1
	global_load_dwordx2 v[20:21], v[14:15], off offset:512
	global_load_dwordx2 v[22:23], v[14:15], off offset:1024
	ds_read2st64_b64 v[4:7], v62 offset0:2 offset1:3
	global_load_dwordx2 v[52:53], v[14:15], off offset:1536
	global_load_dwordx2 v[58:59], v[14:15], off offset:2048
	ds_read2st64_b64 v[8:11], v62 offset0:4 offset1:5
	global_load_dwordx2 v[66:67], v[14:15], off offset:2560
	global_load_dwordx2 v[68:69], v[14:15], off offset:3072
	global_load_dwordx2 v[26:27], v[14:15], off offset:3584
	ds_read2st64_b64 v[28:31], v62 offset0:6 offset1:7
	s_lshl_b64 s[2:3], s[58:59], 13
	s_add_u32 s4, s16, s2
	s_addc_u32 s5, s17, s3
	s_and_b64 vcc, exec, s[54:55]
	s_waitcnt lgkmcnt(0)
	v_lshlrev_b32_e32 v72, 16, v30
	v_and_b32_e32 v73, 0xffff0000, v30
	v_lshlrev_b32_e32 v30, 16, v31
	v_and_b32_e32 v31, 0xffff0000, v31
	v_pk_mul_f32 v[24:25], v[24:25], v[30:31]
	v_lshlrev_b32_e32 v30, 16, v28
	v_and_b32_e32 v31, 0xffff0000, v28
	v_pk_mul_f32 v[30:31], v[44:45], v[30:31]
	v_lshlrev_b32_e32 v28, 16, v29
	v_and_b32_e32 v29, 0xffff0000, v29
	v_pk_mul_f32 v[28:29], v[64:65], v[28:29]
	v_pk_mul_f32 v[18:19], v[18:19], v[72:73]
	s_waitcnt vmcnt(0)
	v_lshlrev_b32_e32 v70, 16, v26
	v_and_b32_e32 v71, 0xffff0000, v26
	v_lshlrev_b32_e32 v26, 16, v27
	v_and_b32_e32 v27, 0xffff0000, v27
	v_pk_fma_f32 v[24:25], v[26:27], s[38:39], v[24:25] op_sel_hi:[1,0,1]
	v_lshlrev_b32_e32 v26, 16, v68
	v_and_b32_e32 v27, 0xffff0000, v68
	v_pk_fma_f32 v[26:27], v[26:27], s[38:39], v[30:31] op_sel_hi:[1,0,1]
	v_lshlrev_b32_e32 v30, 16, v69
	v_and_b32_e32 v31, 0xffff0000, v69
	v_pk_fma_f32 v[44:45], v[30:31], s[38:39], v[28:29] op_sel_hi:[1,0,1]
	v_lshlrev_b32_e32 v30, 16, v10
	v_and_b32_e32 v31, 0xffff0000, v10
	v_lshlrev_b32_e32 v28, 16, v66
	v_and_b32_e32 v29, 0xffff0000, v66
	v_pk_mul_f32 v[30:31], v[60:61], v[30:31]
	v_lshlrev_b32_e32 v10, 16, v11
	v_and_b32_e32 v11, 0xffff0000, v11
	v_pk_fma_f32 v[28:29], v[28:29], s[38:39], v[30:31] op_sel_hi:[1,0,1]
	v_lshlrev_b32_e32 v30, 16, v67
	v_and_b32_e32 v31, 0xffff0000, v67
	v_pk_mul_f32 v[10:11], v[56:57], v[10:11]
	v_lshlrev_b32_e32 v56, 16, v8
	v_and_b32_e32 v57, 0xffff0000, v8
	v_pk_fma_f32 v[10:11], v[30:31], s[38:39], v[10:11] op_sel_hi:[1,0,1]
	v_lshlrev_b32_e32 v30, 16, v58
	v_and_b32_e32 v31, 0xffff0000, v58
	v_pk_mul_f32 v[54:55], v[54:55], v[56:57]
	v_lshlrev_b32_e32 v8, 16, v9
	v_and_b32_e32 v9, 0xffff0000, v9
	v_pk_fma_f32 v[30:31], v[30:31], s[38:39], v[54:55] op_sel_hi:[1,0,1]
	v_lshlrev_b32_e32 v54, 16, v59
	v_and_b32_e32 v55, 0xffff0000, v59
	v_pk_mul_f32 v[8:9], v[50:51], v[8:9]
	v_lshlrev_b32_e32 v50, 16, v52
	v_pk_fma_f32 v[8:9], v[54:55], s[38:39], v[8:9] op_sel_hi:[1,0,1]
	v_lshlrev_b32_e32 v54, 16, v6
	v_and_b32_e32 v55, 0xffff0000, v6
	v_and_b32_e32 v51, 0xffff0000, v52
	v_pk_mul_f32 v[48:49], v[48:49], v[54:55]
	v_lshlrev_b32_e32 v6, 16, v7
	v_and_b32_e32 v7, 0xffff0000, v7
	v_pk_fma_f32 v[48:49], v[50:51], s[38:39], v[48:49] op_sel_hi:[1,0,1]
	v_lshlrev_b32_e32 v50, 16, v53
	v_and_b32_e32 v51, 0xffff0000, v53
	v_pk_mul_f32 v[6:7], v[46:47], v[6:7]
	v_lshlrev_b32_e32 v46, 16, v22
	v_pk_fma_f32 v[6:7], v[50:51], s[38:39], v[6:7] op_sel_hi:[1,0,1]
	v_lshlrev_b32_e32 v50, 16, v4
	v_and_b32_e32 v51, 0xffff0000, v4
	v_lshlrev_b32_e32 v4, 16, v5
	v_and_b32_e32 v5, 0xffff0000, v5
	v_and_b32_e32 v47, 0xffff0000, v22
	v_lshlrev_b32_e32 v22, 16, v23
	v_and_b32_e32 v23, 0xffff0000, v23
	v_pk_mul_f32 v[4:5], v[40:41], v[4:5]
	v_lshlrev_b32_e32 v40, 16, v2
	v_and_b32_e32 v41, 0xffff0000, v2
	v_pk_fma_f32 v[4:5], v[22:23], s[38:39], v[4:5] op_sel_hi:[1,0,1]
	v_lshlrev_b32_e32 v22, 16, v20
	v_and_b32_e32 v23, 0xffff0000, v20
	v_pk_mul_f32 v[38:39], v[38:39], v[40:41]
	v_lshlrev_b32_e32 v40, 16, v0
	v_and_b32_e32 v41, 0xffff0000, v0
	v_pk_fma_f32 v[22:23], v[22:23], s[38:39], v[38:39] op_sel_hi:[1,0,1]
	v_lshlrev_b32_e32 v38, 16, v16
	v_and_b32_e32 v39, 0xffff0000, v16
	v_pk_mul_f32 v[34:35], v[34:35], v[40:41]
	v_lshlrev_b32_e32 v16, 16, v17
	v_pk_fma_f32 v[34:35], v[38:39], s[38:39], v[34:35] op_sel_hi:[1,0,1]
	v_and_b32_e32 v17, 0xffff0000, v17
	v_add_f32_e32 v0, 0, v34
	v_add_f32_e32 v38, v35, v0
	v_lshlrev_b32_e32 v0, 16, v1
	v_and_b32_e32 v1, 0xffff0000, v1
	v_pk_mul_f32 v[0:1], v[32:33], v[0:1]
	v_lshlrev_b32_e32 v2, 16, v3
	v_pk_fma_f32 v[0:1], v[16:17], s[38:39], v[0:1] op_sel_hi:[1,0,1]
	v_and_b32_e32 v3, 0xffff0000, v3
	v_add_f32_e32 v16, v0, v38
	v_add_f32_e32 v16, v1, v16
	v_lshlrev_b32_e32 v20, 16, v21
	v_and_b32_e32 v21, 0xffff0000, v21
	v_pk_mul_f32 v[2:3], v[36:37], v[2:3]
	v_add_f32_e32 v16, v22, v16
	v_pk_fma_f32 v[2:3], v[20:21], s[38:39], v[2:3] op_sel_hi:[1,0,1]
	v_add_f32_e32 v16, v23, v16
	v_pk_mul_f32 v[42:43], v[42:43], v[50:51]
	v_add_f32_e32 v16, v2, v16
	v_pk_fma_f32 v[52:53], v[46:47], s[38:39], v[42:43] op_sel_hi:[1,0,1]
	v_add_f32_e32 v16, v3, v16
	v_add_f32_e32 v16, v52, v16
	v_add_f32_e32 v16, v53, v16
	v_add_f32_e32 v16, v4, v16
	v_add_f32_e32 v16, v5, v16
	v_add_f32_e32 v16, v48, v16
	v_add_f32_e32 v16, v49, v16
	v_add_f32_e32 v16, v6, v16
	v_add_f32_e32 v16, v7, v16
	v_add_f32_e32 v16, v30, v16
	v_add_f32_e32 v16, v31, v16
	v_add_f32_e32 v16, v8, v16
	v_add_f32_e32 v16, v9, v16
	v_add_f32_e32 v16, v28, v16
	v_add_f32_e32 v16, v29, v16
	v_add_f32_e32 v16, v10, v16
	v_add_f32_e32 v16, v11, v16
	v_add_f32_e32 v16, v26, v16
	v_add_f32_e32 v16, v27, v16
	v_add_f32_e32 v16, v44, v16
	v_pk_fma_f32 v[18:19], v[70:71], s[38:39], v[18:19] op_sel_hi:[1,0,1]
	v_add_f32_e32 v16, v45, v16
	v_add_f32_e32 v16, v18, v16
	v_add_f32_e32 v16, v19, v16
	v_add_f32_e32 v16, v24, v16
	v_add_f32_e32 v16, v25, v16
	v_mov_b32_e32 v17, v105
	v_add_u32_e32 v50, v202, v63
	v_add_f32_dpp v16, v16, v16 quad_perm:[1,0,3,2] row_mask:0xf bank_mask:0xf bound_ctrl:1
	v_add_u32_e32 v51, v203, v63
	ds_read_b64 v[20:21], v50
	ds_read_b64 v[36:37], v51
	v_add_f32_dpp v16, v16, v16 quad_perm:[2,3,0,1] row_mask:0xf bank_mask:0xf bound_ctrl:1
	s_waitcnt lgkmcnt(1)
	v_lshlrev_b32_e32 v54, 16, v20
	v_add_f32_dpp v16, v16, v16 row_half_mirror row_mask:0xf bank_mask:0xf bound_ctrl:1
	s_waitcnt lgkmcnt(0)
	v_lshlrev_b32_e32 v56, 16, v36
	v_and_b32_e32 v57, 0xffff0000, v36
	v_add_f32_dpp v16, v16, v16 row_mirror row_mask:0xf bank_mask:0xf bound_ctrl:1
	v_lshlrev_b32_e32 v60, 16, v37
	v_and_b32_e32 v61, 0xffff0000, v37
	v_mov_b32_dpp v17, v16 row_bcast:15 row_mask:0xa bank_mask:0xf
	v_add_f32_e32 v16, v16, v17
	v_mov_b32_e32 v17, v105
	v_and_b32_e32 v55, 0xffff0000, v20
	v_lshlrev_b32_e32 v58, 16, v21
	v_mov_b32_dpp v17, v16 row_bcast:31 row_mask:0xc bank_mask:0xf
	v_add_f32_e32 v16, v16, v17
	v_and_b32_e32 v59, 0xffff0000, v21
	v_readlane_b32 s2, v16, 63
	s_nop 1
	v_mul_f32_e32 v64, s2, v187
	v_pk_add_f32 v[66:67], v[34:35], v[64:65] op_sel_hi:[1,0] neg_lo:[0,1] neg_hi:[0,1]
	v_pk_add_f32 v[70:71], v[0:1], v[64:65] op_sel_hi:[1,0] neg_lo:[0,1] neg_hi:[0,1]
	v_pk_mul_f32 v[68:69], v[66:67], v[66:67]
	v_pk_mul_f32 v[0:1], v[70:71], v[70:71]
	v_add_f32_e32 v63, v68, v69
	v_pk_add_f32 v[46:47], v[22:23], v[64:65] op_sel_hi:[1,0] neg_lo:[0,1] neg_hi:[0,1]
	v_add_f32_e32 v0, v0, v63
	v_pk_mul_f32 v[72:73], v[46:47], v[46:47]
	v_add_f32_e32 v0, v1, v0
	v_pk_add_f32 v[42:43], v[2:3], v[64:65] op_sel_hi:[1,0] neg_lo:[0,1] neg_hi:[0,1]
	v_add_f32_e32 v0, v72, v0
	v_pk_mul_f32 v[2:3], v[42:43], v[42:43]
	v_add_f32_e32 v0, v73, v0
	v_pk_add_f32 v[40:41], v[52:53], v[64:65] op_sel_hi:[1,0] neg_lo:[0,1] neg_hi:[0,1]
	v_add_f32_e32 v0, v2, v0
	v_pk_mul_f32 v[52:53], v[40:41], v[40:41]
	v_add_f32_e32 v0, v3, v0
	v_pk_add_f32 v[22:23], v[4:5], v[64:65] op_sel_hi:[1,0] neg_lo:[0,1] neg_hi:[0,1]
	v_add_f32_e32 v0, v52, v0
	v_pk_mul_f32 v[4:5], v[22:23], v[22:23]
	v_add_f32_e32 v0, v53, v0
	v_pk_add_f32 v[38:39], v[48:49], v[64:65] op_sel_hi:[1,0] neg_lo:[0,1] neg_hi:[0,1]
	v_add_f32_e32 v0, v4, v0
	v_pk_mul_f32 v[48:49], v[38:39], v[38:39]
	v_add_f32_e32 v0, v5, v0
	v_pk_add_f32 v[36:37], v[6:7], v[64:65] op_sel_hi:[1,0] neg_lo:[0,1] neg_hi:[0,1]
	v_add_f32_e32 v0, v48, v0
	v_pk_mul_f32 v[74:75], v[36:37], v[36:37]
	v_add_f32_e32 v0, v49, v0
	v_pk_add_f32 v[34:35], v[30:31], v[64:65] op_sel_hi:[1,0] neg_lo:[0,1] neg_hi:[0,1]
	v_add_f32_e32 v0, v74, v0
	v_pk_mul_f32 v[76:77], v[34:35], v[34:35]
	v_add_f32_e32 v0, v75, v0
	v_pk_add_f32 v[32:33], v[8:9], v[64:65] op_sel_hi:[1,0] neg_lo:[0,1] neg_hi:[0,1]
	v_add_f32_e32 v0, v76, v0
	v_pk_mul_f32 v[78:79], v[32:33], v[32:33]
	v_add_f32_e32 v0, v77, v0
	v_pk_add_f32 v[30:31], v[28:29], v[64:65] op_sel_hi:[1,0] neg_lo:[0,1] neg_hi:[0,1]
	v_add_f32_e32 v0, v78, v0
	v_pk_mul_f32 v[80:81], v[30:31], v[30:31]
	v_add_f32_e32 v0, v79, v0
	v_pk_add_f32 v[28:29], v[10:11], v[64:65] op_sel_hi:[1,0] neg_lo:[0,1] neg_hi:[0,1]
	v_add_f32_e32 v0, v80, v0
	v_pk_mul_f32 v[10:11], v[28:29], v[28:29]
	v_add_f32_e32 v0, v81, v0
	v_pk_add_f32 v[20:21], v[26:27], v[64:65] op_sel_hi:[1,0] neg_lo:[0,1] neg_hi:[0,1]
	v_add_f32_e32 v0, v10, v0
	v_pk_mul_f32 v[26:27], v[20:21], v[20:21]
	v_add_f32_e32 v0, v11, v0
	v_pk_add_f32 v[16:17], v[44:45], v[64:65] op_sel_hi:[1,0] neg_lo:[0,1] neg_hi:[0,1]
	v_add_f32_e32 v0, v26, v0
	v_pk_mul_f32 v[44:45], v[16:17], v[16:17]
	v_add_f32_e32 v0, v27, v0
	v_pk_add_f32 v[8:9], v[18:19], v[64:65] op_sel_hi:[1,0] neg_lo:[0,1] neg_hi:[0,1]
	v_add_f32_e32 v0, v44, v0
	v_pk_mul_f32 v[18:19], v[8:9], v[8:9]
	v_add_f32_e32 v0, v45, v0
	v_pk_add_f32 v[6:7], v[24:25], v[64:65] op_sel_hi:[1,0] neg_lo:[0,1] neg_hi:[0,1]
	v_add_f32_e32 v0, v18, v0
	v_pk_mul_f32 v[24:25], v[6:7], v[6:7]
	v_add_f32_e32 v0, v19, v0
	v_add_f32_e32 v0, v24, v0
	v_add_f32_e32 v0, v25, v0
	v_mov_b32_e32 v1, v105
	s_nop 0
	v_add_f32_dpp v0, v0, v0 quad_perm:[1,0,3,2] row_mask:0xf bank_mask:0xf bound_ctrl:1
	s_nop 1
	v_add_f32_dpp v0, v0, v0 quad_perm:[2,3,0,1] row_mask:0xf bank_mask:0xf bound_ctrl:1
	s_nop 1
	v_add_f32_dpp v0, v0, v0 row_half_mirror row_mask:0xf bank_mask:0xf bound_ctrl:1
	s_nop 1
	v_add_f32_dpp v0, v0, v0 row_mirror row_mask:0xf bank_mask:0xf bound_ctrl:1
	s_nop 1
	v_mov_b32_dpp v1, v0 row_bcast:15 row_mask:0xa bank_mask:0xf
	v_add_f32_e32 v0, v0, v1
	v_mov_b32_e32 v1, v105
	s_nop 1
	v_mov_b32_dpp v1, v0 row_bcast:31 row_mask:0xc bank_mask:0xf
	v_add_f32_e32 v0, v0, v1
	s_nop 0
	v_readlane_b32 s2, v0, 63
	s_nop 1
	v_fma_f32 v0, s2, v187, v183
	v_rsq_f32_e32 v10, v0
	s_mov_b64 s[2:3], -1
	v_pk_mul_f32 v[0:1], v[66:67], v[10:11] op_sel_hi:[1,0]
	v_pk_mul_f32 v[2:3], v[70:71], v[10:11] op_sel_hi:[1,0]
	v_pk_fma_f32 v[0:1], v[0:1], v[54:55], v[56:57]
	v_pk_fma_f32 v[2:3], v[2:3], v[58:59], v[60:61]
	s_cbranch_vccz .LBB0_1142
	ds_read2st64_b64 v[24:27], v62 offset0:8 offset1:16
	v_cvt_pk_bf16_f32 v4, v0, v1
	v_cvt_pk_bf16_f32 v5, v2, v3
	global_store_dwordx2 v[14:15], v[4:5], off
	s_mov_b64 s[2:3], 0
	s_waitcnt lgkmcnt(0)
	v_lshlrev_b32_e32 v18, 16, v26
	v_and_b32_e32 v19, 0xffff0000, v26
	v_lshlrev_b32_e32 v4, 16, v24
	v_and_b32_e32 v5, 0xffff0000, v24
	v_pk_add_f32 v[18:19], v[18:19], 1.0 op_sel_hi:[1,0]
	v_lshlrev_b32_e32 v24, 16, v27
	v_pk_fma_f32 v[4:5], v[0:1], v[18:19], v[4:5]
	v_lshlrev_b32_e32 v18, 16, v25
	v_and_b32_e32 v19, 0xffff0000, v25
	v_and_b32_e32 v25, 0xffff0000, v27
	v_pk_add_f32 v[24:25], v[24:25], 1.0 op_sel_hi:[1,0]
	v_cvt_pk_bf16_f32 v4, v4, v5
	v_pk_fma_f32 v[18:19], v[2:3], v[24:25], v[18:19]
	s_nop 0
	v_cvt_pk_bf16_f32 v5, v18, v19
